# v44 + bf16 GEMM loops (P4-P7) in the same fused per-half schedule
# speedup vs baseline: 1.0049x; 1.0049x over previous
; #define PG8_BAR __builtin_amdgcn_s_barrier()
; template <class Epi, class Sched, bool ALIGN_EPI = true, bool F8 = false>
; __device__ __forceinline__ void gemm_phase(PG8_LAS unsigned char* lds, const Sched& S, const Epi& E) {
;     const int tid = threadIdx.x, wid = __builtin_amdgcn_readfirstlane(tid >> 6), lane = tid & 63, wr = wid >> 2, wc = wid & 3, fr = lane & 15, fq = lane >> 4;
;     int Rs[2], Cs[2];
; #pragma unroll
;     for (int i = 0; i < 2; ++i) stage_rc(tid * 16 + i * 8192, Rs[i], Cs[i]);
;     unsigned voffB[2][2], voffA[2][2], voffAn[2][2];
; #pragma unroll
;     for (int h = 0; h < 2; ++h)
; #pragma unroll
;         for (int i = 0; i < 2; ++i) {
;             if constexpr (HasP16<Epi>::v) { const int r = Rs[i]; voffB[h][i] = S.b_off(64 * (r >> 5) + 16 * ((r & 15) >> 2) + 8 * h + 4 * ((r >> 4) & 1) + (r & 3), Cs[i]); }
;             else { const int Rb = Epi::PERM ? ((Rs[i] & ~31) + perm32(Rs[i] & 31)) : Rs[i]; voffB[h][i] = S.b_off(h * HALF + Rb, Cs[i]); } }
;     const size_t kstep = (size_t)SchedKstep<Sched>::v, kstepB = (size_t)SchedKstepB<Sched>::v;
;     const unsigned ldsw = (unsigned)wid * 1024u;
;     const int aoff = lds_byte(wr * 64 + fr, fq * 8), boff = lds_byte(wc * 32 + fr, fq * 8);
;     ...
;     GUnit cur, nxt; int ui = 0;
;     if (!S.next(0, cur)) return;
;     S.a_off(cur, Rs, Cs, voffA);
; #pragma unroll
;     for (int h = 0; h < 2; ++h)
; #pragma unroll
;         for (int i = 0; i < 2; ++i) voffAn[h][i] = voffA[h][i];
;     f32x4 acc[2][2][4][2];
; #pragma unroll
;     for (int a = 0; a < 2; ++a)
; #pragma unroll
;         for (int b = 0; b < 2; ++b)
; #pragma unroll
;             for (int m = 0; m < 4; ++m)
; #pragma unroll
;                 for (int n = 0; n < 2; ++n) acc[a][b][m][n] = (f32x4){0.f, 0.f, 0.f, 0.f};
;     bf16x8 At[4][2], B0[2][2], B1[2][2]; i32x8 At8[4], B08[2], B18[2];
;     const int f8scale = 0x7F7F7F7F;
;     const char* cA = cur.A; const char* cB = cur.B;
;     PG8_STAGE(PG8_SB(0, 0), cB, voffB[0]); PG8_STAGE(PG8_SB(0, 1), cB, voffB[1]); PG8_STAGE(PG8_SA(0, 0), cA, voffA[0]); PG8_STAGE(PG8_SA(0, 1), cA, voffA[1]);
;     if (wr == 1) PG8_BAR;
;     PG8_WAIT_V(2); PG8_BAR;
; __global__ void __launch_bounds__(NWAVES * 64, 2) fwd_kernel(Args a) {
;     ...
;         { SchedE S{G, bid, (const char*)(ws + WS_A2), (const char*)(ws + WS_WET)}; EpiE E{(float*)(ws + WS_E)}; pg8::gemm_phase<EpiE, SchedE>(lds, S, E); }
.LBB0_481:
	s_cmp_lt_i32 s34, 5
	s_cselect_b64 s[4:5], -1, 0
	s_and_b64 s[0:1], s[4:5], s[40:41]
	s_andn2_b64 vcc, exec, s[0:1]
	s_cbranch_vccnz .LBB0_521
	v_lshlrev_b32_e32 v2, 6, v0
	v_and_b32_e32 v168, 0x3c0, v2
	v_lshlrev_b32_e32 v2, 2, v0
	v_readfirstlane_b32 s10, v0
	v_and_b32_e32 v169, 15, v0
	s_cmpk_gt_i32 s2, 0x7f
	v_and_b32_e32 v172, 32, v2
	s_cbranch_scc1 .LBB0_498
	s_add_u32 s30, s36, 0x32000000
	s_addc_u32 s31, s37, 0
	s_add_u32 s40, s36, 0x3d00000
	v_lshrrev_b32_e32 v3, 3, v0
	s_mul_i32 s1, s2, 0x108
	s_addc_u32 s41, s37, 0
	s_lshr_b32 s8, s10, 6
	v_or_b32_e32 v4, 64, v3
	v_bfe_u32 v5, v0, 2, 4
	s_movk_i32 s0, 0x70
	s_add_i32 s1, s1, 8
	s_lshr_b32 s11, s10, 8
	s_lshl_b32 s14, s8, 10
	v_and_or_b32 v4, v4, s0, v5
	s_ashr_i32 s0, s2, 2
	s_mul_hi_i32 s6, s1, 0x600
	s_mulk_i32 s1, 0x600
	s_add_u32 s22, s30, s1
	s_addc_u32 s23, s31, s6
	s_ashr_i32 s1, s0, 31
	v_lshlrev_b32_e32 v2, 4, v0
	v_and_b32_e32 v6, 32, v0
	s_lshl_b64 s[6:7], s[0:1], 18
	v_bitop3_b32 v10, v2, v6, 48 bitop3:0x6c
	v_and_b32_e32 v11, 64, v0
	s_add_u32 s24, s40, s6
	v_or_b32_e32 v2, v10, v11
	v_and_or_b32 v3, v3, 48, v5
	s_addc_u32 s25, s41, s7
	s_add_i32 s42, s14, 0
	v_lshl_or_b32 v134, v3, 10, v2
	s_add_i32 m0, s42, 0x10000
	v_lshl_or_b32 v130, v4, 10, v2
	global_load_lds_dwordx4 v134, s[24:25]
	s_add_i32 m0, s42, 0x12000
	v_or_b32_e32 v136, 0x20000, v134
	v_lshrrev_b32_e32 v2, 1, v2
	v_mul_u32_u24_e32 v12, 0x300, v3
	global_load_lds_dwordx4 v130, s[24:25]
	s_add_i32 m0, s42, 0x14000
	v_or_b32_e32 v132, 0x20000, v130
	v_or_b32_e32 v3, v2, v12
	v_mul_u32_u24_e32 v13, 0x300, v4
	global_load_lds_dwordx4 v136, s[24:25]
	s_add_i32 m0, s42, 0x16000
	v_lshlrev_b32_e32 v138, 1, v3
	v_or_b32_e32 v2, v13, v2
	global_load_lds_dwordx4 v132, s[24:25]
	s_mov_b32 m0, s42
	s_add_i32 s43, s42, 0x2000
	v_lshlrev_b32_e32 v140, 1, v2
	global_load_lds_dwordx4 v138, s[22:23]
	s_mov_b32 m0, s43
	s_add_i32 s44, s42, 0x4000
	v_add_u32_e32 v142, 0x30000, v138
	global_load_lds_dwordx4 v140, s[22:23]
	s_mov_b32 m0, s44
	s_add_i32 s45, s42, 0x6000
	v_add_u32_e32 v144, 0x30000, v140
	global_load_lds_dwordx4 v142, s[22:23]
	s_mov_b32 m0, s45
	v_mov_b32_e32 v135, 0
	global_load_lds_dwordx4 v144, s[22:23]
	v_mov_b32_e32 v131, v135
	v_mov_b32_e32 v139, v135
	v_mov_b32_e32 v141, v135
	s_cmp_eq_u32 s11, 1
	s_mov_b32 s46, 0
	v_lshl_add_u64 v[6:7], s[24:25], 0, v[134:135]
	v_lshl_add_u64 v[2:3], s[24:25], 0, v[130:131]
	v_mov_b32_e32 v137, v135
	v_mov_b32_e32 v133, v135
	v_lshl_add_u64 v[4:5], s[22:23], 0, v[138:139]
	s_cselect_b64 s[6:7], -1, 0
	s_cmp_lg_u32 s11, 1
	v_lshl_add_u64 v[8:9], s[22:23], 0, v[140:141]
	s_cbranch_scc1 .LBB0_485
.LBB0_485:
	s_lshl_b32 s8, s8, 5
	s_and_b32 s16, s8, 0x60
	s_and_b32 s1, s2, 3
	s_lshl_b32 s15, s11, 13
	s_lshl_b32 s17, s16, 7
	s_mov_b64 s[8:9], 0x80
	s_add_u32 s12, s24, 0x80
	s_addc_u32 s13, s25, 0
	s_add_i32 m0, s42, 0x18000
	v_lshl_add_u64 v[6:7], v[6:7], 0, s[8:9]
	s_waitcnt vmcnt(2)
	s_barrier
	global_load_lds_dwordx4 v[6:7], off
	v_lshl_add_u64 v[2:3], v[2:3], 0, s[8:9]
	s_add_i32 m0, s42, 0x1a000
	s_add_i32 s47, s42, 0x8000
	global_load_lds_dwordx4 v[2:3], off
	v_lshl_add_u64 v[2:3], v[4:5], 0, s[8:9]
	s_mov_b32 m0, s47
	s_add_i32 s48, s42, 0xa000
	global_load_lds_dwordx4 v[2:3], off
	v_lshl_add_u64 v[2:3], v[8:9], 0, s[8:9]
	s_mov_b32 m0, s48
	v_and_b32_e32 v4, 48, v0
	global_load_lds_dwordx4 v[2:3], off
	s_add_i32 m0, s42, 0x1c000
	v_lshl_add_u64 v[2:3], s[12:13], 0, v[136:137]
	global_load_lds_dwordx4 v[2:3], off
	v_lshl_add_u64 v[2:3], s[12:13], 0, v[132:133]
	s_add_i32 m0, s42, 0x1e000
	s_cmpk_lt_u32 s10, 0x100
	global_load_lds_dwordx4 v[2:3], off
	v_lshl_or_b32 v2, s11, 6, v169
	v_lshlrev_b32_e32 v5, 2, v169
	s_cselect_b64 s[10:11], -1, 0
	s_lshl_b32 s12, s16, 2
	v_lshl_or_b32 v3, v169, 6, v4
	v_and_b32_e32 v5, 32, v5
	s_add_u32 s12, s36, s12
	v_bitop3_b32 v6, v3, s15, v5 bitop3:0xde
	s_addc_u32 s13, s37, 0
	v_mov_b32_e32 v5, v135
	v_or_b32_e32 v3, v4, v168
	v_lshl_add_u64 v[4:5], s[12:13], 0, v[4:5]
	s_mov_b64 s[12:13], 0x35200000
	v_lshl_add_u64 v[146:147], v[4:5], 0, s[12:13]
	v_or_b32_e32 v4, 16, v2
	v_mov_b32_e32 v5, v135
	v_lshlrev_b64 v[150:151], 10, v[4:5]
	v_or_b32_e32 v4, 32, v2
	v_lshlrev_b64 v[152:153], 10, v[4:5]
	v_or_b32_e32 v4, 48, v2
	v_lshlrev_b64 v[154:155], 10, v[4:5]
	v_add_u32_e32 v4, 0x80, v2
	v_bitop3_b32 v7, s17, v3, v172 bitop3:0xf6
	v_mov_b32_e32 v3, v135
	v_lshlrev_b64 v[156:157], 10, v[4:5]
	v_add_u32_e32 v4, 0x90, v2
	v_lshlrev_b64 v[148:149], 10, v[2:3]
	v_lshlrev_b64 v[158:159], 10, v[4:5]
	v_add_u32_e32 v4, 0xa0, v2
	v_add_u32_e32 v2, 0xb0, v2
	v_lshlrev_b64 v[162:163], 10, v[2:3]
	v_add_u16_e32 v2, v10, v11
	v_lshlrev_b64 v[160:161], 10, v[4:5]
	v_lshrrev_b16_e32 v4, 1, v2
	v_add_u32_e32 v2, v13, v4
	v_mov_b32_e32 v5, 0x30000
	v_lshl_add_u32 v2, v2, 1, v5
	s_waitcnt vmcnt(6)
	v_lshl_add_u64 v[164:165], v[2:3], 0, s[8:9]
	v_add_u32_e32 v2, v12, v4
	s_add_i32 s51, 0, 0x10000
	s_add_i32 s53, 0, 0x14000
	s_add_i32 s60, 0, 0x18000
	s_add_i32 s62, 0, 0x1c000
	v_lshl_add_u32 v2, v2, 1, v5
	v_add_u32_e32 v173, s51, v7
	v_add_u32_e32 v174, s53, v7
	s_add_i32 s51, s51, s14
	s_add_i32 s53, s53, s14
	v_add_u32_e32 v176, s60, v7
	v_add_u32_e32 v177, s62, v7
	s_add_i32 s60, s60, s14
	s_add_i32 s62, s62, s14
	v_mov_b32_e32 v143, v135
	v_mov_b32_e32 v145, v135
	v_lshl_add_u64 v[166:167], v[2:3], 0, s[8:9]
	v_add_u32_e32 v175, 0, v6
	s_add_i32 s49, s42, 0xc000
	s_add_i32 s50, s42, 0xe000
	s_mov_b64 s[12:13], 0x2000
	s_add_i32 s52, s51, 0x2000
	s_add_i32 s59, s53, 0x2000
	s_add_i32 s61, s60, 0x2000
	s_add_i32 s63, s62, 0x2000
	s_mov_b64 s[18:19], s[24:25]
	s_mov_b64 s[16:17], s[22:23]
	s_barrier
	s_branch .LBB0_488

; #define PG8_STAGE(bufoff, gbase, voff) do { _Pragma("unroll") for (int _i = 0; _i < 2; ++_i) \
;         __builtin_amdgcn_global_load_lds((const unsigned*)((const char*)(gbase) + (voff)[_i]), (PG8_LAS unsigned*)(lds + (bufoff) + ldsw + _i * 8192), 16, 0, 0); } while (0)
; #define PG8_WAIT_V(n) asm volatile("s_waitcnt vmcnt(" #n ")" ::: "memory")
; #define PG8_WAIT_L(n) asm volatile("s_waitcnt lgkmcnt(" #n ")" ::: "memory")
; #define PG8_BAR __builtin_amdgcn_s_barrier()
; #define PG8_SCHED __builtin_amdgcn_sched_barrier(0)
; template <class Epi, class Sched, bool ALIGN_EPI = true, bool F8 = false>
; __device__ __forceinline__ void gemm_phase(PG8_LAS unsigned char* lds, const Sched& S, const Epi& E) {
;     ...
;             PG8_LDB(B0, 0, 0); PG8_LDB(B1, 0, 1); PG8_SCHED; PG8_LDA(At, 0, 0); PG8_STAGE(PG8_SA(1, 1), a1, voffA[1]);
;             PG8_WAIT_V(8); PG8_WAIT_L(0); PG8_BAR; PG8_MMA(0, 0, At, B0); PG8_MMA(0, 1, At, B1); PG8_BAR; PG8_SCHED;
;     ...
; #pragma unroll
;         for (int a = 0; a < 2; ++a)
; #pragma unroll
;             for (int b = 0; b < 2; ++b)
; #pragma unroll
;                 for (int m = 0; m < 4; ++m)
; #pragma unroll
;                     for (int n = 0; n < 2; ++n) acc[a][b][m][n] = (f32x4){0.f, 0.f, 0.f, 0.f};
;         }
;         cur = nxt; cA = nA; cB = nB; ++ui;
; #pragma unroll
;         for (int h = 0; h < 2; ++h)
; #pragma unroll
;             for (int i = 0; i < 2; ++i) voffA[h][i] = voffAn[h][i];
.LBB0_490:
	s_add_u32 s15, s24, 0x100
	v_mov_b32_e32 v2, 0
	s_addc_u32 s65, s25, 0
	s_mov_b32 s66, -2
	v_mov_b32_e32 v3, v2
	v_mov_b32_e32 v4, v2
	v_mov_b32_e32 v5, v2
	v_mov_b32_e32 v6, v2
	v_mov_b32_e32 v7, v2
	v_mov_b32_e32 v8, v2
	v_mov_b32_e32 v9, v2
	v_mov_b32_e32 v10, v2
	v_mov_b32_e32 v11, v2
	v_mov_b32_e32 v12, v2
	v_mov_b32_e32 v13, v2
	v_mov_b32_e32 v14, v2
	v_mov_b32_e32 v15, v2
	v_mov_b32_e32 v16, v2
	v_mov_b32_e32 v17, v2
	v_mov_b32_e32 v18, v2
	v_mov_b32_e32 v19, v2
	v_mov_b32_e32 v20, v2
	v_mov_b32_e32 v21, v2
	v_mov_b32_e32 v22, v2
	v_mov_b32_e32 v23, v2
	v_mov_b32_e32 v24, v2
	v_mov_b32_e32 v25, v2
	v_mov_b32_e32 v30, v2
	v_mov_b32_e32 v31, v2
	v_mov_b32_e32 v32, v2
	v_mov_b32_e32 v33, v2
	v_mov_b32_e32 v38, v2
	v_mov_b32_e32 v39, v2
	v_mov_b32_e32 v40, v2
	v_mov_b32_e32 v41, v2
	v_mov_b32_e32 v26, v2
	v_mov_b32_e32 v27, v2
	v_mov_b32_e32 v28, v2
	v_mov_b32_e32 v29, v2
	v_mov_b32_e32 v34, v2
	v_mov_b32_e32 v35, v2
	v_mov_b32_e32 v36, v2
	v_mov_b32_e32 v37, v2
	v_mov_b32_e32 v42, v2
	v_mov_b32_e32 v43, v2
	v_mov_b32_e32 v44, v2
	v_mov_b32_e32 v45, v2
	v_mov_b32_e32 v46, v2
	v_mov_b32_e32 v47, v2
	v_mov_b32_e32 v48, v2
	v_mov_b32_e32 v49, v2
	v_mov_b32_e32 v50, v2
	v_mov_b32_e32 v51, v2
	v_mov_b32_e32 v52, v2
	v_mov_b32_e32 v53, v2
	v_mov_b32_e32 v54, v2
	v_mov_b32_e32 v55, v2
	v_mov_b32_e32 v56, v2
	v_mov_b32_e32 v57, v2
	v_mov_b32_e32 v58, v2
	v_mov_b32_e32 v59, v2
	v_mov_b32_e32 v60, v2
	v_mov_b32_e32 v61, v2
	v_mov_b32_e32 v62, v2
	v_mov_b32_e32 v63, v2
	v_mov_b32_e32 v64, v2
	v_mov_b32_e32 v65, v2
	v_mov_b32_e32 v66, v2
	v_mov_b32_e32 v67, v2
	v_mov_b32_e32 v68, v2
	v_mov_b32_e32 v69, v2
	v_mov_b32_e32 v70, v2
	v_mov_b32_e32 v71, v2
	v_mov_b32_e32 v72, v2
	v_mov_b32_e32 v73, v2
	v_mov_b32_e32 v74, v2
	v_mov_b32_e32 v75, v2
	v_mov_b32_e32 v76, v2
	v_mov_b32_e32 v77, v2
	v_mov_b32_e32 v78, v2
	v_mov_b32_e32 v79, v2
	v_mov_b32_e32 v80, v2
	v_mov_b32_e32 v81, v2
	v_mov_b32_e32 v82, v2
	v_mov_b32_e32 v83, v2
	v_mov_b32_e32 v84, v2
	v_mov_b32_e32 v85, v2
	v_mov_b32_e32 v86, v2
	v_mov_b32_e32 v87, v2
	v_mov_b32_e32 v88, v2
	v_mov_b32_e32 v89, v2
	v_mov_b32_e32 v94, v2
	v_mov_b32_e32 v95, v2
	v_mov_b32_e32 v96, v2
	v_mov_b32_e32 v97, v2
	v_mov_b32_e32 v102, v2
	v_mov_b32_e32 v103, v2
	v_mov_b32_e32 v104, v2
	v_mov_b32_e32 v105, v2
	v_mov_b32_e32 v90, v2
	v_mov_b32_e32 v91, v2
	v_mov_b32_e32 v92, v2
	v_mov_b32_e32 v93, v2
	v_mov_b32_e32 v98, v2
	v_mov_b32_e32 v99, v2
	v_mov_b32_e32 v100, v2
	v_mov_b32_e32 v101, v2
	v_mov_b32_e32 v106, v2
	v_mov_b32_e32 v107, v2
	v_mov_b32_e32 v108, v2
	v_mov_b32_e32 v109, v2
	v_mov_b32_e32 v110, v2
	v_mov_b32_e32 v111, v2
	v_mov_b32_e32 v112, v2
	v_mov_b32_e32 v113, v2
	v_mov_b32_e32 v114, v2
	v_mov_b32_e32 v115, v2
	v_mov_b32_e32 v116, v2
	v_mov_b32_e32 v117, v2
	v_mov_b32_e32 v118, v2
	v_mov_b32_e32 v119, v2
	v_mov_b32_e32 v120, v2
	v_mov_b32_e32 v121, v2
	v_mov_b32_e32 v122, v2
	v_mov_b32_e32 v123, v2
	v_mov_b32_e32 v124, v2
	v_mov_b32_e32 v125, v2
	v_mov_b32_e32 v126, v2
	v_mov_b32_e32 v127, v2
	v_mov_b32_e32 v128, v2
	v_mov_b32_e32 v129, v2
	s_bitcmp1_b32 s3, 2
	s_cbranch_scc1 .Lh1e_13405
.LBB0_491:
	ds_read_b128 v[178:181], v173
	ds_read_b128 v[182:185], v173 offset:1024
	ds_read_b128 v[186:189], v173 offset:2048
	ds_read_b128 v[190:193], v173 offset:3072
	ds_read_b128 v[194:197], v174
	ds_read_b128 v[198:201], v174 offset:1024
	ds_read_b128 v[202:205], v174 offset:2048
	ds_read_b128 v[206:209], v174 offset:3072
	s_add_u32 s24, s22, 0x100
	s_addc_u32 s25, s23, 0
	s_cmp_eq_u32 s66, 4
	s_cselect_b32 s29, s17, s25
	s_cselect_b32 s28, s16, s24
	s_cselect_b32 s27, s19, s65
	s_cselect_b32 s26, s18, s15
	s_mov_b32 m0, s49
	v_lshl_add_u64 v[242:243], s[22:23], 0, v[166:167]
	ds_read_b128 v[210:213], v175
	ds_read_b128 v[214:217], v175 offset:1024
	ds_read_b128 v[218:221], v175 offset:2048
	ds_read_b128 v[222:225], v175 offset:3072
	ds_read_b128 v[226:229], v175 offset:4096
	ds_read_b128 v[230:233], v175 offset:5120
	ds_read_b128 v[234:237], v175 offset:6144
	ds_read_b128 v[238:241], v175 offset:7168
	global_load_lds_dwordx4 v[242:243], off
	v_lshl_add_u64 v[242:243], s[22:23], 0, v[164:165]
	s_mov_b32 m0, s50
	s_nop 0
	global_load_lds_dwordx4 v[242:243], off
	s_waitcnt vmcnt(8)
	s_waitcnt lgkmcnt(0)
	s_setprio 1
	v_mfma_f32_16x16x32_bf16 v[126:129], v[178:181], v[210:213], v[126:129]
	v_mfma_f32_16x16x32_bf16 v[122:125], v[186:189], v[210:213], v[122:125]
	v_mfma_f32_16x16x32_bf16 v[118:121], v[178:181], v[218:221], v[118:121]
	v_mfma_f32_16x16x32_bf16 v[114:117], v[186:189], v[218:221], v[114:117]
	v_mfma_f32_16x16x32_bf16 v[110:113], v[178:181], v[226:229], v[110:113]
	v_mfma_f32_16x16x32_bf16 v[106:109], v[186:189], v[226:229], v[106:109]
	v_mfma_f32_16x16x32_bf16 v[98:101], v[178:181], v[234:237], v[98:101]
	v_mfma_f32_16x16x32_bf16 v[90:93], v[186:189], v[234:237], v[90:93]
	v_mfma_f32_16x16x32_bf16 v[126:129], v[182:185], v[214:217], v[126:129]
	v_mfma_f32_16x16x32_bf16 v[122:125], v[190:193], v[214:217], v[122:125]
	v_mfma_f32_16x16x32_bf16 v[118:121], v[182:185], v[222:225], v[118:121]
	v_mfma_f32_16x16x32_bf16 v[114:117], v[190:193], v[222:225], v[114:117]
	v_mfma_f32_16x16x32_bf16 v[110:113], v[182:185], v[230:233], v[110:113]
	v_mfma_f32_16x16x32_bf16 v[106:109], v[190:193], v[230:233], v[106:109]
	v_mfma_f32_16x16x32_bf16 v[98:101], v[182:185], v[238:241], v[98:101]
	v_mfma_f32_16x16x32_bf16 v[90:93], v[190:193], v[238:241], v[90:93]
	s_setprio 0
	s_setprio 1
	v_mfma_f32_16x16x32_bf16 v[102:105], v[194:197], v[210:213], v[102:105]
	v_mfma_f32_16x16x32_bf16 v[94:97], v[202:205], v[210:213], v[94:97]
	v_mfma_f32_16x16x32_bf16 v[86:89], v[194:197], v[218:221], v[86:89]
	v_mfma_f32_16x16x32_bf16 v[82:85], v[202:205], v[218:221], v[82:85]
	v_mfma_f32_16x16x32_bf16 v[78:81], v[194:197], v[226:229], v[78:81]
	v_mfma_f32_16x16x32_bf16 v[74:77], v[202:205], v[226:229], v[74:77]
	v_mfma_f32_16x16x32_bf16 v[70:73], v[194:197], v[234:237], v[70:73]
	v_mfma_f32_16x16x32_bf16 v[66:69], v[202:205], v[234:237], v[66:69]
	v_mfma_f32_16x16x32_bf16 v[102:105], v[198:201], v[214:217], v[102:105]
	v_mfma_f32_16x16x32_bf16 v[94:97], v[206:209], v[214:217], v[94:97]
	v_mfma_f32_16x16x32_bf16 v[86:89], v[198:201], v[222:225], v[86:89]
	v_mfma_f32_16x16x32_bf16 v[82:85], v[206:209], v[222:225], v[82:85]
	v_mfma_f32_16x16x32_bf16 v[78:81], v[198:201], v[230:233], v[78:81]
	v_mfma_f32_16x16x32_bf16 v[74:77], v[206:209], v[230:233], v[74:77]
	v_mfma_f32_16x16x32_bf16 v[70:73], v[198:201], v[238:241], v[70:73]
	v_mfma_f32_16x16x32_bf16 v[66:69], v[206:209], v[238:241], v[66:69]
	s_setprio 0
	s_barrier
; #define PG8_STAGE(bufoff, gbase, voff) do { _Pragma("unroll") for (int _i = 0; _i < 2; ++_i) \
;         __builtin_amdgcn_global_load_lds((const unsigned*)((const char*)(gbase) + (voff)[_i]), (PG8_LAS unsigned*)(lds + (bufoff) + ldsw + _i * 8192), 16, 0, 0); } while (0)
; #define PG8_WAIT_V(n) asm volatile("s_waitcnt vmcnt(" #n ")" ::: "memory")
; #define PG8_WAIT_L(n) asm volatile("s_waitcnt lgkmcnt(" #n ")" ::: "memory")
; #define PG8_BAR __builtin_amdgcn_s_barrier()
; #define PG8_SCHED __builtin_amdgcn_sched_barrier(0)
; template <class Epi, class Sched, bool ALIGN_EPI = true, bool F8 = false>
; __device__ __forceinline__ void gemm_phase(PG8_LAS unsigned char* lds, const Sched& S, const Epi& E) {
;     ...
;             PG8_LDA(At, 0, 1); PG8_STAGE(PG8_SB(0, 0), b2, voffB[0]); PG8_STAGE(PG8_SB(0, 1), b2, voffB[1]); PG8_STAGE(PG8_SA(0, 0), a2, vA2[0]);
;             PG8_WAIT_V(8); PG8_WAIT_L(0); PG8_BAR; PG8_MMA(1, 0, At, B0); PG8_MMA(1, 1, At, B1); PG8_BAR; PG8_SCHED;
;             PG8_LDB(B0, 1, 0); PG8_LDB(B1, 1, 1); PG8_SCHED; PG8_LDA(At, 1, 0); PG8_STAGE(PG8_SA(0, 1), a2, vA2[1]);
;             PG8_WAIT_V(8); PG8_WAIT_L(0); PG8_BAR; PG8_MMA(0, 0, At, B0); PG8_MMA(0, 1, At, B1); PG8_BAR; PG8_SCHED;
;             PG8_LDA(At, 1, 1); PG8_STAGE(PG8_SB(1, 0), b3, voffB[0]); PG8_STAGE(PG8_SB(1, 1), b3, voffB[1]); PG8_STAGE(PG8_SA(1, 0), a3, vA2[0]);
	s_mov_b32 m0, s51
	v_lshl_add_u64 v[242:243], s[26:27], 0, v[134:135]
	ds_read_b128 v[210:213], v175 offset:16384
	ds_read_b128 v[214:217], v175 offset:17408
	ds_read_b128 v[218:221], v175 offset:18432
	ds_read_b128 v[222:225], v175 offset:19456
	ds_read_b128 v[226:229], v175 offset:20480
	ds_read_b128 v[230:233], v175 offset:21504
	ds_read_b128 v[234:237], v175 offset:22528
	ds_read_b128 v[238:241], v175 offset:23552
	global_load_lds_dwordx4 v[242:243], off
	v_lshl_add_u64 v[244:245], s[26:27], 0, v[130:131]
	s_mov_b32 m0, s52
	v_lshl_add_u64 v[246:247], s[26:27], 0, v[136:137]
	global_load_lds_dwordx4 v[244:245], off
	s_mov_b32 m0, s53
	v_lshl_add_u64 v[248:249], s[28:29], 0, v[140:141]
	global_load_lds_dwordx4 v[246:247], off
	v_lshl_add_u64 v[246:247], s[26:27], 0, v[132:133]
	s_mov_b32 m0, s59
	s_nop 0
	global_load_lds_dwordx4 v[246:247], off
	v_lshl_add_u64 v[246:247], s[28:29], 0, v[138:139]
	s_mov_b32 m0, s42
	s_nop 0
	global_load_lds_dwordx4 v[246:247], off
	s_mov_b32 m0, s43
	s_nop 0
	global_load_lds_dwordx4 v[248:249], off
	s_waitcnt vmcnt(8)
	s_waitcnt lgkmcnt(0)
	s_setprio 1
	v_mfma_f32_16x16x32_bf16 v[62:65], v[178:181], v[210:213], v[62:65]
	v_mfma_f32_16x16x32_bf16 v[58:61], v[186:189], v[210:213], v[58:61]
	v_mfma_f32_16x16x32_bf16 v[54:57], v[178:181], v[218:221], v[54:57]
	v_mfma_f32_16x16x32_bf16 v[50:53], v[186:189], v[218:221], v[50:53]
	v_mfma_f32_16x16x32_bf16 v[46:49], v[178:181], v[226:229], v[46:49]
	v_mfma_f32_16x16x32_bf16 v[42:45], v[186:189], v[226:229], v[42:45]
	v_mfma_f32_16x16x32_bf16 v[34:37], v[178:181], v[234:237], v[34:37]
	v_mfma_f32_16x16x32_bf16 v[26:29], v[186:189], v[234:237], v[26:29]
	v_mfma_f32_16x16x32_bf16 v[62:65], v[182:185], v[214:217], v[62:65]
	v_mfma_f32_16x16x32_bf16 v[58:61], v[190:193], v[214:217], v[58:61]
	v_mfma_f32_16x16x32_bf16 v[54:57], v[182:185], v[222:225], v[54:57]
	v_mfma_f32_16x16x32_bf16 v[50:53], v[190:193], v[222:225], v[50:53]
	v_mfma_f32_16x16x32_bf16 v[46:49], v[182:185], v[230:233], v[46:49]
	v_mfma_f32_16x16x32_bf16 v[42:45], v[190:193], v[230:233], v[42:45]
	v_mfma_f32_16x16x32_bf16 v[34:37], v[182:185], v[238:241], v[34:37]
	v_mfma_f32_16x16x32_bf16 v[26:29], v[190:193], v[238:241], v[26:29]
	s_setprio 0
	s_setprio 1
	v_mfma_f32_16x16x32_bf16 v[38:41], v[194:197], v[210:213], v[38:41]
	v_mfma_f32_16x16x32_bf16 v[30:33], v[202:205], v[210:213], v[30:33]
	v_mfma_f32_16x16x32_bf16 v[22:25], v[194:197], v[218:221], v[22:25]
	v_mfma_f32_16x16x32_bf16 v[18:21], v[202:205], v[218:221], v[18:21]
	v_mfma_f32_16x16x32_bf16 v[14:17], v[194:197], v[226:229], v[14:17]
	v_mfma_f32_16x16x32_bf16 v[10:13], v[202:205], v[226:229], v[10:13]
	v_mfma_f32_16x16x32_bf16 v[6:9], v[194:197], v[234:237], v[6:9]
	v_mfma_f32_16x16x32_bf16 v[2:5], v[202:205], v[234:237], v[2:5]
	v_mfma_f32_16x16x32_bf16 v[38:41], v[198:201], v[214:217], v[38:41]
	v_mfma_f32_16x16x32_bf16 v[30:33], v[206:209], v[214:217], v[30:33]
	v_mfma_f32_16x16x32_bf16 v[22:25], v[198:201], v[222:225], v[22:25]
	v_mfma_f32_16x16x32_bf16 v[18:21], v[206:209], v[222:225], v[18:21]
	v_mfma_f32_16x16x32_bf16 v[14:17], v[198:201], v[230:233], v[14:17]
	v_mfma_f32_16x16x32_bf16 v[10:13], v[206:209], v[230:233], v[10:13]
	v_mfma_f32_16x16x32_bf16 v[6:9], v[198:201], v[238:241], v[6:9]
	v_mfma_f32_16x16x32_bf16 v[2:5], v[206:209], v[238:241], v[2:5]
	s_setprio 0
	s_barrier
	ds_read_b128 v[178:181], v176
	ds_read_b128 v[182:185], v176 offset:1024
	ds_read_b128 v[186:189], v176 offset:2048
	ds_read_b128 v[190:193], v176 offset:3072
	ds_read_b128 v[194:197], v177
	ds_read_b128 v[198:201], v177 offset:1024
	ds_read_b128 v[202:205], v177 offset:2048
	ds_read_b128 v[206:209], v177 offset:3072
	s_mov_b32 m0, s44
	v_lshl_add_u64 v[250:251], s[28:29], 0, v[142:143]
	ds_read_b128 v[210:213], v175 offset:32768
	ds_read_b128 v[214:217], v175 offset:33792
	ds_read_b128 v[218:221], v175 offset:34816
	ds_read_b128 v[222:225], v175 offset:35840
	ds_read_b128 v[226:229], v175 offset:36864
	ds_read_b128 v[230:233], v175 offset:37888
	ds_read_b128 v[234:237], v175 offset:38912
	ds_read_b128 v[238:241], v175 offset:39936
	global_load_lds_dwordx4 v[250:251], off
	v_lshl_add_u64 v[250:251], s[28:29], 0, v[144:145]
	s_mov_b32 m0, s45
	s_nop 0
	global_load_lds_dwordx4 v[250:251], off
	s_waitcnt vmcnt(8)
	s_waitcnt lgkmcnt(0)
	s_setprio 1
	v_mfma_f32_16x16x32_bf16 v[126:129], v[178:181], v[210:213], v[126:129]
	v_mfma_f32_16x16x32_bf16 v[122:125], v[186:189], v[210:213], v[122:125]
	v_mfma_f32_16x16x32_bf16 v[118:121], v[178:181], v[218:221], v[118:121]
	v_mfma_f32_16x16x32_bf16 v[114:117], v[186:189], v[218:221], v[114:117]
	v_mfma_f32_16x16x32_bf16 v[110:113], v[178:181], v[226:229], v[110:113]
	v_mfma_f32_16x16x32_bf16 v[106:109], v[186:189], v[226:229], v[106:109]
	v_mfma_f32_16x16x32_bf16 v[98:101], v[178:181], v[234:237], v[98:101]
	v_mfma_f32_16x16x32_bf16 v[90:93], v[186:189], v[234:237], v[90:93]
	v_mfma_f32_16x16x32_bf16 v[126:129], v[182:185], v[214:217], v[126:129]
	v_mfma_f32_16x16x32_bf16 v[122:125], v[190:193], v[214:217], v[122:125]
	v_mfma_f32_16x16x32_bf16 v[118:121], v[182:185], v[222:225], v[118:121]
	v_mfma_f32_16x16x32_bf16 v[114:117], v[190:193], v[222:225], v[114:117]
	v_mfma_f32_16x16x32_bf16 v[110:113], v[182:185], v[230:233], v[110:113]
	v_mfma_f32_16x16x32_bf16 v[106:109], v[190:193], v[230:233], v[106:109]
	v_mfma_f32_16x16x32_bf16 v[98:101], v[182:185], v[238:241], v[98:101]
	v_mfma_f32_16x16x32_bf16 v[90:93], v[190:193], v[238:241], v[90:93]
	s_setprio 0
	s_setprio 1
	v_mfma_f32_16x16x32_bf16 v[102:105], v[194:197], v[210:213], v[102:105]
	v_mfma_f32_16x16x32_bf16 v[94:97], v[202:205], v[210:213], v[94:97]
	v_mfma_f32_16x16x32_bf16 v[86:89], v[194:197], v[218:221], v[86:89]
	v_mfma_f32_16x16x32_bf16 v[82:85], v[202:205], v[218:221], v[82:85]
	v_mfma_f32_16x16x32_bf16 v[78:81], v[194:197], v[226:229], v[78:81]
	v_mfma_f32_16x16x32_bf16 v[74:77], v[202:205], v[226:229], v[74:77]
	v_mfma_f32_16x16x32_bf16 v[70:73], v[194:197], v[234:237], v[70:73]
	v_mfma_f32_16x16x32_bf16 v[66:69], v[202:205], v[234:237], v[66:69]
	v_mfma_f32_16x16x32_bf16 v[102:105], v[198:201], v[214:217], v[102:105]
	v_mfma_f32_16x16x32_bf16 v[94:97], v[206:209], v[214:217], v[94:97]
	v_mfma_f32_16x16x32_bf16 v[86:89], v[198:201], v[222:225], v[86:89]
	v_mfma_f32_16x16x32_bf16 v[82:85], v[206:209], v[222:225], v[82:85]
	v_mfma_f32_16x16x32_bf16 v[78:81], v[198:201], v[230:233], v[78:81]
	v_mfma_f32_16x16x32_bf16 v[74:77], v[206:209], v[230:233], v[74:77]
	v_mfma_f32_16x16x32_bf16 v[70:73], v[198:201], v[238:241], v[70:73]
	v_mfma_f32_16x16x32_bf16 v[66:69], v[206:209], v[238:241], v[66:69]
	s_setprio 0
	s_barrier
; #define PG8_STAGE(bufoff, gbase, voff) do { _Pragma("unroll") for (int _i = 0; _i < 2; ++_i) \
;         __builtin_amdgcn_global_load_lds((const unsigned*)((const char*)(gbase) + (voff)[_i]), (PG8_LAS unsigned*)(lds + (bufoff) + ldsw + _i * 8192), 16, 0, 0); } while (0)
; #define PG8_WAIT_V(n) asm volatile("s_waitcnt vmcnt(" #n ")" ::: "memory")
; #define PG8_WAIT_L(n) asm volatile("s_waitcnt lgkmcnt(" #n ")" ::: "memory")
; #define PG8_BAR __builtin_amdgcn_s_barrier()
; #define PG8_SCHED __builtin_amdgcn_sched_barrier(0)
; template <class Epi, class Sched, bool ALIGN_EPI = true, bool F8 = false>
; __device__ __forceinline__ void gemm_phase(PG8_LAS unsigned char* lds, const Sched& S, const Epi& E) {
;     ...
;         for (int t = 0; t < nt; t += 2) {
;             const bool last = (t == nt - 2);
;             if constexpr (Sched::GATHER) { if (last && has_next) S.a_off(nxt, Rs, Cs, voffAn); }
;             const char* a1 = cA + (size_t)(t + 1) * kstep;
;             const char* a2 = last ? nA : cA + (size_t)(t + 2) * kstep; const char* b2 = last ? nB : cB + (size_t)(t + 2) * kstepB;
;     ...
;             PG8_LDA(At, 1, 1); PG8_STAGE(PG8_SB(1, 0), b3, voffB[0]); PG8_STAGE(PG8_SB(1, 1), b3, voffB[1]); PG8_STAGE(PG8_SA(1, 0), a3, vA2[0]);
;             PG8_WAIT_V(8); PG8_WAIT_L(0); PG8_BAR; PG8_MMA(1, 0, At, B0); PG8_MMA(1, 1, At, B1); PG8_BAR; PG8_SCHED;
	s_mov_b32 m0, s60
	s_add_u32 s22, s26, 0x80
	v_lshl_add_u64 v[242:243], v[242:243], 0, s[8:9]
	ds_read_b128 v[210:213], v175 offset:49152
	ds_read_b128 v[214:217], v175 offset:50176
	ds_read_b128 v[218:221], v175 offset:51200
	ds_read_b128 v[222:225], v175 offset:52224
	ds_read_b128 v[226:229], v175 offset:53248
	ds_read_b128 v[230:233], v175 offset:54272
	ds_read_b128 v[234:237], v175 offset:55296
	ds_read_b128 v[238:241], v175 offset:56320
	s_addc_u32 s23, s27, 0
	global_load_lds_dwordx4 v[242:243], off
	v_lshl_add_u64 v[242:243], v[244:245], 0, s[8:9]
	s_mov_b32 m0, s61
	s_nop 0
	global_load_lds_dwordx4 v[242:243], off
	v_lshl_add_u64 v[242:243], s[22:23], 0, v[136:137]
	s_mov_b32 m0, s62
	s_nop 0
	global_load_lds_dwordx4 v[242:243], off
	v_lshl_add_u64 v[242:243], s[22:23], 0, v[132:133]
	s_mov_b32 m0, s63
	s_nop 0
	global_load_lds_dwordx4 v[242:243], off
	v_lshl_add_u64 v[242:243], v[246:247], 0, s[8:9]
	s_mov_b32 m0, s47
	s_nop 0
	global_load_lds_dwordx4 v[242:243], off
	v_lshl_add_u64 v[242:243], v[248:249], 0, s[8:9]
	s_mov_b32 m0, s48
	s_nop 0
	global_load_lds_dwordx4 v[242:243], off
	s_waitcnt vmcnt(8)
	s_waitcnt lgkmcnt(0)
	s_setprio 1
	v_mfma_f32_16x16x32_bf16 v[62:65], v[178:181], v[210:213], v[62:65]
	v_mfma_f32_16x16x32_bf16 v[58:61], v[186:189], v[210:213], v[58:61]
	v_mfma_f32_16x16x32_bf16 v[54:57], v[178:181], v[218:221], v[54:57]
	v_mfma_f32_16x16x32_bf16 v[50:53], v[186:189], v[218:221], v[50:53]
	v_mfma_f32_16x16x32_bf16 v[46:49], v[178:181], v[226:229], v[46:49]
	v_mfma_f32_16x16x32_bf16 v[42:45], v[186:189], v[226:229], v[42:45]
	v_mfma_f32_16x16x32_bf16 v[34:37], v[178:181], v[234:237], v[34:37]
	v_mfma_f32_16x16x32_bf16 v[26:29], v[186:189], v[234:237], v[26:29]
	v_mfma_f32_16x16x32_bf16 v[62:65], v[182:185], v[214:217], v[62:65]
	v_mfma_f32_16x16x32_bf16 v[58:61], v[190:193], v[214:217], v[58:61]
	v_mfma_f32_16x16x32_bf16 v[54:57], v[182:185], v[222:225], v[54:57]
	v_mfma_f32_16x16x32_bf16 v[50:53], v[190:193], v[222:225], v[50:53]
	v_mfma_f32_16x16x32_bf16 v[46:49], v[182:185], v[230:233], v[46:49]
	v_mfma_f32_16x16x32_bf16 v[42:45], v[190:193], v[230:233], v[42:45]
	v_mfma_f32_16x16x32_bf16 v[34:37], v[182:185], v[238:241], v[34:37]
	v_mfma_f32_16x16x32_bf16 v[26:29], v[190:193], v[238:241], v[26:29]
	s_setprio 0
	s_setprio 1
	v_mfma_f32_16x16x32_bf16 v[38:41], v[194:197], v[210:213], v[38:41]
	v_mfma_f32_16x16x32_bf16 v[30:33], v[202:205], v[210:213], v[30:33]
	v_mfma_f32_16x16x32_bf16 v[22:25], v[194:197], v[218:221], v[22:25]
	v_mfma_f32_16x16x32_bf16 v[18:21], v[202:205], v[218:221], v[18:21]
	v_mfma_f32_16x16x32_bf16 v[14:17], v[194:197], v[226:229], v[14:17]
	v_mfma_f32_16x16x32_bf16 v[10:13], v[202:205], v[226:229], v[10:13]
	v_mfma_f32_16x16x32_bf16 v[6:9], v[194:197], v[234:237], v[6:9]
	v_mfma_f32_16x16x32_bf16 v[2:5], v[202:205], v[234:237], v[2:5]
	v_mfma_f32_16x16x32_bf16 v[38:41], v[198:201], v[214:217], v[38:41]
	v_mfma_f32_16x16x32_bf16 v[30:33], v[206:209], v[214:217], v[30:33]
	v_mfma_f32_16x16x32_bf16 v[22:25], v[198:201], v[222:225], v[22:25]
	v_mfma_f32_16x16x32_bf16 v[18:21], v[206:209], v[222:225], v[18:21]
	v_mfma_f32_16x16x32_bf16 v[14:17], v[198:201], v[230:233], v[14:17]
	v_mfma_f32_16x16x32_bf16 v[10:13], v[206:209], v[230:233], v[10:13]
	v_mfma_f32_16x16x32_bf16 v[6:9], v[198:201], v[238:241], v[6:9]
	v_mfma_f32_16x16x32_bf16 v[2:5], v[206:209], v[238:241], v[2:5]
	s_setprio 0
	s_barrier
	s_add_i32 s66, s66, 2
	s_add_u32 s15, s15, 0x100
	s_addc_u32 s65, s65, 0
	s_cmp_gt_u32 s66, 5
	s_mov_b64 s[22:23], s[24:25]
	s_cbranch_scc0 .LBB0_491
	s_branch .Lfx_13405
.Lh1e_13405:
.Lh1_491:
	ds_read_b128 v[178:181], v173
	ds_read_b128 v[182:185], v173 offset:1024
	ds_read_b128 v[186:189], v173 offset:2048
	ds_read_b128 v[190:193], v173 offset:3072
	ds_read_b128 v[194:197], v174
	ds_read_b128 v[198:201], v174 offset:1024
	ds_read_b128 v[202:205], v174 offset:2048
	ds_read_b128 v[206:209], v174 offset:3072
	s_add_u32 s24, s22, 0x100
	s_addc_u32 s25, s23, 0
	s_cmp_eq_u32 s66, 4
	s_cselect_b32 s29, s17, s25
	s_cselect_b32 s28, s16, s24
	s_cselect_b32 s27, s19, s65
	s_cselect_b32 s26, s18, s15
	s_mov_b32 m0, s49
	v_lshl_add_u64 v[242:243], s[22:23], 0, v[166:167]
	ds_read_b128 v[210:213], v175
	ds_read_b128 v[214:217], v175 offset:1024
	ds_read_b128 v[218:221], v175 offset:2048
	ds_read_b128 v[222:225], v175 offset:3072
	ds_read_b128 v[226:229], v175 offset:4096
	ds_read_b128 v[230:233], v175 offset:5120
	ds_read_b128 v[234:237], v175 offset:6144
	ds_read_b128 v[238:241], v175 offset:7168
	global_load_lds_dwordx4 v[242:243], off
	v_lshl_add_u64 v[242:243], s[22:23], 0, v[164:165]
	s_mov_b32 m0, s50
	s_nop 0
	global_load_lds_dwordx4 v[242:243], off
	s_waitcnt vmcnt(8)
	s_waitcnt lgkmcnt(0)
	s_barrier
; #define PG8_STAGE(bufoff, gbase, voff) do { _Pragma("unroll") for (int _i = 0; _i < 2; ++_i) \
;         __builtin_amdgcn_global_load_lds((const unsigned*)((const char*)(gbase) + (voff)[_i]), (PG8_LAS unsigned*)(lds + (bufoff) + ldsw + _i * 8192), 16, 0, 0); } while (0)
; #define PG8_WAIT_V(n) asm volatile("s_waitcnt vmcnt(" #n ")" ::: "memory")
; #define PG8_WAIT_L(n) asm volatile("s_waitcnt lgkmcnt(" #n ")" ::: "memory")
; #define PG8_BAR __builtin_amdgcn_s_barrier()
; #define PG8_SCHED __builtin_amdgcn_sched_barrier(0)
; template <class Epi, class Sched, bool ALIGN_EPI = true, bool F8 = false>
; __device__ __forceinline__ void gemm_phase(PG8_LAS unsigned char* lds, const Sched& S, const Epi& E) {
;     ...
;             PG8_LDB(B0, 0, 0); PG8_LDB(B1, 0, 1); PG8_SCHED; PG8_LDA(At, 0, 0); PG8_STAGE(PG8_SA(1, 1), a1, voffA[1]);
;             PG8_WAIT_V(8); PG8_WAIT_L(0); PG8_BAR; PG8_MMA(0, 0, At, B0); PG8_MMA(0, 1, At, B1); PG8_BAR; PG8_SCHED;
;             PG8_LDA(At, 0, 1); PG8_STAGE(PG8_SB(0, 0), b2, voffB[0]); PG8_STAGE(PG8_SB(0, 1), b2, voffB[1]); PG8_STAGE(PG8_SA(0, 0), a2, vA2[0]);
;             PG8_WAIT_V(8); PG8_WAIT_L(0); PG8_BAR; PG8_MMA(1, 0, At, B0); PG8_MMA(1, 1, At, B1); PG8_BAR; PG8_SCHED;
;             PG8_LDB(B0, 1, 0); PG8_LDB(B1, 1, 1); PG8_SCHED; PG8_LDA(At, 1, 0); PG8_STAGE(PG8_SA(0, 1), a2, vA2[1]);
;             PG8_WAIT_V(8); PG8_WAIT_L(0); PG8_BAR; PG8_MMA(0, 0, At, B0); PG8_MMA(0, 1, At, B1); PG8_BAR; PG8_SCHED;
	s_setprio 2
	v_mfma_f32_16x16x32_bf16 v[126:129], v[178:181], v[210:213], v[126:129]
	v_mfma_f32_16x16x32_bf16 v[122:125], v[186:189], v[210:213], v[122:125]
	v_mfma_f32_16x16x32_bf16 v[118:121], v[178:181], v[218:221], v[118:121]
	v_mfma_f32_16x16x32_bf16 v[114:117], v[186:189], v[218:221], v[114:117]
	v_mfma_f32_16x16x32_bf16 v[110:113], v[178:181], v[226:229], v[110:113]
	v_mfma_f32_16x16x32_bf16 v[106:109], v[186:189], v[226:229], v[106:109]
	v_mfma_f32_16x16x32_bf16 v[98:101], v[178:181], v[234:237], v[98:101]
	v_mfma_f32_16x16x32_bf16 v[90:93], v[186:189], v[234:237], v[90:93]
	v_mfma_f32_16x16x32_bf16 v[126:129], v[182:185], v[214:217], v[126:129]
	v_mfma_f32_16x16x32_bf16 v[122:125], v[190:193], v[214:217], v[122:125]
	v_mfma_f32_16x16x32_bf16 v[118:121], v[182:185], v[222:225], v[118:121]
	v_mfma_f32_16x16x32_bf16 v[114:117], v[190:193], v[222:225], v[114:117]
	v_mfma_f32_16x16x32_bf16 v[110:113], v[182:185], v[230:233], v[110:113]
	v_mfma_f32_16x16x32_bf16 v[106:109], v[190:193], v[230:233], v[106:109]
	v_mfma_f32_16x16x32_bf16 v[98:101], v[182:185], v[238:241], v[98:101]
	v_mfma_f32_16x16x32_bf16 v[90:93], v[190:193], v[238:241], v[90:93]
	s_setprio 0
	s_setprio 2
	v_mfma_f32_16x16x32_bf16 v[102:105], v[194:197], v[210:213], v[102:105]
	v_mfma_f32_16x16x32_bf16 v[94:97], v[202:205], v[210:213], v[94:97]
	v_mfma_f32_16x16x32_bf16 v[86:89], v[194:197], v[218:221], v[86:89]
	v_mfma_f32_16x16x32_bf16 v[82:85], v[202:205], v[218:221], v[82:85]
	v_mfma_f32_16x16x32_bf16 v[78:81], v[194:197], v[226:229], v[78:81]
	v_mfma_f32_16x16x32_bf16 v[74:77], v[202:205], v[226:229], v[74:77]
	v_mfma_f32_16x16x32_bf16 v[70:73], v[194:197], v[234:237], v[70:73]
	v_mfma_f32_16x16x32_bf16 v[66:69], v[202:205], v[234:237], v[66:69]
	v_mfma_f32_16x16x32_bf16 v[102:105], v[198:201], v[214:217], v[102:105]
	v_mfma_f32_16x16x32_bf16 v[94:97], v[206:209], v[214:217], v[94:97]
	v_mfma_f32_16x16x32_bf16 v[86:89], v[198:201], v[222:225], v[86:89]
	v_mfma_f32_16x16x32_bf16 v[82:85], v[206:209], v[222:225], v[82:85]
	v_mfma_f32_16x16x32_bf16 v[78:81], v[198:201], v[230:233], v[78:81]
	v_mfma_f32_16x16x32_bf16 v[74:77], v[206:209], v[230:233], v[74:77]
	v_mfma_f32_16x16x32_bf16 v[70:73], v[198:201], v[238:241], v[70:73]
	v_mfma_f32_16x16x32_bf16 v[66:69], v[206:209], v[238:241], v[66:69]
	s_setprio 0
	s_mov_b32 m0, s51
	v_lshl_add_u64 v[242:243], s[26:27], 0, v[134:135]
	ds_read_b128 v[210:213], v175 offset:16384
	ds_read_b128 v[214:217], v175 offset:17408
	ds_read_b128 v[218:221], v175 offset:18432
	ds_read_b128 v[222:225], v175 offset:19456
	ds_read_b128 v[226:229], v175 offset:20480
	ds_read_b128 v[230:233], v175 offset:21504
	ds_read_b128 v[234:237], v175 offset:22528
	ds_read_b128 v[238:241], v175 offset:23552
	global_load_lds_dwordx4 v[242:243], off
	v_lshl_add_u64 v[244:245], s[26:27], 0, v[130:131]
	s_mov_b32 m0, s52
	v_lshl_add_u64 v[246:247], s[26:27], 0, v[136:137]
	global_load_lds_dwordx4 v[244:245], off
	s_mov_b32 m0, s53
	v_lshl_add_u64 v[248:249], s[28:29], 0, v[140:141]
	global_load_lds_dwordx4 v[246:247], off
	v_lshl_add_u64 v[246:247], s[26:27], 0, v[132:133]
	s_mov_b32 m0, s59
	s_nop 0
	global_load_lds_dwordx4 v[246:247], off
	v_lshl_add_u64 v[246:247], s[28:29], 0, v[138:139]
	s_mov_b32 m0, s42
	s_nop 0
	global_load_lds_dwordx4 v[246:247], off
	s_mov_b32 m0, s43
	s_nop 0
	global_load_lds_dwordx4 v[248:249], off
	s_waitcnt vmcnt(8)
	s_waitcnt lgkmcnt(0)
	s_barrier
	s_setprio 2
	v_mfma_f32_16x16x32_bf16 v[62:65], v[178:181], v[210:213], v[62:65]
	v_mfma_f32_16x16x32_bf16 v[58:61], v[186:189], v[210:213], v[58:61]
	v_mfma_f32_16x16x32_bf16 v[54:57], v[178:181], v[218:221], v[54:57]
	v_mfma_f32_16x16x32_bf16 v[50:53], v[186:189], v[218:221], v[50:53]
	v_mfma_f32_16x16x32_bf16 v[46:49], v[178:181], v[226:229], v[46:49]
	v_mfma_f32_16x16x32_bf16 v[42:45], v[186:189], v[226:229], v[42:45]
	v_mfma_f32_16x16x32_bf16 v[34:37], v[178:181], v[234:237], v[34:37]
	v_mfma_f32_16x16x32_bf16 v[26:29], v[186:189], v[234:237], v[26:29]
	v_mfma_f32_16x16x32_bf16 v[62:65], v[182:185], v[214:217], v[62:65]
	v_mfma_f32_16x16x32_bf16 v[58:61], v[190:193], v[214:217], v[58:61]
	v_mfma_f32_16x16x32_bf16 v[54:57], v[182:185], v[222:225], v[54:57]
	v_mfma_f32_16x16x32_bf16 v[50:53], v[190:193], v[222:225], v[50:53]
	v_mfma_f32_16x16x32_bf16 v[46:49], v[182:185], v[230:233], v[46:49]
	v_mfma_f32_16x16x32_bf16 v[42:45], v[190:193], v[230:233], v[42:45]
	v_mfma_f32_16x16x32_bf16 v[34:37], v[182:185], v[238:241], v[34:37]
	v_mfma_f32_16x16x32_bf16 v[26:29], v[190:193], v[238:241], v[26:29]
	s_setprio 0
	s_setprio 2
	v_mfma_f32_16x16x32_bf16 v[38:41], v[194:197], v[210:213], v[38:41]
	v_mfma_f32_16x16x32_bf16 v[30:33], v[202:205], v[210:213], v[30:33]
	v_mfma_f32_16x16x32_bf16 v[22:25], v[194:197], v[218:221], v[22:25]
	v_mfma_f32_16x16x32_bf16 v[18:21], v[202:205], v[218:221], v[18:21]
	v_mfma_f32_16x16x32_bf16 v[14:17], v[194:197], v[226:229], v[14:17]
	v_mfma_f32_16x16x32_bf16 v[10:13], v[202:205], v[226:229], v[10:13]
	v_mfma_f32_16x16x32_bf16 v[6:9], v[194:197], v[234:237], v[6:9]
	v_mfma_f32_16x16x32_bf16 v[2:5], v[202:205], v[234:237], v[2:5]
	v_mfma_f32_16x16x32_bf16 v[38:41], v[198:201], v[214:217], v[38:41]
	v_mfma_f32_16x16x32_bf16 v[30:33], v[206:209], v[214:217], v[30:33]
	v_mfma_f32_16x16x32_bf16 v[22:25], v[198:201], v[222:225], v[22:25]
	v_mfma_f32_16x16x32_bf16 v[18:21], v[206:209], v[222:225], v[18:21]
	v_mfma_f32_16x16x32_bf16 v[14:17], v[198:201], v[230:233], v[14:17]
	v_mfma_f32_16x16x32_bf16 v[10:13], v[206:209], v[230:233], v[10:13]
	v_mfma_f32_16x16x32_bf16 v[6:9], v[198:201], v[238:241], v[6:9]
	v_mfma_f32_16x16x32_bf16 v[2:5], v[206:209], v[238:241], v[2:5]
	s_setprio 0
	ds_read_b128 v[178:181], v176
	ds_read_b128 v[182:185], v176 offset:1024
	ds_read_b128 v[186:189], v176 offset:2048
	ds_read_b128 v[190:193], v176 offset:3072
	ds_read_b128 v[194:197], v177
	ds_read_b128 v[198:201], v177 offset:1024
	ds_read_b128 v[202:205], v177 offset:2048
	ds_read_b128 v[206:209], v177 offset:3072
	s_mov_b32 m0, s44
	v_lshl_add_u64 v[250:251], s[28:29], 0, v[142:143]
	ds_read_b128 v[210:213], v175 offset:32768
	ds_read_b128 v[214:217], v175 offset:33792
	ds_read_b128 v[218:221], v175 offset:34816
	ds_read_b128 v[222:225], v175 offset:35840
	ds_read_b128 v[226:229], v175 offset:36864
	ds_read_b128 v[230:233], v175 offset:37888
	ds_read_b128 v[234:237], v175 offset:38912
	ds_read_b128 v[238:241], v175 offset:39936
	global_load_lds_dwordx4 v[250:251], off
	v_lshl_add_u64 v[250:251], s[28:29], 0, v[144:145]
	s_mov_b32 m0, s45
	s_nop 0
	global_load_lds_dwordx4 v[250:251], off
	s_waitcnt vmcnt(8)
	s_waitcnt lgkmcnt(0)
	s_barrier
; #define PG8_STAGE(bufoff, gbase, voff) do { _Pragma("unroll") for (int _i = 0; _i < 2; ++_i) \
;         __builtin_amdgcn_global_load_lds((const unsigned*)((const char*)(gbase) + (voff)[_i]), (PG8_LAS unsigned*)(lds + (bufoff) + ldsw + _i * 8192), 16, 0, 0); } while (0)
; #define PG8_WAIT_V(n) asm volatile("s_waitcnt vmcnt(" #n ")" ::: "memory")
; #define PG8_WAIT_L(n) asm volatile("s_waitcnt lgkmcnt(" #n ")" ::: "memory")
; #define PG8_BAR __builtin_amdgcn_s_barrier()
; #define PG8_SCHED __builtin_amdgcn_sched_barrier(0)
; template <class Epi, class Sched, bool ALIGN_EPI = true, bool F8 = false>
; __device__ __forceinline__ void gemm_phase(PG8_LAS unsigned char* lds, const Sched& S, const Epi& E) {
;     ...
;         for (int t = 0; t < nt; t += 2) {
;             const bool last = (t == nt - 2);
;             if constexpr (Sched::GATHER) { if (last && has_next) S.a_off(nxt, Rs, Cs, voffAn); }
;             const char* a1 = cA + (size_t)(t + 1) * kstep;
;             const char* a2 = last ? nA : cA + (size_t)(t + 2) * kstep; const char* b2 = last ? nB : cB + (size_t)(t + 2) * kstepB;
;     ...
;             PG8_WAIT_V(8); PG8_WAIT_L(0); PG8_BAR; PG8_MMA(0, 0, At, B0); PG8_MMA(0, 1, At, B1); PG8_BAR; PG8_SCHED;
;             PG8_LDA(At, 1, 1); PG8_STAGE(PG8_SB(1, 0), b3, voffB[0]); PG8_STAGE(PG8_SB(1, 1), b3, voffB[1]); PG8_STAGE(PG8_SA(1, 0), a3, vA2[0]);
;             PG8_WAIT_V(8); PG8_WAIT_L(0); PG8_BAR; PG8_MMA(1, 0, At, B0); PG8_MMA(1, 1, At, B1); PG8_BAR; PG8_SCHED;
	s_setprio 2
	v_mfma_f32_16x16x32_bf16 v[126:129], v[178:181], v[210:213], v[126:129]
	v_mfma_f32_16x16x32_bf16 v[122:125], v[186:189], v[210:213], v[122:125]
	v_mfma_f32_16x16x32_bf16 v[118:121], v[178:181], v[218:221], v[118:121]
	v_mfma_f32_16x16x32_bf16 v[114:117], v[186:189], v[218:221], v[114:117]
	v_mfma_f32_16x16x32_bf16 v[110:113], v[178:181], v[226:229], v[110:113]
	v_mfma_f32_16x16x32_bf16 v[106:109], v[186:189], v[226:229], v[106:109]
	v_mfma_f32_16x16x32_bf16 v[98:101], v[178:181], v[234:237], v[98:101]
	v_mfma_f32_16x16x32_bf16 v[90:93], v[186:189], v[234:237], v[90:93]
	v_mfma_f32_16x16x32_bf16 v[126:129], v[182:185], v[214:217], v[126:129]
	v_mfma_f32_16x16x32_bf16 v[122:125], v[190:193], v[214:217], v[122:125]
	v_mfma_f32_16x16x32_bf16 v[118:121], v[182:185], v[222:225], v[118:121]
	v_mfma_f32_16x16x32_bf16 v[114:117], v[190:193], v[222:225], v[114:117]
	v_mfma_f32_16x16x32_bf16 v[110:113], v[182:185], v[230:233], v[110:113]
	v_mfma_f32_16x16x32_bf16 v[106:109], v[190:193], v[230:233], v[106:109]
	v_mfma_f32_16x16x32_bf16 v[98:101], v[182:185], v[238:241], v[98:101]
	v_mfma_f32_16x16x32_bf16 v[90:93], v[190:193], v[238:241], v[90:93]
	s_setprio 0
	s_setprio 2
	v_mfma_f32_16x16x32_bf16 v[102:105], v[194:197], v[210:213], v[102:105]
	v_mfma_f32_16x16x32_bf16 v[94:97], v[202:205], v[210:213], v[94:97]
	v_mfma_f32_16x16x32_bf16 v[86:89], v[194:197], v[218:221], v[86:89]
	v_mfma_f32_16x16x32_bf16 v[82:85], v[202:205], v[218:221], v[82:85]
	v_mfma_f32_16x16x32_bf16 v[78:81], v[194:197], v[226:229], v[78:81]
	v_mfma_f32_16x16x32_bf16 v[74:77], v[202:205], v[226:229], v[74:77]
	v_mfma_f32_16x16x32_bf16 v[70:73], v[194:197], v[234:237], v[70:73]
	v_mfma_f32_16x16x32_bf16 v[66:69], v[202:205], v[234:237], v[66:69]
	v_mfma_f32_16x16x32_bf16 v[102:105], v[198:201], v[214:217], v[102:105]
	v_mfma_f32_16x16x32_bf16 v[94:97], v[206:209], v[214:217], v[94:97]
	v_mfma_f32_16x16x32_bf16 v[86:89], v[198:201], v[222:225], v[86:89]
	v_mfma_f32_16x16x32_bf16 v[82:85], v[206:209], v[222:225], v[82:85]
	v_mfma_f32_16x16x32_bf16 v[78:81], v[198:201], v[230:233], v[78:81]
	v_mfma_f32_16x16x32_bf16 v[74:77], v[206:209], v[230:233], v[74:77]
	v_mfma_f32_16x16x32_bf16 v[70:73], v[198:201], v[238:241], v[70:73]
	v_mfma_f32_16x16x32_bf16 v[66:69], v[206:209], v[238:241], v[66:69]
	s_setprio 0
	s_mov_b32 m0, s60
	s_add_u32 s22, s26, 0x80
	v_lshl_add_u64 v[242:243], v[242:243], 0, s[8:9]
	ds_read_b128 v[210:213], v175 offset:49152
	ds_read_b128 v[214:217], v175 offset:50176
	ds_read_b128 v[218:221], v175 offset:51200
	ds_read_b128 v[222:225], v175 offset:52224
	ds_read_b128 v[226:229], v175 offset:53248
	ds_read_b128 v[230:233], v175 offset:54272
	ds_read_b128 v[234:237], v175 offset:55296
	ds_read_b128 v[238:241], v175 offset:56320
	s_addc_u32 s23, s27, 0
	global_load_lds_dwordx4 v[242:243], off
	v_lshl_add_u64 v[242:243], v[244:245], 0, s[8:9]
	s_mov_b32 m0, s61
	s_nop 0
	global_load_lds_dwordx4 v[242:243], off
	v_lshl_add_u64 v[242:243], s[22:23], 0, v[136:137]
	s_mov_b32 m0, s62
	s_nop 0
	global_load_lds_dwordx4 v[242:243], off
	v_lshl_add_u64 v[242:243], s[22:23], 0, v[132:133]
	s_mov_b32 m0, s63
	s_nop 0
	global_load_lds_dwordx4 v[242:243], off
	v_lshl_add_u64 v[242:243], v[246:247], 0, s[8:9]
	s_mov_b32 m0, s47
	s_nop 0
	global_load_lds_dwordx4 v[242:243], off
	v_lshl_add_u64 v[242:243], v[248:249], 0, s[8:9]
	s_mov_b32 m0, s48
	s_nop 0
	global_load_lds_dwordx4 v[242:243], off
	s_waitcnt vmcnt(8)
	s_waitcnt lgkmcnt(0)
	s_barrier
	s_setprio 2
	v_mfma_f32_16x16x32_bf16 v[62:65], v[178:181], v[210:213], v[62:65]
	v_mfma_f32_16x16x32_bf16 v[58:61], v[186:189], v[210:213], v[58:61]
	v_mfma_f32_16x16x32_bf16 v[54:57], v[178:181], v[218:221], v[54:57]
	v_mfma_f32_16x16x32_bf16 v[50:53], v[186:189], v[218:221], v[50:53]
	v_mfma_f32_16x16x32_bf16 v[46:49], v[178:181], v[226:229], v[46:49]
	v_mfma_f32_16x16x32_bf16 v[42:45], v[186:189], v[226:229], v[42:45]
	v_mfma_f32_16x16x32_bf16 v[34:37], v[178:181], v[234:237], v[34:37]
	v_mfma_f32_16x16x32_bf16 v[26:29], v[186:189], v[234:237], v[26:29]
	v_mfma_f32_16x16x32_bf16 v[62:65], v[182:185], v[214:217], v[62:65]
	v_mfma_f32_16x16x32_bf16 v[58:61], v[190:193], v[214:217], v[58:61]
	v_mfma_f32_16x16x32_bf16 v[54:57], v[182:185], v[222:225], v[54:57]
	v_mfma_f32_16x16x32_bf16 v[50:53], v[190:193], v[222:225], v[50:53]
	v_mfma_f32_16x16x32_bf16 v[46:49], v[182:185], v[230:233], v[46:49]
	v_mfma_f32_16x16x32_bf16 v[42:45], v[190:193], v[230:233], v[42:45]
	v_mfma_f32_16x16x32_bf16 v[34:37], v[182:185], v[238:241], v[34:37]
	v_mfma_f32_16x16x32_bf16 v[26:29], v[190:193], v[238:241], v[26:29]
	s_setprio 0
	s_setprio 2
	v_mfma_f32_16x16x32_bf16 v[38:41], v[194:197], v[210:213], v[38:41]
	v_mfma_f32_16x16x32_bf16 v[30:33], v[202:205], v[210:213], v[30:33]
	v_mfma_f32_16x16x32_bf16 v[22:25], v[194:197], v[218:221], v[22:25]
	v_mfma_f32_16x16x32_bf16 v[18:21], v[202:205], v[218:221], v[18:21]
	v_mfma_f32_16x16x32_bf16 v[14:17], v[194:197], v[226:229], v[14:17]
	v_mfma_f32_16x16x32_bf16 v[10:13], v[202:205], v[226:229], v[10:13]
	v_mfma_f32_16x16x32_bf16 v[6:9], v[194:197], v[234:237], v[6:9]
	v_mfma_f32_16x16x32_bf16 v[2:5], v[202:205], v[234:237], v[2:5]
	v_mfma_f32_16x16x32_bf16 v[38:41], v[198:201], v[214:217], v[38:41]
	v_mfma_f32_16x16x32_bf16 v[30:33], v[206:209], v[214:217], v[30:33]
	v_mfma_f32_16x16x32_bf16 v[22:25], v[198:201], v[222:225], v[22:25]
	v_mfma_f32_16x16x32_bf16 v[18:21], v[206:209], v[222:225], v[18:21]
	v_mfma_f32_16x16x32_bf16 v[14:17], v[198:201], v[230:233], v[14:17]
	v_mfma_f32_16x16x32_bf16 v[10:13], v[206:209], v[230:233], v[10:13]
	v_mfma_f32_16x16x32_bf16 v[6:9], v[198:201], v[238:241], v[6:9]
	v_mfma_f32_16x16x32_bf16 v[2:5], v[206:209], v[238:241], v[2:5]
	s_setprio 0
	s_add_i32 s66, s66, 2
	s_add_u32 s15, s15, 0x100
	s_addc_u32 s65, s65, 0
	s_cmp_gt_u32 s66, 5
	s_mov_b64 s[22:23], s[24:25]
	s_cbranch_scc0 .Lh1_491
; #define PG8_BAR __builtin_amdgcn_s_barrier()
; template <class Epi, class Sched, bool ALIGN_EPI = true, bool F8 = false>
; __device__ __forceinline__ void gemm_phase(PG8_LAS unsigned char* lds, const Sched& S, const Epi& E) {
;     ...
;         if constexpr (ALIGN_EPI) { if (wr == 0) PG8_BAR; }
;         if constexpr (F8) {
; #pragma unroll
;             for (int a = 0; a < 2; ++a)
; #pragma unroll
;                 for (int b = 0; b < 2; ++b)
;                     asm volatile("s_nop 15\n\ts_nop 7" : "+v"(acc[a][b][0][0]), "+v"(acc[a][b][0][1]), "+v"(acc[a][b][1][0]), "+v"(acc[a][b][1][1]), "+v"(acc[a][b][2][0]), "+v"(acc[a][b][2][1]), "+v"(acc[a][b][3][0]), "+v"(acc[a][b][3][1]));
;         }
;         E(acc, cur, wr, wc, fr, fq);
;         if (!has_next) break;
;         if (!(HasSeg<Epi>::v && cur.x2 == 0)) {
; #pragma unroll
;         for (int a = 0; a < 2; ++a)
; #pragma unroll
;             for (int b = 0; b < 2; ++b)
; #pragma unroll
;                 for (int m = 0; m < 4; ++m)
; #pragma unroll
;                     for (int n = 0; n < 2; ++n) acc[a][b][m][n] = (f32x4){0.f, 0.f, 0.f, 0.f};
;         }
;         cur = nxt; cA = nA; cB = nB; ++ui;
; #pragma unroll
;         for (int h = 0; h < 2; ++h)
; #pragma unroll
;             for (int i = 0; i < 2; ++i) voffA[h][i] = voffAn[h][i];
;         if constexpr (ALIGN_EPI) { if (wr == 1) PG8_BAR; }
.Lfx_13405:
	s_and_b64 vcc, exec, s[10:11]
	s_cbranch_vccz .LBB0_494
.LBB0_494:
	s_lshl_b32 s0, s0, 2
	s_add_i32 s0, s0, s1
	s_mulk_i32 s0, 0x108
	s_ashr_i32 s1, s0, 31
	s_lshl_b64 s[0:1], s[0:1], 10
	v_lshl_add_u64 v[178:179], v[146:147], 0, s[0:1]
	v_lshl_add_u64 v[178:179], v[178:179], 0, s[12:13]
	v_lshl_add_u64 v[180:181], v[178:179], 0, v[148:149]
	flat_store_dwordx4 v[180:181], v[126:129]
	flat_store_dwordx4 v[180:181], v[122:125] offset:64
	flat_store_dwordx4 v[180:181], v[102:105] offset:512
	flat_store_dwordx4 v[180:181], v[94:97] offset:576
	s_andn2_b64 vcc, exec, s[20:21]
	s_mov_b64 s[0:1], -1
	v_lshl_add_u64 v[94:95], v[178:179], 0, v[150:151]
	flat_store_dwordx4 v[94:95], v[118:121]
	flat_store_dwordx4 v[94:95], v[114:117] offset:64
	flat_store_dwordx4 v[94:95], v[86:89] offset:512
	flat_store_dwordx4 v[94:95], v[82:85] offset:576
	s_nop 1
	v_lshl_add_u64 v[82:83], v[178:179], 0, v[152:153]
	flat_store_dwordx4 v[82:83], v[110:113]
	flat_store_dwordx4 v[82:83], v[106:109] offset:64
	flat_store_dwordx4 v[82:83], v[78:81] offset:512
	flat_store_dwordx4 v[82:83], v[74:77] offset:576
	s_nop 1
	v_lshl_add_u64 v[74:75], v[178:179], 0, v[154:155]
	flat_store_dwordx4 v[74:75], v[98:101]
	flat_store_dwordx4 v[74:75], v[90:93] offset:64
	flat_store_dwordx4 v[74:75], v[70:73] offset:512
	flat_store_dwordx4 v[74:75], v[66:69] offset:576
	s_nop 1
	v_lshl_add_u64 v[66:67], v[178:179], 0, v[156:157]
	flat_store_dwordx4 v[66:67], v[62:65]
	flat_store_dwordx4 v[66:67], v[58:61] offset:64
	flat_store_dwordx4 v[66:67], v[38:41] offset:512
	flat_store_dwordx4 v[66:67], v[30:33] offset:576
	s_nop 1
	v_lshl_add_u64 v[30:31], v[178:179], 0, v[158:159]
	flat_store_dwordx4 v[30:31], v[54:57]
	flat_store_dwordx4 v[30:31], v[50:53] offset:64
	flat_store_dwordx4 v[30:31], v[22:25] offset:512
	flat_store_dwordx4 v[30:31], v[18:21] offset:576
	s_nop 1
	v_lshl_add_u64 v[18:19], v[178:179], 0, v[160:161]
	flat_store_dwordx4 v[18:19], v[46:49]
	flat_store_dwordx4 v[18:19], v[42:45] offset:64
	flat_store_dwordx4 v[18:19], v[14:17] offset:512
	flat_store_dwordx4 v[18:19], v[10:13] offset:576
	s_nop 1
	v_lshl_add_u64 v[10:11], v[178:179], 0, v[162:163]
	flat_store_dwordx4 v[10:11], v[34:37]
	flat_store_dwordx4 v[10:11], v[26:29] offset:64
	flat_store_dwordx4 v[10:11], v[6:9] offset:512
	flat_store_dwordx4 v[10:11], v[2:5] offset:576
	s_cbranch_vccnz .LBB0_487
	s_andn2_b64 vcc, exec, s[6:7]
	s_cbranch_vccnz .LBB0_486
	s_branch .LBB0_486

; #define PG8_STAGE(bufoff, gbase, voff) do { _Pragma("unroll") for (int _i = 0; _i < 2; ++_i) \
;         __builtin_amdgcn_global_load_lds((const unsigned*)((const char*)(gbase) + (voff)[_i]), (PG8_LAS unsigned*)(lds + (bufoff) + ldsw + _i * 8192), 16, 0, 0); } while (0)
; #define PG8_WAIT_V(n) asm volatile("s_waitcnt vmcnt(" #n ")" ::: "memory")
; #define PG8_BAR __builtin_amdgcn_s_barrier()
;     __device__ __forceinline__ unsigned b_off(int R, int C) const { return (unsigned)(R * ldb + C) * 2u; }
; template <class Epi, class Sched, bool ALIGN_EPI = true, bool F8 = false>
; __device__ __forceinline__ void gemm_phase(PG8_LAS unsigned char* lds, const Sched& S, const Epi& E) {
;     ...
;     GUnit cur, nxt; int ui = 0;
;     if (!S.next(0, cur)) return;
;     S.a_off(cur, Rs, Cs, voffA);
; #pragma unroll
;     for (int h = 0; h < 2; ++h)
; #pragma unroll
;         for (int i = 0; i < 2; ++i) voffAn[h][i] = voffA[h][i];
;     f32x4 acc[2][2][4][2];
; #pragma unroll
;     for (int a = 0; a < 2; ++a)
; #pragma unroll
;         for (int b = 0; b < 2; ++b)
; #pragma unroll
;             for (int m = 0; m < 4; ++m)
; #pragma unroll
;                 for (int n = 0; n < 2; ++n) acc[a][b][m][n] = (f32x4){0.f, 0.f, 0.f, 0.f};
;     bf16x8 At[4][2], B0[2][2], B1[2][2]; i32x8 At8[4], B08[2], B18[2];
;     const int f8scale = 0x7F7F7F7F;
;     const char* cA = cur.A; const char* cB = cur.B;
;     PG8_STAGE(PG8_SB(0, 0), cB, voffB[0]); PG8_STAGE(PG8_SB(0, 1), cB, voffB[1]); PG8_STAGE(PG8_SA(0, 0), cA, voffA[0]); PG8_STAGE(PG8_SA(0, 1), cA, voffA[1]);
;     if (wr == 1) PG8_BAR;
;     PG8_WAIT_V(2); PG8_BAR;
;     PG8_STAGE(PG8_SB(1, 0), cB + kstepB, voffB[0]); PG8_STAGE(PG8_SA(1, 0), cA + kstep, voffA[0]); PG8_STAGE(PG8_SB(1, 1), cB + kstepB, voffB[1]);
;     PG8_WAIT_V(6); PG8_BAR;
;         u.A = FkT + (size_t)pm * 256 * 256 * 2; u.B = UF + (size_t)pn * 64 * FW * 2; u.nt = 4; u.x0 = pm; u.x1 = pn; u.x2 = 0; u.x3 = 0; return true; }
;     __device__ __forceinline__ unsigned b_off(int R, int C) const { const int g = R >> 6, cc = R & 63; return (unsigned)(cc * FW + g * 256 + C) * 2u; }
; __global__ void __launch_bounds__(NWAVES * 64, 2) fwd_kernel(Args a) {
;     ...
;         { SchedF1 S{G, bid, (const char*)(ws + WS_FKT), (const char*)(ws + WS_UF)}; EpiF1 E{(bf16*)(ws + WS_R3)}; pg8::gemm_phase<EpiF1, SchedF1>(lds, S, E); }
.LBB0_505:
	s_cmpk_gt_i32 s2, 0x3ff
	v_readfirstlane_b32 s0, v0
	s_cbranch_scc1 .LBB0_521
	s_add_u32 s46, s36, 0x1100000
	s_addc_u32 s47, s37, 0
	s_add_u32 s48, s36, 0x2e000000
	s_addc_u32 s49, s37, 0
	s_ashr_i32 s16, s2, 1
	s_lshr_b32 s13, s0, 6
	s_and_b32 s14, s2, 1
	s_ashr_i32 s17, s16, 31
	v_lshlrev_b32_e32 v3, 4, v0
	v_and_b32_e32 v6, 32, v0
	s_lshr_b32 s12, s0, 8
	s_lshl_b32 s15, s13, 10
	s_lshl_b32 s1, s14, 17
	s_lshl_b64 s[6:7], s[16:17], 17
	v_or_b32_e32 v4, 0x2000, v3
	v_bitop3_b32 v3, v3, v6, 48 bitop3:0x6c
	s_add_u32 s22, s46, s1
	v_and_or_b32 v3, v0, 64, v3
	v_lshrrev_b32_e32 v8, 5, v0
	v_and_b32_e32 v2, 48, v0
	s_addc_u32 s23, s47, 0
	v_lshrrev_b32_e32 v5, 7, v4
	v_lshrrev_b32_e32 v4, 4, v4
	v_lshrrev_b32_e32 v6, 1, v3
	s_movk_i32 s1, 0x300
	v_bfe_u32 v7, v0, 2, 2
	v_and_b32_e32 v8, 4, v8
	s_add_u32 s26, s48, s6
	v_and_or_b32 v4, v4, s1, v6
	v_or3_b32 v7, v8, v7, v2
	v_mov_b32_e32 v8, 0x2000
	s_movk_i32 s1, 0x100
	s_addc_u32 s27, s49, s7
	v_lshl_or_b32 v8, v7, 10, v8
	v_and_or_b32 v6, v0, s1, v6
	v_lshlrev_b32_e32 v7, 11, v7
	s_add_i32 s50, s15, 0
	v_lshl_or_b32 v136, v6, 1, v7
	s_add_i32 m0, s50, 0x10000
	v_or_b32_e32 v9, v4, v8
	v_or_b32_e32 v8, v6, v8
	v_lshl_or_b32 v134, v4, 1, v7
	global_load_lds_dwordx4 v136, s[26:27]
	s_add_i32 m0, s50, 0x12000
	v_lshlrev_b32_e32 v132, 1, v8
	v_bfe_u32 v4, v0, 2, 4
	s_movk_i32 s1, 0x70
	v_lshrrev_b32_e32 v6, 3, v0
	global_load_lds_dwordx4 v134, s[26:27]
	s_add_i32 m0, s50, 0x14000
	v_lshlrev_b32_e32 v130, 1, v9
	v_and_or_b32 v5, v5, s1, v4
	v_and_or_b32 v4, v6, 48, v4
	global_load_lds_dwordx4 v132, s[26:27]
	s_add_i32 m0, s50, 0x16000
	v_lshl_or_b32 v138, v4, 9, v3
	global_load_lds_dwordx4 v130, s[26:27]
	s_mov_b32 m0, s50
	s_add_i32 s51, s50, 0x2000
	v_lshl_or_b32 v140, v5, 9, v3
	global_load_lds_dwordx4 v138, s[22:23]
	s_mov_b32 m0, s51
	s_add_i32 s52, s50, 0x4000
	v_or_b32_e32 v142, 0x10000, v138
	global_load_lds_dwordx4 v140, s[22:23]
	s_mov_b32 m0, s52
	s_add_i32 s53, s50, 0x6000
	v_or_b32_e32 v144, 0x10000, v140
	global_load_lds_dwordx4 v142, s[22:23]
	s_mov_b32 m0, s53
	v_mov_b32_e32 v147, 0
	global_load_lds_dwordx4 v144, s[22:23]
	v_mov_b32_e32 v137, v147
	v_mov_b32_e32 v135, v147
	v_mov_b32_e32 v133, v147
	v_mov_b32_e32 v131, v147
	v_mov_b32_e32 v139, v147
	v_mov_b32_e32 v141, v147
	s_cmp_eq_u32 s12, 1
	s_mov_b32 s1, 0
	v_lshl_add_u64 v[12:13], s[26:27], 0, v[136:137]
	v_lshl_add_u64 v[8:9], s[26:27], 0, v[134:135]
	v_lshl_add_u64 v[6:7], s[26:27], 0, v[132:133]
	v_lshl_add_u64 v[4:5], s[26:27], 0, v[130:131]
	v_lshl_add_u64 v[14:15], s[22:23], 0, v[138:139]
	s_cselect_b64 s[6:7], -1, 0
	s_cmp_lg_u32 s12, 1
	v_lshl_add_u64 v[16:17], s[22:23], 0, v[140:141]
	s_cbranch_scc1 .LBB0_508
.LBB0_508:
	s_add_u32 s8, s36, 0x1e000000
	s_mov_b64 s[10:11], 0x80
	s_addc_u32 s9, s37, 0
	s_add_i32 m0, s50, 0x18000
	v_lshl_add_u64 v[12:13], v[12:13], 0, s[10:11]
	s_waitcnt vmcnt(2)
	s_barrier
	global_load_lds_dwordx4 v[12:13], off
	v_lshl_add_u64 v[8:9], v[8:9], 0, s[10:11]
	s_add_i32 m0, s50, 0x1a000
	s_add_i32 s59, s50, 0x8000
	global_load_lds_dwordx4 v[8:9], off
	v_lshl_add_u64 v[8:9], v[14:15], 0, s[10:11]
	s_mov_b32 m0, s59
	s_add_i32 s60, s50, 0xa000
	global_load_lds_dwordx4 v[8:9], off
	v_lshl_add_u64 v[8:9], v[16:17], 0, s[10:11]
	s_mov_b32 m0, s60
	v_lshl_add_u64 v[6:7], v[6:7], 0, s[10:11]
	global_load_lds_dwordx4 v[8:9], off
	s_add_i32 m0, s50, 0x1c000
	v_lshl_add_u64 v[4:5], v[4:5], 0, s[10:11]
	global_load_lds_dwordx4 v[6:7], off
	s_add_i32 m0, s50, 0x1e000
	s_and_b32 s17, s13, 3
	global_load_lds_dwordx4 v[4:5], off
	v_lshl_or_b32 v148, s12, 6, v169
	v_lshl_or_b32 v3, v169, 6, v2
	s_lshl_b32 s12, s12, 13
	v_and_b32_e32 v4, 32, v10
	v_bitop3_b32 v3, v3, s12, v4 bitop3:0xde
	s_lshl_b32 s12, s17, 12
	v_or_b32_e32 v4, v168, v2
	s_cmpk_lt_u32 s0, 0x100
	v_bitop3_b32 v4, s12, v4, v172 bitop3:0xf6
	s_cselect_b64 s[12:13], -1, 0
	s_lshl_b32 s0, s17, 8
	s_add_i32 s17, 0, 0x10000
	s_waitcnt vmcnt(6)
	s_add_i32 s65, 0, 0x14000
	s_add_i32 s63, s17, s15
	v_add_u32_e32 v164, s17, v4
	s_add_i32 s17, 0, 0x18000
	s_add_i32 s18, 0, 0x1c000
	v_add_u32_e32 v165, s65, v4
	s_add_i32 s65, s65, s15
	s_add_i32 s67, s17, s15
	s_add_i32 s69, s18, s15
	v_mov_b32_e32 v143, v147
	v_mov_b32_e32 v145, v147
	v_mov_b32_e32 v149, v147
	v_or_b32_e32 v150, 16, v148
	v_mov_b32_e32 v151, v147
	v_or_b32_e32 v152, 32, v148
	v_mov_b32_e32 v153, v147
	v_or_b32_e32 v154, 48, v148
	v_mov_b32_e32 v155, v147
	v_add_u32_e32 v156, 0x80, v148
	v_mov_b32_e32 v157, v147
	v_add_u32_e32 v158, 0x90, v148
	v_mov_b32_e32 v159, v147
	v_add_u32_e32 v160, 0xa0, v148
	v_mov_b32_e32 v161, v147
	v_add_u32_e32 v162, 0xb0, v148
	v_mov_b32_e32 v163, v147
	s_add_i32 s61, s50, 0xc000
	s_add_i32 s62, s50, 0xe000
	s_add_i32 s64, s63, 0x2000
	v_add_u32_e32 v166, 0, v3
	v_lshlrev_b32_e32 v146, 1, v2
	s_add_i32 s66, s65, 0x2000
	s_add_i32 s68, s67, 0x2000
	s_add_i32 s70, s69, 0x2000
	v_add_u32_e32 v167, s17, v4
	v_add_u32_e32 v168, s18, v4
	s_mov_b32 s71, s1
	s_mov_b64 s[20:21], s[26:27]
	s_mov_b64 s[24:25], s[22:23]
	s_barrier
	s_branch .LBB0_511

; #define PG8_STAGE(bufoff, gbase, voff) do { _Pragma("unroll") for (int _i = 0; _i < 2; ++_i) \
;         __builtin_amdgcn_global_load_lds((const unsigned*)((const char*)(gbase) + (voff)[_i]), (PG8_LAS unsigned*)(lds + (bufoff) + ldsw + _i * 8192), 16, 0, 0); } while (0)
; #define PG8_WAIT_V(n) asm volatile("s_waitcnt vmcnt(" #n ")" ::: "memory")
; #define PG8_WAIT_L(n) asm volatile("s_waitcnt lgkmcnt(" #n ")" ::: "memory")
; #define PG8_BAR __builtin_amdgcn_s_barrier()
; #define PG8_SCHED __builtin_amdgcn_sched_barrier(0)
; template <class Epi, class Sched, bool ALIGN_EPI = true, bool F8 = false>
; __device__ __forceinline__ void gemm_phase(PG8_LAS unsigned char* lds, const Sched& S, const Epi& E) {
;     ...
;     f32x4 acc[2][2][4][2];
; #pragma unroll
;     for (int a = 0; a < 2; ++a)
; #pragma unroll
;         for (int b = 0; b < 2; ++b)
; #pragma unroll
;             for (int m = 0; m < 4; ++m)
; #pragma unroll
;                 for (int n = 0; n < 2; ++n) acc[a][b][m][n] = (f32x4){0.f, 0.f, 0.f, 0.f};
;     ...
;         for (int t = 0; t < nt; t += 2) {
;             const bool last = (t == nt - 2);
;             if constexpr (Sched::GATHER) { if (last && has_next) S.a_off(nxt, Rs, Cs, voffAn); }
;             const char* a1 = cA + (size_t)(t + 1) * kstep;
;             const char* a2 = last ? nA : cA + (size_t)(t + 2) * kstep; const char* b2 = last ? nB : cB + (size_t)(t + 2) * kstepB;
;             const char* a3 = a2 + kstep; const char* b3 = b2 + kstepB;
;             unsigned vA2[2][2];
; #pragma unroll
;             for (int h = 0; h < 2; ++h)
; #pragma unroll
;                 for (int i = 0; i < 2; ++i) { if constexpr (Sched::GATHER) vA2[h][i] = (last && has_next) ? voffAn[h][i] : voffA[h][i]; else vA2[h][i] = voffA[h][i]; }
;             PG8_LDB(B0, 0, 0); PG8_LDB(B1, 0, 1); PG8_SCHED; PG8_LDA(At, 0, 0); PG8_STAGE(PG8_SA(1, 1), a1, voffA[1]);
;             PG8_WAIT_V(8); PG8_WAIT_L(0); PG8_BAR; PG8_MMA(0, 0, At, B0); PG8_MMA(0, 1, At, B1); PG8_BAR; PG8_SCHED;
.LBB0_513:
	v_mov_b32_e32 v2, 0
	s_mov_b32 s15, 0
	s_mov_b64 s[30:31], -1
	s_mov_b64 s[40:41], 0
	v_mov_b32_e32 v3, v2
	v_mov_b32_e32 v4, v2
	v_mov_b32_e32 v5, v2
	v_mov_b32_e32 v6, v2
	v_mov_b32_e32 v7, v2
	v_mov_b32_e32 v8, v2
	v_mov_b32_e32 v9, v2
	v_mov_b32_e32 v10, v2
	v_mov_b32_e32 v11, v2
	v_mov_b32_e32 v12, v2
	v_mov_b32_e32 v13, v2
	v_mov_b32_e32 v14, v2
	v_mov_b32_e32 v15, v2
	v_mov_b32_e32 v16, v2
	v_mov_b32_e32 v17, v2
	v_mov_b32_e32 v26, v2
	v_mov_b32_e32 v27, v2
	v_mov_b32_e32 v28, v2
	v_mov_b32_e32 v29, v2
	v_mov_b32_e32 v30, v2
	v_mov_b32_e32 v31, v2
	v_mov_b32_e32 v32, v2
	v_mov_b32_e32 v33, v2
	v_mov_b32_e32 v42, v2
	v_mov_b32_e32 v43, v2
	v_mov_b32_e32 v44, v2
	v_mov_b32_e32 v45, v2
	v_mov_b32_e32 v46, v2
	v_mov_b32_e32 v47, v2
	v_mov_b32_e32 v48, v2
	v_mov_b32_e32 v49, v2
	v_mov_b32_e32 v18, v2
	v_mov_b32_e32 v19, v2
	v_mov_b32_e32 v20, v2
	v_mov_b32_e32 v21, v2
	v_mov_b32_e32 v22, v2
	v_mov_b32_e32 v23, v2
	v_mov_b32_e32 v24, v2
	v_mov_b32_e32 v25, v2
	v_mov_b32_e32 v34, v2
	v_mov_b32_e32 v35, v2
	v_mov_b32_e32 v36, v2
	v_mov_b32_e32 v37, v2
	v_mov_b32_e32 v38, v2
	v_mov_b32_e32 v39, v2
	v_mov_b32_e32 v40, v2
	v_mov_b32_e32 v41, v2
	v_mov_b32_e32 v50, v2
	v_mov_b32_e32 v51, v2
	v_mov_b32_e32 v52, v2
	v_mov_b32_e32 v53, v2
	v_mov_b32_e32 v54, v2
	v_mov_b32_e32 v55, v2
	v_mov_b32_e32 v56, v2
	v_mov_b32_e32 v57, v2
	v_mov_b32_e32 v58, v2
	v_mov_b32_e32 v59, v2
	v_mov_b32_e32 v60, v2
	v_mov_b32_e32 v61, v2
	v_mov_b32_e32 v62, v2
	v_mov_b32_e32 v63, v2
	v_mov_b32_e32 v64, v2
	v_mov_b32_e32 v65, v2
	v_mov_b32_e32 v66, v2
	v_mov_b32_e32 v67, v2
	v_mov_b32_e32 v68, v2
	v_mov_b32_e32 v69, v2
	v_mov_b32_e32 v70, v2
	v_mov_b32_e32 v71, v2
	v_mov_b32_e32 v72, v2
	v_mov_b32_e32 v73, v2
	v_mov_b32_e32 v74, v2
	v_mov_b32_e32 v75, v2
	v_mov_b32_e32 v76, v2
	v_mov_b32_e32 v77, v2
	v_mov_b32_e32 v78, v2
	v_mov_b32_e32 v79, v2
	v_mov_b32_e32 v80, v2
	v_mov_b32_e32 v81, v2
	v_mov_b32_e32 v90, v2
	v_mov_b32_e32 v91, v2
	v_mov_b32_e32 v92, v2
	v_mov_b32_e32 v93, v2
	v_mov_b32_e32 v94, v2
	v_mov_b32_e32 v95, v2
	v_mov_b32_e32 v96, v2
	v_mov_b32_e32 v97, v2
	v_mov_b32_e32 v106, v2
	v_mov_b32_e32 v107, v2
	v_mov_b32_e32 v108, v2
	v_mov_b32_e32 v109, v2
	v_mov_b32_e32 v110, v2
	v_mov_b32_e32 v111, v2
	v_mov_b32_e32 v112, v2
	v_mov_b32_e32 v113, v2
	v_mov_b32_e32 v82, v2
	v_mov_b32_e32 v83, v2
	v_mov_b32_e32 v84, v2
	v_mov_b32_e32 v85, v2
	v_mov_b32_e32 v86, v2
	v_mov_b32_e32 v87, v2
	v_mov_b32_e32 v88, v2
	v_mov_b32_e32 v89, v2
	v_mov_b32_e32 v98, v2
	v_mov_b32_e32 v99, v2
	v_mov_b32_e32 v100, v2
	v_mov_b32_e32 v101, v2
	v_mov_b32_e32 v102, v2
	v_mov_b32_e32 v103, v2
	v_mov_b32_e32 v104, v2
	v_mov_b32_e32 v105, v2
	v_mov_b32_e32 v114, v2
	v_mov_b32_e32 v115, v2
	v_mov_b32_e32 v116, v2
	v_mov_b32_e32 v117, v2
	v_mov_b32_e32 v118, v2
	v_mov_b32_e32 v119, v2
	v_mov_b32_e32 v120, v2
	v_mov_b32_e32 v121, v2
	v_mov_b32_e32 v122, v2
	v_mov_b32_e32 v123, v2
	v_mov_b32_e32 v124, v2
	v_mov_b32_e32 v125, v2
	v_mov_b32_e32 v126, v2
	v_mov_b32_e32 v127, v2
	v_mov_b32_e32 v128, v2
	v_mov_b32_e32 v129, v2
	s_bitcmp1_b32 s3, 2
	s_cbranch_scc1 .Lh1e_14299
.LBB0_514:
	s_add_u32 s44, s22, s15
	ds_read_b128 v[172:175], v164
	ds_read_b128 v[176:179], v164 offset:1024
	ds_read_b128 v[180:183], v164 offset:2048
	ds_read_b128 v[184:187], v164 offset:3072
	ds_read_b128 v[188:191], v165
	ds_read_b128 v[192:195], v165 offset:1024
	ds_read_b128 v[196:199], v165 offset:2048
	ds_read_b128 v[200:203], v165 offset:3072
	s_addc_u32 s45, s23, 0
	s_add_u32 s17, s44, 0x100
	s_addc_u32 s72, s45, 0
	s_and_b64 s[42:43], s[40:41], exec
	s_cselect_b32 s42, s24, s17
	s_cselect_b32 s43, s25, s72
	s_add_u32 s15, s26, s15
	s_addc_u32 s17, s27, 0
	s_add_u32 s15, s15, 0x100
	s_addc_u32 s17, s17, 0
	s_and_b64 s[40:41], s[40:41], exec
	s_cselect_b32 s40, s20, s15
	s_cselect_b32 s41, s21, s17
	v_lshl_add_u64 v[236:237], s[44:45], 0, v[142:143]
	s_mov_b32 m0, s61
	v_lshl_add_u64 v[236:237], v[236:237], 0, s[10:11]
	ds_read_b128 v[204:207], v166
	ds_read_b128 v[208:211], v166 offset:1024
	ds_read_b128 v[212:215], v166 offset:2048
	ds_read_b128 v[216:219], v166 offset:3072
	ds_read_b128 v[220:223], v166 offset:4096
	ds_read_b128 v[224:227], v166 offset:5120
	ds_read_b128 v[228:231], v166 offset:6144
	ds_read_b128 v[232:235], v166 offset:7168
	global_load_lds_dwordx4 v[236:237], off
	v_lshl_add_u64 v[236:237], s[44:45], 0, v[144:145]
	v_lshl_add_u64 v[236:237], v[236:237], 0, s[10:11]
	s_mov_b32 m0, s62
	s_nop 0
	global_load_lds_dwordx4 v[236:237], off
	s_waitcnt vmcnt(8)
	s_waitcnt lgkmcnt(0)
	s_setprio 1
	v_mfma_f32_16x16x32_bf16 v[126:129], v[172:175], v[204:207], v[126:129]
	v_mfma_f32_16x16x32_bf16 v[122:125], v[180:183], v[204:207], v[122:125]
	v_mfma_f32_16x16x32_bf16 v[118:121], v[172:175], v[212:215], v[118:121]
	v_mfma_f32_16x16x32_bf16 v[114:117], v[180:183], v[212:215], v[114:117]
	v_mfma_f32_16x16x32_bf16 v[102:105], v[172:175], v[220:223], v[102:105]
	v_mfma_f32_16x16x32_bf16 v[98:101], v[180:183], v[220:223], v[98:101]
	v_mfma_f32_16x16x32_bf16 v[86:89], v[172:175], v[228:231], v[86:89]
	v_mfma_f32_16x16x32_bf16 v[82:85], v[180:183], v[228:231], v[82:85]
	v_mfma_f32_16x16x32_bf16 v[126:129], v[176:179], v[208:211], v[126:129]
	v_mfma_f32_16x16x32_bf16 v[122:125], v[184:187], v[208:211], v[122:125]
	v_mfma_f32_16x16x32_bf16 v[118:121], v[176:179], v[216:219], v[118:121]
	v_mfma_f32_16x16x32_bf16 v[114:117], v[184:187], v[216:219], v[114:117]
	v_mfma_f32_16x16x32_bf16 v[102:105], v[176:179], v[224:227], v[102:105]
	v_mfma_f32_16x16x32_bf16 v[98:101], v[184:187], v[224:227], v[98:101]
	v_mfma_f32_16x16x32_bf16 v[86:89], v[176:179], v[232:235], v[86:89]
	v_mfma_f32_16x16x32_bf16 v[82:85], v[184:187], v[232:235], v[82:85]
	s_setprio 0
	s_setprio 1
	v_mfma_f32_16x16x32_bf16 v[110:113], v[188:191], v[204:207], v[110:113]
	v_mfma_f32_16x16x32_bf16 v[106:109], v[196:199], v[204:207], v[106:109]
	v_mfma_f32_16x16x32_bf16 v[94:97], v[188:191], v[212:215], v[94:97]
	v_mfma_f32_16x16x32_bf16 v[90:93], v[196:199], v[212:215], v[90:93]
	v_mfma_f32_16x16x32_bf16 v[78:81], v[188:191], v[220:223], v[78:81]
	v_mfma_f32_16x16x32_bf16 v[74:77], v[196:199], v[220:223], v[74:77]
	v_mfma_f32_16x16x32_bf16 v[70:73], v[188:191], v[228:231], v[70:73]
	v_mfma_f32_16x16x32_bf16 v[66:69], v[196:199], v[228:231], v[66:69]
	v_mfma_f32_16x16x32_bf16 v[110:113], v[192:195], v[208:211], v[110:113]
	v_mfma_f32_16x16x32_bf16 v[106:109], v[200:203], v[208:211], v[106:109]
	v_mfma_f32_16x16x32_bf16 v[94:97], v[192:195], v[216:219], v[94:97]
	v_mfma_f32_16x16x32_bf16 v[90:93], v[200:203], v[216:219], v[90:93]
	v_mfma_f32_16x16x32_bf16 v[78:81], v[192:195], v[224:227], v[78:81]
	v_mfma_f32_16x16x32_bf16 v[74:77], v[200:203], v[224:227], v[74:77]
	v_mfma_f32_16x16x32_bf16 v[70:73], v[192:195], v[232:235], v[70:73]
	v_mfma_f32_16x16x32_bf16 v[66:69], v[200:203], v[232:235], v[66:69]
	s_setprio 0
	s_barrier
; #define PG8_STAGE(bufoff, gbase, voff) do { _Pragma("unroll") for (int _i = 0; _i < 2; ++_i) \
;         __builtin_amdgcn_global_load_lds((const unsigned*)((const char*)(gbase) + (voff)[_i]), (PG8_LAS unsigned*)(lds + (bufoff) + ldsw + _i * 8192), 16, 0, 0); } while (0)
; #define PG8_WAIT_V(n) asm volatile("s_waitcnt vmcnt(" #n ")" ::: "memory")
; #define PG8_WAIT_L(n) asm volatile("s_waitcnt lgkmcnt(" #n ")" ::: "memory")
; #define PG8_BAR __builtin_amdgcn_s_barrier()
; #define PG8_SCHED __builtin_amdgcn_sched_barrier(0)
; template <class Epi, class Sched, bool ALIGN_EPI = true, bool F8 = false>
; __device__ __forceinline__ void gemm_phase(PG8_LAS unsigned char* lds, const Sched& S, const Epi& E) {
;     ...
;             PG8_WAIT_V(8); PG8_WAIT_L(0); PG8_BAR; PG8_MMA(0, 0, At, B0); PG8_MMA(0, 1, At, B1); PG8_BAR; PG8_SCHED;
;             PG8_LDA(At, 0, 1); PG8_STAGE(PG8_SB(0, 0), b2, voffB[0]); PG8_STAGE(PG8_SB(0, 1), b2, voffB[1]); PG8_STAGE(PG8_SA(0, 0), a2, vA2[0]);
;             PG8_WAIT_V(8); PG8_WAIT_L(0); PG8_BAR; PG8_MMA(1, 0, At, B0); PG8_MMA(1, 1, At, B1); PG8_BAR; PG8_SCHED;
;             PG8_LDB(B0, 1, 0); PG8_LDB(B1, 1, 1); PG8_SCHED; PG8_LDA(At, 1, 0); PG8_STAGE(PG8_SA(0, 1), a2, vA2[1]);
;             PG8_WAIT_V(8); PG8_WAIT_L(0); PG8_BAR; PG8_MMA(0, 0, At, B0); PG8_MMA(0, 1, At, B1); PG8_BAR; PG8_SCHED;
	s_mov_b32 m0, s63
	v_lshl_add_u64 v[236:237], s[40:41], 0, v[136:137]
	ds_read_b128 v[204:207], v166 offset:16384
	ds_read_b128 v[208:211], v166 offset:17408
	ds_read_b128 v[212:215], v166 offset:18432
	ds_read_b128 v[216:219], v166 offset:19456
	ds_read_b128 v[220:223], v166 offset:20480
	ds_read_b128 v[224:227], v166 offset:21504
	ds_read_b128 v[228:231], v166 offset:22528
	ds_read_b128 v[232:235], v166 offset:23552
	global_load_lds_dwordx4 v[236:237], off
	v_lshl_add_u64 v[238:239], s[40:41], 0, v[134:135]
	s_mov_b32 m0, s64
	v_lshl_add_u64 v[240:241], s[40:41], 0, v[132:133]
	global_load_lds_dwordx4 v[238:239], off
	s_mov_b32 m0, s65
	v_lshl_add_u64 v[242:243], s[40:41], 0, v[130:131]
	global_load_lds_dwordx4 v[240:241], off
	s_mov_b32 m0, s66
	v_lshl_add_u64 v[244:245], s[42:43], 0, v[138:139]
	global_load_lds_dwordx4 v[242:243], off
	s_mov_b32 m0, s50
	v_lshl_add_u64 v[246:247], s[42:43], 0, v[140:141]
	global_load_lds_dwordx4 v[244:245], off
	s_mov_b32 m0, s51
	s_nop 0
	global_load_lds_dwordx4 v[246:247], off
	s_waitcnt vmcnt(8)
	s_waitcnt lgkmcnt(0)
	s_setprio 1
	v_mfma_f32_16x16x32_bf16 v[62:65], v[172:175], v[204:207], v[62:65]
	v_mfma_f32_16x16x32_bf16 v[58:61], v[180:183], v[204:207], v[58:61]
	v_mfma_f32_16x16x32_bf16 v[54:57], v[172:175], v[212:215], v[54:57]
	v_mfma_f32_16x16x32_bf16 v[50:53], v[180:183], v[212:215], v[50:53]
	v_mfma_f32_16x16x32_bf16 v[38:41], v[172:175], v[220:223], v[38:41]
	v_mfma_f32_16x16x32_bf16 v[34:37], v[180:183], v[220:223], v[34:37]
	v_mfma_f32_16x16x32_bf16 v[22:25], v[172:175], v[228:231], v[22:25]
	v_mfma_f32_16x16x32_bf16 v[18:21], v[180:183], v[228:231], v[18:21]
	v_mfma_f32_16x16x32_bf16 v[62:65], v[176:179], v[208:211], v[62:65]
	v_mfma_f32_16x16x32_bf16 v[58:61], v[184:187], v[208:211], v[58:61]
	v_mfma_f32_16x16x32_bf16 v[54:57], v[176:179], v[216:219], v[54:57]
	v_mfma_f32_16x16x32_bf16 v[50:53], v[184:187], v[216:219], v[50:53]
	v_mfma_f32_16x16x32_bf16 v[38:41], v[176:179], v[224:227], v[38:41]
	v_mfma_f32_16x16x32_bf16 v[34:37], v[184:187], v[224:227], v[34:37]
	v_mfma_f32_16x16x32_bf16 v[22:25], v[176:179], v[232:235], v[22:25]
	v_mfma_f32_16x16x32_bf16 v[18:21], v[184:187], v[232:235], v[18:21]
	s_setprio 0
	s_setprio 1
	v_mfma_f32_16x16x32_bf16 v[46:49], v[188:191], v[204:207], v[46:49]
	v_mfma_f32_16x16x32_bf16 v[42:45], v[196:199], v[204:207], v[42:45]
	v_mfma_f32_16x16x32_bf16 v[30:33], v[188:191], v[212:215], v[30:33]
	v_mfma_f32_16x16x32_bf16 v[26:29], v[196:199], v[212:215], v[26:29]
	v_mfma_f32_16x16x32_bf16 v[14:17], v[188:191], v[220:223], v[14:17]
	v_mfma_f32_16x16x32_bf16 v[10:13], v[196:199], v[220:223], v[10:13]
	v_mfma_f32_16x16x32_bf16 v[6:9], v[188:191], v[228:231], v[6:9]
	v_mfma_f32_16x16x32_bf16 v[2:5], v[196:199], v[228:231], v[2:5]
	v_mfma_f32_16x16x32_bf16 v[46:49], v[192:195], v[208:211], v[46:49]
	v_mfma_f32_16x16x32_bf16 v[42:45], v[200:203], v[208:211], v[42:45]
	v_mfma_f32_16x16x32_bf16 v[30:33], v[192:195], v[216:219], v[30:33]
	v_mfma_f32_16x16x32_bf16 v[26:29], v[200:203], v[216:219], v[26:29]
	v_mfma_f32_16x16x32_bf16 v[14:17], v[192:195], v[224:227], v[14:17]
	v_mfma_f32_16x16x32_bf16 v[10:13], v[200:203], v[224:227], v[10:13]
	v_mfma_f32_16x16x32_bf16 v[6:9], v[192:195], v[232:235], v[6:9]
	v_mfma_f32_16x16x32_bf16 v[2:5], v[200:203], v[232:235], v[2:5]
	s_setprio 0
	s_barrier
	ds_read_b128 v[172:175], v167
	ds_read_b128 v[176:179], v167 offset:1024
	ds_read_b128 v[180:183], v167 offset:2048
	ds_read_b128 v[184:187], v167 offset:3072
	ds_read_b128 v[188:191], v168
	ds_read_b128 v[192:195], v168 offset:1024
	ds_read_b128 v[196:199], v168 offset:2048
	ds_read_b128 v[200:203], v168 offset:3072
	s_mov_b32 m0, s52
	v_lshl_add_u64 v[248:249], s[42:43], 0, v[142:143]
	ds_read_b128 v[204:207], v166 offset:32768
	ds_read_b128 v[208:211], v166 offset:33792
	ds_read_b128 v[212:215], v166 offset:34816
	ds_read_b128 v[216:219], v166 offset:35840
	ds_read_b128 v[220:223], v166 offset:36864
	ds_read_b128 v[224:227], v166 offset:37888
	ds_read_b128 v[228:231], v166 offset:38912
	ds_read_b128 v[232:235], v166 offset:39936
	global_load_lds_dwordx4 v[248:249], off
	v_lshl_add_u64 v[248:249], s[42:43], 0, v[144:145]
	s_mov_b32 m0, s53
	s_nop 0
	global_load_lds_dwordx4 v[248:249], off
	s_waitcnt vmcnt(8)
	s_waitcnt lgkmcnt(0)
	s_setprio 1
	v_mfma_f32_16x16x32_bf16 v[126:129], v[172:175], v[204:207], v[126:129]
	v_mfma_f32_16x16x32_bf16 v[122:125], v[180:183], v[204:207], v[122:125]
	v_mfma_f32_16x16x32_bf16 v[118:121], v[172:175], v[212:215], v[118:121]
	v_mfma_f32_16x16x32_bf16 v[114:117], v[180:183], v[212:215], v[114:117]
	v_mfma_f32_16x16x32_bf16 v[102:105], v[172:175], v[220:223], v[102:105]
	v_mfma_f32_16x16x32_bf16 v[98:101], v[180:183], v[220:223], v[98:101]
	v_mfma_f32_16x16x32_bf16 v[86:89], v[172:175], v[228:231], v[86:89]
	v_mfma_f32_16x16x32_bf16 v[82:85], v[180:183], v[228:231], v[82:85]
	v_mfma_f32_16x16x32_bf16 v[126:129], v[176:179], v[208:211], v[126:129]
	v_mfma_f32_16x16x32_bf16 v[122:125], v[184:187], v[208:211], v[122:125]
	v_mfma_f32_16x16x32_bf16 v[118:121], v[176:179], v[216:219], v[118:121]
	v_mfma_f32_16x16x32_bf16 v[114:117], v[184:187], v[216:219], v[114:117]
	v_mfma_f32_16x16x32_bf16 v[102:105], v[176:179], v[224:227], v[102:105]
	v_mfma_f32_16x16x32_bf16 v[98:101], v[184:187], v[224:227], v[98:101]
	v_mfma_f32_16x16x32_bf16 v[86:89], v[176:179], v[232:235], v[86:89]
	v_mfma_f32_16x16x32_bf16 v[82:85], v[184:187], v[232:235], v[82:85]
	s_setprio 0
	s_setprio 1
	v_mfma_f32_16x16x32_bf16 v[110:113], v[188:191], v[204:207], v[110:113]
	v_mfma_f32_16x16x32_bf16 v[106:109], v[196:199], v[204:207], v[106:109]
	v_mfma_f32_16x16x32_bf16 v[94:97], v[188:191], v[212:215], v[94:97]
	v_mfma_f32_16x16x32_bf16 v[90:93], v[196:199], v[212:215], v[90:93]
	v_mfma_f32_16x16x32_bf16 v[78:81], v[188:191], v[220:223], v[78:81]
	v_mfma_f32_16x16x32_bf16 v[74:77], v[196:199], v[220:223], v[74:77]
	v_mfma_f32_16x16x32_bf16 v[70:73], v[188:191], v[228:231], v[70:73]
	v_mfma_f32_16x16x32_bf16 v[66:69], v[196:199], v[228:231], v[66:69]
	v_mfma_f32_16x16x32_bf16 v[110:113], v[192:195], v[208:211], v[110:113]
	v_mfma_f32_16x16x32_bf16 v[106:109], v[200:203], v[208:211], v[106:109]
	v_mfma_f32_16x16x32_bf16 v[94:97], v[192:195], v[216:219], v[94:97]
	v_mfma_f32_16x16x32_bf16 v[90:93], v[200:203], v[216:219], v[90:93]
	v_mfma_f32_16x16x32_bf16 v[78:81], v[192:195], v[224:227], v[78:81]
	v_mfma_f32_16x16x32_bf16 v[74:77], v[200:203], v[224:227], v[74:77]
	v_mfma_f32_16x16x32_bf16 v[70:73], v[192:195], v[232:235], v[70:73]
	v_mfma_f32_16x16x32_bf16 v[66:69], v[200:203], v[232:235], v[66:69]
	s_setprio 0
	s_barrier
; #define PG8_STAGE(bufoff, gbase, voff) do { _Pragma("unroll") for (int _i = 0; _i < 2; ++_i) \
;         __builtin_amdgcn_global_load_lds((const unsigned*)((const char*)(gbase) + (voff)[_i]), (PG8_LAS unsigned*)(lds + (bufoff) + ldsw + _i * 8192), 16, 0, 0); } while (0)
; #define PG8_WAIT_V(n) asm volatile("s_waitcnt vmcnt(" #n ")" ::: "memory")
; #define PG8_WAIT_L(n) asm volatile("s_waitcnt lgkmcnt(" #n ")" ::: "memory")
; #define PG8_BAR __builtin_amdgcn_s_barrier()
; #define PG8_SCHED __builtin_amdgcn_sched_barrier(0)
; template <class Epi, class Sched, bool ALIGN_EPI = true, bool F8 = false>
; __device__ __forceinline__ void gemm_phase(PG8_LAS unsigned char* lds, const Sched& S, const Epi& E) {
;     ...
;             PG8_LDB(B0, 0, 0); PG8_LDB(B1, 0, 1); PG8_SCHED; PG8_LDA(At, 0, 0); PG8_STAGE(PG8_SA(1, 1), a1, voffA[1]);
;             PG8_WAIT_V(8); PG8_WAIT_L(0); PG8_BAR; PG8_MMA(0, 0, At, B0); PG8_MMA(0, 1, At, B1); PG8_BAR; PG8_SCHED;
;     ...
;             PG8_LDA(At, 1, 1); PG8_STAGE(PG8_SB(1, 0), b3, voffB[0]); PG8_STAGE(PG8_SB(1, 1), b3, voffB[1]); PG8_STAGE(PG8_SA(1, 0), a3, vA2[0]);
;             PG8_WAIT_V(8); PG8_WAIT_L(0); PG8_BAR; PG8_MMA(1, 0, At, B0); PG8_MMA(1, 1, At, B1); PG8_BAR; PG8_SCHED;
;         }
	s_mov_b32 m0, s67
	v_lshl_add_u64 v[236:237], v[236:237], 0, s[10:11]
	ds_read_b128 v[204:207], v166 offset:49152
	ds_read_b128 v[208:211], v166 offset:50176
	ds_read_b128 v[212:215], v166 offset:51200
	ds_read_b128 v[216:219], v166 offset:52224
	ds_read_b128 v[220:223], v166 offset:53248
	ds_read_b128 v[224:227], v166 offset:54272
	ds_read_b128 v[228:231], v166 offset:55296
	ds_read_b128 v[232:235], v166 offset:56320
	global_load_lds_dwordx4 v[236:237], off
	v_lshl_add_u64 v[236:237], v[238:239], 0, s[10:11]
	s_mov_b32 m0, s68
	s_nop 0
	global_load_lds_dwordx4 v[236:237], off
	v_lshl_add_u64 v[236:237], v[240:241], 0, s[10:11]
	s_mov_b32 m0, s69
	s_nop 0
	global_load_lds_dwordx4 v[236:237], off
	v_lshl_add_u64 v[236:237], v[242:243], 0, s[10:11]
	s_mov_b32 m0, s70
	s_nop 0
	global_load_lds_dwordx4 v[236:237], off
	v_lshl_add_u64 v[236:237], v[244:245], 0, s[10:11]
	s_mov_b32 m0, s59
	s_nop 0
	global_load_lds_dwordx4 v[236:237], off
	v_lshl_add_u64 v[236:237], v[246:247], 0, s[10:11]
	s_mov_b32 m0, s60
	s_nop 0
	global_load_lds_dwordx4 v[236:237], off
	s_waitcnt vmcnt(8)
	s_waitcnt lgkmcnt(0)
	s_setprio 1
	v_mfma_f32_16x16x32_bf16 v[62:65], v[172:175], v[204:207], v[62:65]
	v_mfma_f32_16x16x32_bf16 v[58:61], v[180:183], v[204:207], v[58:61]
	v_mfma_f32_16x16x32_bf16 v[54:57], v[172:175], v[212:215], v[54:57]
	v_mfma_f32_16x16x32_bf16 v[50:53], v[180:183], v[212:215], v[50:53]
	v_mfma_f32_16x16x32_bf16 v[38:41], v[172:175], v[220:223], v[38:41]
	v_mfma_f32_16x16x32_bf16 v[34:37], v[180:183], v[220:223], v[34:37]
	v_mfma_f32_16x16x32_bf16 v[22:25], v[172:175], v[228:231], v[22:25]
	v_mfma_f32_16x16x32_bf16 v[18:21], v[180:183], v[228:231], v[18:21]
	v_mfma_f32_16x16x32_bf16 v[62:65], v[176:179], v[208:211], v[62:65]
	v_mfma_f32_16x16x32_bf16 v[58:61], v[184:187], v[208:211], v[58:61]
	v_mfma_f32_16x16x32_bf16 v[54:57], v[176:179], v[216:219], v[54:57]
	v_mfma_f32_16x16x32_bf16 v[50:53], v[184:187], v[216:219], v[50:53]
	v_mfma_f32_16x16x32_bf16 v[38:41], v[176:179], v[224:227], v[38:41]
	v_mfma_f32_16x16x32_bf16 v[34:37], v[184:187], v[224:227], v[34:37]
	v_mfma_f32_16x16x32_bf16 v[22:25], v[176:179], v[232:235], v[22:25]
	v_mfma_f32_16x16x32_bf16 v[18:21], v[184:187], v[232:235], v[18:21]
	s_setprio 0
	s_setprio 1
	v_mfma_f32_16x16x32_bf16 v[46:49], v[188:191], v[204:207], v[46:49]
	v_mfma_f32_16x16x32_bf16 v[42:45], v[196:199], v[204:207], v[42:45]
	v_mfma_f32_16x16x32_bf16 v[30:33], v[188:191], v[212:215], v[30:33]
	v_mfma_f32_16x16x32_bf16 v[26:29], v[196:199], v[212:215], v[26:29]
	v_mfma_f32_16x16x32_bf16 v[14:17], v[188:191], v[220:223], v[14:17]
	v_mfma_f32_16x16x32_bf16 v[10:13], v[196:199], v[220:223], v[10:13]
	v_mfma_f32_16x16x32_bf16 v[6:9], v[188:191], v[228:231], v[6:9]
	v_mfma_f32_16x16x32_bf16 v[2:5], v[196:199], v[228:231], v[2:5]
	v_mfma_f32_16x16x32_bf16 v[46:49], v[192:195], v[208:211], v[46:49]
	v_mfma_f32_16x16x32_bf16 v[42:45], v[200:203], v[208:211], v[42:45]
	v_mfma_f32_16x16x32_bf16 v[30:33], v[192:195], v[216:219], v[30:33]
	v_mfma_f32_16x16x32_bf16 v[26:29], v[200:203], v[216:219], v[26:29]
	v_mfma_f32_16x16x32_bf16 v[14:17], v[192:195], v[224:227], v[14:17]
	v_mfma_f32_16x16x32_bf16 v[10:13], v[200:203], v[224:227], v[10:13]
	v_mfma_f32_16x16x32_bf16 v[6:9], v[192:195], v[232:235], v[6:9]
	v_mfma_f32_16x16x32_bf16 v[2:5], v[200:203], v[232:235], v[2:5]
	s_setprio 0
	s_barrier
	s_movk_i32 s15, 0x100
	s_andn2_b64 vcc, exec, s[30:31]
	s_mov_b64 s[40:41], -1
	s_mov_b64 s[30:31], 0
	s_cbranch_vccz .LBB0_514
	s_branch .Lfx_14299
.Lh1e_14299:
.Lh1_514:
	s_add_u32 s44, s22, s15
	ds_read_b128 v[172:175], v164
	ds_read_b128 v[176:179], v164 offset:1024
	ds_read_b128 v[180:183], v164 offset:2048
	ds_read_b128 v[184:187], v164 offset:3072
	ds_read_b128 v[188:191], v165
	ds_read_b128 v[192:195], v165 offset:1024
	ds_read_b128 v[196:199], v165 offset:2048
	ds_read_b128 v[200:203], v165 offset:3072
	s_addc_u32 s45, s23, 0
	s_add_u32 s17, s44, 0x100
	s_addc_u32 s72, s45, 0
	s_and_b64 s[42:43], s[40:41], exec
	s_cselect_b32 s42, s24, s17
	s_cselect_b32 s43, s25, s72
	s_add_u32 s15, s26, s15
	s_addc_u32 s17, s27, 0
	s_add_u32 s15, s15, 0x100
	s_addc_u32 s17, s17, 0
	s_and_b64 s[40:41], s[40:41], exec
	s_cselect_b32 s40, s20, s15
	s_cselect_b32 s41, s21, s17
	v_lshl_add_u64 v[236:237], s[44:45], 0, v[142:143]
	s_mov_b32 m0, s61
	v_lshl_add_u64 v[236:237], v[236:237], 0, s[10:11]
	ds_read_b128 v[204:207], v166
	ds_read_b128 v[208:211], v166 offset:1024
	ds_read_b128 v[212:215], v166 offset:2048
	ds_read_b128 v[216:219], v166 offset:3072
	ds_read_b128 v[220:223], v166 offset:4096
	ds_read_b128 v[224:227], v166 offset:5120
	ds_read_b128 v[228:231], v166 offset:6144
	ds_read_b128 v[232:235], v166 offset:7168
	global_load_lds_dwordx4 v[236:237], off
	v_lshl_add_u64 v[236:237], s[44:45], 0, v[144:145]
	v_lshl_add_u64 v[236:237], v[236:237], 0, s[10:11]
	s_mov_b32 m0, s62
	s_nop 0
	global_load_lds_dwordx4 v[236:237], off
	s_waitcnt vmcnt(8)
	s_waitcnt lgkmcnt(0)
	s_barrier
; #define PG8_STAGE(bufoff, gbase, voff) do { _Pragma("unroll") for (int _i = 0; _i < 2; ++_i) \
;         __builtin_amdgcn_global_load_lds((const unsigned*)((const char*)(gbase) + (voff)[_i]), (PG8_LAS unsigned*)(lds + (bufoff) + ldsw + _i * 8192), 16, 0, 0); } while (0)
; #define PG8_WAIT_V(n) asm volatile("s_waitcnt vmcnt(" #n ")" ::: "memory")
; #define PG8_WAIT_L(n) asm volatile("s_waitcnt lgkmcnt(" #n ")" ::: "memory")
; #define PG8_BAR __builtin_amdgcn_s_barrier()
; #define PG8_SCHED __builtin_amdgcn_sched_barrier(0)
; template <class Epi, class Sched, bool ALIGN_EPI = true, bool F8 = false>
; __device__ __forceinline__ void gemm_phase(PG8_LAS unsigned char* lds, const Sched& S, const Epi& E) {
;     ...
;             PG8_WAIT_V(8); PG8_WAIT_L(0); PG8_BAR; PG8_MMA(0, 0, At, B0); PG8_MMA(0, 1, At, B1); PG8_BAR; PG8_SCHED;
;             PG8_LDA(At, 0, 1); PG8_STAGE(PG8_SB(0, 0), b2, voffB[0]); PG8_STAGE(PG8_SB(0, 1), b2, voffB[1]); PG8_STAGE(PG8_SA(0, 0), a2, vA2[0]);
;             PG8_WAIT_V(8); PG8_WAIT_L(0); PG8_BAR; PG8_MMA(1, 0, At, B0); PG8_MMA(1, 1, At, B1); PG8_BAR; PG8_SCHED;
;             PG8_LDB(B0, 1, 0); PG8_LDB(B1, 1, 1); PG8_SCHED; PG8_LDA(At, 1, 0); PG8_STAGE(PG8_SA(0, 1), a2, vA2[1]);
;             PG8_WAIT_V(8); PG8_WAIT_L(0); PG8_BAR; PG8_MMA(0, 0, At, B0); PG8_MMA(0, 1, At, B1); PG8_BAR; PG8_SCHED;
	s_setprio 2
	v_mfma_f32_16x16x32_bf16 v[126:129], v[172:175], v[204:207], v[126:129]
	v_mfma_f32_16x16x32_bf16 v[122:125], v[180:183], v[204:207], v[122:125]
	v_mfma_f32_16x16x32_bf16 v[118:121], v[172:175], v[212:215], v[118:121]
	v_mfma_f32_16x16x32_bf16 v[114:117], v[180:183], v[212:215], v[114:117]
	v_mfma_f32_16x16x32_bf16 v[102:105], v[172:175], v[220:223], v[102:105]
	v_mfma_f32_16x16x32_bf16 v[98:101], v[180:183], v[220:223], v[98:101]
	v_mfma_f32_16x16x32_bf16 v[86:89], v[172:175], v[228:231], v[86:89]
	v_mfma_f32_16x16x32_bf16 v[82:85], v[180:183], v[228:231], v[82:85]
	v_mfma_f32_16x16x32_bf16 v[126:129], v[176:179], v[208:211], v[126:129]
	v_mfma_f32_16x16x32_bf16 v[122:125], v[184:187], v[208:211], v[122:125]
	v_mfma_f32_16x16x32_bf16 v[118:121], v[176:179], v[216:219], v[118:121]
	v_mfma_f32_16x16x32_bf16 v[114:117], v[184:187], v[216:219], v[114:117]
	v_mfma_f32_16x16x32_bf16 v[102:105], v[176:179], v[224:227], v[102:105]
	v_mfma_f32_16x16x32_bf16 v[98:101], v[184:187], v[224:227], v[98:101]
	v_mfma_f32_16x16x32_bf16 v[86:89], v[176:179], v[232:235], v[86:89]
	v_mfma_f32_16x16x32_bf16 v[82:85], v[184:187], v[232:235], v[82:85]
	s_setprio 0
	s_setprio 2
	v_mfma_f32_16x16x32_bf16 v[110:113], v[188:191], v[204:207], v[110:113]
	v_mfma_f32_16x16x32_bf16 v[106:109], v[196:199], v[204:207], v[106:109]
	v_mfma_f32_16x16x32_bf16 v[94:97], v[188:191], v[212:215], v[94:97]
	v_mfma_f32_16x16x32_bf16 v[90:93], v[196:199], v[212:215], v[90:93]
	v_mfma_f32_16x16x32_bf16 v[78:81], v[188:191], v[220:223], v[78:81]
	v_mfma_f32_16x16x32_bf16 v[74:77], v[196:199], v[220:223], v[74:77]
	v_mfma_f32_16x16x32_bf16 v[70:73], v[188:191], v[228:231], v[70:73]
	v_mfma_f32_16x16x32_bf16 v[66:69], v[196:199], v[228:231], v[66:69]
	v_mfma_f32_16x16x32_bf16 v[110:113], v[192:195], v[208:211], v[110:113]
	v_mfma_f32_16x16x32_bf16 v[106:109], v[200:203], v[208:211], v[106:109]
	v_mfma_f32_16x16x32_bf16 v[94:97], v[192:195], v[216:219], v[94:97]
	v_mfma_f32_16x16x32_bf16 v[90:93], v[200:203], v[216:219], v[90:93]
	v_mfma_f32_16x16x32_bf16 v[78:81], v[192:195], v[224:227], v[78:81]
	v_mfma_f32_16x16x32_bf16 v[74:77], v[200:203], v[224:227], v[74:77]
	v_mfma_f32_16x16x32_bf16 v[70:73], v[192:195], v[232:235], v[70:73]
	v_mfma_f32_16x16x32_bf16 v[66:69], v[200:203], v[232:235], v[66:69]
	s_setprio 0
	s_mov_b32 m0, s63
	v_lshl_add_u64 v[236:237], s[40:41], 0, v[136:137]
	ds_read_b128 v[204:207], v166 offset:16384
	ds_read_b128 v[208:211], v166 offset:17408
	ds_read_b128 v[212:215], v166 offset:18432
	ds_read_b128 v[216:219], v166 offset:19456
	ds_read_b128 v[220:223], v166 offset:20480
	ds_read_b128 v[224:227], v166 offset:21504
	ds_read_b128 v[228:231], v166 offset:22528
	ds_read_b128 v[232:235], v166 offset:23552
	global_load_lds_dwordx4 v[236:237], off
	v_lshl_add_u64 v[238:239], s[40:41], 0, v[134:135]
	s_mov_b32 m0, s64
	v_lshl_add_u64 v[240:241], s[40:41], 0, v[132:133]
	global_load_lds_dwordx4 v[238:239], off
	s_mov_b32 m0, s65
	v_lshl_add_u64 v[242:243], s[40:41], 0, v[130:131]
	global_load_lds_dwordx4 v[240:241], off
	s_mov_b32 m0, s66
	v_lshl_add_u64 v[244:245], s[42:43], 0, v[138:139]
	global_load_lds_dwordx4 v[242:243], off
	s_mov_b32 m0, s50
	v_lshl_add_u64 v[246:247], s[42:43], 0, v[140:141]
	global_load_lds_dwordx4 v[244:245], off
	s_mov_b32 m0, s51
	s_nop 0
	global_load_lds_dwordx4 v[246:247], off
	s_waitcnt vmcnt(8)
	s_waitcnt lgkmcnt(0)
	s_barrier
	s_setprio 2
	v_mfma_f32_16x16x32_bf16 v[62:65], v[172:175], v[204:207], v[62:65]
	v_mfma_f32_16x16x32_bf16 v[58:61], v[180:183], v[204:207], v[58:61]
	v_mfma_f32_16x16x32_bf16 v[54:57], v[172:175], v[212:215], v[54:57]
	v_mfma_f32_16x16x32_bf16 v[50:53], v[180:183], v[212:215], v[50:53]
	v_mfma_f32_16x16x32_bf16 v[38:41], v[172:175], v[220:223], v[38:41]
	v_mfma_f32_16x16x32_bf16 v[34:37], v[180:183], v[220:223], v[34:37]
	v_mfma_f32_16x16x32_bf16 v[22:25], v[172:175], v[228:231], v[22:25]
	v_mfma_f32_16x16x32_bf16 v[18:21], v[180:183], v[228:231], v[18:21]
	v_mfma_f32_16x16x32_bf16 v[62:65], v[176:179], v[208:211], v[62:65]
	v_mfma_f32_16x16x32_bf16 v[58:61], v[184:187], v[208:211], v[58:61]
	v_mfma_f32_16x16x32_bf16 v[54:57], v[176:179], v[216:219], v[54:57]
	v_mfma_f32_16x16x32_bf16 v[50:53], v[184:187], v[216:219], v[50:53]
	v_mfma_f32_16x16x32_bf16 v[38:41], v[176:179], v[224:227], v[38:41]
	v_mfma_f32_16x16x32_bf16 v[34:37], v[184:187], v[224:227], v[34:37]
	v_mfma_f32_16x16x32_bf16 v[22:25], v[176:179], v[232:235], v[22:25]
	v_mfma_f32_16x16x32_bf16 v[18:21], v[184:187], v[232:235], v[18:21]
	s_setprio 0
	s_setprio 2
	v_mfma_f32_16x16x32_bf16 v[46:49], v[188:191], v[204:207], v[46:49]
	v_mfma_f32_16x16x32_bf16 v[42:45], v[196:199], v[204:207], v[42:45]
	v_mfma_f32_16x16x32_bf16 v[30:33], v[188:191], v[212:215], v[30:33]
	v_mfma_f32_16x16x32_bf16 v[26:29], v[196:199], v[212:215], v[26:29]
	v_mfma_f32_16x16x32_bf16 v[14:17], v[188:191], v[220:223], v[14:17]
	v_mfma_f32_16x16x32_bf16 v[10:13], v[196:199], v[220:223], v[10:13]
	v_mfma_f32_16x16x32_bf16 v[6:9], v[188:191], v[228:231], v[6:9]
	v_mfma_f32_16x16x32_bf16 v[2:5], v[196:199], v[228:231], v[2:5]
	v_mfma_f32_16x16x32_bf16 v[46:49], v[192:195], v[208:211], v[46:49]
	v_mfma_f32_16x16x32_bf16 v[42:45], v[200:203], v[208:211], v[42:45]
	v_mfma_f32_16x16x32_bf16 v[30:33], v[192:195], v[216:219], v[30:33]
	v_mfma_f32_16x16x32_bf16 v[26:29], v[200:203], v[216:219], v[26:29]
	v_mfma_f32_16x16x32_bf16 v[14:17], v[192:195], v[224:227], v[14:17]
	v_mfma_f32_16x16x32_bf16 v[10:13], v[200:203], v[224:227], v[10:13]
	v_mfma_f32_16x16x32_bf16 v[6:9], v[192:195], v[232:235], v[6:9]
	v_mfma_f32_16x16x32_bf16 v[2:5], v[200:203], v[232:235], v[2:5]
	s_setprio 0
	ds_read_b128 v[172:175], v167
	ds_read_b128 v[176:179], v167 offset:1024
	ds_read_b128 v[180:183], v167 offset:2048
	ds_read_b128 v[184:187], v167 offset:3072
	ds_read_b128 v[188:191], v168
	ds_read_b128 v[192:195], v168 offset:1024
	ds_read_b128 v[196:199], v168 offset:2048
	ds_read_b128 v[200:203], v168 offset:3072
	s_mov_b32 m0, s52
	v_lshl_add_u64 v[248:249], s[42:43], 0, v[142:143]
	ds_read_b128 v[204:207], v166 offset:32768
	ds_read_b128 v[208:211], v166 offset:33792
	ds_read_b128 v[212:215], v166 offset:34816
	ds_read_b128 v[216:219], v166 offset:35840
	ds_read_b128 v[220:223], v166 offset:36864
	ds_read_b128 v[224:227], v166 offset:37888
	ds_read_b128 v[228:231], v166 offset:38912
	ds_read_b128 v[232:235], v166 offset:39936
	global_load_lds_dwordx4 v[248:249], off
	v_lshl_add_u64 v[248:249], s[42:43], 0, v[144:145]
	s_mov_b32 m0, s53
	s_nop 0
	global_load_lds_dwordx4 v[248:249], off
	s_waitcnt vmcnt(8)
	s_waitcnt lgkmcnt(0)
	s_barrier
; #define PG8_STAGE(bufoff, gbase, voff) do { _Pragma("unroll") for (int _i = 0; _i < 2; ++_i) \
;         __builtin_amdgcn_global_load_lds((const unsigned*)((const char*)(gbase) + (voff)[_i]), (PG8_LAS unsigned*)(lds + (bufoff) + ldsw + _i * 8192), 16, 0, 0); } while (0)
; #define PG8_WAIT_V(n) asm volatile("s_waitcnt vmcnt(" #n ")" ::: "memory")
; #define PG8_WAIT_L(n) asm volatile("s_waitcnt lgkmcnt(" #n ")" ::: "memory")
; #define PG8_BAR __builtin_amdgcn_s_barrier()
; #define PG8_SCHED __builtin_amdgcn_sched_barrier(0)
; template <class Epi, class Sched, bool ALIGN_EPI = true, bool F8 = false>
; __device__ __forceinline__ void gemm_phase(PG8_LAS unsigned char* lds, const Sched& S, const Epi& E) {
;     ...
;             PG8_LDB(B0, 1, 0); PG8_LDB(B1, 1, 1); PG8_SCHED; PG8_LDA(At, 1, 0); PG8_STAGE(PG8_SA(0, 1), a2, vA2[1]);
;             PG8_WAIT_V(8); PG8_WAIT_L(0); PG8_BAR; PG8_MMA(0, 0, At, B0); PG8_MMA(0, 1, At, B1); PG8_BAR; PG8_SCHED;
;             PG8_LDA(At, 1, 1); PG8_STAGE(PG8_SB(1, 0), b3, voffB[0]); PG8_STAGE(PG8_SB(1, 1), b3, voffB[1]); PG8_STAGE(PG8_SA(1, 0), a3, vA2[0]);
;             PG8_WAIT_V(8); PG8_WAIT_L(0); PG8_BAR; PG8_MMA(1, 0, At, B0); PG8_MMA(1, 1, At, B1); PG8_BAR; PG8_SCHED;
;         }
	s_setprio 2
	v_mfma_f32_16x16x32_bf16 v[126:129], v[172:175], v[204:207], v[126:129]
	v_mfma_f32_16x16x32_bf16 v[122:125], v[180:183], v[204:207], v[122:125]
	v_mfma_f32_16x16x32_bf16 v[118:121], v[172:175], v[212:215], v[118:121]
	v_mfma_f32_16x16x32_bf16 v[114:117], v[180:183], v[212:215], v[114:117]
	v_mfma_f32_16x16x32_bf16 v[102:105], v[172:175], v[220:223], v[102:105]
	v_mfma_f32_16x16x32_bf16 v[98:101], v[180:183], v[220:223], v[98:101]
	v_mfma_f32_16x16x32_bf16 v[86:89], v[172:175], v[228:231], v[86:89]
	v_mfma_f32_16x16x32_bf16 v[82:85], v[180:183], v[228:231], v[82:85]
	v_mfma_f32_16x16x32_bf16 v[126:129], v[176:179], v[208:211], v[126:129]
	v_mfma_f32_16x16x32_bf16 v[122:125], v[184:187], v[208:211], v[122:125]
	v_mfma_f32_16x16x32_bf16 v[118:121], v[176:179], v[216:219], v[118:121]
	v_mfma_f32_16x16x32_bf16 v[114:117], v[184:187], v[216:219], v[114:117]
	v_mfma_f32_16x16x32_bf16 v[102:105], v[176:179], v[224:227], v[102:105]
	v_mfma_f32_16x16x32_bf16 v[98:101], v[184:187], v[224:227], v[98:101]
	v_mfma_f32_16x16x32_bf16 v[86:89], v[176:179], v[232:235], v[86:89]
	v_mfma_f32_16x16x32_bf16 v[82:85], v[184:187], v[232:235], v[82:85]
	s_setprio 0
	s_setprio 2
	v_mfma_f32_16x16x32_bf16 v[110:113], v[188:191], v[204:207], v[110:113]
	v_mfma_f32_16x16x32_bf16 v[106:109], v[196:199], v[204:207], v[106:109]
	v_mfma_f32_16x16x32_bf16 v[94:97], v[188:191], v[212:215], v[94:97]
	v_mfma_f32_16x16x32_bf16 v[90:93], v[196:199], v[212:215], v[90:93]
	v_mfma_f32_16x16x32_bf16 v[78:81], v[188:191], v[220:223], v[78:81]
	v_mfma_f32_16x16x32_bf16 v[74:77], v[196:199], v[220:223], v[74:77]
	v_mfma_f32_16x16x32_bf16 v[70:73], v[188:191], v[228:231], v[70:73]
	v_mfma_f32_16x16x32_bf16 v[66:69], v[196:199], v[228:231], v[66:69]
	v_mfma_f32_16x16x32_bf16 v[110:113], v[192:195], v[208:211], v[110:113]
	v_mfma_f32_16x16x32_bf16 v[106:109], v[200:203], v[208:211], v[106:109]
	v_mfma_f32_16x16x32_bf16 v[94:97], v[192:195], v[216:219], v[94:97]
	v_mfma_f32_16x16x32_bf16 v[90:93], v[200:203], v[216:219], v[90:93]
	v_mfma_f32_16x16x32_bf16 v[78:81], v[192:195], v[224:227], v[78:81]
	v_mfma_f32_16x16x32_bf16 v[74:77], v[200:203], v[224:227], v[74:77]
	v_mfma_f32_16x16x32_bf16 v[70:73], v[192:195], v[232:235], v[70:73]
	v_mfma_f32_16x16x32_bf16 v[66:69], v[200:203], v[232:235], v[66:69]
	s_setprio 0
	s_mov_b32 m0, s67
	v_lshl_add_u64 v[236:237], v[236:237], 0, s[10:11]
	ds_read_b128 v[204:207], v166 offset:49152
	ds_read_b128 v[208:211], v166 offset:50176
	ds_read_b128 v[212:215], v166 offset:51200
	ds_read_b128 v[216:219], v166 offset:52224
	ds_read_b128 v[220:223], v166 offset:53248
	ds_read_b128 v[224:227], v166 offset:54272
	ds_read_b128 v[228:231], v166 offset:55296
	ds_read_b128 v[232:235], v166 offset:56320
	global_load_lds_dwordx4 v[236:237], off
	v_lshl_add_u64 v[236:237], v[238:239], 0, s[10:11]
	s_mov_b32 m0, s68
	s_nop 0
	global_load_lds_dwordx4 v[236:237], off
	v_lshl_add_u64 v[236:237], v[240:241], 0, s[10:11]
	s_mov_b32 m0, s69
	s_nop 0
	global_load_lds_dwordx4 v[236:237], off
	v_lshl_add_u64 v[236:237], v[242:243], 0, s[10:11]
	s_mov_b32 m0, s70
	s_nop 0
	global_load_lds_dwordx4 v[236:237], off
	v_lshl_add_u64 v[236:237], v[244:245], 0, s[10:11]
	s_mov_b32 m0, s59
	s_nop 0
	global_load_lds_dwordx4 v[236:237], off
	v_lshl_add_u64 v[236:237], v[246:247], 0, s[10:11]
	s_mov_b32 m0, s60
	s_nop 0
	global_load_lds_dwordx4 v[236:237], off
	s_waitcnt vmcnt(8)
	s_waitcnt lgkmcnt(0)
	s_barrier
	s_setprio 2
	v_mfma_f32_16x16x32_bf16 v[62:65], v[172:175], v[204:207], v[62:65]
	v_mfma_f32_16x16x32_bf16 v[58:61], v[180:183], v[204:207], v[58:61]
	v_mfma_f32_16x16x32_bf16 v[54:57], v[172:175], v[212:215], v[54:57]
	v_mfma_f32_16x16x32_bf16 v[50:53], v[180:183], v[212:215], v[50:53]
	v_mfma_f32_16x16x32_bf16 v[38:41], v[172:175], v[220:223], v[38:41]
	v_mfma_f32_16x16x32_bf16 v[34:37], v[180:183], v[220:223], v[34:37]
	v_mfma_f32_16x16x32_bf16 v[22:25], v[172:175], v[228:231], v[22:25]
	v_mfma_f32_16x16x32_bf16 v[18:21], v[180:183], v[228:231], v[18:21]
	v_mfma_f32_16x16x32_bf16 v[62:65], v[176:179], v[208:211], v[62:65]
	v_mfma_f32_16x16x32_bf16 v[58:61], v[184:187], v[208:211], v[58:61]
	v_mfma_f32_16x16x32_bf16 v[54:57], v[176:179], v[216:219], v[54:57]
	v_mfma_f32_16x16x32_bf16 v[50:53], v[184:187], v[216:219], v[50:53]
	v_mfma_f32_16x16x32_bf16 v[38:41], v[176:179], v[224:227], v[38:41]
	v_mfma_f32_16x16x32_bf16 v[34:37], v[184:187], v[224:227], v[34:37]
	v_mfma_f32_16x16x32_bf16 v[22:25], v[176:179], v[232:235], v[22:25]
	v_mfma_f32_16x16x32_bf16 v[18:21], v[184:187], v[232:235], v[18:21]
	s_setprio 0
	s_setprio 2
	v_mfma_f32_16x16x32_bf16 v[46:49], v[188:191], v[204:207], v[46:49]
	v_mfma_f32_16x16x32_bf16 v[42:45], v[196:199], v[204:207], v[42:45]
	v_mfma_f32_16x16x32_bf16 v[30:33], v[188:191], v[212:215], v[30:33]
	v_mfma_f32_16x16x32_bf16 v[26:29], v[196:199], v[212:215], v[26:29]
	v_mfma_f32_16x16x32_bf16 v[14:17], v[188:191], v[220:223], v[14:17]
	v_mfma_f32_16x16x32_bf16 v[10:13], v[196:199], v[220:223], v[10:13]
	v_mfma_f32_16x16x32_bf16 v[6:9], v[188:191], v[228:231], v[6:9]
	v_mfma_f32_16x16x32_bf16 v[2:5], v[196:199], v[228:231], v[2:5]
	v_mfma_f32_16x16x32_bf16 v[46:49], v[192:195], v[208:211], v[46:49]
	v_mfma_f32_16x16x32_bf16 v[42:45], v[200:203], v[208:211], v[42:45]
	v_mfma_f32_16x16x32_bf16 v[30:33], v[192:195], v[216:219], v[30:33]
	v_mfma_f32_16x16x32_bf16 v[26:29], v[200:203], v[216:219], v[26:29]
	v_mfma_f32_16x16x32_bf16 v[14:17], v[192:195], v[224:227], v[14:17]
	v_mfma_f32_16x16x32_bf16 v[10:13], v[200:203], v[224:227], v[10:13]
	v_mfma_f32_16x16x32_bf16 v[6:9], v[192:195], v[232:235], v[6:9]
	v_mfma_f32_16x16x32_bf16 v[2:5], v[200:203], v[232:235], v[2:5]
	s_setprio 0
	s_movk_i32 s15, 0x100
	s_andn2_b64 vcc, exec, s[30:31]
	s_mov_b64 s[40:41], -1
	s_mov_b64 s[30:31], 0
	s_cbranch_vccz .Lh1_514

; #define PG8_BAR __builtin_amdgcn_s_barrier()
; template <class Epi, class Sched, bool ALIGN_EPI = true, bool F8 = false>
; __device__ __forceinline__ void gemm_phase(PG8_LAS unsigned char* lds, const Sched& S, const Epi& E) {
;     ...
;         if constexpr (ALIGN_EPI) { if (wr == 0) PG8_BAR; }
;         if constexpr (F8) {
; #pragma unroll
;             for (int a = 0; a < 2; ++a)
; #pragma unroll
;                 for (int b = 0; b < 2; ++b)
;                     asm volatile("s_nop 15\n\ts_nop 7" : "+v"(acc[a][b][0][0]), "+v"(acc[a][b][0][1]), "+v"(acc[a][b][1][0]), "+v"(acc[a][b][1][1]), "+v"(acc[a][b][2][0]), "+v"(acc[a][b][2][1]), "+v"(acc[a][b][3][0]), "+v"(acc[a][b][3][1]));
;         }
;         E(acc, cur, wr, wc, fr, fq);
;         if (!has_next) break;
;         if (!(HasSeg<Epi>::v && cur.x2 == 0)) {
; #pragma unroll
;         for (int a = 0; a < 2; ++a)
; #pragma unroll
;             for (int b = 0; b < 2; ++b)
; #pragma unroll
;                 for (int m = 0; m < 4; ++m)
; #pragma unroll
;                     for (int n = 0; n < 2; ++n) acc[a][b][m][n] = (f32x4){0.f, 0.f, 0.f, 0.f};
;         }
;         cur = nxt; cA = nA; cB = nB; ++ui;
; #pragma unroll
;         for (int h = 0; h < 2; ++h)
; #pragma unroll
;             for (int i = 0; i < 2; ++i) voffA[h][i] = voffAn[h][i];
;         if constexpr (ALIGN_EPI) { if (wr == 1) PG8_BAR; }
;     __device__ __forceinline__ void operator()(AccRef acc, const GUnit& u, int wr, int wc, int fr, int fq) const {
;         const int reim = u.x0, br = u.x1;
; #pragma unroll
;         for (int ai = 0; ai < 2; ++ai)
; #pragma unroll
;             for (int m = 0; m < 4; ++m) { const int kp = ai * 128 + wr * 64 + m * 16 + fr;
;                 st16_bf16(Z1T + ((((size_t)br * 4 + wc) * 256 + kp) * 2 + reim) * 64 + 16 * fq, acc[ai][0][m][0], acc[ai][0][m][1], acc[ai][1][m][0], acc[ai][1][m][1]); }
;     }
.LBB0_517:
	s_ashr_i32 s17, s16, 31
	s_lshl_b64 s[16:17], s[16:17], 10
	s_or_b64 s[16:17], s[16:17], s[0:1]
	v_lshl_add_u64 v[172:173], s[16:17], 0, v[148:149]
	s_ashr_i32 s15, s14, 31
	v_lshlrev_b64 v[172:173], 8, v[172:173]
	v_cvt_pk_bf16_f32 v110, v110, v111
	v_cvt_pk_bf16_f32 v111, v112, v113
	v_cvt_pk_bf16_f32 v112, v106, v107
	v_lshl_add_u64 v[106:107], s[16:17], 0, v[150:151]
	s_lshl_b64 s[14:15], s[14:15], 7
	v_lshl_add_u64 v[172:173], s[8:9], 0, v[172:173]
	v_lshlrev_b64 v[106:107], 8, v[106:107]
	v_cvt_pk_bf16_f32 v94, v94, v95
	v_cvt_pk_bf16_f32 v95, v96, v97
	v_cvt_pk_bf16_f32 v96, v90, v91
	v_lshl_add_u64 v[90:91], s[16:17], 0, v[152:153]
	v_lshl_add_u64 v[172:173], v[172:173], 0, s[14:15]
	v_lshl_add_u64 v[106:107], s[8:9], 0, v[106:107]
	v_lshlrev_b64 v[90:91], 8, v[90:91]
	v_cvt_pk_bf16_f32 v78, v78, v79
	v_cvt_pk_bf16_f32 v79, v80, v81
	v_cvt_pk_bf16_f32 v80, v74, v75
	v_lshl_add_u64 v[74:75], s[16:17], 0, v[154:155]
	v_cvt_pk_bf16_f32 v70, v70, v71
	v_cvt_pk_bf16_f32 v71, v72, v73
	v_cvt_pk_bf16_f32 v72, v66, v67
	v_lshl_add_u64 v[66:67], s[16:17], 0, v[156:157]
	v_lshl_add_u64 v[172:173], v[172:173], 0, v[146:147]
	v_cvt_pk_bf16_f32 v126, v126, v127
	v_cvt_pk_bf16_f32 v127, v128, v129
	v_cvt_pk_bf16_f32 v128, v122, v123
	v_cvt_pk_bf16_f32 v129, v124, v125
	v_lshl_add_u64 v[106:107], v[106:107], 0, s[14:15]
	v_lshl_add_u64 v[90:91], s[8:9], 0, v[90:91]
	v_lshlrev_b64 v[74:75], 8, v[74:75]
	v_lshlrev_b64 v[66:67], 8, v[66:67]
	v_cvt_pk_bf16_f32 v46, v46, v47
	v_cvt_pk_bf16_f32 v47, v48, v49
	v_cvt_pk_bf16_f32 v48, v42, v43
	v_lshl_add_u64 v[42:43], s[16:17], 0, v[158:159]
	v_cvt_pk_bf16_f32 v113, v108, v109
	flat_store_dwordx4 v[172:173], v[126:129]
	flat_store_dwordx4 v[172:173], v[110:113] offset:16
	v_cvt_pk_bf16_f32 v108, v114, v115
	v_cvt_pk_bf16_f32 v109, v116, v117
	v_lshl_add_u64 v[110:111], v[106:107], 0, v[146:147]
	v_cvt_pk_bf16_f32 v106, v118, v119
	v_cvt_pk_bf16_f32 v107, v120, v121
	v_lshl_add_u64 v[90:91], v[90:91], 0, s[14:15]
	v_lshl_add_u64 v[74:75], s[8:9], 0, v[74:75]
	v_lshl_add_u64 v[66:67], s[8:9], 0, v[66:67]
	v_lshlrev_b64 v[42:43], 8, v[42:43]
	v_cvt_pk_bf16_f32 v30, v30, v31
	v_cvt_pk_bf16_f32 v31, v32, v33
	v_cvt_pk_bf16_f32 v32, v26, v27
	v_lshl_add_u64 v[26:27], s[16:17], 0, v[160:161]
	v_cvt_pk_bf16_f32 v97, v92, v93
	flat_store_dwordx4 v[110:111], v[106:109]
	flat_store_dwordx4 v[110:111], v[94:97] offset:16
	v_cvt_pk_bf16_f32 v92, v98, v99
	v_cvt_pk_bf16_f32 v93, v100, v101
	v_lshl_add_u64 v[94:95], v[90:91], 0, v[146:147]
	v_cvt_pk_bf16_f32 v90, v102, v103
	v_cvt_pk_bf16_f32 v91, v104, v105
	v_lshl_add_u64 v[74:75], v[74:75], 0, s[14:15]
	v_lshl_add_u64 v[66:67], v[66:67], 0, s[14:15]
	v_lshl_add_u64 v[42:43], s[8:9], 0, v[42:43]
	v_lshlrev_b64 v[26:27], 8, v[26:27]
	v_cvt_pk_bf16_f32 v14, v14, v15
	v_cvt_pk_bf16_f32 v15, v16, v17
	v_cvt_pk_bf16_f32 v16, v10, v11
	v_lshl_add_u64 v[10:11], s[16:17], 0, v[162:163]
	v_cvt_pk_bf16_f32 v81, v76, v77
	flat_store_dwordx4 v[94:95], v[90:93]
	flat_store_dwordx4 v[94:95], v[78:81] offset:16
	v_cvt_pk_bf16_f32 v76, v82, v83
	v_cvt_pk_bf16_f32 v77, v84, v85
	v_lshl_add_u64 v[78:79], v[74:75], 0, v[146:147]
	v_cvt_pk_bf16_f32 v74, v86, v87
	v_cvt_pk_bf16_f32 v75, v88, v89
	v_lshl_add_u64 v[66:67], v[66:67], 0, v[146:147]
	v_cvt_pk_bf16_f32 v62, v62, v63
	v_cvt_pk_bf16_f32 v63, v64, v65
	v_cvt_pk_bf16_f32 v64, v58, v59
	v_cvt_pk_bf16_f32 v65, v60, v61
	v_lshl_add_u64 v[42:43], v[42:43], 0, s[14:15]
	v_lshl_add_u64 v[26:27], s[8:9], 0, v[26:27]
	v_lshlrev_b64 v[10:11], 8, v[10:11]
	v_cvt_pk_bf16_f32 v73, v68, v69
	flat_store_dwordx4 v[78:79], v[74:77]
	flat_store_dwordx4 v[78:79], v[70:73] offset:16
	v_cvt_pk_bf16_f32 v49, v44, v45
	flat_store_dwordx4 v[66:67], v[62:65]
	flat_store_dwordx4 v[66:67], v[46:49] offset:16
	v_cvt_pk_bf16_f32 v44, v50, v51
	v_cvt_pk_bf16_f32 v45, v52, v53
	v_lshl_add_u64 v[46:47], v[42:43], 0, v[146:147]
	v_cvt_pk_bf16_f32 v42, v54, v55
	v_cvt_pk_bf16_f32 v43, v56, v57
	v_lshl_add_u64 v[26:27], v[26:27], 0, s[14:15]
	v_lshl_add_u64 v[10:11], s[8:9], 0, v[10:11]
	v_cvt_pk_bf16_f32 v33, v28, v29
	flat_store_dwordx4 v[46:47], v[42:45]
	flat_store_dwordx4 v[46:47], v[30:33] offset:16
	v_cvt_pk_bf16_f32 v28, v34, v35
	v_cvt_pk_bf16_f32 v29, v36, v37
	v_lshl_add_u64 v[30:31], v[26:27], 0, v[146:147]
	v_cvt_pk_bf16_f32 v26, v38, v39
	v_cvt_pk_bf16_f32 v27, v40, v41
	v_lshl_add_u64 v[10:11], v[10:11], 0, s[14:15]
	v_cvt_pk_bf16_f32 v17, v12, v13
	flat_store_dwordx4 v[30:31], v[26:29]
	flat_store_dwordx4 v[30:31], v[14:17] offset:16
	v_cvt_pk_bf16_f32 v12, v18, v19
	v_cvt_pk_bf16_f32 v13, v20, v21
	v_lshl_add_u64 v[14:15], v[10:11], 0, v[146:147]
	v_cvt_pk_bf16_f32 v10, v22, v23
	v_cvt_pk_bf16_f32 v11, v24, v25
	s_andn2_b64 vcc, exec, s[28:29]
	s_mov_b64 s[14:15], -1
	v_cvt_pk_bf16_f32 v6, v6, v7
	v_cvt_pk_bf16_f32 v7, v8, v9
	v_cvt_pk_bf16_f32 v8, v2, v3
	v_cvt_pk_bf16_f32 v9, v4, v5
	flat_store_dwordx4 v[14:15], v[10:13]
	flat_store_dwordx4 v[14:15], v[6:9] offset:16
	s_cbranch_vccnz .LBB0_510
	s_andn2_b64 vcc, exec, s[6:7]
	s_cbranch_vccnz .LBB0_509
	s_branch .LBB0_509

; #define PG8_WAIT_V(n) asm volatile("s_waitcnt vmcnt(" #n ")" ::: "memory")
; template <class Epi, class Sched, bool ALIGN_EPI = true, bool F8 = false>
; __device__ __forceinline__ void gemm_phase(PG8_LAS unsigned char* lds, const Sched& S, const Epi& E) {
;     const int tid = threadIdx.x, wid = __builtin_amdgcn_readfirstlane(tid >> 6), lane = tid & 63, wr = wid >> 2, wc = wid & 3, fr = lane & 15, fq = lane >> 4;
;     int Rs[2], Cs[2];
; #pragma unroll
;     for (int i = 0; i < 2; ++i) stage_rc(tid * 16 + i * 8192, Rs[i], Cs[i]);
;     unsigned voffB[2][2], voffA[2][2], voffAn[2][2];
; #pragma unroll
;     for (int h = 0; h < 2; ++h)
; #pragma unroll
;         for (int i = 0; i < 2; ++i) {
;             if constexpr (HasP16<Epi>::v) { const int r = Rs[i]; voffB[h][i] = S.b_off(64 * (r >> 5) + 16 * ((r & 15) >> 2) + 8 * h + 4 * ((r >> 4) & 1) + (r & 3), Cs[i]); }
;             else { const int Rb = Epi::PERM ? ((Rs[i] & ~31) + perm32(Rs[i] & 31)) : Rs[i]; voffB[h][i] = S.b_off(h * HALF + Rb, Cs[i]); } }
;     const size_t kstep = (size_t)SchedKstep<Sched>::v, kstepB = (size_t)SchedKstepB<Sched>::v;
;     const unsigned ldsw = (unsigned)wid * 1024u;
;     const int aoff = lds_byte(wr * 64 + fr, fq * 8), boff = lds_byte(wc * 32 + fr, fq * 8);
;     ...
;     GUnit cur, nxt; int ui = 0;
;     if (!S.next(0, cur)) return;
;     S.a_off(cur, Rs, Cs, voffA);
; #pragma unroll
;     for (int h = 0; h < 2; ++h)
; #pragma unroll
;         for (int i = 0; i < 2; ++i) voffAn[h][i] = voffA[h][i];
;     f32x4 acc[2][2][4][2];
; #pragma unroll
;     for (int a = 0; a < 2; ++a)
; #pragma unroll
;         for (int b = 0; b < 2; ++b)
; #pragma unroll
;             for (int m = 0; m < 4; ++m)
; #pragma unroll
;                 for (int n = 0; n < 2; ++n) acc[a][b][m][n] = (f32x4){0.f, 0.f, 0.f, 0.f};
;     bf16x8 At[4][2], B0[2][2], B1[2][2]; i32x8 At8[4], B08[2], B18[2];
;     const int f8scale = 0x7F7F7F7F;
;     const char* cA = cur.A; const char* cB = cur.B;
;     PG8_STAGE(PG8_SB(0, 0), cB, voffB[0]); PG8_STAGE(PG8_SB(0, 1), cB, voffB[1]); PG8_STAGE(PG8_SA(0, 0), cA, voffA[0]); PG8_STAGE(PG8_SA(0, 1), cA, voffA[1]);
;     if (wr == 1) PG8_BAR;
;     PG8_WAIT_V(2); PG8_BAR;
;     PG8_STAGE(PG8_SB(1, 0), cB + kstepB, voffB[0]); PG8_STAGE(PG8_SA(1, 0), cA + kstep, voffA[0]); PG8_STAGE(PG8_SB(1, 1), cB + kstepB, voffB[1]);
;     PG8_WAIT_V(6); PG8_BAR;
.LBB0_606:
	s_cmpk_gt_i32 s2, 0x7ff
	v_readfirstlane_b32 s16, v0
	s_waitcnt vmcnt(0)
	s_barrier
	s_cbranch_scc1 .LBB0_620
	s_add_u32 s18, s36, 0x1e000000
	s_addc_u32 s19, s37, 0
	s_lshr_b32 s17, s16, 6
	s_lshr_b32 s20, s16, 8
	s_lshl_b32 s15, s17, 10
	v_lshrrev_b32_e32 v3, 3, v0
	s_add_u32 s0, s36, 0x1140000
	v_or_b32_e32 v4, 64, v3
	v_bfe_u32 v6, v0, 2, 4
	s_movk_i32 s6, 0x70
	s_addc_u32 s1, s37, 0
	v_and_or_b32 v4, v4, s6, v6
	s_bfe_u32 s12, s2, 0x20007
	s_and_b32 s6, s2, 0xfffffe00
	s_or_b32 s6, s12, s6
	s_lshl_b32 s8, s2, 1
	v_lshlrev_b32_e32 v2, 4, v0
	v_and_b32_e32 v7, 32, v0
	s_ashr_i32 s7, s6, 31
	s_and_b32 s13, s8, 0xfe
	v_bitop3_b32 v2, v2, v7, 48 bitop3:0x6c
	v_lshrrev_b32_e32 v7, 5, v0
	s_lshl_b32 s8, s13, 8
	s_lshl_b64 s[6:7], s[6:7], 16
	v_lshrrev_b32_e32 v5, 2, v0
	v_and_b32_e32 v7, 4, v7
	s_add_u32 s6, s18, s6
	v_and_b32_e32 v18, 48, v0
	v_and_or_b32 v7, v5, 3, v7
	v_and_b32_e32 v5, 64, v5
	s_addc_u32 s7, s19, s7
	v_or3_b32 v5, v18, v5, v7
	s_add_u32 s6, s6, s8
	v_and_or_b32 v2, v0, 64, v2
	v_lshlrev_b32_e32 v5, 18, v5
	s_addc_u32 s7, s7, 0
	s_add_i32 s21, s15, 0
	v_or_b32_e32 v66, v2, v5
	s_add_i32 m0, s21, 0x10000
	v_or_b32_e32 v68, 0x100, v66
	global_load_lds_dwordx4 v66, s[6:7]
	s_add_i32 m0, s21, 0x12000
	v_or_b32_e32 v72, 0x200000, v66
	global_load_lds_dwordx4 v68, s[6:7]
	s_add_i32 m0, s21, 0x14000
	v_or_b32_e32 v70, 0x200100, v66
	v_and_or_b32 v3, v3, 48, v6
	global_load_lds_dwordx4 v72, s[6:7]
	s_add_i32 m0, s21, 0x16000
	v_lshl_or_b32 v8, v3, 8, v2
	global_load_lds_dwordx4 v70, s[6:7]
	s_mov_b32 m0, s21
	s_add_i32 s22, s21, 0x2000
	v_lshl_or_b32 v6, v4, 8, v2
	global_load_lds_dwordx4 v8, s[0:1]
	s_mov_b32 m0, s22
	s_add_i32 s23, s21, 0x4000
	v_or_b32_e32 v4, 0x8000, v8
	global_load_lds_dwordx4 v6, s[0:1]
	s_mov_b32 m0, s23
	s_add_i32 s24, s21, 0x6000
	v_or_b32_e32 v2, 0x8000, v6
	global_load_lds_dwordx4 v4, s[0:1]
	s_mov_b32 m0, s24
	v_mov_b32_e32 v67, 0
	global_load_lds_dwordx4 v2, s[0:1]
	v_mov_b32_e32 v69, v67
	v_mov_b32_e32 v73, v67
	v_mov_b32_e32 v71, v67
	s_cmp_eq_u32 s20, 1
	v_lshl_add_u64 v[16:17], s[6:7], 0, v[66:67]
	v_lshl_add_u64 v[14:15], s[6:7], 0, v[68:69]
	v_lshl_add_u64 v[12:13], s[6:7], 0, v[72:73]
	v_lshl_add_u64 v[10:11], s[6:7], 0, v[70:71]
	v_mov_b32_e32 v9, v67
	v_mov_b32_e32 v7, v67
	v_mov_b32_e32 v5, v67
	s_cselect_b64 s[8:9], -1, 0
	s_cmp_lg_u32 s20, 1
	v_mov_b32_e32 v3, v67
	s_cbranch_scc1 .LBB0_609
.LBB0_609:
	s_and_b32 s10, s17, 3
	s_lshl_b32 s30, s10, 12
	s_mov_b64 s[10:11], 0x80
	s_add_i32 m0, s21, 0x18000
	v_lshl_add_u64 v[16:17], v[16:17], 0, s[10:11]
	s_ashr_i32 s14, s2, 9
	s_lshl_b32 s27, s20, 13
	s_waitcnt vmcnt(2)
	s_barrier
	global_load_lds_dwordx4 v[16:17], off
	s_add_i32 m0, s21, 0x1a000
	s_add_u32 s28, s36, 0x1140080
	v_lshl_add_u64 v[14:15], v[14:15], 0, s[10:11]
	s_addc_u32 s29, s37, 0
	s_add_i32 s25, s21, 0x8000
	global_load_lds_dwordx4 v[14:15], off
	v_lshl_add_u64 v[74:75], s[28:29], 0, v[8:9]
	s_mov_b32 m0, s25
	s_add_i32 s26, s21, 0xa000
	global_load_lds_dwordx4 v[74:75], off
	v_lshl_add_u64 v[76:77], s[28:29], 0, v[6:7]
	s_mov_b32 m0, s26
	v_lshl_add_u64 v[12:13], v[12:13], 0, s[10:11]
	global_load_lds_dwordx4 v[76:77], off
	s_add_i32 m0, s21, 0x1c000
	v_lshl_add_u64 v[10:11], v[10:11], 0, s[10:11]
	global_load_lds_dwordx4 v[12:13], off
	s_add_i32 m0, s21, 0x1e000
	v_lshl_add_u64 v[78:79], s[0:1], 0, v[8:9]
	global_load_lds_dwordx4 v[10:11], off
	v_lshl_add_u64 v[80:81], s[0:1], 0, v[6:7]
	v_and_b32_e32 v6, 15, v0
	v_lshlrev_b32_e32 v8, 2, v0
	v_lshl_or_b32 v7, v6, 6, v18
	v_and_b32_e32 v8, 32, v8
	v_lshl_add_u64 v[82:83], s[0:1], 0, v[4:5]
	v_lshl_add_u64 v[84:85], s[0:1], 0, v[2:3]
	v_bitop3_b32 v9, s27, v7, v8 bitop3:0xf6
	v_lshlrev_b32_e32 v7, 6, v0
	s_movk_i32 s0, 0x3c0
	s_cmpk_lt_u32 s16, 0x100
	v_and_or_b32 v7, v7, s0, v18
	s_cselect_b64 s[0:1], -1, 0
	s_lshl_b32 s16, s17, 6
	v_bitop3_b32 v8, s30, v7, v8 bitop3:0xf6
	v_and_or_b32 v7, s16, 64, v18
	s_waitcnt vmcnt(6)
	v_lshlrev_b32_e32 v86, 1, v6
	v_lshlrev_b32_e32 v6, 1, v7
	v_mov_b32_e32 v7, v67
	s_add_i32 s41, 0, 0x10000
	s_add_i32 s43, 0, 0x14000
	s_add_i32 s45, 0, 0x18000
	s_add_i32 s47, 0, 0x1c000
	s_bfe_u32 s27, s17, 0x10001
	v_lshl_add_u64 v[6:7], s[36:37], 0, v[6:7]
	s_mov_b64 s[16:17], 0x26000000
	v_lshl_add_u64 v[96:97], s[28:29], 0, v[4:5]
	v_lshl_add_u64 v[98:99], s[28:29], 0, v[2:3]
	s_add_i32 s28, s2, s33
	v_add_u32_e32 v100, s41, v8
	v_add_u32_e32 v101, s43, v8
	s_add_i32 s41, s41, s15
	s_add_i32 s43, s43, s15
	v_add_u32_e32 v103, s45, v8
	v_add_u32_e32 v104, s47, v8
	s_add_i32 s45, s45, s15
	s_add_i32 s47, s47, s15
	v_cndmask_b32_e64 v2, 0, 1, s[0:1]
	v_mov_b32_e32 v87, v67
	v_lshl_add_u64 v[88:89], v[6:7], 0, s[16:17]
	v_or_b32_e32 v90, 32, v86
	v_mov_b32_e32 v91, v67
	v_or_b32_e32 v92, 64, v86
	v_mov_b32_e32 v93, v67
	v_or_b32_e32 v94, 0x60, v86
	v_mov_b32_e32 v95, v67
	s_lshl_b32 s29, s28, 1
	s_lshl_b32 s30, s33, 1
	v_add_u32_e32 v102, 0, v9
	s_add_i32 s31, s21, 0xc000
	s_add_i32 s40, s21, 0xe000
	s_add_i32 s42, s41, 0x2000
	s_add_i32 s44, s43, 0x2000
	s_add_i32 s46, s45, 0x2000
	s_add_i32 s48, s47, 0x2000
	v_cmp_ne_u32_e64 s[0:1], 1, v2
	s_barrier
	s_branch .LBB0_612

; #define PG8_STAGE(bufoff, gbase, voff) do { _Pragma("unroll") for (int _i = 0; _i < 2; ++_i) \
;         __builtin_amdgcn_global_load_lds((const unsigned*)((const char*)(gbase) + (voff)[_i]), (PG8_LAS unsigned*)(lds + (bufoff) + ldsw + _i * 8192), 16, 0, 0); } while (0)
; #define PG8_WAIT_V(n) asm volatile("s_waitcnt vmcnt(" #n ")" ::: "memory")
; #define PG8_WAIT_L(n) asm volatile("s_waitcnt lgkmcnt(" #n ")" ::: "memory")
; #define PG8_BAR __builtin_amdgcn_s_barrier()
; #define PG8_SCHED __builtin_amdgcn_sched_barrier(0)
; template <class Epi, class Sched, bool ALIGN_EPI = true, bool F8 = false>
; __device__ __forceinline__ void gemm_phase(PG8_LAS unsigned char* lds, const Sched& S, const Epi& E) {
;     ...
;             PG8_LDB(B0, 0, 0); PG8_LDB(B1, 0, 1); PG8_SCHED; PG8_LDA(At, 0, 0); PG8_STAGE(PG8_SA(1, 1), a1, voffA[1]);
;             PG8_WAIT_V(8); PG8_WAIT_L(0); PG8_BAR; PG8_MMA(0, 0, At, B0); PG8_MMA(0, 1, At, B1); PG8_BAR; PG8_SCHED;
;             PG8_LDA(At, 0, 1); PG8_STAGE(PG8_SB(0, 0), b2, voffB[0]); PG8_STAGE(PG8_SB(0, 1), b2, voffB[1]); PG8_STAGE(PG8_SA(0, 0), a2, vA2[0]);
;             PG8_WAIT_V(8); PG8_WAIT_L(0); PG8_BAR; PG8_MMA(1, 0, At, B0); PG8_MMA(1, 1, At, B1); PG8_BAR; PG8_SCHED;
;             PG8_LDB(B0, 1, 0); PG8_LDB(B1, 1, 1); PG8_SCHED; PG8_LDA(At, 1, 0); PG8_STAGE(PG8_SA(0, 1), a2, vA2[1]);
;             PG8_WAIT_V(8); PG8_WAIT_L(0); PG8_BAR; PG8_MMA(0, 0, At, B0); PG8_MMA(0, 1, At, B1); PG8_BAR; PG8_SCHED;
.LBB0_614:
	s_bitcmp1_b32 s3, 2
	s_cbranch_scc1 .Lh1e_16296
	ds_read_b128 v[2:5], v100
	ds_read_b128 v[6:9], v100 offset:1024
	ds_read_b128 v[10:13], v100 offset:2048
	ds_read_b128 v[14:17], v100 offset:3072
	ds_read_b128 v[18:21], v101
	ds_read_b128 v[22:25], v101 offset:1024
	ds_read_b128 v[26:29], v101 offset:2048
	ds_read_b128 v[30:33], v101 offset:3072
	s_mov_b32 m0, s31
	ds_read_b128 v[34:37], v102
	ds_read_b128 v[38:41], v102 offset:1024
	ds_read_b128 v[42:45], v102 offset:2048
	ds_read_b128 v[46:49], v102 offset:3072
	ds_read_b128 v[50:53], v102 offset:4096
	ds_read_b128 v[54:57], v102 offset:5120
	ds_read_b128 v[58:61], v102 offset:6144
	ds_read_b128 v[62:65], v102 offset:7168
	global_load_lds_dwordx4 v[96:97], off
	s_mov_b32 m0, s40
	s_nop 0
	global_load_lds_dwordx4 v[98:99], off
	s_waitcnt vmcnt(8)
	s_waitcnt lgkmcnt(0)
	s_setprio 1
	v_mfma_f32_16x16x32_bf16 v[106:109], v[2:5], v[34:37], 0
	v_mfma_f32_16x16x32_bf16 v[114:117], v[2:5], v[42:45], 0
	v_mfma_f32_16x16x32_bf16 v[122:125], v[2:5], v[50:53], 0
	v_mfma_f32_16x16x32_bf16 v[2:5], v[2:5], v[58:61], 0
	v_mfma_f32_16x16x32_bf16 v[106:109], v[6:9], v[38:41], v[106:109]
	v_mfma_f32_16x16x32_bf16 v[114:117], v[6:9], v[46:49], v[114:117]
	v_mfma_f32_16x16x32_bf16 v[122:125], v[6:9], v[54:57], v[122:125]
	v_mfma_f32_16x16x32_bf16 v[2:5], v[6:9], v[62:65], v[2:5]
	v_mfma_f32_16x16x32_bf16 v[6:9], v[10:13], v[58:61], 0
	v_mfma_f32_16x16x32_bf16 v[110:113], v[10:13], v[34:37], 0
	v_mfma_f32_16x16x32_bf16 v[118:121], v[10:13], v[42:45], 0
	v_mfma_f32_16x16x32_bf16 v[126:129], v[10:13], v[50:53], 0
	v_mfma_f32_16x16x32_bf16 v[6:9], v[14:17], v[62:65], v[6:9]
	v_mfma_f32_16x16x32_bf16 v[110:113], v[14:17], v[38:41], v[110:113]
	v_mfma_f32_16x16x32_bf16 v[118:121], v[14:17], v[46:49], v[118:121]
	v_mfma_f32_16x16x32_bf16 v[126:129], v[14:17], v[54:57], v[126:129]
	s_setprio 0
	s_setprio 1
	v_mfma_f32_16x16x32_bf16 v[10:13], v[18:21], v[34:37], 0
	v_mfma_f32_16x16x32_bf16 v[14:17], v[26:29], v[34:37], 0
	v_mfma_f32_16x16x32_bf16 v[34:37], v[18:21], v[42:45], 0
	v_mfma_f32_16x16x32_bf16 v[130:133], v[22:25], v[46:49], v[34:37]
	v_mfma_f32_16x16x32_bf16 v[34:37], v[26:29], v[42:45], 0
	v_mfma_f32_16x16x32_bf16 v[46:49], v[30:33], v[46:49], v[34:37]
	v_mfma_f32_16x16x32_bf16 v[34:37], v[18:21], v[50:53], 0
	v_mfma_f32_16x16x32_bf16 v[18:21], v[18:21], v[58:61], 0
	v_mfma_f32_16x16x32_bf16 v[10:13], v[22:25], v[38:41], v[10:13]
	v_mfma_f32_16x16x32_bf16 v[14:17], v[30:33], v[38:41], v[14:17]
	v_mfma_f32_16x16x32_bf16 v[134:137], v[22:25], v[54:57], v[34:37]
	v_mfma_f32_16x16x32_bf16 v[34:37], v[26:29], v[50:53], 0
	v_mfma_f32_16x16x32_bf16 v[142:145], v[22:25], v[62:65], v[18:21]
	v_mfma_f32_16x16x32_bf16 v[18:21], v[26:29], v[58:61], 0
	v_mfma_f32_16x16x32_bf16 v[138:141], v[30:33], v[54:57], v[34:37]
	v_mfma_f32_16x16x32_bf16 v[146:149], v[30:33], v[62:65], v[18:21]
	s_setprio 0
	s_barrier
	s_mov_b32 m0, s41
	v_lshl_add_u64 v[196:197], s[6:7], 0, v[66:67]
	global_load_lds_dwordx4 v[196:197], off
	v_lshl_add_u64 v[198:199], s[6:7], 0, v[68:69]
	s_mov_b32 m0, s42
	v_lshl_add_u64 v[200:201], s[6:7], 0, v[72:73]
	global_load_lds_dwordx4 v[198:199], off
	s_mov_b32 m0, s43
	v_lshl_add_u64 v[202:203], s[6:7], 0, v[70:71]
	global_load_lds_dwordx4 v[200:201], off
	s_mov_b32 m0, s44
	s_nop 0
	global_load_lds_dwordx4 v[202:203], off
	s_mov_b32 m0, s21
	s_nop 0
	global_load_lds_dwordx4 v[78:79], off
	s_mov_b32 m0, s22
	s_nop 0
	global_load_lds_dwordx4 v[80:81], off
	s_waitcnt vmcnt(8)
	s_waitcnt lgkmcnt(0)
	s_setprio 1
	s_setprio 0
	s_setprio 1
	s_setprio 0
	s_barrier
	ds_read_b128 v[26:29], v103
	ds_read_b128 v[30:33], v103 offset:1024
	ds_read_b128 v[42:45], v103 offset:2048
	ds_read_b128 v[58:61], v103 offset:3072
	ds_read_b128 v[150:153], v104
	ds_read_b128 v[154:157], v104 offset:1024
	ds_read_b128 v[158:161], v104 offset:2048
	ds_read_b128 v[162:165], v104 offset:3072
	s_mov_b32 m0, s23
	ds_read_b128 v[62:65], v102 offset:32768
	ds_read_b128 v[166:169], v102 offset:33792
	ds_read_b128 v[172:175], v102 offset:34816
	ds_read_b128 v[176:179], v102 offset:35840
	ds_read_b128 v[180:183], v102 offset:36864
	ds_read_b128 v[184:187], v102 offset:37888
	ds_read_b128 v[188:191], v102 offset:38912
	ds_read_b128 v[192:195], v102 offset:39936
	global_load_lds_dwordx4 v[82:83], off
	s_mov_b32 m0, s24
	s_nop 0
	global_load_lds_dwordx4 v[84:85], off
	s_waitcnt vmcnt(8)
	s_waitcnt lgkmcnt(0)
	s_setprio 1
	v_mfma_f32_16x16x32_bf16 v[18:21], v[26:29], v[62:65], v[106:109]
	v_mfma_f32_16x16x32_bf16 v[50:53], v[30:33], v[166:169], v[18:21]
	v_mfma_f32_16x16x32_bf16 v[18:21], v[42:45], v[62:65], v[110:113]
	v_mfma_f32_16x16x32_bf16 v[54:57], v[58:61], v[166:169], v[18:21]
	v_mfma_f32_16x16x32_bf16 v[18:21], v[26:29], v[172:175], v[114:117]
	v_mfma_f32_16x16x32_bf16 v[34:37], v[30:33], v[176:179], v[18:21]
	v_mfma_f32_16x16x32_bf16 v[18:21], v[42:45], v[172:175], v[118:121]
	v_mfma_f32_16x16x32_bf16 v[38:41], v[58:61], v[176:179], v[18:21]
	v_mfma_f32_16x16x32_bf16 v[18:21], v[26:29], v[180:183], v[122:125]
	v_mfma_f32_16x16x32_bf16 v[22:25], v[42:45], v[180:183], v[126:129]
	v_mfma_f32_16x16x32_bf16 v[2:5], v[26:29], v[188:191], v[2:5]
	v_mfma_f32_16x16x32_bf16 v[6:9], v[42:45], v[188:191], v[6:9]
	v_mfma_f32_16x16x32_bf16 v[18:21], v[30:33], v[184:187], v[18:21]
	v_mfma_f32_16x16x32_bf16 v[22:25], v[58:61], v[184:187], v[22:25]
	v_mfma_f32_16x16x32_bf16 v[2:5], v[30:33], v[192:195], v[2:5]
	v_mfma_f32_16x16x32_bf16 v[6:9], v[58:61], v[192:195], v[6:9]
	s_setprio 0
	s_setprio 1
	v_mfma_f32_16x16x32_bf16 v[10:13], v[150:153], v[62:65], v[10:13]
	v_mfma_f32_16x16x32_bf16 v[58:61], v[154:157], v[166:169], v[10:13]
	v_mfma_f32_16x16x32_bf16 v[10:13], v[158:161], v[62:65], v[14:17]
	v_mfma_f32_16x16x32_bf16 v[62:65], v[162:165], v[166:169], v[10:13]
	v_mfma_f32_16x16x32_bf16 v[10:13], v[150:153], v[172:175], v[130:133]
	v_mfma_f32_16x16x32_bf16 v[42:45], v[154:157], v[176:179], v[10:13]
	v_mfma_f32_16x16x32_bf16 v[10:13], v[158:161], v[172:175], v[46:49]
	v_mfma_f32_16x16x32_bf16 v[46:49], v[162:165], v[176:179], v[10:13]
	v_mfma_f32_16x16x32_bf16 v[10:13], v[150:153], v[180:183], v[134:137]
	v_mfma_f32_16x16x32_bf16 v[26:29], v[154:157], v[184:187], v[10:13]
	v_mfma_f32_16x16x32_bf16 v[10:13], v[158:161], v[180:183], v[138:141]
	v_mfma_f32_16x16x32_bf16 v[30:33], v[162:165], v[184:187], v[10:13]
	v_mfma_f32_16x16x32_bf16 v[10:13], v[150:153], v[188:191], v[142:145]
	v_mfma_f32_16x16x32_bf16 v[14:17], v[158:161], v[188:191], v[146:149]
	v_mfma_f32_16x16x32_bf16 v[10:13], v[154:157], v[192:195], v[10:13]
	v_mfma_f32_16x16x32_bf16 v[14:17], v[162:165], v[192:195], v[14:17]
	s_setprio 0
	s_barrier
; #define PG8_STAGE(bufoff, gbase, voff) do { _Pragma("unroll") for (int _i = 0; _i < 2; ++_i) \
;         __builtin_amdgcn_global_load_lds((const unsigned*)((const char*)(gbase) + (voff)[_i]), (PG8_LAS unsigned*)(lds + (bufoff) + ldsw + _i * 8192), 16, 0, 0); } while (0)
; #define PG8_WAIT_V(n) asm volatile("s_waitcnt vmcnt(" #n ")" ::: "memory")
; #define PG8_WAIT_L(n) asm volatile("s_waitcnt lgkmcnt(" #n ")" ::: "memory")
; #define PG8_BAR __builtin_amdgcn_s_barrier()
; #define PG8_SCHED __builtin_amdgcn_sched_barrier(0)
; template <class Epi, class Sched, bool ALIGN_EPI = true, bool F8 = false>
; __device__ __forceinline__ void gemm_phase(PG8_LAS unsigned char* lds, const Sched& S, const Epi& E) {
;     ...
;             PG8_LDB(B0, 0, 0); PG8_LDB(B1, 0, 1); PG8_SCHED; PG8_LDA(At, 0, 0); PG8_STAGE(PG8_SA(1, 1), a1, voffA[1]);
;             PG8_WAIT_V(8); PG8_WAIT_L(0); PG8_BAR; PG8_MMA(0, 0, At, B0); PG8_MMA(0, 1, At, B1); PG8_BAR; PG8_SCHED;
;             PG8_LDA(At, 0, 1); PG8_STAGE(PG8_SB(0, 0), b2, voffB[0]); PG8_STAGE(PG8_SB(0, 1), b2, voffB[1]); PG8_STAGE(PG8_SA(0, 0), a2, vA2[0]);
;             PG8_WAIT_V(8); PG8_WAIT_L(0); PG8_BAR; PG8_MMA(1, 0, At, B0); PG8_MMA(1, 1, At, B1); PG8_BAR; PG8_SCHED;
;     ...
;             PG8_LDA(At, 1, 1); PG8_STAGE(PG8_SB(1, 0), b3, voffB[0]); PG8_STAGE(PG8_SB(1, 1), b3, voffB[1]); PG8_STAGE(PG8_SA(1, 0), a3, vA2[0]);
;             PG8_WAIT_V(8); PG8_WAIT_L(0); PG8_BAR; PG8_MMA(1, 0, At, B0); PG8_MMA(1, 1, At, B1); PG8_BAR; PG8_SCHED;
	s_mov_b32 m0, s45
	v_lshl_add_u64 v[106:107], v[196:197], 0, s[10:11]
	global_load_lds_dwordx4 v[106:107], off
	v_lshl_add_u64 v[106:107], v[198:199], 0, s[10:11]
	s_mov_b32 m0, s46
	s_nop 0
	global_load_lds_dwordx4 v[106:107], off
	v_lshl_add_u64 v[106:107], v[200:201], 0, s[10:11]
	s_mov_b32 m0, s47
	s_nop 0
	global_load_lds_dwordx4 v[106:107], off
	v_lshl_add_u64 v[106:107], v[202:203], 0, s[10:11]
	s_mov_b32 m0, s48
	s_nop 0
	global_load_lds_dwordx4 v[106:107], off
	s_mov_b32 m0, s25
	s_nop 0
	global_load_lds_dwordx4 v[74:75], off
	s_mov_b32 m0, s26
	s_nop 0
	global_load_lds_dwordx4 v[76:77], off
	s_waitcnt vmcnt(8)
	s_waitcnt lgkmcnt(0)
	s_setprio 1
	s_setprio 0
	s_setprio 1
	s_setprio 0
	s_barrier
	s_branch .Lfx_16296
.Lh1e_16296:
	ds_read_b128 v[2:5], v100
	ds_read_b128 v[6:9], v100 offset:1024
	ds_read_b128 v[10:13], v100 offset:2048
	ds_read_b128 v[14:17], v100 offset:3072
	ds_read_b128 v[18:21], v101
	ds_read_b128 v[22:25], v101 offset:1024
	ds_read_b128 v[26:29], v101 offset:2048
	ds_read_b128 v[30:33], v101 offset:3072
	s_mov_b32 m0, s31
	ds_read_b128 v[34:37], v102
	ds_read_b128 v[38:41], v102 offset:1024
	ds_read_b128 v[42:45], v102 offset:2048
	ds_read_b128 v[46:49], v102 offset:3072
	ds_read_b128 v[50:53], v102 offset:4096
	ds_read_b128 v[54:57], v102 offset:5120
	ds_read_b128 v[58:61], v102 offset:6144
	ds_read_b128 v[62:65], v102 offset:7168
	global_load_lds_dwordx4 v[96:97], off
	s_mov_b32 m0, s40
	s_nop 0
	global_load_lds_dwordx4 v[98:99], off
	s_waitcnt vmcnt(8)
	s_waitcnt lgkmcnt(0)
	s_barrier
	s_setprio 2
	v_mfma_f32_16x16x32_bf16 v[106:109], v[2:5], v[34:37], 0
	v_mfma_f32_16x16x32_bf16 v[114:117], v[2:5], v[42:45], 0
	v_mfma_f32_16x16x32_bf16 v[122:125], v[2:5], v[50:53], 0
	v_mfma_f32_16x16x32_bf16 v[2:5], v[2:5], v[58:61], 0
	v_mfma_f32_16x16x32_bf16 v[106:109], v[6:9], v[38:41], v[106:109]
	v_mfma_f32_16x16x32_bf16 v[114:117], v[6:9], v[46:49], v[114:117]
	v_mfma_f32_16x16x32_bf16 v[122:125], v[6:9], v[54:57], v[122:125]
	v_mfma_f32_16x16x32_bf16 v[2:5], v[6:9], v[62:65], v[2:5]
	v_mfma_f32_16x16x32_bf16 v[6:9], v[10:13], v[58:61], 0
	v_mfma_f32_16x16x32_bf16 v[110:113], v[10:13], v[34:37], 0
	v_mfma_f32_16x16x32_bf16 v[118:121], v[10:13], v[42:45], 0
	v_mfma_f32_16x16x32_bf16 v[126:129], v[10:13], v[50:53], 0
	v_mfma_f32_16x16x32_bf16 v[6:9], v[14:17], v[62:65], v[6:9]
	v_mfma_f32_16x16x32_bf16 v[110:113], v[14:17], v[38:41], v[110:113]
	v_mfma_f32_16x16x32_bf16 v[118:121], v[14:17], v[46:49], v[118:121]
	v_mfma_f32_16x16x32_bf16 v[126:129], v[14:17], v[54:57], v[126:129]
	s_setprio 0
	s_setprio 2
	v_mfma_f32_16x16x32_bf16 v[10:13], v[18:21], v[34:37], 0
	v_mfma_f32_16x16x32_bf16 v[14:17], v[26:29], v[34:37], 0
	v_mfma_f32_16x16x32_bf16 v[34:37], v[18:21], v[42:45], 0
	v_mfma_f32_16x16x32_bf16 v[130:133], v[22:25], v[46:49], v[34:37]
	v_mfma_f32_16x16x32_bf16 v[34:37], v[26:29], v[42:45], 0
	v_mfma_f32_16x16x32_bf16 v[46:49], v[30:33], v[46:49], v[34:37]
	v_mfma_f32_16x16x32_bf16 v[34:37], v[18:21], v[50:53], 0
	v_mfma_f32_16x16x32_bf16 v[18:21], v[18:21], v[58:61], 0
	v_mfma_f32_16x16x32_bf16 v[10:13], v[22:25], v[38:41], v[10:13]
	v_mfma_f32_16x16x32_bf16 v[14:17], v[30:33], v[38:41], v[14:17]
	v_mfma_f32_16x16x32_bf16 v[134:137], v[22:25], v[54:57], v[34:37]
	v_mfma_f32_16x16x32_bf16 v[34:37], v[26:29], v[50:53], 0
	v_mfma_f32_16x16x32_bf16 v[142:145], v[22:25], v[62:65], v[18:21]
	v_mfma_f32_16x16x32_bf16 v[18:21], v[26:29], v[58:61], 0
	v_mfma_f32_16x16x32_bf16 v[138:141], v[30:33], v[54:57], v[34:37]
	v_mfma_f32_16x16x32_bf16 v[146:149], v[30:33], v[62:65], v[18:21]
	s_setprio 0
	s_mov_b32 m0, s41
	v_lshl_add_u64 v[196:197], s[6:7], 0, v[66:67]
	global_load_lds_dwordx4 v[196:197], off
	v_lshl_add_u64 v[198:199], s[6:7], 0, v[68:69]
	s_mov_b32 m0, s42
	v_lshl_add_u64 v[200:201], s[6:7], 0, v[72:73]
	global_load_lds_dwordx4 v[198:199], off
	s_mov_b32 m0, s43
	v_lshl_add_u64 v[202:203], s[6:7], 0, v[70:71]
	global_load_lds_dwordx4 v[200:201], off
	s_mov_b32 m0, s44
	s_nop 0
	global_load_lds_dwordx4 v[202:203], off
	s_mov_b32 m0, s21
	s_nop 0
	global_load_lds_dwordx4 v[78:79], off
	s_mov_b32 m0, s22
	s_nop 0
	global_load_lds_dwordx4 v[80:81], off
	s_waitcnt vmcnt(8)
	s_waitcnt lgkmcnt(0)
	s_barrier
	s_setprio 2
	s_setprio 0
	s_setprio 2
	s_setprio 0
	ds_read_b128 v[26:29], v103
	ds_read_b128 v[30:33], v103 offset:1024
	ds_read_b128 v[42:45], v103 offset:2048
	ds_read_b128 v[58:61], v103 offset:3072
	ds_read_b128 v[150:153], v104
	ds_read_b128 v[154:157], v104 offset:1024
	ds_read_b128 v[158:161], v104 offset:2048
	ds_read_b128 v[162:165], v104 offset:3072
	s_mov_b32 m0, s23
	ds_read_b128 v[62:65], v102 offset:32768
	ds_read_b128 v[166:169], v102 offset:33792
	ds_read_b128 v[172:175], v102 offset:34816
	ds_read_b128 v[176:179], v102 offset:35840
	ds_read_b128 v[180:183], v102 offset:36864
	ds_read_b128 v[184:187], v102 offset:37888
	ds_read_b128 v[188:191], v102 offset:38912
	ds_read_b128 v[192:195], v102 offset:39936
	global_load_lds_dwordx4 v[82:83], off
	s_mov_b32 m0, s24
	s_nop 0
	global_load_lds_dwordx4 v[84:85], off
	s_waitcnt vmcnt(8)
	s_waitcnt lgkmcnt(0)
	s_barrier
; #define PG8_STAGE(bufoff, gbase, voff) do { _Pragma("unroll") for (int _i = 0; _i < 2; ++_i) \
;         __builtin_amdgcn_global_load_lds((const unsigned*)((const char*)(gbase) + (voff)[_i]), (PG8_LAS unsigned*)(lds + (bufoff) + ldsw + _i * 8192), 16, 0, 0); } while (0)
; #define PG8_WAIT_V(n) asm volatile("s_waitcnt vmcnt(" #n ")" ::: "memory")
; #define PG8_WAIT_L(n) asm volatile("s_waitcnt lgkmcnt(" #n ")" ::: "memory")
; #define PG8_BAR __builtin_amdgcn_s_barrier()
; #define PG8_SCHED __builtin_amdgcn_sched_barrier(0)
; template <class Epi, class Sched, bool ALIGN_EPI = true, bool F8 = false>
; __device__ __forceinline__ void gemm_phase(PG8_LAS unsigned char* lds, const Sched& S, const Epi& E) {
;     ...
;             PG8_LDA(At, 1, 1); PG8_STAGE(PG8_SB(1, 0), b3, voffB[0]); PG8_STAGE(PG8_SB(1, 1), b3, voffB[1]); PG8_STAGE(PG8_SA(1, 0), a3, vA2[0]);
;             PG8_WAIT_V(8); PG8_WAIT_L(0); PG8_BAR; PG8_MMA(1, 0, At, B0); PG8_MMA(1, 1, At, B1); PG8_BAR; PG8_SCHED;
;     __device__ __forceinline__ void operator()(AccRef acc, const GUnit& u, int wr, int wc, int fr, int fq) const {
;         const int b = u.x0, g = u.x1, k0 = u.x2; const int kp = k0 + (wc >> 1), r0 = (wc & 1) * 64 + 16 * fq;
; #pragma unroll
;         for (int m = 0; m < 4; ++m) { const int mm = wr * 64 + m * 16 + fr, reim = mm >> 6, cp = mm & 63;
;             st16_bf16(Z2T + (((((size_t)b * 4 + g) * 256 + kp) * 64 + cp) * 2 + reim) * 128 + r0, acc[0][0][m][0], acc[0][0][m][1], acc[0][1][m][0], acc[0][1][m][1]); }
;     }
	s_setprio 2
	v_mfma_f32_16x16x32_bf16 v[18:21], v[26:29], v[62:65], v[106:109]
	v_mfma_f32_16x16x32_bf16 v[50:53], v[30:33], v[166:169], v[18:21]
	v_mfma_f32_16x16x32_bf16 v[18:21], v[42:45], v[62:65], v[110:113]
	v_mfma_f32_16x16x32_bf16 v[54:57], v[58:61], v[166:169], v[18:21]
	v_mfma_f32_16x16x32_bf16 v[18:21], v[26:29], v[172:175], v[114:117]
	v_mfma_f32_16x16x32_bf16 v[34:37], v[30:33], v[176:179], v[18:21]
	v_mfma_f32_16x16x32_bf16 v[18:21], v[42:45], v[172:175], v[118:121]
	v_mfma_f32_16x16x32_bf16 v[38:41], v[58:61], v[176:179], v[18:21]
	v_mfma_f32_16x16x32_bf16 v[18:21], v[26:29], v[180:183], v[122:125]
	v_mfma_f32_16x16x32_bf16 v[22:25], v[42:45], v[180:183], v[126:129]
	v_mfma_f32_16x16x32_bf16 v[2:5], v[26:29], v[188:191], v[2:5]
	v_mfma_f32_16x16x32_bf16 v[6:9], v[42:45], v[188:191], v[6:9]
	v_mfma_f32_16x16x32_bf16 v[18:21], v[30:33], v[184:187], v[18:21]
	v_mfma_f32_16x16x32_bf16 v[22:25], v[58:61], v[184:187], v[22:25]
	v_mfma_f32_16x16x32_bf16 v[2:5], v[30:33], v[192:195], v[2:5]
	v_mfma_f32_16x16x32_bf16 v[6:9], v[58:61], v[192:195], v[6:9]
	s_setprio 0
	s_setprio 2
	v_mfma_f32_16x16x32_bf16 v[10:13], v[150:153], v[62:65], v[10:13]
	v_mfma_f32_16x16x32_bf16 v[58:61], v[154:157], v[166:169], v[10:13]
	v_mfma_f32_16x16x32_bf16 v[10:13], v[158:161], v[62:65], v[14:17]
	v_mfma_f32_16x16x32_bf16 v[62:65], v[162:165], v[166:169], v[10:13]
	v_mfma_f32_16x16x32_bf16 v[10:13], v[150:153], v[172:175], v[130:133]
	v_mfma_f32_16x16x32_bf16 v[42:45], v[154:157], v[176:179], v[10:13]
	v_mfma_f32_16x16x32_bf16 v[10:13], v[158:161], v[172:175], v[46:49]
	v_mfma_f32_16x16x32_bf16 v[46:49], v[162:165], v[176:179], v[10:13]
	v_mfma_f32_16x16x32_bf16 v[10:13], v[150:153], v[180:183], v[134:137]
	v_mfma_f32_16x16x32_bf16 v[26:29], v[154:157], v[184:187], v[10:13]
	v_mfma_f32_16x16x32_bf16 v[10:13], v[158:161], v[180:183], v[138:141]
	v_mfma_f32_16x16x32_bf16 v[30:33], v[162:165], v[184:187], v[10:13]
	v_mfma_f32_16x16x32_bf16 v[10:13], v[150:153], v[188:191], v[142:145]
	v_mfma_f32_16x16x32_bf16 v[14:17], v[158:161], v[188:191], v[146:149]
	v_mfma_f32_16x16x32_bf16 v[10:13], v[154:157], v[192:195], v[10:13]
	v_mfma_f32_16x16x32_bf16 v[14:17], v[162:165], v[192:195], v[14:17]
	s_setprio 0
	s_mov_b32 m0, s45
	v_lshl_add_u64 v[106:107], v[196:197], 0, s[10:11]
	global_load_lds_dwordx4 v[106:107], off
	v_lshl_add_u64 v[106:107], v[198:199], 0, s[10:11]
	s_mov_b32 m0, s46
	s_nop 0
	global_load_lds_dwordx4 v[106:107], off
	v_lshl_add_u64 v[106:107], v[200:201], 0, s[10:11]
	s_mov_b32 m0, s47
	s_nop 0
	global_load_lds_dwordx4 v[106:107], off
	v_lshl_add_u64 v[106:107], v[202:203], 0, s[10:11]
	s_mov_b32 m0, s48
	s_nop 0
	global_load_lds_dwordx4 v[106:107], off
	s_mov_b32 m0, s25
	s_nop 0
	global_load_lds_dwordx4 v[74:75], off
	s_mov_b32 m0, s26
	s_nop 0
	global_load_lds_dwordx4 v[76:77], off
	s_waitcnt vmcnt(8)
	s_waitcnt lgkmcnt(0)
	s_barrier
	s_setprio 2
	s_setprio 0
	s_setprio 2
	s_setprio 0
.Lfx_16296:
	s_and_b64 vcc, exec, s[0:1]
	s_cbranch_vccnz .LBB0_616
.LBB0_616:
	s_add_i32 s52, s13, s27
	s_ashr_i32 s15, s14, 31
	s_ashr_i32 s13, s12, 31
	s_lshl_b64 s[14:15], s[14:15], 10
	s_lshl_b64 s[12:13], s[12:13], 8
	s_add_u32 s12, s12, s14
	s_addc_u32 s13, s13, s15
	s_ashr_i32 s14, s52, 31
	s_add_u32 s12, s12, s52
	s_addc_u32 s13, s13, s14
	s_lshl_b64 s[12:13], s[12:13], 7
	s_add_u32 s12, s12, s20
	s_addc_u32 s13, s13, 0
	v_lshl_add_u64 v[106:107], s[12:13], 0, v[86:87]
	v_lshlrev_b64 v[106:107], 8, v[106:107]
	v_lshl_add_u64 v[106:107], v[88:89], 0, v[106:107]
	v_cvt_pk_bf16_f32 v50, v50, v51
	v_cvt_pk_bf16_f32 v51, v52, v53
	v_cvt_pk_bf16_f32 v52, v54, v55
	v_cvt_pk_bf16_f32 v53, v56, v57
	v_cvt_pk_bf16_f32 v54, v58, v59
	v_cvt_pk_bf16_f32 v55, v60, v61
	v_cvt_pk_bf16_f32 v56, v62, v63
	v_cvt_pk_bf16_f32 v57, v64, v65
	flat_store_dwordx4 v[106:107], v[50:53]
	flat_store_dwordx4 v[106:107], v[54:57] offset:16
	v_cvt_pk_bf16_f32 v34, v34, v35
	v_lshl_add_u64 v[50:51], s[12:13], 0, v[90:91]
	v_lshlrev_b64 v[50:51], 8, v[50:51]
	v_lshl_add_u64 v[50:51], v[88:89], 0, v[50:51]
	v_cvt_pk_bf16_f32 v35, v36, v37
	v_cvt_pk_bf16_f32 v36, v38, v39
	v_cvt_pk_bf16_f32 v37, v40, v41
	v_cvt_pk_bf16_f32 v38, v42, v43
	v_cvt_pk_bf16_f32 v39, v44, v45
	v_cvt_pk_bf16_f32 v40, v46, v47
	v_cvt_pk_bf16_f32 v41, v48, v49
	flat_store_dwordx4 v[50:51], v[34:37]
	flat_store_dwordx4 v[50:51], v[38:41] offset:16
	v_cvt_pk_bf16_f32 v18, v18, v19
	v_lshl_add_u64 v[34:35], s[12:13], 0, v[92:93]
	v_lshlrev_b64 v[34:35], 8, v[34:35]
	v_lshl_add_u64 v[34:35], v[88:89], 0, v[34:35]
	v_cvt_pk_bf16_f32 v19, v20, v21
	v_cvt_pk_bf16_f32 v20, v22, v23
	v_cvt_pk_bf16_f32 v21, v24, v25
	v_cvt_pk_bf16_f32 v22, v26, v27
	v_cvt_pk_bf16_f32 v23, v28, v29
	v_cvt_pk_bf16_f32 v24, v30, v31
	v_cvt_pk_bf16_f32 v25, v32, v33
	flat_store_dwordx4 v[34:35], v[18:21]
	flat_store_dwordx4 v[34:35], v[22:25] offset:16
	v_cvt_pk_bf16_f32 v2, v2, v3
	v_lshl_add_u64 v[18:19], s[12:13], 0, v[94:95]
	v_lshlrev_b64 v[18:19], 8, v[18:19]
	v_lshl_add_u64 v[18:19], v[88:89], 0, v[18:19]
	v_cvt_pk_bf16_f32 v3, v4, v5
	v_cvt_pk_bf16_f32 v4, v6, v7
	v_cvt_pk_bf16_f32 v5, v8, v9
	s_andn2_b64 vcc, exec, s[16:17]
	s_mov_b64 s[12:13], -1
	v_cvt_pk_bf16_f32 v6, v10, v11
	v_cvt_pk_bf16_f32 v7, v12, v13
	v_cvt_pk_bf16_f32 v8, v14, v15
	v_cvt_pk_bf16_f32 v9, v16, v17
	flat_store_dwordx4 v[18:19], v[2:5]
	flat_store_dwordx4 v[18:19], v[6:9] offset:16
	s_cbranch_vccnz .LBB0_611
	s_andn2_b64 vcc, exec, s[8:9]
	s_cbranch_vccnz .LBB0_610
	s_branch .LBB0_610

; #define PG8_WAIT_V(n) asm volatile("s_waitcnt vmcnt(" #n ")" ::: "memory")
; template <class Epi, class Sched, bool ALIGN_EPI = true, bool F8 = false>
; __device__ __forceinline__ void gemm_phase(PG8_LAS unsigned char* lds, const Sched& S, const Epi& E) {
;     const int tid = threadIdx.x, wid = __builtin_amdgcn_readfirstlane(tid >> 6), lane = tid & 63, wr = wid >> 2, wc = wid & 3, fr = lane & 15, fq = lane >> 4;
;     int Rs[2], Cs[2];
; #pragma unroll
;     for (int i = 0; i < 2; ++i) stage_rc(tid * 16 + i * 8192, Rs[i], Cs[i]);
;     unsigned voffB[2][2], voffA[2][2], voffAn[2][2];
; #pragma unroll
;     for (int h = 0; h < 2; ++h)
; #pragma unroll
;         for (int i = 0; i < 2; ++i) {
;             if constexpr (HasP16<Epi>::v) { const int r = Rs[i]; voffB[h][i] = S.b_off(64 * (r >> 5) + 16 * ((r & 15) >> 2) + 8 * h + 4 * ((r >> 4) & 1) + (r & 3), Cs[i]); }
;             else { const int Rb = Epi::PERM ? ((Rs[i] & ~31) + perm32(Rs[i] & 31)) : Rs[i]; voffB[h][i] = S.b_off(h * HALF + Rb, Cs[i]); } }
;     const size_t kstep = (size_t)SchedKstep<Sched>::v, kstepB = (size_t)SchedKstepB<Sched>::v;
;     const unsigned ldsw = (unsigned)wid * 1024u;
;     const int aoff = lds_byte(wr * 64 + fr, fq * 8), boff = lds_byte(wc * 32 + fr, fq * 8);
;     ...
;     GUnit cur, nxt; int ui = 0;
;     if (!S.next(0, cur)) return;
;     S.a_off(cur, Rs, Cs, voffA);
; #pragma unroll
;     for (int h = 0; h < 2; ++h)
; #pragma unroll
;         for (int i = 0; i < 2; ++i) voffAn[h][i] = voffA[h][i];
;     f32x4 acc[2][2][4][2];
; #pragma unroll
;     for (int a = 0; a < 2; ++a)
; #pragma unroll
;         for (int b = 0; b < 2; ++b)
; #pragma unroll
;             for (int m = 0; m < 4; ++m)
; #pragma unroll
;                 for (int n = 0; n < 2; ++n) acc[a][b][m][n] = (f32x4){0.f, 0.f, 0.f, 0.f};
;     bf16x8 At[4][2], B0[2][2], B1[2][2]; i32x8 At8[4], B08[2], B18[2];
;     const int f8scale = 0x7F7F7F7F;
;     const char* cA = cur.A; const char* cB = cur.B;
;     PG8_STAGE(PG8_SB(0, 0), cB, voffB[0]); PG8_STAGE(PG8_SB(0, 1), cB, voffB[1]); PG8_STAGE(PG8_SA(0, 0), cA, voffA[0]); PG8_STAGE(PG8_SA(0, 1), cA, voffA[1]);
;     if (wr == 1) PG8_BAR;
;     PG8_WAIT_V(2); PG8_BAR;
;     PG8_STAGE(PG8_SB(1, 0), cB + kstepB, voffB[0]); PG8_STAGE(PG8_SA(1, 0), cA + kstep, voffA[0]); PG8_STAGE(PG8_SB(1, 1), cB + kstepB, voffB[1]);
;     PG8_WAIT_V(6); PG8_BAR;
.LBB0_666:
	s_cmp_lt_i32 s34, 7
	s_cselect_b64 s[0:1], -1, 0
	s_and_b64 s[4:5], s[0:1], s[40:41]
	s_andn2_b64 vcc, exec, s[4:5]
	s_cbranch_vccnz .LBB0_699
	v_lshlrev_b32_e32 v2, 2, v0
	v_and_b32_e32 v16, 32, v2
	v_lshlrev_b32_e32 v2, 6, v0
	v_and_b32_e32 v168, 48, v0
	v_and_b32_e32 v169, 0x3c0, v2
	v_readfirstlane_b32 s10, v0
	s_cmpk_gt_i32 s2, 0xff
	v_bitop3_b32 v172, v169, v16, v168 bitop3:0x36
	s_cbranch_scc1 .LBB0_683
	v_lshlrev_b32_e32 v2, 4, v0
	v_or_b32_e32 v3, 0x2000, v2
	v_lshrrev_b32_e32 v4, 7, v3
	v_lshrrev_b32_e32 v3, 6, v3
	v_lshrrev_b32_e32 v5, 5, v0
	v_lshrrev_b32_e32 v6, 2, v0
	s_movk_i32 s4, 0xc0
	v_and_b32_e32 v8, 32, v0
	v_and_b32_e32 v5, 4, v5
	v_bfe_u32 v7, v0, 2, 2
	v_and_or_b32 v3, v3, s4, v168
	v_bitop3_b32 v14, v2, v8, 48 bitop3:0x6c
	v_and_b32_e32 v15, 64, v0
	v_and_or_b32 v6, v6, 64, v168
	s_add_u32 s26, s36, 0x32000000
	v_or3_b32 v3, v3, v5, v7
	v_or_b32_e32 v2, v14, v15
	v_or3_b32 v5, v6, v5, v7
	s_addc_u32 s27, s37, 0
	v_lshrrev_b32_e32 v2, 1, v2
	v_mul_u32_u24_e32 v5, 0x300, v5
	s_add_u32 s28, s36, 0x4500000
	v_or_b32_e32 v5, v5, v2
	s_addc_u32 s29, s37, 0
	v_lshlrev_b32_e32 v134, 1, v5
	v_bfe_u32 v5, v0, 2, 4
	s_movk_i32 s4, 0x70
	s_ashr_i32 s62, s2, 3
	v_and_or_b32 v4, v4, s4, v5
	s_bfe_u32 s18, s2, 0x20001
	s_lshl_b32 s4, s62, 2
	s_or_b32 s4, s4, s18
	s_mulk_i32 s4, 0x108
	s_lshr_b32 s11, s10, 6
	s_add_i32 s4, s4, 8
	s_lshr_b32 s13, s10, 8
	s_lshl_b32 s12, s11, 10
	s_and_b32 s19, s2, 1
	s_mul_hi_i32 s5, s4, 0x600
	s_mulk_i32 s4, 0x600
	s_add_u32 s20, s26, s4
	s_addc_u32 s21, s27, s5
	s_lshl_b32 s4, s62, 9
	s_lshl_b32 s5, s19, 8
	s_or_b32 s4, s4, s5
	s_mul_hi_i32 s5, s4, 0x600
	s_mulk_i32 s4, 0x600
	v_mul_u32_u24_e32 v3, 0x300, v3
	s_add_u32 s22, s28, s4
	v_or_b32_e32 v3, v3, v2
	s_addc_u32 s23, s29, s5
	s_add_i32 s30, s12, 0
	v_lshlrev_b32_e32 v130, 1, v3
	v_lshrrev_b32_e32 v3, 3, v0
	s_add_i32 m0, s30, 0x10000
	v_and_or_b32 v3, v3, 48, v5
	global_load_lds_dwordx4 v134, s[22:23]
	s_add_i32 m0, s30, 0x12000
	v_add_u32_e32 v136, 0x3000, v134
	v_mul_u32_u24_e32 v17, 0x300, v3
	global_load_lds_dwordx4 v130, s[22:23]
	s_add_i32 m0, s30, 0x14000
	v_add_u32_e32 v132, 0x3000, v130
	v_or_b32_e32 v3, v2, v17
	v_mul_u32_u24_e32 v18, 0x300, v4
	global_load_lds_dwordx4 v136, s[22:23]
	s_add_i32 m0, s30, 0x16000
	v_lshlrev_b32_e32 v138, 1, v3
	v_or_b32_e32 v2, v18, v2
	global_load_lds_dwordx4 v132, s[22:23]
	s_mov_b32 m0, s30
	s_add_i32 s31, s30, 0x2000
	v_lshlrev_b32_e32 v140, 1, v2
	global_load_lds_dwordx4 v138, s[20:21]
	s_mov_b32 m0, s31
	s_add_i32 s40, s30, 0x4000
	v_add_u32_e32 v142, 0x30000, v138
	global_load_lds_dwordx4 v140, s[20:21]
	s_mov_b32 m0, s40
	s_add_i32 s41, s30, 0x6000
	v_add_u32_e32 v144, 0x30000, v140
	global_load_lds_dwordx4 v142, s[20:21]
	s_mov_b32 m0, s41
	v_mov_b32_e32 v135, 0
	global_load_lds_dwordx4 v144, s[20:21]
	v_mov_b32_e32 v131, v135
	v_mov_b32_e32 v137, v135
	v_mov_b32_e32 v133, v135
	v_mov_b32_e32 v139, v135
	v_mov_b32_e32 v141, v135
	s_cmp_eq_u32 s13, 1
	s_mov_b32 s42, 0
	v_lshl_add_u64 v[8:9], s[22:23], 0, v[134:135]
	v_lshl_add_u64 v[6:7], s[22:23], 0, v[130:131]
	v_lshl_add_u64 v[4:5], s[22:23], 0, v[136:137]
	v_lshl_add_u64 v[2:3], s[22:23], 0, v[132:133]
	v_lshl_add_u64 v[10:11], s[20:21], 0, v[138:139]
	s_cselect_b64 s[4:5], -1, 0
	s_cmp_lg_u32 s13, 1
	v_lshl_add_u64 v[12:13], s[20:21], 0, v[140:141]
	s_cbranch_scc1 .LBB0_670
.LBB0_670:
	s_add_u32 s6, s36, 0x37400000
	s_mov_b64 s[8:9], 0x80
	s_addc_u32 s7, s37, 0
	s_add_i32 m0, s30, 0x18000
	v_lshl_add_u64 v[8:9], v[8:9], 0, s[8:9]
	s_waitcnt vmcnt(2)
	s_barrier
	global_load_lds_dwordx4 v[8:9], off
	v_lshl_add_u64 v[6:7], v[6:7], 0, s[8:9]
	s_add_i32 m0, s30, 0x1a000
	s_add_i32 s43, s30, 0x8000
	global_load_lds_dwordx4 v[6:7], off
	v_lshl_add_u64 v[6:7], v[10:11], 0, s[8:9]
	s_mov_b32 m0, s43
	s_add_i32 s44, s30, 0xa000
	global_load_lds_dwordx4 v[6:7], off
	v_lshl_add_u64 v[6:7], v[12:13], 0, s[8:9]
	s_mov_b32 m0, s44
	v_lshl_add_u64 v[4:5], v[4:5], 0, s[8:9]
	global_load_lds_dwordx4 v[6:7], off
	s_add_i32 m0, s30, 0x1c000
	v_lshl_add_u64 v[2:3], v[2:3], 0, s[8:9]
	global_load_lds_dwordx4 v[4:5], off
	s_add_i32 m0, s30, 0x1e000
	s_and_b32 s14, s11, 3
	global_load_lds_dwordx4 v[2:3], off
	v_and_b32_e32 v2, 15, v0
	v_lshl_or_b32 v3, v2, 6, v168
	v_lshlrev_b32_e32 v2, 5, v2
	v_lshl_or_b32 v146, s13, 11, v2
	v_add_u16_e32 v2, v14, v15
	v_lshrrev_b16_e32 v6, 1, v2
	s_lshl_b32 s11, s13, 13
	v_add_u32_e32 v2, v18, v6
	v_mov_b32_e32 v7, 0x30000
	v_bitop3_b32 v4, s11, v3, v16 bitop3:0xf6
	s_cmpk_lt_u32 s10, 0x100
	v_lshl_add_u32 v2, v2, 1, v7
	v_mov_b32_e32 v3, v135
	v_lshl_or_b32 v5, s14, 12, v172
	s_waitcnt vmcnt(6)
	s_cselect_b64 s[10:11], -1, 0
	v_lshl_add_u64 v[162:163], v[2:3], 0, s[8:9]
	v_add_u32_e32 v2, v17, v6
	s_add_i32 s47, 0, 0x10000
	s_add_i32 s49, 0, 0x14000
	s_add_i32 s51, 0, 0x18000
	s_add_i32 s53, 0, 0x1c000
	v_or_b32_e32 v148, 0x200, v146
	v_or_b32_e32 v150, 0x400, v146
	v_or_b32_e32 v152, 0x600, v146
	v_add_u32_e32 v154, 0x1000, v146
	v_add_u32_e32 v156, 0x1200, v146
	v_add_u32_e32 v158, 0x1400, v146
	v_add_u32_e32 v160, 0x1600, v146
	v_lshl_add_u32 v2, v2, 1, v7
	v_add_u32_e32 v174, s47, v5
	v_add_u32_e32 v175, s49, v5
	s_add_i32 s47, s47, s12
	s_add_i32 s49, s49, s12
	v_add_u32_e32 v177, s51, v5
	v_add_u32_e32 v178, s53, v5
	s_add_i32 s51, s51, s12
	s_add_i32 s53, s53, s12
	v_mov_b32_e32 v143, v135
	v_mov_b32_e32 v145, v135
	v_ashrrev_i32_e32 v147, 31, v146
	v_ashrrev_i32_e32 v149, 31, v148
	v_ashrrev_i32_e32 v151, 31, v150
	v_ashrrev_i32_e32 v153, 31, v152
	v_ashrrev_i32_e32 v155, 31, v154
	v_ashrrev_i32_e32 v157, 31, v156
	v_ashrrev_i32_e32 v159, 31, v158
	v_ashrrev_i32_e32 v161, 31, v160
	v_lshl_or_b32 v173, s14, 6, v168
	v_lshl_add_u64 v[164:165], v[2:3], 0, s[8:9]
	v_add_u32_e32 v176, 0, v4
	s_add_i32 s45, s30, 0xc000
	s_add_i32 s46, s30, 0xe000
	s_add_i32 s48, s47, 0x2000
	s_add_i32 s50, s49, 0x2000
	s_add_i32 s52, s51, 0x2000
	s_add_i32 s58, s53, 0x2000
	s_mov_b64 s[14:15], s[22:23]
	s_mov_b64 s[12:13], s[20:21]
	s_barrier
	s_branch .LBB0_673

; #define PG8_STAGE(bufoff, gbase, voff) do { _Pragma("unroll") for (int _i = 0; _i < 2; ++_i) \
;         __builtin_amdgcn_global_load_lds((const unsigned*)((const char*)(gbase) + (voff)[_i]), (PG8_LAS unsigned*)(lds + (bufoff) + ldsw + _i * 8192), 16, 0, 0); } while (0)
; #define PG8_WAIT_V(n) asm volatile("s_waitcnt vmcnt(" #n ")" ::: "memory")
; #define PG8_WAIT_L(n) asm volatile("s_waitcnt lgkmcnt(" #n ")" ::: "memory")
; #define PG8_BAR __builtin_amdgcn_s_barrier()
; #define PG8_SCHED __builtin_amdgcn_sched_barrier(0)
; template <class Epi, class Sched, bool ALIGN_EPI = true, bool F8 = false>
; __device__ __forceinline__ void gemm_phase(PG8_LAS unsigned char* lds, const Sched& S, const Epi& E) {
;     ...
;     f32x4 acc[2][2][4][2];
; #pragma unroll
;     for (int a = 0; a < 2; ++a)
; #pragma unroll
;         for (int b = 0; b < 2; ++b)
; #pragma unroll
;             for (int m = 0; m < 4; ++m)
; #pragma unroll
;                 for (int n = 0; n < 2; ++n) acc[a][b][m][n] = (f32x4){0.f, 0.f, 0.f, 0.f};
;     ...
;             PG8_LDB(B0, 0, 0); PG8_LDB(B1, 0, 1); PG8_SCHED; PG8_LDA(At, 0, 0); PG8_STAGE(PG8_SA(1, 1), a1, voffA[1]);
;             PG8_WAIT_V(8); PG8_WAIT_L(0); PG8_BAR; PG8_MMA(0, 0, At, B0); PG8_MMA(0, 1, At, B1); PG8_BAR; PG8_SCHED;
.LBB0_675:
	s_add_u32 s63, s22, 0x100
	v_mov_b32_e32 v2, 0
	s_addc_u32 s64, s23, 0
	s_mov_b32 s65, -2
	v_mov_b32_e32 v3, v2
	v_mov_b32_e32 v4, v2
	v_mov_b32_e32 v5, v2
	v_mov_b32_e32 v6, v2
	v_mov_b32_e32 v7, v2
	v_mov_b32_e32 v8, v2
	v_mov_b32_e32 v9, v2
	v_mov_b32_e32 v18, v2
	v_mov_b32_e32 v19, v2
	v_mov_b32_e32 v20, v2
	v_mov_b32_e32 v21, v2
	v_mov_b32_e32 v22, v2
	v_mov_b32_e32 v23, v2
	v_mov_b32_e32 v24, v2
	v_mov_b32_e32 v25, v2
	v_mov_b32_e32 v34, v2
	v_mov_b32_e32 v35, v2
	v_mov_b32_e32 v36, v2
	v_mov_b32_e32 v37, v2
	v_mov_b32_e32 v38, v2
	v_mov_b32_e32 v39, v2
	v_mov_b32_e32 v40, v2
	v_mov_b32_e32 v41, v2
	v_mov_b32_e32 v50, v2
	v_mov_b32_e32 v51, v2
	v_mov_b32_e32 v52, v2
	v_mov_b32_e32 v53, v2
	v_mov_b32_e32 v54, v2
	v_mov_b32_e32 v55, v2
	v_mov_b32_e32 v56, v2
	v_mov_b32_e32 v57, v2
	v_mov_b32_e32 v10, v2
	v_mov_b32_e32 v11, v2
	v_mov_b32_e32 v12, v2
	v_mov_b32_e32 v13, v2
	v_mov_b32_e32 v14, v2
	v_mov_b32_e32 v15, v2
	v_mov_b32_e32 v16, v2
	v_mov_b32_e32 v17, v2
	v_mov_b32_e32 v26, v2
	v_mov_b32_e32 v27, v2
	v_mov_b32_e32 v28, v2
	v_mov_b32_e32 v29, v2
	v_mov_b32_e32 v30, v2
	v_mov_b32_e32 v31, v2
	v_mov_b32_e32 v32, v2
	v_mov_b32_e32 v33, v2
	v_mov_b32_e32 v42, v2
	v_mov_b32_e32 v43, v2
	v_mov_b32_e32 v44, v2
	v_mov_b32_e32 v45, v2
	v_mov_b32_e32 v46, v2
	v_mov_b32_e32 v47, v2
	v_mov_b32_e32 v48, v2
	v_mov_b32_e32 v49, v2
	v_mov_b32_e32 v58, v2
	v_mov_b32_e32 v59, v2
	v_mov_b32_e32 v60, v2
	v_mov_b32_e32 v61, v2
	v_mov_b32_e32 v62, v2
	v_mov_b32_e32 v63, v2
	v_mov_b32_e32 v64, v2
	v_mov_b32_e32 v65, v2
	v_mov_b32_e32 v66, v2
	v_mov_b32_e32 v67, v2
	v_mov_b32_e32 v68, v2
	v_mov_b32_e32 v69, v2
	v_mov_b32_e32 v70, v2
	v_mov_b32_e32 v71, v2
	v_mov_b32_e32 v72, v2
	v_mov_b32_e32 v73, v2
	v_mov_b32_e32 v82, v2
	v_mov_b32_e32 v83, v2
	v_mov_b32_e32 v84, v2
	v_mov_b32_e32 v85, v2
	v_mov_b32_e32 v86, v2
	v_mov_b32_e32 v87, v2
	v_mov_b32_e32 v88, v2
	v_mov_b32_e32 v89, v2
	v_mov_b32_e32 v98, v2
	v_mov_b32_e32 v99, v2
	v_mov_b32_e32 v100, v2
	v_mov_b32_e32 v101, v2
	v_mov_b32_e32 v102, v2
	v_mov_b32_e32 v103, v2
	v_mov_b32_e32 v104, v2
	v_mov_b32_e32 v105, v2
	v_mov_b32_e32 v114, v2
	v_mov_b32_e32 v115, v2
	v_mov_b32_e32 v116, v2
	v_mov_b32_e32 v117, v2
	v_mov_b32_e32 v118, v2
	v_mov_b32_e32 v119, v2
	v_mov_b32_e32 v120, v2
	v_mov_b32_e32 v121, v2
	v_mov_b32_e32 v74, v2
	v_mov_b32_e32 v75, v2
	v_mov_b32_e32 v76, v2
	v_mov_b32_e32 v77, v2
	v_mov_b32_e32 v78, v2
	v_mov_b32_e32 v79, v2
	v_mov_b32_e32 v80, v2
	v_mov_b32_e32 v81, v2
	v_mov_b32_e32 v90, v2
	v_mov_b32_e32 v91, v2
	v_mov_b32_e32 v92, v2
	v_mov_b32_e32 v93, v2
	v_mov_b32_e32 v94, v2
	v_mov_b32_e32 v95, v2
	v_mov_b32_e32 v96, v2
	v_mov_b32_e32 v97, v2
	v_mov_b32_e32 v106, v2
	v_mov_b32_e32 v107, v2
	v_mov_b32_e32 v108, v2
	v_mov_b32_e32 v109, v2
	v_mov_b32_e32 v110, v2
	v_mov_b32_e32 v111, v2
	v_mov_b32_e32 v112, v2
	v_mov_b32_e32 v113, v2
	v_mov_b32_e32 v122, v2
	v_mov_b32_e32 v123, v2
	v_mov_b32_e32 v124, v2
	v_mov_b32_e32 v125, v2
	v_mov_b32_e32 v126, v2
	v_mov_b32_e32 v127, v2
	v_mov_b32_e32 v128, v2
	v_mov_b32_e32 v129, v2
	s_bitcmp1_b32 s3, 2
	s_cbranch_scc1 .Lh1e_17518
.LBB0_676:
	ds_read_b128 v[180:183], v174
	ds_read_b128 v[184:187], v174 offset:1024
	ds_read_b128 v[188:191], v174 offset:2048
	ds_read_b128 v[192:195], v174 offset:3072
	ds_read_b128 v[196:199], v175
	ds_read_b128 v[200:203], v175 offset:1024
	ds_read_b128 v[204:207], v175 offset:2048
	ds_read_b128 v[208:211], v175 offset:3072
	s_add_u32 s22, s20, 0x100
	s_addc_u32 s23, s21, 0
	s_cmp_eq_u32 s65, 8
	s_cselect_b32 s25, s13, s23
	s_cselect_b32 s24, s12, s22
	s_cselect_b32 s67, s15, s64
	s_cselect_b32 s66, s14, s63
	s_mov_b32 m0, s45
	v_lshl_add_u64 v[166:167], s[20:21], 0, v[164:165]
	ds_read_b128 v[212:215], v176
	ds_read_b128 v[216:219], v176 offset:1024
	ds_read_b128 v[220:223], v176 offset:2048
	ds_read_b128 v[224:227], v176 offset:3072
	ds_read_b128 v[228:231], v176 offset:4096
	ds_read_b128 v[232:235], v176 offset:5120
	ds_read_b128 v[236:239], v176 offset:6144
	ds_read_b128 v[240:243], v176 offset:7168
	global_load_lds_dwordx4 v[166:167], off
	v_lshl_add_u64 v[166:167], s[20:21], 0, v[162:163]
	s_mov_b32 m0, s46
	s_nop 0
	global_load_lds_dwordx4 v[166:167], off
	s_waitcnt vmcnt(8)
	s_waitcnt lgkmcnt(0)
	s_setprio 1
	v_mfma_f32_16x16x32_bf16 v[126:129], v[180:183], v[212:215], v[126:129]
	v_mfma_f32_16x16x32_bf16 v[122:125], v[188:191], v[212:215], v[122:125]
	v_mfma_f32_16x16x32_bf16 v[110:113], v[180:183], v[220:223], v[110:113]
	v_mfma_f32_16x16x32_bf16 v[106:109], v[188:191], v[220:223], v[106:109]
	v_mfma_f32_16x16x32_bf16 v[94:97], v[180:183], v[228:231], v[94:97]
	v_mfma_f32_16x16x32_bf16 v[90:93], v[188:191], v[228:231], v[90:93]
	v_mfma_f32_16x16x32_bf16 v[78:81], v[180:183], v[236:239], v[78:81]
	v_mfma_f32_16x16x32_bf16 v[74:77], v[188:191], v[236:239], v[74:77]
	v_mfma_f32_16x16x32_bf16 v[126:129], v[184:187], v[216:219], v[126:129]
	v_mfma_f32_16x16x32_bf16 v[122:125], v[192:195], v[216:219], v[122:125]
	v_mfma_f32_16x16x32_bf16 v[110:113], v[184:187], v[224:227], v[110:113]
	v_mfma_f32_16x16x32_bf16 v[106:109], v[192:195], v[224:227], v[106:109]
	v_mfma_f32_16x16x32_bf16 v[94:97], v[184:187], v[232:235], v[94:97]
	v_mfma_f32_16x16x32_bf16 v[90:93], v[192:195], v[232:235], v[90:93]
	v_mfma_f32_16x16x32_bf16 v[78:81], v[184:187], v[240:243], v[78:81]
	v_mfma_f32_16x16x32_bf16 v[74:77], v[192:195], v[240:243], v[74:77]
	s_setprio 0
	s_setprio 1
	v_mfma_f32_16x16x32_bf16 v[118:121], v[196:199], v[212:215], v[118:121]
	v_mfma_f32_16x16x32_bf16 v[114:117], v[204:207], v[212:215], v[114:117]
	v_mfma_f32_16x16x32_bf16 v[102:105], v[196:199], v[220:223], v[102:105]
	v_mfma_f32_16x16x32_bf16 v[98:101], v[204:207], v[220:223], v[98:101]
	v_mfma_f32_16x16x32_bf16 v[86:89], v[196:199], v[228:231], v[86:89]
	v_mfma_f32_16x16x32_bf16 v[82:85], v[204:207], v[228:231], v[82:85]
	v_mfma_f32_16x16x32_bf16 v[70:73], v[196:199], v[236:239], v[70:73]
	v_mfma_f32_16x16x32_bf16 v[66:69], v[204:207], v[236:239], v[66:69]
	v_mfma_f32_16x16x32_bf16 v[118:121], v[200:203], v[216:219], v[118:121]
	v_mfma_f32_16x16x32_bf16 v[114:117], v[208:211], v[216:219], v[114:117]
	v_mfma_f32_16x16x32_bf16 v[102:105], v[200:203], v[224:227], v[102:105]
	v_mfma_f32_16x16x32_bf16 v[98:101], v[208:211], v[224:227], v[98:101]
	v_mfma_f32_16x16x32_bf16 v[86:89], v[200:203], v[232:235], v[86:89]
	v_mfma_f32_16x16x32_bf16 v[82:85], v[208:211], v[232:235], v[82:85]
	v_mfma_f32_16x16x32_bf16 v[70:73], v[200:203], v[240:243], v[70:73]
	v_mfma_f32_16x16x32_bf16 v[66:69], v[208:211], v[240:243], v[66:69]
	s_setprio 0
	s_barrier
; #define PG8_STAGE(bufoff, gbase, voff) do { _Pragma("unroll") for (int _i = 0; _i < 2; ++_i) \
;         __builtin_amdgcn_global_load_lds((const unsigned*)((const char*)(gbase) + (voff)[_i]), (PG8_LAS unsigned*)(lds + (bufoff) + ldsw + _i * 8192), 16, 0, 0); } while (0)
; #define PG8_WAIT_V(n) asm volatile("s_waitcnt vmcnt(" #n ")" ::: "memory")
; #define PG8_WAIT_L(n) asm volatile("s_waitcnt lgkmcnt(" #n ")" ::: "memory")
; #define PG8_BAR __builtin_amdgcn_s_barrier()
; #define PG8_SCHED __builtin_amdgcn_sched_barrier(0)
; template <class Epi, class Sched, bool ALIGN_EPI = true, bool F8 = false>
; __device__ __forceinline__ void gemm_phase(PG8_LAS unsigned char* lds, const Sched& S, const Epi& E) {
;     ...
;             PG8_LDA(At, 0, 1); PG8_STAGE(PG8_SB(0, 0), b2, voffB[0]); PG8_STAGE(PG8_SB(0, 1), b2, voffB[1]); PG8_STAGE(PG8_SA(0, 0), a2, vA2[0]);
;             PG8_WAIT_V(8); PG8_WAIT_L(0); PG8_BAR; PG8_MMA(1, 0, At, B0); PG8_MMA(1, 1, At, B1); PG8_BAR; PG8_SCHED;
;             PG8_LDB(B0, 1, 0); PG8_LDB(B1, 1, 1); PG8_SCHED; PG8_LDA(At, 1, 0); PG8_STAGE(PG8_SA(0, 1), a2, vA2[1]);
;             PG8_WAIT_V(8); PG8_WAIT_L(0); PG8_BAR; PG8_MMA(0, 0, At, B0); PG8_MMA(0, 1, At, B1); PG8_BAR; PG8_SCHED;
	s_mov_b32 m0, s47
	v_lshl_add_u64 v[166:167], s[66:67], 0, v[134:135]
	ds_read_b128 v[212:215], v176 offset:16384
	ds_read_b128 v[216:219], v176 offset:17408
	ds_read_b128 v[220:223], v176 offset:18432
	ds_read_b128 v[224:227], v176 offset:19456
	ds_read_b128 v[228:231], v176 offset:20480
	ds_read_b128 v[232:235], v176 offset:21504
	ds_read_b128 v[236:239], v176 offset:22528
	ds_read_b128 v[240:243], v176 offset:23552
	global_load_lds_dwordx4 v[166:167], off
	v_lshl_add_u64 v[244:245], s[66:67], 0, v[130:131]
	s_mov_b32 m0, s48
	v_lshl_add_u64 v[246:247], s[66:67], 0, v[136:137]
	global_load_lds_dwordx4 v[244:245], off
	s_mov_b32 m0, s49
	v_lshl_add_u64 v[248:249], s[66:67], 0, v[132:133]
	global_load_lds_dwordx4 v[246:247], off
	s_mov_b32 m0, s50
	v_lshl_add_u64 v[250:251], s[24:25], 0, v[138:139]
	global_load_lds_dwordx4 v[248:249], off
	s_mov_b32 m0, s30
	v_lshl_add_u64 v[252:253], s[24:25], 0, v[140:141]
	global_load_lds_dwordx4 v[250:251], off
	s_mov_b32 m0, s31
	s_nop 0
	global_load_lds_dwordx4 v[252:253], off
	s_waitcnt vmcnt(8)
	s_waitcnt lgkmcnt(0)
	s_setprio 1
	v_mfma_f32_16x16x32_bf16 v[62:65], v[180:183], v[212:215], v[62:65]
	v_mfma_f32_16x16x32_bf16 v[58:61], v[188:191], v[212:215], v[58:61]
	v_mfma_f32_16x16x32_bf16 v[46:49], v[180:183], v[220:223], v[46:49]
	v_mfma_f32_16x16x32_bf16 v[42:45], v[188:191], v[220:223], v[42:45]
	v_mfma_f32_16x16x32_bf16 v[30:33], v[180:183], v[228:231], v[30:33]
	v_mfma_f32_16x16x32_bf16 v[26:29], v[188:191], v[228:231], v[26:29]
	v_mfma_f32_16x16x32_bf16 v[14:17], v[180:183], v[236:239], v[14:17]
	v_mfma_f32_16x16x32_bf16 v[10:13], v[188:191], v[236:239], v[10:13]
	v_mfma_f32_16x16x32_bf16 v[62:65], v[184:187], v[216:219], v[62:65]
	v_mfma_f32_16x16x32_bf16 v[58:61], v[192:195], v[216:219], v[58:61]
	v_mfma_f32_16x16x32_bf16 v[46:49], v[184:187], v[224:227], v[46:49]
	v_mfma_f32_16x16x32_bf16 v[42:45], v[192:195], v[224:227], v[42:45]
	v_mfma_f32_16x16x32_bf16 v[30:33], v[184:187], v[232:235], v[30:33]
	v_mfma_f32_16x16x32_bf16 v[26:29], v[192:195], v[232:235], v[26:29]
	v_mfma_f32_16x16x32_bf16 v[14:17], v[184:187], v[240:243], v[14:17]
	v_mfma_f32_16x16x32_bf16 v[10:13], v[192:195], v[240:243], v[10:13]
	s_setprio 0
	s_setprio 1
	v_mfma_f32_16x16x32_bf16 v[54:57], v[196:199], v[212:215], v[54:57]
	v_mfma_f32_16x16x32_bf16 v[50:53], v[204:207], v[212:215], v[50:53]
	v_mfma_f32_16x16x32_bf16 v[38:41], v[196:199], v[220:223], v[38:41]
	v_mfma_f32_16x16x32_bf16 v[34:37], v[204:207], v[220:223], v[34:37]
	v_mfma_f32_16x16x32_bf16 v[22:25], v[196:199], v[228:231], v[22:25]
	v_mfma_f32_16x16x32_bf16 v[18:21], v[204:207], v[228:231], v[18:21]
	v_mfma_f32_16x16x32_bf16 v[6:9], v[196:199], v[236:239], v[6:9]
	v_mfma_f32_16x16x32_bf16 v[2:5], v[204:207], v[236:239], v[2:5]
	v_mfma_f32_16x16x32_bf16 v[54:57], v[200:203], v[216:219], v[54:57]
	v_mfma_f32_16x16x32_bf16 v[50:53], v[208:211], v[216:219], v[50:53]
	v_mfma_f32_16x16x32_bf16 v[38:41], v[200:203], v[224:227], v[38:41]
	v_mfma_f32_16x16x32_bf16 v[34:37], v[208:211], v[224:227], v[34:37]
	v_mfma_f32_16x16x32_bf16 v[22:25], v[200:203], v[232:235], v[22:25]
	v_mfma_f32_16x16x32_bf16 v[18:21], v[208:211], v[232:235], v[18:21]
	v_mfma_f32_16x16x32_bf16 v[6:9], v[200:203], v[240:243], v[6:9]
	v_mfma_f32_16x16x32_bf16 v[2:5], v[208:211], v[240:243], v[2:5]
	s_setprio 0
	s_barrier
	ds_read_b128 v[180:183], v177
	ds_read_b128 v[184:187], v177 offset:1024
	ds_read_b128 v[188:191], v177 offset:2048
	ds_read_b128 v[192:195], v177 offset:3072
	ds_read_b128 v[196:199], v178
	ds_read_b128 v[200:203], v178 offset:1024
	ds_read_b128 v[204:207], v178 offset:2048
	ds_read_b128 v[208:211], v178 offset:3072
	s_mov_b32 m0, s40
	v_lshl_add_u64 v[254:255], s[24:25], 0, v[142:143]
	ds_read_b128 v[212:215], v176 offset:32768
	ds_read_b128 v[216:219], v176 offset:33792
	ds_read_b128 v[220:223], v176 offset:34816
	ds_read_b128 v[224:227], v176 offset:35840
	ds_read_b128 v[228:231], v176 offset:36864
	ds_read_b128 v[232:235], v176 offset:37888
	ds_read_b128 v[236:239], v176 offset:38912
	ds_read_b128 v[240:243], v176 offset:39936
	global_load_lds_dwordx4 v[254:255], off
	v_lshl_add_u64 v[254:255], s[24:25], 0, v[144:145]
	s_mov_b32 m0, s41
	s_nop 0
	global_load_lds_dwordx4 v[254:255], off
	s_waitcnt vmcnt(8)
	s_waitcnt lgkmcnt(0)
	s_setprio 1
	v_mfma_f32_16x16x32_bf16 v[126:129], v[180:183], v[212:215], v[126:129]
	v_mfma_f32_16x16x32_bf16 v[122:125], v[188:191], v[212:215], v[122:125]
	v_mfma_f32_16x16x32_bf16 v[110:113], v[180:183], v[220:223], v[110:113]
	v_mfma_f32_16x16x32_bf16 v[106:109], v[188:191], v[220:223], v[106:109]
	v_mfma_f32_16x16x32_bf16 v[94:97], v[180:183], v[228:231], v[94:97]
	v_mfma_f32_16x16x32_bf16 v[90:93], v[188:191], v[228:231], v[90:93]
	v_mfma_f32_16x16x32_bf16 v[78:81], v[180:183], v[236:239], v[78:81]
	v_mfma_f32_16x16x32_bf16 v[74:77], v[188:191], v[236:239], v[74:77]
	v_mfma_f32_16x16x32_bf16 v[126:129], v[184:187], v[216:219], v[126:129]
	v_mfma_f32_16x16x32_bf16 v[122:125], v[192:195], v[216:219], v[122:125]
	v_mfma_f32_16x16x32_bf16 v[110:113], v[184:187], v[224:227], v[110:113]
	v_mfma_f32_16x16x32_bf16 v[106:109], v[192:195], v[224:227], v[106:109]
	v_mfma_f32_16x16x32_bf16 v[94:97], v[184:187], v[232:235], v[94:97]
	v_mfma_f32_16x16x32_bf16 v[90:93], v[192:195], v[232:235], v[90:93]
	v_mfma_f32_16x16x32_bf16 v[78:81], v[184:187], v[240:243], v[78:81]
	v_mfma_f32_16x16x32_bf16 v[74:77], v[192:195], v[240:243], v[74:77]
	s_setprio 0
	s_setprio 1
	v_mfma_f32_16x16x32_bf16 v[118:121], v[196:199], v[212:215], v[118:121]
	v_mfma_f32_16x16x32_bf16 v[114:117], v[204:207], v[212:215], v[114:117]
	v_mfma_f32_16x16x32_bf16 v[102:105], v[196:199], v[220:223], v[102:105]
	v_mfma_f32_16x16x32_bf16 v[98:101], v[204:207], v[220:223], v[98:101]
	v_mfma_f32_16x16x32_bf16 v[86:89], v[196:199], v[228:231], v[86:89]
	v_mfma_f32_16x16x32_bf16 v[82:85], v[204:207], v[228:231], v[82:85]
	v_mfma_f32_16x16x32_bf16 v[70:73], v[196:199], v[236:239], v[70:73]
	v_mfma_f32_16x16x32_bf16 v[66:69], v[204:207], v[236:239], v[66:69]
	v_mfma_f32_16x16x32_bf16 v[118:121], v[200:203], v[216:219], v[118:121]
	v_mfma_f32_16x16x32_bf16 v[114:117], v[208:211], v[216:219], v[114:117]
	v_mfma_f32_16x16x32_bf16 v[102:105], v[200:203], v[224:227], v[102:105]
	v_mfma_f32_16x16x32_bf16 v[98:101], v[208:211], v[224:227], v[98:101]
	v_mfma_f32_16x16x32_bf16 v[86:89], v[200:203], v[232:235], v[86:89]
	v_mfma_f32_16x16x32_bf16 v[82:85], v[208:211], v[232:235], v[82:85]
	v_mfma_f32_16x16x32_bf16 v[70:73], v[200:203], v[240:243], v[70:73]
	v_mfma_f32_16x16x32_bf16 v[66:69], v[208:211], v[240:243], v[66:69]
	s_setprio 0
	s_barrier
; #define PG8_STAGE(bufoff, gbase, voff) do { _Pragma("unroll") for (int _i = 0; _i < 2; ++_i) \
;         __builtin_amdgcn_global_load_lds((const unsigned*)((const char*)(gbase) + (voff)[_i]), (PG8_LAS unsigned*)(lds + (bufoff) + ldsw + _i * 8192), 16, 0, 0); } while (0)
; #define PG8_WAIT_V(n) asm volatile("s_waitcnt vmcnt(" #n ")" ::: "memory")
; #define PG8_WAIT_L(n) asm volatile("s_waitcnt lgkmcnt(" #n ")" ::: "memory")
; #define PG8_BAR __builtin_amdgcn_s_barrier()
; #define PG8_SCHED __builtin_amdgcn_sched_barrier(0)
; template <class Epi, class Sched, bool ALIGN_EPI = true, bool F8 = false>
; __device__ __forceinline__ void gemm_phase(PG8_LAS unsigned char* lds, const Sched& S, const Epi& E) {
;     ...
;             PG8_LDB(B0, 0, 0); PG8_LDB(B1, 0, 1); PG8_SCHED; PG8_LDA(At, 0, 0); PG8_STAGE(PG8_SA(1, 1), a1, voffA[1]);
;             PG8_WAIT_V(8); PG8_WAIT_L(0); PG8_BAR; PG8_MMA(0, 0, At, B0); PG8_MMA(0, 1, At, B1); PG8_BAR; PG8_SCHED;
;     ...
;             PG8_LDA(At, 1, 1); PG8_STAGE(PG8_SB(1, 0), b3, voffB[0]); PG8_STAGE(PG8_SB(1, 1), b3, voffB[1]); PG8_STAGE(PG8_SA(1, 0), a3, vA2[0]);
;             PG8_WAIT_V(8); PG8_WAIT_L(0); PG8_BAR; PG8_MMA(1, 0, At, B0); PG8_MMA(1, 1, At, B1); PG8_BAR; PG8_SCHED;
;         }
	s_mov_b32 m0, s51
	v_lshl_add_u64 v[166:167], v[166:167], 0, s[8:9]
	ds_read_b128 v[212:215], v176 offset:49152
	ds_read_b128 v[216:219], v176 offset:50176
	ds_read_b128 v[220:223], v176 offset:51200
	ds_read_b128 v[224:227], v176 offset:52224
	ds_read_b128 v[228:231], v176 offset:53248
	ds_read_b128 v[232:235], v176 offset:54272
	ds_read_b128 v[236:239], v176 offset:55296
	ds_read_b128 v[240:243], v176 offset:56320
	global_load_lds_dwordx4 v[166:167], off
	v_lshl_add_u64 v[166:167], v[244:245], 0, s[8:9]
	s_mov_b32 m0, s52
	s_nop 0
	global_load_lds_dwordx4 v[166:167], off
	v_lshl_add_u64 v[166:167], v[246:247], 0, s[8:9]
	s_mov_b32 m0, s53
	s_nop 0
	global_load_lds_dwordx4 v[166:167], off
	v_lshl_add_u64 v[166:167], v[248:249], 0, s[8:9]
	s_mov_b32 m0, s58
	s_nop 0
	global_load_lds_dwordx4 v[166:167], off
	v_lshl_add_u64 v[166:167], v[250:251], 0, s[8:9]
	s_mov_b32 m0, s43
	s_nop 0
	global_load_lds_dwordx4 v[166:167], off
	v_lshl_add_u64 v[166:167], v[252:253], 0, s[8:9]
	s_mov_b32 m0, s44
	s_nop 0
	global_load_lds_dwordx4 v[166:167], off
	s_waitcnt vmcnt(8)
	s_waitcnt lgkmcnt(0)
	s_setprio 1
	v_mfma_f32_16x16x32_bf16 v[62:65], v[180:183], v[212:215], v[62:65]
	v_mfma_f32_16x16x32_bf16 v[58:61], v[188:191], v[212:215], v[58:61]
	v_mfma_f32_16x16x32_bf16 v[46:49], v[180:183], v[220:223], v[46:49]
	v_mfma_f32_16x16x32_bf16 v[42:45], v[188:191], v[220:223], v[42:45]
	v_mfma_f32_16x16x32_bf16 v[30:33], v[180:183], v[228:231], v[30:33]
	v_mfma_f32_16x16x32_bf16 v[26:29], v[188:191], v[228:231], v[26:29]
	v_mfma_f32_16x16x32_bf16 v[14:17], v[180:183], v[236:239], v[14:17]
	v_mfma_f32_16x16x32_bf16 v[10:13], v[188:191], v[236:239], v[10:13]
	v_mfma_f32_16x16x32_bf16 v[62:65], v[184:187], v[216:219], v[62:65]
	v_mfma_f32_16x16x32_bf16 v[58:61], v[192:195], v[216:219], v[58:61]
	v_mfma_f32_16x16x32_bf16 v[46:49], v[184:187], v[224:227], v[46:49]
	v_mfma_f32_16x16x32_bf16 v[42:45], v[192:195], v[224:227], v[42:45]
	v_mfma_f32_16x16x32_bf16 v[30:33], v[184:187], v[232:235], v[30:33]
	v_mfma_f32_16x16x32_bf16 v[26:29], v[192:195], v[232:235], v[26:29]
	v_mfma_f32_16x16x32_bf16 v[14:17], v[184:187], v[240:243], v[14:17]
	v_mfma_f32_16x16x32_bf16 v[10:13], v[192:195], v[240:243], v[10:13]
	s_setprio 0
	s_setprio 1
	v_mfma_f32_16x16x32_bf16 v[54:57], v[196:199], v[212:215], v[54:57]
	v_mfma_f32_16x16x32_bf16 v[50:53], v[204:207], v[212:215], v[50:53]
	v_mfma_f32_16x16x32_bf16 v[38:41], v[196:199], v[220:223], v[38:41]
	v_mfma_f32_16x16x32_bf16 v[34:37], v[204:207], v[220:223], v[34:37]
	v_mfma_f32_16x16x32_bf16 v[22:25], v[196:199], v[228:231], v[22:25]
	v_mfma_f32_16x16x32_bf16 v[18:21], v[204:207], v[228:231], v[18:21]
	v_mfma_f32_16x16x32_bf16 v[6:9], v[196:199], v[236:239], v[6:9]
	v_mfma_f32_16x16x32_bf16 v[2:5], v[204:207], v[236:239], v[2:5]
	v_mfma_f32_16x16x32_bf16 v[54:57], v[200:203], v[216:219], v[54:57]
	v_mfma_f32_16x16x32_bf16 v[50:53], v[208:211], v[216:219], v[50:53]
	v_mfma_f32_16x16x32_bf16 v[38:41], v[200:203], v[224:227], v[38:41]
	v_mfma_f32_16x16x32_bf16 v[34:37], v[208:211], v[224:227], v[34:37]
	v_mfma_f32_16x16x32_bf16 v[22:25], v[200:203], v[232:235], v[22:25]
	v_mfma_f32_16x16x32_bf16 v[18:21], v[208:211], v[232:235], v[18:21]
	v_mfma_f32_16x16x32_bf16 v[6:9], v[200:203], v[240:243], v[6:9]
	v_mfma_f32_16x16x32_bf16 v[2:5], v[208:211], v[240:243], v[2:5]
	s_setprio 0
	s_barrier
	s_add_i32 s65, s65, 2
	s_add_u32 s63, s63, 0x100
	s_addc_u32 s64, s64, 0
	s_cmp_gt_u32 s65, 9
	s_mov_b64 s[20:21], s[22:23]
	s_cbranch_scc0 .LBB0_676
	s_branch .Lfx_17518
.Lh1e_17518:
.Lh1_676:
	ds_read_b128 v[180:183], v174
	ds_read_b128 v[184:187], v174 offset:1024
	ds_read_b128 v[188:191], v174 offset:2048
	ds_read_b128 v[192:195], v174 offset:3072
	ds_read_b128 v[196:199], v175
	ds_read_b128 v[200:203], v175 offset:1024
	ds_read_b128 v[204:207], v175 offset:2048
	ds_read_b128 v[208:211], v175 offset:3072
	s_add_u32 s22, s20, 0x100
	s_addc_u32 s23, s21, 0
	s_cmp_eq_u32 s65, 8
	s_cselect_b32 s25, s13, s23
	s_cselect_b32 s24, s12, s22
	s_cselect_b32 s67, s15, s64
	s_cselect_b32 s66, s14, s63
	s_mov_b32 m0, s45
	v_lshl_add_u64 v[166:167], s[20:21], 0, v[164:165]
	ds_read_b128 v[212:215], v176
	ds_read_b128 v[216:219], v176 offset:1024
	ds_read_b128 v[220:223], v176 offset:2048
	ds_read_b128 v[224:227], v176 offset:3072
	ds_read_b128 v[228:231], v176 offset:4096
	ds_read_b128 v[232:235], v176 offset:5120
	ds_read_b128 v[236:239], v176 offset:6144
	ds_read_b128 v[240:243], v176 offset:7168
	global_load_lds_dwordx4 v[166:167], off
	v_lshl_add_u64 v[166:167], s[20:21], 0, v[162:163]
	s_mov_b32 m0, s46
	s_nop 0
	global_load_lds_dwordx4 v[166:167], off
	s_waitcnt vmcnt(8)
	s_waitcnt lgkmcnt(0)
	s_barrier
; #define PG8_STAGE(bufoff, gbase, voff) do { _Pragma("unroll") for (int _i = 0; _i < 2; ++_i) \
;         __builtin_amdgcn_global_load_lds((const unsigned*)((const char*)(gbase) + (voff)[_i]), (PG8_LAS unsigned*)(lds + (bufoff) + ldsw + _i * 8192), 16, 0, 0); } while (0)
; #define PG8_WAIT_V(n) asm volatile("s_waitcnt vmcnt(" #n ")" ::: "memory")
; #define PG8_WAIT_L(n) asm volatile("s_waitcnt lgkmcnt(" #n ")" ::: "memory")
; #define PG8_BAR __builtin_amdgcn_s_barrier()
; #define PG8_SCHED __builtin_amdgcn_sched_barrier(0)
; template <class Epi, class Sched, bool ALIGN_EPI = true, bool F8 = false>
; __device__ __forceinline__ void gemm_phase(PG8_LAS unsigned char* lds, const Sched& S, const Epi& E) {
;     ...
;             PG8_WAIT_V(8); PG8_WAIT_L(0); PG8_BAR; PG8_MMA(0, 0, At, B0); PG8_MMA(0, 1, At, B1); PG8_BAR; PG8_SCHED;
;             PG8_LDA(At, 0, 1); PG8_STAGE(PG8_SB(0, 0), b2, voffB[0]); PG8_STAGE(PG8_SB(0, 1), b2, voffB[1]); PG8_STAGE(PG8_SA(0, 0), a2, vA2[0]);
;             PG8_WAIT_V(8); PG8_WAIT_L(0); PG8_BAR; PG8_MMA(1, 0, At, B0); PG8_MMA(1, 1, At, B1); PG8_BAR; PG8_SCHED;
;             PG8_LDB(B0, 1, 0); PG8_LDB(B1, 1, 1); PG8_SCHED; PG8_LDA(At, 1, 0); PG8_STAGE(PG8_SA(0, 1), a2, vA2[1]);
;             PG8_WAIT_V(8); PG8_WAIT_L(0); PG8_BAR; PG8_MMA(0, 0, At, B0); PG8_MMA(0, 1, At, B1); PG8_BAR; PG8_SCHED;
	s_setprio 2
	v_mfma_f32_16x16x32_bf16 v[126:129], v[180:183], v[212:215], v[126:129]
	v_mfma_f32_16x16x32_bf16 v[122:125], v[188:191], v[212:215], v[122:125]
	v_mfma_f32_16x16x32_bf16 v[110:113], v[180:183], v[220:223], v[110:113]
	v_mfma_f32_16x16x32_bf16 v[106:109], v[188:191], v[220:223], v[106:109]
	v_mfma_f32_16x16x32_bf16 v[94:97], v[180:183], v[228:231], v[94:97]
	v_mfma_f32_16x16x32_bf16 v[90:93], v[188:191], v[228:231], v[90:93]
	v_mfma_f32_16x16x32_bf16 v[78:81], v[180:183], v[236:239], v[78:81]
	v_mfma_f32_16x16x32_bf16 v[74:77], v[188:191], v[236:239], v[74:77]
	v_mfma_f32_16x16x32_bf16 v[126:129], v[184:187], v[216:219], v[126:129]
	v_mfma_f32_16x16x32_bf16 v[122:125], v[192:195], v[216:219], v[122:125]
	v_mfma_f32_16x16x32_bf16 v[110:113], v[184:187], v[224:227], v[110:113]
	v_mfma_f32_16x16x32_bf16 v[106:109], v[192:195], v[224:227], v[106:109]
	v_mfma_f32_16x16x32_bf16 v[94:97], v[184:187], v[232:235], v[94:97]
	v_mfma_f32_16x16x32_bf16 v[90:93], v[192:195], v[232:235], v[90:93]
	v_mfma_f32_16x16x32_bf16 v[78:81], v[184:187], v[240:243], v[78:81]
	v_mfma_f32_16x16x32_bf16 v[74:77], v[192:195], v[240:243], v[74:77]
	s_setprio 0
	s_setprio 2
	v_mfma_f32_16x16x32_bf16 v[118:121], v[196:199], v[212:215], v[118:121]
	v_mfma_f32_16x16x32_bf16 v[114:117], v[204:207], v[212:215], v[114:117]
	v_mfma_f32_16x16x32_bf16 v[102:105], v[196:199], v[220:223], v[102:105]
	v_mfma_f32_16x16x32_bf16 v[98:101], v[204:207], v[220:223], v[98:101]
	v_mfma_f32_16x16x32_bf16 v[86:89], v[196:199], v[228:231], v[86:89]
	v_mfma_f32_16x16x32_bf16 v[82:85], v[204:207], v[228:231], v[82:85]
	v_mfma_f32_16x16x32_bf16 v[70:73], v[196:199], v[236:239], v[70:73]
	v_mfma_f32_16x16x32_bf16 v[66:69], v[204:207], v[236:239], v[66:69]
	v_mfma_f32_16x16x32_bf16 v[118:121], v[200:203], v[216:219], v[118:121]
	v_mfma_f32_16x16x32_bf16 v[114:117], v[208:211], v[216:219], v[114:117]
	v_mfma_f32_16x16x32_bf16 v[102:105], v[200:203], v[224:227], v[102:105]
	v_mfma_f32_16x16x32_bf16 v[98:101], v[208:211], v[224:227], v[98:101]
	v_mfma_f32_16x16x32_bf16 v[86:89], v[200:203], v[232:235], v[86:89]
	v_mfma_f32_16x16x32_bf16 v[82:85], v[208:211], v[232:235], v[82:85]
	v_mfma_f32_16x16x32_bf16 v[70:73], v[200:203], v[240:243], v[70:73]
	v_mfma_f32_16x16x32_bf16 v[66:69], v[208:211], v[240:243], v[66:69]
	s_setprio 0
	s_mov_b32 m0, s47
	v_lshl_add_u64 v[166:167], s[66:67], 0, v[134:135]
	ds_read_b128 v[212:215], v176 offset:16384
	ds_read_b128 v[216:219], v176 offset:17408
	ds_read_b128 v[220:223], v176 offset:18432
	ds_read_b128 v[224:227], v176 offset:19456
	ds_read_b128 v[228:231], v176 offset:20480
	ds_read_b128 v[232:235], v176 offset:21504
	ds_read_b128 v[236:239], v176 offset:22528
	ds_read_b128 v[240:243], v176 offset:23552
	global_load_lds_dwordx4 v[166:167], off
	v_lshl_add_u64 v[244:245], s[66:67], 0, v[130:131]
	s_mov_b32 m0, s48
	v_lshl_add_u64 v[246:247], s[66:67], 0, v[136:137]
	global_load_lds_dwordx4 v[244:245], off
	s_mov_b32 m0, s49
	v_lshl_add_u64 v[248:249], s[66:67], 0, v[132:133]
	global_load_lds_dwordx4 v[246:247], off
	s_mov_b32 m0, s50
	v_lshl_add_u64 v[250:251], s[24:25], 0, v[138:139]
	global_load_lds_dwordx4 v[248:249], off
	s_mov_b32 m0, s30
	v_lshl_add_u64 v[252:253], s[24:25], 0, v[140:141]
	global_load_lds_dwordx4 v[250:251], off
	s_mov_b32 m0, s31
	s_nop 0
	global_load_lds_dwordx4 v[252:253], off
	s_waitcnt vmcnt(8)
	s_waitcnt lgkmcnt(0)
	s_barrier
	s_setprio 2
	v_mfma_f32_16x16x32_bf16 v[62:65], v[180:183], v[212:215], v[62:65]
	v_mfma_f32_16x16x32_bf16 v[58:61], v[188:191], v[212:215], v[58:61]
	v_mfma_f32_16x16x32_bf16 v[46:49], v[180:183], v[220:223], v[46:49]
	v_mfma_f32_16x16x32_bf16 v[42:45], v[188:191], v[220:223], v[42:45]
	v_mfma_f32_16x16x32_bf16 v[30:33], v[180:183], v[228:231], v[30:33]
	v_mfma_f32_16x16x32_bf16 v[26:29], v[188:191], v[228:231], v[26:29]
	v_mfma_f32_16x16x32_bf16 v[14:17], v[180:183], v[236:239], v[14:17]
	v_mfma_f32_16x16x32_bf16 v[10:13], v[188:191], v[236:239], v[10:13]
	v_mfma_f32_16x16x32_bf16 v[62:65], v[184:187], v[216:219], v[62:65]
	v_mfma_f32_16x16x32_bf16 v[58:61], v[192:195], v[216:219], v[58:61]
	v_mfma_f32_16x16x32_bf16 v[46:49], v[184:187], v[224:227], v[46:49]
	v_mfma_f32_16x16x32_bf16 v[42:45], v[192:195], v[224:227], v[42:45]
	v_mfma_f32_16x16x32_bf16 v[30:33], v[184:187], v[232:235], v[30:33]
	v_mfma_f32_16x16x32_bf16 v[26:29], v[192:195], v[232:235], v[26:29]
	v_mfma_f32_16x16x32_bf16 v[14:17], v[184:187], v[240:243], v[14:17]
	v_mfma_f32_16x16x32_bf16 v[10:13], v[192:195], v[240:243], v[10:13]
	s_setprio 0
	s_setprio 2
	v_mfma_f32_16x16x32_bf16 v[54:57], v[196:199], v[212:215], v[54:57]
	v_mfma_f32_16x16x32_bf16 v[50:53], v[204:207], v[212:215], v[50:53]
	v_mfma_f32_16x16x32_bf16 v[38:41], v[196:199], v[220:223], v[38:41]
	v_mfma_f32_16x16x32_bf16 v[34:37], v[204:207], v[220:223], v[34:37]
	v_mfma_f32_16x16x32_bf16 v[22:25], v[196:199], v[228:231], v[22:25]
	v_mfma_f32_16x16x32_bf16 v[18:21], v[204:207], v[228:231], v[18:21]
	v_mfma_f32_16x16x32_bf16 v[6:9], v[196:199], v[236:239], v[6:9]
	v_mfma_f32_16x16x32_bf16 v[2:5], v[204:207], v[236:239], v[2:5]
	v_mfma_f32_16x16x32_bf16 v[54:57], v[200:203], v[216:219], v[54:57]
	v_mfma_f32_16x16x32_bf16 v[50:53], v[208:211], v[216:219], v[50:53]
	v_mfma_f32_16x16x32_bf16 v[38:41], v[200:203], v[224:227], v[38:41]
	v_mfma_f32_16x16x32_bf16 v[34:37], v[208:211], v[224:227], v[34:37]
	v_mfma_f32_16x16x32_bf16 v[22:25], v[200:203], v[232:235], v[22:25]
	v_mfma_f32_16x16x32_bf16 v[18:21], v[208:211], v[232:235], v[18:21]
	v_mfma_f32_16x16x32_bf16 v[6:9], v[200:203], v[240:243], v[6:9]
	v_mfma_f32_16x16x32_bf16 v[2:5], v[208:211], v[240:243], v[2:5]
	s_setprio 0
	ds_read_b128 v[180:183], v177
	ds_read_b128 v[184:187], v177 offset:1024
	ds_read_b128 v[188:191], v177 offset:2048
	ds_read_b128 v[192:195], v177 offset:3072
	ds_read_b128 v[196:199], v178
	ds_read_b128 v[200:203], v178 offset:1024
	ds_read_b128 v[204:207], v178 offset:2048
	ds_read_b128 v[208:211], v178 offset:3072
	s_mov_b32 m0, s40
	v_lshl_add_u64 v[254:255], s[24:25], 0, v[142:143]
	ds_read_b128 v[212:215], v176 offset:32768
	ds_read_b128 v[216:219], v176 offset:33792
	ds_read_b128 v[220:223], v176 offset:34816
	ds_read_b128 v[224:227], v176 offset:35840
	ds_read_b128 v[228:231], v176 offset:36864
	ds_read_b128 v[232:235], v176 offset:37888
	ds_read_b128 v[236:239], v176 offset:38912
	ds_read_b128 v[240:243], v176 offset:39936
	global_load_lds_dwordx4 v[254:255], off
	v_lshl_add_u64 v[254:255], s[24:25], 0, v[144:145]
	s_mov_b32 m0, s41
	s_nop 0
	global_load_lds_dwordx4 v[254:255], off
	s_waitcnt vmcnt(8)
	s_waitcnt lgkmcnt(0)
	s_barrier
; #define PG8_STAGE(bufoff, gbase, voff) do { _Pragma("unroll") for (int _i = 0; _i < 2; ++_i) \
;         __builtin_amdgcn_global_load_lds((const unsigned*)((const char*)(gbase) + (voff)[_i]), (PG8_LAS unsigned*)(lds + (bufoff) + ldsw + _i * 8192), 16, 0, 0); } while (0)
; #define PG8_WAIT_V(n) asm volatile("s_waitcnt vmcnt(" #n ")" ::: "memory")
; #define PG8_WAIT_L(n) asm volatile("s_waitcnt lgkmcnt(" #n ")" ::: "memory")
; #define PG8_BAR __builtin_amdgcn_s_barrier()
; #define PG8_SCHED __builtin_amdgcn_sched_barrier(0)
; template <class Epi, class Sched, bool ALIGN_EPI = true, bool F8 = false>
; __device__ __forceinline__ void gemm_phase(PG8_LAS unsigned char* lds, const Sched& S, const Epi& E) {
;     ...
;             PG8_LDB(B0, 1, 0); PG8_LDB(B1, 1, 1); PG8_SCHED; PG8_LDA(At, 1, 0); PG8_STAGE(PG8_SA(0, 1), a2, vA2[1]);
;             PG8_WAIT_V(8); PG8_WAIT_L(0); PG8_BAR; PG8_MMA(0, 0, At, B0); PG8_MMA(0, 1, At, B1); PG8_BAR; PG8_SCHED;
;             PG8_LDA(At, 1, 1); PG8_STAGE(PG8_SB(1, 0), b3, voffB[0]); PG8_STAGE(PG8_SB(1, 1), b3, voffB[1]); PG8_STAGE(PG8_SA(1, 0), a3, vA2[0]);
;             PG8_WAIT_V(8); PG8_WAIT_L(0); PG8_BAR; PG8_MMA(1, 0, At, B0); PG8_MMA(1, 1, At, B1); PG8_BAR; PG8_SCHED;
;         }
	s_setprio 2
	v_mfma_f32_16x16x32_bf16 v[126:129], v[180:183], v[212:215], v[126:129]
	v_mfma_f32_16x16x32_bf16 v[122:125], v[188:191], v[212:215], v[122:125]
	v_mfma_f32_16x16x32_bf16 v[110:113], v[180:183], v[220:223], v[110:113]
	v_mfma_f32_16x16x32_bf16 v[106:109], v[188:191], v[220:223], v[106:109]
	v_mfma_f32_16x16x32_bf16 v[94:97], v[180:183], v[228:231], v[94:97]
	v_mfma_f32_16x16x32_bf16 v[90:93], v[188:191], v[228:231], v[90:93]
	v_mfma_f32_16x16x32_bf16 v[78:81], v[180:183], v[236:239], v[78:81]
	v_mfma_f32_16x16x32_bf16 v[74:77], v[188:191], v[236:239], v[74:77]
	v_mfma_f32_16x16x32_bf16 v[126:129], v[184:187], v[216:219], v[126:129]
	v_mfma_f32_16x16x32_bf16 v[122:125], v[192:195], v[216:219], v[122:125]
	v_mfma_f32_16x16x32_bf16 v[110:113], v[184:187], v[224:227], v[110:113]
	v_mfma_f32_16x16x32_bf16 v[106:109], v[192:195], v[224:227], v[106:109]
	v_mfma_f32_16x16x32_bf16 v[94:97], v[184:187], v[232:235], v[94:97]
	v_mfma_f32_16x16x32_bf16 v[90:93], v[192:195], v[232:235], v[90:93]
	v_mfma_f32_16x16x32_bf16 v[78:81], v[184:187], v[240:243], v[78:81]
	v_mfma_f32_16x16x32_bf16 v[74:77], v[192:195], v[240:243], v[74:77]
	s_setprio 0
	s_setprio 2
	v_mfma_f32_16x16x32_bf16 v[118:121], v[196:199], v[212:215], v[118:121]
	v_mfma_f32_16x16x32_bf16 v[114:117], v[204:207], v[212:215], v[114:117]
	v_mfma_f32_16x16x32_bf16 v[102:105], v[196:199], v[220:223], v[102:105]
	v_mfma_f32_16x16x32_bf16 v[98:101], v[204:207], v[220:223], v[98:101]
	v_mfma_f32_16x16x32_bf16 v[86:89], v[196:199], v[228:231], v[86:89]
	v_mfma_f32_16x16x32_bf16 v[82:85], v[204:207], v[228:231], v[82:85]
	v_mfma_f32_16x16x32_bf16 v[70:73], v[196:199], v[236:239], v[70:73]
	v_mfma_f32_16x16x32_bf16 v[66:69], v[204:207], v[236:239], v[66:69]
	v_mfma_f32_16x16x32_bf16 v[118:121], v[200:203], v[216:219], v[118:121]
	v_mfma_f32_16x16x32_bf16 v[114:117], v[208:211], v[216:219], v[114:117]
	v_mfma_f32_16x16x32_bf16 v[102:105], v[200:203], v[224:227], v[102:105]
	v_mfma_f32_16x16x32_bf16 v[98:101], v[208:211], v[224:227], v[98:101]
	v_mfma_f32_16x16x32_bf16 v[86:89], v[200:203], v[232:235], v[86:89]
	v_mfma_f32_16x16x32_bf16 v[82:85], v[208:211], v[232:235], v[82:85]
	v_mfma_f32_16x16x32_bf16 v[70:73], v[200:203], v[240:243], v[70:73]
	v_mfma_f32_16x16x32_bf16 v[66:69], v[208:211], v[240:243], v[66:69]
	s_setprio 0
	s_mov_b32 m0, s51
	v_lshl_add_u64 v[166:167], v[166:167], 0, s[8:9]
	ds_read_b128 v[212:215], v176 offset:49152
	ds_read_b128 v[216:219], v176 offset:50176
	ds_read_b128 v[220:223], v176 offset:51200
	ds_read_b128 v[224:227], v176 offset:52224
	ds_read_b128 v[228:231], v176 offset:53248
	ds_read_b128 v[232:235], v176 offset:54272
	ds_read_b128 v[236:239], v176 offset:55296
	ds_read_b128 v[240:243], v176 offset:56320
	global_load_lds_dwordx4 v[166:167], off
	v_lshl_add_u64 v[166:167], v[244:245], 0, s[8:9]
	s_mov_b32 m0, s52
	s_nop 0
	global_load_lds_dwordx4 v[166:167], off
	v_lshl_add_u64 v[166:167], v[246:247], 0, s[8:9]
	s_mov_b32 m0, s53
	s_nop 0
	global_load_lds_dwordx4 v[166:167], off
	v_lshl_add_u64 v[166:167], v[248:249], 0, s[8:9]
	s_mov_b32 m0, s58
	s_nop 0
	global_load_lds_dwordx4 v[166:167], off
	v_lshl_add_u64 v[166:167], v[250:251], 0, s[8:9]
	s_mov_b32 m0, s43
	s_nop 0
	global_load_lds_dwordx4 v[166:167], off
	v_lshl_add_u64 v[166:167], v[252:253], 0, s[8:9]
	s_mov_b32 m0, s44
	s_nop 0
	global_load_lds_dwordx4 v[166:167], off
	s_waitcnt vmcnt(8)
	s_waitcnt lgkmcnt(0)
	s_barrier
	s_setprio 2
	v_mfma_f32_16x16x32_bf16 v[62:65], v[180:183], v[212:215], v[62:65]
	v_mfma_f32_16x16x32_bf16 v[58:61], v[188:191], v[212:215], v[58:61]
	v_mfma_f32_16x16x32_bf16 v[46:49], v[180:183], v[220:223], v[46:49]
	v_mfma_f32_16x16x32_bf16 v[42:45], v[188:191], v[220:223], v[42:45]
	v_mfma_f32_16x16x32_bf16 v[30:33], v[180:183], v[228:231], v[30:33]
	v_mfma_f32_16x16x32_bf16 v[26:29], v[188:191], v[228:231], v[26:29]
	v_mfma_f32_16x16x32_bf16 v[14:17], v[180:183], v[236:239], v[14:17]
	v_mfma_f32_16x16x32_bf16 v[10:13], v[188:191], v[236:239], v[10:13]
	v_mfma_f32_16x16x32_bf16 v[62:65], v[184:187], v[216:219], v[62:65]
	v_mfma_f32_16x16x32_bf16 v[58:61], v[192:195], v[216:219], v[58:61]
	v_mfma_f32_16x16x32_bf16 v[46:49], v[184:187], v[224:227], v[46:49]
	v_mfma_f32_16x16x32_bf16 v[42:45], v[192:195], v[224:227], v[42:45]
	v_mfma_f32_16x16x32_bf16 v[30:33], v[184:187], v[232:235], v[30:33]
	v_mfma_f32_16x16x32_bf16 v[26:29], v[192:195], v[232:235], v[26:29]
	v_mfma_f32_16x16x32_bf16 v[14:17], v[184:187], v[240:243], v[14:17]
	v_mfma_f32_16x16x32_bf16 v[10:13], v[192:195], v[240:243], v[10:13]
	s_setprio 0
	s_setprio 2
	v_mfma_f32_16x16x32_bf16 v[54:57], v[196:199], v[212:215], v[54:57]
	v_mfma_f32_16x16x32_bf16 v[50:53], v[204:207], v[212:215], v[50:53]
	v_mfma_f32_16x16x32_bf16 v[38:41], v[196:199], v[220:223], v[38:41]
	v_mfma_f32_16x16x32_bf16 v[34:37], v[204:207], v[220:223], v[34:37]
	v_mfma_f32_16x16x32_bf16 v[22:25], v[196:199], v[228:231], v[22:25]
	v_mfma_f32_16x16x32_bf16 v[18:21], v[204:207], v[228:231], v[18:21]
	v_mfma_f32_16x16x32_bf16 v[6:9], v[196:199], v[236:239], v[6:9]
	v_mfma_f32_16x16x32_bf16 v[2:5], v[204:207], v[236:239], v[2:5]
	v_mfma_f32_16x16x32_bf16 v[54:57], v[200:203], v[216:219], v[54:57]
	v_mfma_f32_16x16x32_bf16 v[50:53], v[208:211], v[216:219], v[50:53]
	v_mfma_f32_16x16x32_bf16 v[38:41], v[200:203], v[224:227], v[38:41]
	v_mfma_f32_16x16x32_bf16 v[34:37], v[208:211], v[224:227], v[34:37]
	v_mfma_f32_16x16x32_bf16 v[22:25], v[200:203], v[232:235], v[22:25]
	v_mfma_f32_16x16x32_bf16 v[18:21], v[208:211], v[232:235], v[18:21]
	v_mfma_f32_16x16x32_bf16 v[6:9], v[200:203], v[240:243], v[6:9]
	v_mfma_f32_16x16x32_bf16 v[2:5], v[208:211], v[240:243], v[2:5]
	s_setprio 0
	s_add_i32 s65, s65, 2
	s_add_u32 s63, s63, 0x100
	s_addc_u32 s64, s64, 0
	s_cmp_gt_u32 s65, 9
	s_mov_b64 s[20:21], s[22:23]
	s_cbranch_scc0 .Lh1_676

; __device__ __forceinline__ float gelu_tanh(float x) { return x * fsigmoid(1.5957691216f * (x + 0.044715f * x * x * x)); }
;     __device__ __forceinline__ void operator()(AccRef acc, const GUnit& u, int wr, int wc, int fr, int fq) const {
;         const int g = u.x0, b = u.x1, pn = u.x2; const int tt = (pn * 256 + wc * 64 + 16 * fq) >> 4;
; #pragma unroll
;         for (int ai = 0; ai < 2; ++ai)
; #pragma unroll
;             for (int m = 0; m < 4; ++m) { const int ch = ai * 128 + wr * 64 + m * 16 + fr; const size_t tok = (size_t)b * SEQ + ch * LC + tt;
;                 f32x4 v0 = acc[ai][0][m][0], v1 = acc[ai][0][m][1], v2 = acc[ai][1][m][0], v3 = acc[ai][1][m][1];
; #pragma unroll
;                 for (int j = 0; j < 4; ++j) { v0[j] = gelu_tanh(v0[j]); v1[j] = gelu_tanh(v1[j]); v2[j] = gelu_tanh(v2[j]); v3[j] = gelu_tanh(v3[j]); }
;                 st16_bf16(YS + tok * SW + g * 16, v0, v1, v2, v3); }
.LBB0_679:
	v_mul_f32_e32 v179, 0x3d372713, v126
	v_mul_f32_e32 v180, 0x3d372713, v122
	v_mul_f32_e32 v179, v126, v179
	v_mul_f32_e32 v180, v122, v180
	v_fma_f32 v179, v126, v179, v126
	v_fma_f32 v180, v122, v180, v122
	v_mul_f32_e32 v179, 0x3fcc422a, v179
	v_mul_f32_e32 v180, 0x3fcc422a, v180
	v_mul_f32_e32 v179, 0xbfb8aa3b, v179
	v_mul_f32_e32 v180, 0xbfb8aa3b, v180
	v_exp_f32_e32 v179, v179
	v_exp_f32_e32 v181, v180
	v_mul_f32_e32 v180, 0x3d372713, v118
	v_mul_f32_e32 v180, v118, v180
	v_fma_f32 v180, v118, v180, v118
	v_mul_f32_e32 v180, 0x3fcc422a, v180
	v_add_f32_e32 v179, 1.0, v179
	v_mul_f32_e32 v180, 0xbfb8aa3b, v180
	v_exp_f32_e32 v183, v180
	v_rcp_f32_e32 v180, v179
	v_add_f32_e32 v179, 1.0, v181
	v_mul_f32_e32 v181, 0x3d372713, v114
	v_mul_f32_e32 v181, v114, v181
	v_fma_f32 v181, v114, v181, v114
	v_mul_f32_e32 v181, 0x3fcc422a, v181
	v_mul_f32_e32 v181, 0xbfb8aa3b, v181
	v_rcp_f32_e32 v182, v179
	v_add_f32_e32 v179, 1.0, v183
	v_exp_f32_e32 v181, v181
	v_mul_f32_e32 v183, 0x3d372713, v127
	v_mul_f32_e32 v183, v127, v183
	v_fma_f32 v183, v127, v183, v127
	v_mul_f32_e32 v183, 0x3fcc422a, v183
	v_mul_f32_e32 v183, 0xbfb8aa3b, v183
	v_rcp_f32_e32 v184, v179
	v_add_f32_e32 v179, 1.0, v181
	v_mul_f32_e32 v181, 0x3d372713, v123
	v_exp_f32_e32 v183, v183
	v_mul_f32_e32 v181, v123, v181
	v_fma_f32 v181, v123, v181, v123
	v_mul_f32_e32 v181, 0x3fcc422a, v181
	v_mul_f32_e32 v181, 0xbfb8aa3b, v181
	v_rcp_f32_e32 v186, v179
	v_add_f32_e32 v179, 1.0, v183
	v_exp_f32_e32 v183, v181
	v_mul_f32_e32 v181, 0x3d372713, v119
	v_mul_f32_e32 v181, v119, v181
	v_fma_f32 v181, v119, v181, v119
	v_mul_f32_e32 v181, 0x3fcc422a, v181
	v_mul_f32_e32 v181, 0xbfb8aa3b, v181
	v_exp_f32_e32 v185, v181
	v_rcp_f32_e32 v181, v179
	v_add_f32_e32 v179, 1.0, v183
	v_rcp_f32_e32 v183, v179
	v_add_f32_e32 v179, 1.0, v185
	v_rcp_f32_e32 v185, v179
	v_mul_f32_e32 v179, 0x3d372713, v115
	v_mul_f32_e32 v179, v115, v179
	v_fma_f32 v179, v115, v179, v115
	v_mul_f32_e32 v179, 0x3fcc422a, v179
	v_mul_f32_e32 v179, 0xbfb8aa3b, v179
	v_exp_f32_e32 v179, v179
	v_pk_mul_f32 v[126:127], v[126:127], v[180:181]
	v_mul_f32_e32 v180, 0x3d372713, v124
	v_mul_f32_e32 v180, v124, v180
	v_add_f32_e32 v179, 1.0, v179
	v_rcp_f32_e32 v187, v179
	v_mul_f32_e32 v179, 0x3d372713, v128
	v_mul_f32_e32 v179, v128, v179
	v_fma_f32 v179, v128, v179, v128
	v_mul_f32_e32 v179, 0x3fcc422a, v179
	v_fma_f32 v180, v124, v180, v124
	v_mul_f32_e32 v179, 0xbfb8aa3b, v179
	v_mul_f32_e32 v180, 0x3fcc422a, v180
	v_exp_f32_e32 v179, v179
	v_mul_f32_e32 v180, 0xbfb8aa3b, v180
	v_pk_mul_f32 v[122:123], v[122:123], v[182:183]
	v_exp_f32_e32 v182, v180
	v_pk_mul_f32 v[180:181], v[114:115], v[186:187]
	v_add_f32_e32 v114, 1.0, v179
	v_mul_f32_e32 v179, 0x3d372713, v120
	v_add_f32_e32 v115, 1.0, v182
	v_mul_f32_e32 v179, v120, v179
	v_mul_f32_e32 v182, 0x3d372713, v116
	v_fma_f32 v179, v120, v179, v120
	v_mul_f32_e32 v182, v116, v182
	v_mul_f32_e32 v179, 0x3fcc422a, v179
	v_fma_f32 v182, v116, v182, v116
	v_mul_f32_e32 v179, 0xbfb8aa3b, v179
	v_mul_f32_e32 v182, 0x3fcc422a, v182
	v_exp_f32_e32 v179, v179
	v_mul_f32_e32 v182, 0xbfb8aa3b, v182
	v_exp_f32_e32 v183, v182
	v_rcp_f32_e32 v182, v115
	v_add_f32_e32 v115, 1.0, v179
	v_pk_mul_f32 v[118:119], v[118:119], v[184:185]
	v_rcp_f32_e32 v184, v115
	v_add_f32_e32 v115, 1.0, v183
	v_mul_f32_e32 v179, 0x3d372713, v129
	v_mul_f32_e32 v183, 0x3d372713, v125
	v_mul_f32_e32 v179, v129, v179
	v_mul_f32_e32 v183, v125, v183
	v_fma_f32 v179, v129, v179, v129
	v_fma_f32 v183, v125, v183, v125
	v_mul_f32_e32 v179, 0x3fcc422a, v179
	v_mul_f32_e32 v183, 0x3fcc422a, v183
	v_mul_f32_e32 v179, 0xbfb8aa3b, v179
	v_mul_f32_e32 v183, 0xbfb8aa3b, v183
	v_exp_f32_e32 v179, v179
	v_exp_f32_e32 v183, v183
	v_rcp_f32_e32 v186, v115
	v_lshl_or_b32 v166, s19, 8, v173
	v_add_f32_e32 v115, 1.0, v179
	v_add_f32_e32 v179, 1.0, v183
	v_mul_f32_e32 v183, 0x3d372713, v121
	v_mul_f32_e32 v183, v121, v183
	v_fma_f32 v183, v121, v183, v121
	v_mul_f32_e32 v183, 0x3fcc422a, v183
	v_mul_f32_e32 v183, 0xbfb8aa3b, v183
	v_exp_f32_e32 v185, v183
	v_mul_f32_e32 v183, 0x3d372713, v117
	v_mul_f32_e32 v183, v117, v183
	v_fma_f32 v183, v117, v183, v117
	v_mul_f32_e32 v183, 0x3fcc422a, v183
	v_mul_f32_e32 v183, 0xbfb8aa3b, v183
	v_exp_f32_e32 v187, v183
	v_rcp_f32_e32 v183, v179
	v_add_f32_e32 v179, 1.0, v185
	v_rcp_f32_e32 v185, v179
	v_rcp_f32_e32 v114, v114
	v_rcp_f32_e32 v115, v115
	v_ashrrev_i32_e32 v166, 4, v166
	s_ashr_i32 s19, s18, 31
	s_lshl_b64 s[18:19], s[18:19], 13
	v_ashrrev_i32_e32 v167, 31, v166
	v_add_f32_e32 v179, 1.0, v187
	v_pk_mul_f32 v[120:121], v[120:121], v[184:185]
	v_lshl_add_u64 v[166:167], s[18:19], 0, v[166:167]
	v_rcp_f32_e32 v187, v179
	v_cvt_pk_bf16_f32 v118, v118, v119
	v_cvt_pk_bf16_f32 v119, v120, v121
	v_mul_f32_e32 v121, 0x3d372713, v110
	s_lshl_b32 s18, s62, 4
	v_pk_mul_f32 v[128:129], v[128:129], v[114:115]
	v_lshl_add_u64 v[114:115], v[166:167], 0, v[146:147]
	v_mul_f32_e32 v121, v110, v121
	s_ashr_i32 s19, s18, 31
	v_lshlrev_b64 v[114:115], 10, v[114:115]
	v_fma_f32 v121, v110, v121, v110
	v_pk_mul_f32 v[124:125], v[124:125], v[182:183]
	v_lshl_add_u64 v[114:115], s[6:7], 0, v[114:115]
	s_lshl_b64 s[18:19], s[18:19], 1
	v_mul_f32_e32 v121, 0x3fcc422a, v121
	v_pk_mul_f32 v[182:183], v[116:117], v[186:187]
	v_lshl_add_u64 v[184:185], v[114:115], 0, s[18:19]
	v_cvt_pk_bf16_f32 v114, v126, v127
	v_cvt_pk_bf16_f32 v115, v128, v129
	v_cvt_pk_bf16_f32 v116, v122, v123
	v_cvt_pk_bf16_f32 v117, v124, v125
	v_mul_f32_e32 v121, 0xbfb8aa3b, v121
	v_cvt_pk_bf16_f32 v120, v180, v181
	v_exp_f32_e32 v122, v121
	v_cvt_pk_bf16_f32 v121, v182, v183
	flat_store_dwordx4 v[184:185], v[114:117]
; __device__ __forceinline__ float gelu_tanh(float x) { return x * fsigmoid(1.5957691216f * (x + 0.044715f * x * x * x)); }
;     __device__ __forceinline__ void operator()(AccRef acc, const GUnit& u, int wr, int wc, int fr, int fq) const {
;         const int g = u.x0, b = u.x1, pn = u.x2; const int tt = (pn * 256 + wc * 64 + 16 * fq) >> 4;
; #pragma unroll
;         for (int ai = 0; ai < 2; ++ai)
; #pragma unroll
;             for (int m = 0; m < 4; ++m) { const int ch = ai * 128 + wr * 64 + m * 16 + fr; const size_t tok = (size_t)b * SEQ + ch * LC + tt;
;                 f32x4 v0 = acc[ai][0][m][0], v1 = acc[ai][0][m][1], v2 = acc[ai][1][m][0], v3 = acc[ai][1][m][1];
; #pragma unroll
;                 for (int j = 0; j < 4; ++j) { v0[j] = gelu_tanh(v0[j]); v1[j] = gelu_tanh(v1[j]); v2[j] = gelu_tanh(v2[j]); v3[j] = gelu_tanh(v3[j]); }
;                 st16_bf16(YS + tok * SW + g * 16, v0, v1, v2, v3); }
	flat_store_dwordx4 v[184:185], v[118:121] offset:16
	s_andn2_b64 vcc, exec, s[16:17]
	v_mul_f32_e32 v115, 0x3d372713, v106
	v_mul_f32_e32 v115, v106, v115
	v_mul_f32_e32 v116, 0x3d372713, v102
	v_fma_f32 v115, v106, v115, v106
	v_mul_f32_e32 v116, v102, v116
	v_mul_f32_e32 v115, 0x3fcc422a, v115
	v_fma_f32 v116, v102, v116, v102
	v_mul_f32_e32 v115, 0xbfb8aa3b, v115
	v_mul_f32_e32 v116, 0x3fcc422a, v116
	v_exp_f32_e32 v115, v115
	v_mul_f32_e32 v116, 0xbfb8aa3b, v116
	v_exp_f32_e32 v117, v116
	v_mul_f32_e32 v118, 0x3d372713, v111
	v_add_f32_e32 v115, 1.0, v115
	v_rcp_f32_e32 v116, v115
	v_add_f32_e32 v115, 1.0, v117
	v_mul_f32_e32 v117, 0x3d372713, v98
	v_mul_f32_e32 v117, v98, v117
	v_fma_f32 v117, v98, v117, v98
	v_mul_f32_e32 v117, 0x3fcc422a, v117
	v_mul_f32_e32 v117, 0xbfb8aa3b, v117
	v_mul_f32_e32 v118, v111, v118
	v_exp_f32_e32 v117, v117
	v_fma_f32 v118, v111, v118, v111
	v_mul_f32_e32 v118, 0x3fcc422a, v118
	v_mul_f32_e32 v118, 0xbfb8aa3b, v118
	v_exp_f32_e32 v119, v118
	v_mul_f32_e32 v121, 0x3d372713, v99
	v_rcp_f32_e32 v118, v115
	v_add_f32_e32 v115, 1.0, v117
	v_mul_f32_e32 v117, 0x3d372713, v107
	v_mul_f32_e32 v121, v99, v121
	v_mul_f32_e32 v117, v107, v117
	v_fma_f32 v121, v99, v121, v99
	v_fma_f32 v117, v107, v117, v107
	v_mul_f32_e32 v121, 0x3fcc422a, v121
	v_add_f32_e32 v114, 1.0, v122
	v_rcp_f32_e32 v120, v115
	v_add_f32_e32 v115, 1.0, v119
	v_mul_f32_e32 v117, 0x3fcc422a, v117
	v_mul_f32_e32 v121, 0xbfb8aa3b, v121
	v_rcp_f32_e32 v114, v114
	v_mul_f32_e32 v117, 0xbfb8aa3b, v117
	v_rcp_f32_e32 v115, v115
	v_exp_f32_e32 v121, v121
	v_exp_f32_e32 v117, v117
	v_mul_f32_e32 v119, 0x3d372713, v103
	v_pk_mul_f32 v[110:111], v[110:111], v[114:115]
	v_add_f32_e32 v114, 1.0, v121
	v_add_f32_e32 v117, 1.0, v117
	v_rcp_f32_e32 v121, v114
	v_mul_f32_e32 v114, 0x3d372713, v112
	v_rcp_f32_e32 v117, v117
	v_mul_f32_e32 v114, v112, v114
	v_fma_f32 v114, v112, v114, v112
	v_mul_f32_e32 v114, 0x3fcc422a, v114
	v_mul_f32_e32 v114, 0xbfb8aa3b, v114
	v_pk_mul_f32 v[106:107], v[106:107], v[116:117]
	v_exp_f32_e32 v116, v114
	v_mul_f32_e32 v114, 0x3d372713, v108
	v_mul_f32_e32 v114, v108, v114
	v_mul_f32_e32 v119, v103, v119
	v_fma_f32 v114, v108, v114, v108
	v_fma_f32 v119, v103, v119, v103
	v_mul_f32_e32 v114, 0x3fcc422a, v114
	v_mul_f32_e32 v119, 0x3fcc422a, v119
	v_mul_f32_e32 v114, 0xbfb8aa3b, v114
	v_mul_f32_e32 v119, 0xbfb8aa3b, v119
	v_exp_f32_e32 v117, v114
	v_pk_mul_f32 v[114:115], v[98:99], v[120:121]
	v_add_f32_e32 v98, 1.0, v116
	v_mul_f32_e32 v116, 0x3d372713, v104
	v_exp_f32_e32 v119, v119
	v_mul_f32_e32 v116, v104, v116
	v_fma_f32 v116, v104, v116, v104
	v_mul_f32_e32 v116, 0x3fcc422a, v116
	v_mul_f32_e32 v116, 0xbfb8aa3b, v116
	v_add_f32_e32 v119, 1.0, v119
	v_add_f32_e32 v99, 1.0, v117
	v_exp_f32_e32 v117, v116
	v_mul_f32_e32 v116, 0x3d372713, v100
	v_rcp_f32_e32 v119, v119
	v_mul_f32_e32 v116, v100, v116
	v_fma_f32 v116, v100, v116, v100
	v_mul_f32_e32 v116, 0x3fcc422a, v116
	v_mul_f32_e32 v116, 0xbfb8aa3b, v116
	v_pk_mul_f32 v[102:103], v[102:103], v[118:119]
	v_exp_f32_e32 v119, v116
	v_rcp_f32_e32 v116, v99
	v_add_f32_e32 v99, 1.0, v117
	v_rcp_f32_e32 v118, v99
	v_add_f32_e32 v99, 1.0, v119
	v_mul_f32_e32 v117, 0x3d372713, v113
	v_mul_f32_e32 v119, 0x3d372713, v109
	v_mul_f32_e32 v117, v113, v117
	v_mul_f32_e32 v119, v109, v119
	v_fma_f32 v117, v113, v117, v113
	v_fma_f32 v119, v109, v119, v109
	v_mul_f32_e32 v117, 0x3fcc422a, v117
	v_mul_f32_e32 v119, 0x3fcc422a, v119
	v_mul_f32_e32 v117, 0xbfb8aa3b, v117
	v_mul_f32_e32 v119, 0xbfb8aa3b, v119
	v_exp_f32_e32 v117, v117
	v_exp_f32_e32 v119, v119
	v_rcp_f32_e32 v120, v99
	v_mul_f32_e32 v121, 0x3d372713, v101
	v_add_f32_e32 v99, 1.0, v117
	v_add_f32_e32 v117, 1.0, v119
	v_mul_f32_e32 v119, 0x3d372713, v105
	v_mul_f32_e32 v119, v105, v119
	v_fma_f32 v119, v105, v119, v105
	v_mul_f32_e32 v119, 0x3fcc422a, v119
	v_mul_f32_e32 v119, 0xbfb8aa3b, v119
	v_exp_f32_e32 v119, v119
	v_mul_f32_e32 v121, v101, v121
	v_fma_f32 v121, v101, v121, v101
	v_mul_f32_e32 v121, 0x3fcc422a, v121
	v_mul_f32_e32 v121, 0xbfb8aa3b, v121
	v_add_f32_e32 v119, 1.0, v119
	v_exp_f32_e32 v121, v121
	v_rcp_f32_e32 v119, v119
	v_rcp_f32_e32 v98, v98
	v_rcp_f32_e32 v99, v99
	v_rcp_f32_e32 v117, v117
	v_add_f32_e32 v121, 1.0, v121
	v_pk_mul_f32 v[104:105], v[104:105], v[118:119]
	v_rcp_f32_e32 v121, v121
	v_cvt_pk_bf16_f32 v102, v102, v103
	v_cvt_pk_bf16_f32 v103, v104, v105
	v_mul_f32_e32 v105, 0x3d372713, v94
	v_pk_mul_f32 v[112:113], v[112:113], v[98:99]
	v_lshl_add_u64 v[98:99], v[166:167], 0, v[148:149]
	v_mul_f32_e32 v105, v94, v105
	v_lshlrev_b64 v[98:99], 10, v[98:99]
	v_fma_f32 v105, v94, v105, v94
	v_pk_mul_f32 v[108:109], v[108:109], v[116:117]
	v_lshl_add_u64 v[98:99], s[6:7], 0, v[98:99]
	v_mul_f32_e32 v105, 0x3fcc422a, v105
	v_pk_mul_f32 v[116:117], v[100:101], v[120:121]
	v_lshl_add_u64 v[118:119], v[98:99], 0, s[18:19]
	v_cvt_pk_bf16_f32 v98, v110, v111
	v_cvt_pk_bf16_f32 v99, v112, v113
	v_cvt_pk_bf16_f32 v100, v106, v107
	v_cvt_pk_bf16_f32 v101, v108, v109
	v_mul_f32_e32 v105, 0xbfb8aa3b, v105
	v_cvt_pk_bf16_f32 v104, v114, v115
	v_exp_f32_e32 v106, v105
	v_cvt_pk_bf16_f32 v105, v116, v117
	flat_store_dwordx4 v[118:119], v[98:101]
	flat_store_dwordx4 v[118:119], v[102:105] offset:16
	s_mov_b64 s[16:17], -1
	v_mul_f32_e32 v99, 0x3d372713, v90
	v_mul_f32_e32 v99, v90, v99
	v_mul_f32_e32 v100, 0x3d372713, v86
	v_fma_f32 v99, v90, v99, v90
	v_mul_f32_e32 v100, v86, v100
	v_mul_f32_e32 v99, 0x3fcc422a, v99
	v_fma_f32 v100, v86, v100, v86
	v_mul_f32_e32 v99, 0xbfb8aa3b, v99
	v_mul_f32_e32 v100, 0x3fcc422a, v100
	v_exp_f32_e32 v99, v99
	v_mul_f32_e32 v100, 0xbfb8aa3b, v100
	v_exp_f32_e32 v101, v100
; __device__ __forceinline__ float gelu_tanh(float x) { return x * fsigmoid(1.5957691216f * (x + 0.044715f * x * x * x)); }
;     __device__ __forceinline__ void operator()(AccRef acc, const GUnit& u, int wr, int wc, int fr, int fq) const {
;         const int g = u.x0, b = u.x1, pn = u.x2; const int tt = (pn * 256 + wc * 64 + 16 * fq) >> 4;
; #pragma unroll
;         for (int ai = 0; ai < 2; ++ai)
; #pragma unroll
;             for (int m = 0; m < 4; ++m) { const int ch = ai * 128 + wr * 64 + m * 16 + fr; const size_t tok = (size_t)b * SEQ + ch * LC + tt;
;                 f32x4 v0 = acc[ai][0][m][0], v1 = acc[ai][0][m][1], v2 = acc[ai][1][m][0], v3 = acc[ai][1][m][1];
; #pragma unroll
;                 for (int j = 0; j < 4; ++j) { v0[j] = gelu_tanh(v0[j]); v1[j] = gelu_tanh(v1[j]); v2[j] = gelu_tanh(v2[j]); v3[j] = gelu_tanh(v3[j]); }
;                 st16_bf16(YS + tok * SW + g * 16, v0, v1, v2, v3); }
	v_mul_f32_e32 v102, 0x3d372713, v95
	v_add_f32_e32 v99, 1.0, v99
	v_rcp_f32_e32 v100, v99
	v_add_f32_e32 v99, 1.0, v101
	v_mul_f32_e32 v101, 0x3d372713, v82
	v_mul_f32_e32 v101, v82, v101
	v_fma_f32 v101, v82, v101, v82
	v_mul_f32_e32 v101, 0x3fcc422a, v101
	v_mul_f32_e32 v101, 0xbfb8aa3b, v101
	v_mul_f32_e32 v102, v95, v102
	v_exp_f32_e32 v101, v101
	v_fma_f32 v102, v95, v102, v95
	v_mul_f32_e32 v102, 0x3fcc422a, v102
	v_mul_f32_e32 v102, 0xbfb8aa3b, v102
	v_exp_f32_e32 v103, v102
	v_mul_f32_e32 v105, 0x3d372713, v83
	v_rcp_f32_e32 v102, v99
	v_add_f32_e32 v99, 1.0, v101
	v_mul_f32_e32 v101, 0x3d372713, v91
	v_mul_f32_e32 v105, v83, v105
	v_mul_f32_e32 v101, v91, v101
	v_fma_f32 v105, v83, v105, v83
	v_fma_f32 v101, v91, v101, v91
	v_mul_f32_e32 v105, 0x3fcc422a, v105
	v_add_f32_e32 v98, 1.0, v106
	v_rcp_f32_e32 v104, v99
	v_add_f32_e32 v99, 1.0, v103
	v_mul_f32_e32 v101, 0x3fcc422a, v101
	v_mul_f32_e32 v105, 0xbfb8aa3b, v105
	v_rcp_f32_e32 v98, v98
	v_mul_f32_e32 v101, 0xbfb8aa3b, v101
	v_rcp_f32_e32 v99, v99
	v_exp_f32_e32 v105, v105
	v_exp_f32_e32 v101, v101
	v_mul_f32_e32 v103, 0x3d372713, v87
	v_pk_mul_f32 v[94:95], v[94:95], v[98:99]
	v_add_f32_e32 v98, 1.0, v105
	v_add_f32_e32 v101, 1.0, v101
	v_rcp_f32_e32 v105, v98
	v_mul_f32_e32 v98, 0x3d372713, v96
	v_rcp_f32_e32 v101, v101
	v_mul_f32_e32 v98, v96, v98
	v_fma_f32 v98, v96, v98, v96
	v_mul_f32_e32 v98, 0x3fcc422a, v98
	v_mul_f32_e32 v98, 0xbfb8aa3b, v98
	v_pk_mul_f32 v[90:91], v[90:91], v[100:101]
	v_exp_f32_e32 v100, v98
	v_mul_f32_e32 v98, 0x3d372713, v92
	v_mul_f32_e32 v98, v92, v98
	v_mul_f32_e32 v103, v87, v103
	v_fma_f32 v98, v92, v98, v92
	v_fma_f32 v103, v87, v103, v87
	v_mul_f32_e32 v98, 0x3fcc422a, v98
	v_mul_f32_e32 v103, 0x3fcc422a, v103
	v_mul_f32_e32 v98, 0xbfb8aa3b, v98
	v_mul_f32_e32 v103, 0xbfb8aa3b, v103
	v_exp_f32_e32 v101, v98
	v_pk_mul_f32 v[98:99], v[82:83], v[104:105]
	v_add_f32_e32 v82, 1.0, v100
	v_mul_f32_e32 v100, 0x3d372713, v88
	v_exp_f32_e32 v103, v103
	v_mul_f32_e32 v100, v88, v100
	v_fma_f32 v100, v88, v100, v88
	v_mul_f32_e32 v100, 0x3fcc422a, v100
	v_mul_f32_e32 v100, 0xbfb8aa3b, v100
	v_add_f32_e32 v103, 1.0, v103
	v_add_f32_e32 v83, 1.0, v101
	v_exp_f32_e32 v101, v100
	v_mul_f32_e32 v100, 0x3d372713, v84
	v_rcp_f32_e32 v103, v103
	v_mul_f32_e32 v100, v84, v100
	v_fma_f32 v100, v84, v100, v84
	v_mul_f32_e32 v100, 0x3fcc422a, v100
	v_mul_f32_e32 v100, 0xbfb8aa3b, v100
	v_pk_mul_f32 v[86:87], v[86:87], v[102:103]
	v_exp_f32_e32 v103, v100
	v_rcp_f32_e32 v100, v83
	v_add_f32_e32 v83, 1.0, v101
	v_rcp_f32_e32 v102, v83
	v_add_f32_e32 v83, 1.0, v103
	v_mul_f32_e32 v101, 0x3d372713, v97
	v_mul_f32_e32 v103, 0x3d372713, v93
	v_mul_f32_e32 v101, v97, v101
	v_mul_f32_e32 v103, v93, v103
	v_fma_f32 v101, v97, v101, v97
	v_fma_f32 v103, v93, v103, v93
	v_mul_f32_e32 v101, 0x3fcc422a, v101
	v_mul_f32_e32 v103, 0x3fcc422a, v103
	v_mul_f32_e32 v101, 0xbfb8aa3b, v101
	v_mul_f32_e32 v103, 0xbfb8aa3b, v103
	v_exp_f32_e32 v101, v101
	v_exp_f32_e32 v103, v103
	v_rcp_f32_e32 v104, v83
	v_mul_f32_e32 v105, 0x3d372713, v85
	v_add_f32_e32 v83, 1.0, v101
	v_add_f32_e32 v101, 1.0, v103
	v_mul_f32_e32 v103, 0x3d372713, v89
	v_mul_f32_e32 v103, v89, v103
	v_fma_f32 v103, v89, v103, v89
	v_mul_f32_e32 v103, 0x3fcc422a, v103
	v_mul_f32_e32 v103, 0xbfb8aa3b, v103
	v_exp_f32_e32 v103, v103
	v_mul_f32_e32 v105, v85, v105
	v_fma_f32 v105, v85, v105, v85
	v_mul_f32_e32 v105, 0x3fcc422a, v105
	v_mul_f32_e32 v105, 0xbfb8aa3b, v105
	v_add_f32_e32 v103, 1.0, v103
	v_exp_f32_e32 v105, v105
	v_rcp_f32_e32 v103, v103
	v_rcp_f32_e32 v82, v82
	v_rcp_f32_e32 v83, v83
	v_rcp_f32_e32 v101, v101
	v_add_f32_e32 v105, 1.0, v105
	v_pk_mul_f32 v[88:89], v[88:89], v[102:103]
	v_rcp_f32_e32 v105, v105
	v_cvt_pk_bf16_f32 v86, v86, v87
	v_cvt_pk_bf16_f32 v87, v88, v89
	v_mul_f32_e32 v89, 0x3d372713, v78
	v_pk_mul_f32 v[96:97], v[96:97], v[82:83]
	v_lshl_add_u64 v[82:83], v[166:167], 0, v[150:151]
	v_mul_f32_e32 v89, v78, v89
	v_lshlrev_b64 v[82:83], 10, v[82:83]
	v_fma_f32 v89, v78, v89, v78
	v_pk_mul_f32 v[92:93], v[92:93], v[100:101]
	v_lshl_add_u64 v[82:83], s[6:7], 0, v[82:83]
	v_mul_f32_e32 v89, 0x3fcc422a, v89
	v_pk_mul_f32 v[100:101], v[84:85], v[104:105]
	v_lshl_add_u64 v[102:103], v[82:83], 0, s[18:19]
	v_cvt_pk_bf16_f32 v82, v94, v95
	v_cvt_pk_bf16_f32 v83, v96, v97
	v_cvt_pk_bf16_f32 v84, v90, v91
	v_cvt_pk_bf16_f32 v85, v92, v93
	v_mul_f32_e32 v89, 0xbfb8aa3b, v89
	v_cvt_pk_bf16_f32 v88, v98, v99
	v_exp_f32_e32 v90, v89
	v_cvt_pk_bf16_f32 v89, v100, v101
	flat_store_dwordx4 v[102:103], v[82:85]
	flat_store_dwordx4 v[102:103], v[86:89] offset:16
	s_nop 0
	v_mul_f32_e32 v83, 0x3d372713, v74
	v_mul_f32_e32 v83, v74, v83
	v_mul_f32_e32 v84, 0x3d372713, v70
	v_fma_f32 v83, v74, v83, v74
	v_mul_f32_e32 v84, v70, v84
	v_mul_f32_e32 v83, 0x3fcc422a, v83
	v_fma_f32 v84, v70, v84, v70
	v_mul_f32_e32 v83, 0xbfb8aa3b, v83
	v_mul_f32_e32 v84, 0x3fcc422a, v84
	v_exp_f32_e32 v83, v83
	v_mul_f32_e32 v84, 0xbfb8aa3b, v84
	v_exp_f32_e32 v85, v84
	v_mul_f32_e32 v86, 0x3d372713, v79
	v_add_f32_e32 v83, 1.0, v83
	v_rcp_f32_e32 v84, v83
	v_add_f32_e32 v83, 1.0, v85
	v_mul_f32_e32 v85, 0x3d372713, v66
	v_mul_f32_e32 v85, v66, v85
	v_fma_f32 v85, v66, v85, v66
	v_mul_f32_e32 v85, 0x3fcc422a, v85
	v_mul_f32_e32 v85, 0xbfb8aa3b, v85
	v_mul_f32_e32 v86, v79, v86
	v_exp_f32_e32 v85, v85
	v_fma_f32 v86, v79, v86, v79
	v_mul_f32_e32 v86, 0x3fcc422a, v86
	v_mul_f32_e32 v86, 0xbfb8aa3b, v86
	v_exp_f32_e32 v87, v86
	v_mul_f32_e32 v89, 0x3d372713, v67
	v_rcp_f32_e32 v86, v83
	v_add_f32_e32 v83, 1.0, v85
	v_mul_f32_e32 v85, 0x3d372713, v75
	v_mul_f32_e32 v89, v67, v89
	v_mul_f32_e32 v85, v75, v85
	v_fma_f32 v89, v67, v89, v67
; __device__ __forceinline__ float gelu_tanh(float x) { return x * fsigmoid(1.5957691216f * (x + 0.044715f * x * x * x)); }
;     __device__ __forceinline__ void operator()(AccRef acc, const GUnit& u, int wr, int wc, int fr, int fq) const {
;         const int g = u.x0, b = u.x1, pn = u.x2; const int tt = (pn * 256 + wc * 64 + 16 * fq) >> 4;
; #pragma unroll
;         for (int ai = 0; ai < 2; ++ai)
; #pragma unroll
;             for (int m = 0; m < 4; ++m) { const int ch = ai * 128 + wr * 64 + m * 16 + fr; const size_t tok = (size_t)b * SEQ + ch * LC + tt;
;                 f32x4 v0 = acc[ai][0][m][0], v1 = acc[ai][0][m][1], v2 = acc[ai][1][m][0], v3 = acc[ai][1][m][1];
; #pragma unroll
;                 for (int j = 0; j < 4; ++j) { v0[j] = gelu_tanh(v0[j]); v1[j] = gelu_tanh(v1[j]); v2[j] = gelu_tanh(v2[j]); v3[j] = gelu_tanh(v3[j]); }
;                 st16_bf16(YS + tok * SW + g * 16, v0, v1, v2, v3); }
	v_fma_f32 v85, v75, v85, v75
	v_mul_f32_e32 v89, 0x3fcc422a, v89
	v_add_f32_e32 v82, 1.0, v90
	v_rcp_f32_e32 v88, v83
	v_add_f32_e32 v83, 1.0, v87
	v_mul_f32_e32 v85, 0x3fcc422a, v85
	v_mul_f32_e32 v89, 0xbfb8aa3b, v89
	v_rcp_f32_e32 v82, v82
	v_mul_f32_e32 v85, 0xbfb8aa3b, v85
	v_rcp_f32_e32 v83, v83
	v_exp_f32_e32 v89, v89
	v_exp_f32_e32 v85, v85
	v_mul_f32_e32 v87, 0x3d372713, v71
	v_pk_mul_f32 v[78:79], v[78:79], v[82:83]
	v_add_f32_e32 v82, 1.0, v89
	v_add_f32_e32 v85, 1.0, v85
	v_rcp_f32_e32 v89, v82
	v_mul_f32_e32 v82, 0x3d372713, v80
	v_rcp_f32_e32 v85, v85
	v_mul_f32_e32 v82, v80, v82
	v_fma_f32 v82, v80, v82, v80
	v_mul_f32_e32 v82, 0x3fcc422a, v82
	v_mul_f32_e32 v82, 0xbfb8aa3b, v82
	v_pk_mul_f32 v[74:75], v[74:75], v[84:85]
	v_exp_f32_e32 v84, v82
	v_mul_f32_e32 v82, 0x3d372713, v76
	v_mul_f32_e32 v82, v76, v82
	v_mul_f32_e32 v87, v71, v87
	v_fma_f32 v82, v76, v82, v76
	v_fma_f32 v87, v71, v87, v71
	v_mul_f32_e32 v82, 0x3fcc422a, v82
	v_mul_f32_e32 v87, 0x3fcc422a, v87
	v_mul_f32_e32 v82, 0xbfb8aa3b, v82
	v_mul_f32_e32 v87, 0xbfb8aa3b, v87
	v_exp_f32_e32 v85, v82
	v_pk_mul_f32 v[82:83], v[66:67], v[88:89]
	v_add_f32_e32 v66, 1.0, v84
	v_mul_f32_e32 v84, 0x3d372713, v72
	v_exp_f32_e32 v87, v87
	v_mul_f32_e32 v84, v72, v84
	v_fma_f32 v84, v72, v84, v72
	v_mul_f32_e32 v84, 0x3fcc422a, v84
	v_mul_f32_e32 v84, 0xbfb8aa3b, v84
	v_add_f32_e32 v87, 1.0, v87
	v_add_f32_e32 v67, 1.0, v85
	v_exp_f32_e32 v85, v84
	v_mul_f32_e32 v84, 0x3d372713, v68
	v_rcp_f32_e32 v87, v87
	v_mul_f32_e32 v84, v68, v84
	v_fma_f32 v84, v68, v84, v68
	v_mul_f32_e32 v84, 0x3fcc422a, v84
	v_mul_f32_e32 v84, 0xbfb8aa3b, v84
	v_pk_mul_f32 v[70:71], v[70:71], v[86:87]
	v_exp_f32_e32 v87, v84
	v_rcp_f32_e32 v84, v67
	v_add_f32_e32 v67, 1.0, v85
	v_rcp_f32_e32 v86, v67
	v_add_f32_e32 v67, 1.0, v87
	v_mul_f32_e32 v85, 0x3d372713, v81
	v_mul_f32_e32 v87, 0x3d372713, v77
	v_mul_f32_e32 v85, v81, v85
	v_mul_f32_e32 v87, v77, v87
	v_fma_f32 v85, v81, v85, v81
	v_fma_f32 v87, v77, v87, v77
	v_mul_f32_e32 v85, 0x3fcc422a, v85
	v_mul_f32_e32 v87, 0x3fcc422a, v87
	v_mul_f32_e32 v85, 0xbfb8aa3b, v85
	v_mul_f32_e32 v87, 0xbfb8aa3b, v87
	v_exp_f32_e32 v85, v85
	v_exp_f32_e32 v87, v87
	v_rcp_f32_e32 v88, v67
	v_mul_f32_e32 v89, 0x3d372713, v69
	v_add_f32_e32 v67, 1.0, v85
	v_add_f32_e32 v85, 1.0, v87
	v_mul_f32_e32 v87, 0x3d372713, v73
	v_mul_f32_e32 v87, v73, v87
	v_fma_f32 v87, v73, v87, v73
	v_mul_f32_e32 v87, 0x3fcc422a, v87
	v_mul_f32_e32 v87, 0xbfb8aa3b, v87
	v_exp_f32_e32 v87, v87
	v_mul_f32_e32 v89, v69, v89
	v_fma_f32 v89, v69, v89, v69
	v_mul_f32_e32 v89, 0x3fcc422a, v89
	v_mul_f32_e32 v89, 0xbfb8aa3b, v89
	v_add_f32_e32 v87, 1.0, v87
	v_exp_f32_e32 v89, v89
	v_rcp_f32_e32 v87, v87
	v_rcp_f32_e32 v66, v66
	v_rcp_f32_e32 v67, v67
	v_rcp_f32_e32 v85, v85
	v_add_f32_e32 v89, 1.0, v89
	v_pk_mul_f32 v[72:73], v[72:73], v[86:87]
	v_rcp_f32_e32 v89, v89
	v_cvt_pk_bf16_f32 v70, v70, v71
	v_cvt_pk_bf16_f32 v71, v72, v73
	v_mul_f32_e32 v73, 0x3d372713, v62
	v_pk_mul_f32 v[80:81], v[80:81], v[66:67]
	v_lshl_add_u64 v[66:67], v[166:167], 0, v[152:153]
	v_mul_f32_e32 v73, v62, v73
	v_lshlrev_b64 v[66:67], 10, v[66:67]
	v_fma_f32 v73, v62, v73, v62
	v_pk_mul_f32 v[76:77], v[76:77], v[84:85]
	v_lshl_add_u64 v[66:67], s[6:7], 0, v[66:67]
	v_mul_f32_e32 v73, 0x3fcc422a, v73
	v_pk_mul_f32 v[84:85], v[68:69], v[88:89]
	v_lshl_add_u64 v[86:87], v[66:67], 0, s[18:19]
	v_cvt_pk_bf16_f32 v66, v78, v79
	v_cvt_pk_bf16_f32 v67, v80, v81
	v_cvt_pk_bf16_f32 v68, v74, v75
	v_cvt_pk_bf16_f32 v69, v76, v77
	v_mul_f32_e32 v73, 0xbfb8aa3b, v73
	v_cvt_pk_bf16_f32 v72, v82, v83
	v_exp_f32_e32 v74, v73
	v_cvt_pk_bf16_f32 v73, v84, v85
	flat_store_dwordx4 v[86:87], v[66:69]
	flat_store_dwordx4 v[86:87], v[70:73] offset:16
	s_nop 0
	v_mul_f32_e32 v67, 0x3d372713, v58
	v_mul_f32_e32 v67, v58, v67
	v_mul_f32_e32 v68, 0x3d372713, v54
	v_fma_f32 v67, v58, v67, v58
	v_mul_f32_e32 v68, v54, v68
	v_mul_f32_e32 v67, 0x3fcc422a, v67
	v_fma_f32 v68, v54, v68, v54
	v_mul_f32_e32 v67, 0xbfb8aa3b, v67
	v_mul_f32_e32 v68, 0x3fcc422a, v68
	v_exp_f32_e32 v67, v67
	v_mul_f32_e32 v68, 0xbfb8aa3b, v68
	v_exp_f32_e32 v69, v68
	v_mul_f32_e32 v70, 0x3d372713, v63
	v_add_f32_e32 v67, 1.0, v67
	v_rcp_f32_e32 v68, v67
	v_add_f32_e32 v67, 1.0, v69
	v_mul_f32_e32 v69, 0x3d372713, v50
	v_mul_f32_e32 v69, v50, v69
	v_fma_f32 v69, v50, v69, v50
	v_mul_f32_e32 v69, 0x3fcc422a, v69
	v_mul_f32_e32 v69, 0xbfb8aa3b, v69
	v_mul_f32_e32 v70, v63, v70
	v_exp_f32_e32 v69, v69
	v_fma_f32 v70, v63, v70, v63
	v_mul_f32_e32 v70, 0x3fcc422a, v70
	v_mul_f32_e32 v70, 0xbfb8aa3b, v70
	v_exp_f32_e32 v71, v70
	v_mul_f32_e32 v73, 0x3d372713, v51
	v_rcp_f32_e32 v70, v67
	v_add_f32_e32 v67, 1.0, v69
	v_mul_f32_e32 v69, 0x3d372713, v59
	v_mul_f32_e32 v73, v51, v73
	v_mul_f32_e32 v69, v59, v69
	v_fma_f32 v73, v51, v73, v51
	v_fma_f32 v69, v59, v69, v59
	v_mul_f32_e32 v73, 0x3fcc422a, v73
	v_add_f32_e32 v66, 1.0, v74
	v_rcp_f32_e32 v72, v67
	v_add_f32_e32 v67, 1.0, v71
	v_mul_f32_e32 v69, 0x3fcc422a, v69
	v_mul_f32_e32 v73, 0xbfb8aa3b, v73
	v_rcp_f32_e32 v66, v66
	v_mul_f32_e32 v69, 0xbfb8aa3b, v69
	v_rcp_f32_e32 v67, v67
	v_exp_f32_e32 v73, v73
	v_exp_f32_e32 v69, v69
	v_mul_f32_e32 v71, 0x3d372713, v55
	v_pk_mul_f32 v[62:63], v[62:63], v[66:67]
	v_add_f32_e32 v66, 1.0, v73
	v_add_f32_e32 v69, 1.0, v69
	v_rcp_f32_e32 v73, v66
	v_mul_f32_e32 v66, 0x3d372713, v64
	v_rcp_f32_e32 v69, v69
	v_mul_f32_e32 v66, v64, v66
	v_fma_f32 v66, v64, v66, v64
	v_mul_f32_e32 v66, 0x3fcc422a, v66
	v_mul_f32_e32 v66, 0xbfb8aa3b, v66
	v_pk_mul_f32 v[58:59], v[58:59], v[68:69]
	v_exp_f32_e32 v68, v66
	v_mul_f32_e32 v66, 0x3d372713, v60
	v_mul_f32_e32 v66, v60, v66
; __device__ __forceinline__ float gelu_tanh(float x) { return x * fsigmoid(1.5957691216f * (x + 0.044715f * x * x * x)); }
;     __device__ __forceinline__ void operator()(AccRef acc, const GUnit& u, int wr, int wc, int fr, int fq) const {
;         const int g = u.x0, b = u.x1, pn = u.x2; const int tt = (pn * 256 + wc * 64 + 16 * fq) >> 4;
; #pragma unroll
;         for (int ai = 0; ai < 2; ++ai)
; #pragma unroll
;             for (int m = 0; m < 4; ++m) { const int ch = ai * 128 + wr * 64 + m * 16 + fr; const size_t tok = (size_t)b * SEQ + ch * LC + tt;
;                 f32x4 v0 = acc[ai][0][m][0], v1 = acc[ai][0][m][1], v2 = acc[ai][1][m][0], v3 = acc[ai][1][m][1];
; #pragma unroll
;                 for (int j = 0; j < 4; ++j) { v0[j] = gelu_tanh(v0[j]); v1[j] = gelu_tanh(v1[j]); v2[j] = gelu_tanh(v2[j]); v3[j] = gelu_tanh(v3[j]); }
;                 st16_bf16(YS + tok * SW + g * 16, v0, v1, v2, v3); }
	v_mul_f32_e32 v71, v55, v71
	v_fma_f32 v66, v60, v66, v60
	v_fma_f32 v71, v55, v71, v55
	v_mul_f32_e32 v66, 0x3fcc422a, v66
	v_mul_f32_e32 v71, 0x3fcc422a, v71
	v_mul_f32_e32 v66, 0xbfb8aa3b, v66
	v_mul_f32_e32 v71, 0xbfb8aa3b, v71
	v_exp_f32_e32 v69, v66
	v_pk_mul_f32 v[66:67], v[50:51], v[72:73]
	v_add_f32_e32 v50, 1.0, v68
	v_mul_f32_e32 v68, 0x3d372713, v56
	v_exp_f32_e32 v71, v71
	v_mul_f32_e32 v68, v56, v68
	v_fma_f32 v68, v56, v68, v56
	v_mul_f32_e32 v68, 0x3fcc422a, v68
	v_mul_f32_e32 v68, 0xbfb8aa3b, v68
	v_add_f32_e32 v71, 1.0, v71
	v_add_f32_e32 v51, 1.0, v69
	v_exp_f32_e32 v69, v68
	v_mul_f32_e32 v68, 0x3d372713, v52
	v_rcp_f32_e32 v71, v71
	v_mul_f32_e32 v68, v52, v68
	v_fma_f32 v68, v52, v68, v52
	v_mul_f32_e32 v68, 0x3fcc422a, v68
	v_mul_f32_e32 v68, 0xbfb8aa3b, v68
	v_pk_mul_f32 v[54:55], v[54:55], v[70:71]
	v_exp_f32_e32 v71, v68
	v_rcp_f32_e32 v68, v51
	v_add_f32_e32 v51, 1.0, v69
	v_rcp_f32_e32 v70, v51
	v_add_f32_e32 v51, 1.0, v71
	v_mul_f32_e32 v69, 0x3d372713, v65
	v_mul_f32_e32 v71, 0x3d372713, v61
	v_mul_f32_e32 v69, v65, v69
	v_mul_f32_e32 v71, v61, v71
	v_fma_f32 v69, v65, v69, v65
	v_fma_f32 v71, v61, v71, v61
	v_mul_f32_e32 v69, 0x3fcc422a, v69
	v_mul_f32_e32 v71, 0x3fcc422a, v71
	v_mul_f32_e32 v69, 0xbfb8aa3b, v69
	v_mul_f32_e32 v71, 0xbfb8aa3b, v71
	v_exp_f32_e32 v69, v69
	v_exp_f32_e32 v71, v71
	v_rcp_f32_e32 v72, v51
	v_mul_f32_e32 v73, 0x3d372713, v53
	v_add_f32_e32 v51, 1.0, v69
	v_add_f32_e32 v69, 1.0, v71
	v_mul_f32_e32 v71, 0x3d372713, v57
	v_mul_f32_e32 v71, v57, v71
	v_fma_f32 v71, v57, v71, v57
	v_mul_f32_e32 v71, 0x3fcc422a, v71
	v_mul_f32_e32 v71, 0xbfb8aa3b, v71
	v_exp_f32_e32 v71, v71
	v_mul_f32_e32 v73, v53, v73
	v_fma_f32 v73, v53, v73, v53
	v_mul_f32_e32 v73, 0x3fcc422a, v73
	v_mul_f32_e32 v73, 0xbfb8aa3b, v73
	v_add_f32_e32 v71, 1.0, v71
	v_exp_f32_e32 v73, v73
	v_rcp_f32_e32 v71, v71
	v_rcp_f32_e32 v50, v50
	v_rcp_f32_e32 v51, v51
	v_rcp_f32_e32 v69, v69
	v_add_f32_e32 v73, 1.0, v73
	v_pk_mul_f32 v[56:57], v[56:57], v[70:71]
	v_rcp_f32_e32 v73, v73
	v_cvt_pk_bf16_f32 v54, v54, v55
	v_cvt_pk_bf16_f32 v55, v56, v57
	v_mul_f32_e32 v57, 0x3d372713, v46
	v_pk_mul_f32 v[64:65], v[64:65], v[50:51]
	v_lshl_add_u64 v[50:51], v[166:167], 0, v[154:155]
	v_mul_f32_e32 v57, v46, v57
	v_lshlrev_b64 v[50:51], 10, v[50:51]
	v_fma_f32 v57, v46, v57, v46
	v_pk_mul_f32 v[60:61], v[60:61], v[68:69]
	v_lshl_add_u64 v[50:51], s[6:7], 0, v[50:51]
	v_mul_f32_e32 v57, 0x3fcc422a, v57
	v_pk_mul_f32 v[68:69], v[52:53], v[72:73]
	v_lshl_add_u64 v[70:71], v[50:51], 0, s[18:19]
	v_cvt_pk_bf16_f32 v50, v62, v63
	v_cvt_pk_bf16_f32 v51, v64, v65
	v_cvt_pk_bf16_f32 v52, v58, v59
	v_cvt_pk_bf16_f32 v53, v60, v61
	v_mul_f32_e32 v57, 0xbfb8aa3b, v57
	v_cvt_pk_bf16_f32 v56, v66, v67
	v_exp_f32_e32 v58, v57
	v_cvt_pk_bf16_f32 v57, v68, v69
	flat_store_dwordx4 v[70:71], v[50:53]
	flat_store_dwordx4 v[70:71], v[54:57] offset:16
	s_nop 0
	v_mul_f32_e32 v51, 0x3d372713, v42
	v_mul_f32_e32 v51, v42, v51
	v_mul_f32_e32 v52, 0x3d372713, v38
	v_fma_f32 v51, v42, v51, v42
	v_mul_f32_e32 v52, v38, v52
	v_mul_f32_e32 v51, 0x3fcc422a, v51
	v_fma_f32 v52, v38, v52, v38
	v_mul_f32_e32 v51, 0xbfb8aa3b, v51
	v_mul_f32_e32 v52, 0x3fcc422a, v52
	v_exp_f32_e32 v51, v51
	v_mul_f32_e32 v52, 0xbfb8aa3b, v52
	v_exp_f32_e32 v53, v52
	v_mul_f32_e32 v54, 0x3d372713, v47
	v_add_f32_e32 v51, 1.0, v51
	v_rcp_f32_e32 v52, v51
	v_add_f32_e32 v51, 1.0, v53
	v_mul_f32_e32 v53, 0x3d372713, v34
	v_mul_f32_e32 v53, v34, v53
	v_fma_f32 v53, v34, v53, v34
	v_mul_f32_e32 v53, 0x3fcc422a, v53
	v_mul_f32_e32 v53, 0xbfb8aa3b, v53
	v_mul_f32_e32 v54, v47, v54
	v_exp_f32_e32 v53, v53
	v_fma_f32 v54, v47, v54, v47
	v_mul_f32_e32 v54, 0x3fcc422a, v54
	v_mul_f32_e32 v54, 0xbfb8aa3b, v54
	v_exp_f32_e32 v55, v54
	v_mul_f32_e32 v57, 0x3d372713, v35
	v_rcp_f32_e32 v54, v51
	v_add_f32_e32 v51, 1.0, v53
	v_mul_f32_e32 v53, 0x3d372713, v43
	v_mul_f32_e32 v57, v35, v57
	v_mul_f32_e32 v53, v43, v53
	v_fma_f32 v57, v35, v57, v35
	v_fma_f32 v53, v43, v53, v43
	v_mul_f32_e32 v57, 0x3fcc422a, v57
	v_add_f32_e32 v50, 1.0, v58
	v_rcp_f32_e32 v56, v51
	v_add_f32_e32 v51, 1.0, v55
	v_mul_f32_e32 v53, 0x3fcc422a, v53
	v_mul_f32_e32 v57, 0xbfb8aa3b, v57
	v_rcp_f32_e32 v50, v50
	v_mul_f32_e32 v53, 0xbfb8aa3b, v53
	v_rcp_f32_e32 v51, v51
	v_exp_f32_e32 v57, v57
	v_exp_f32_e32 v53, v53
	v_mul_f32_e32 v55, 0x3d372713, v39
	v_pk_mul_f32 v[46:47], v[46:47], v[50:51]
	v_add_f32_e32 v50, 1.0, v57
	v_add_f32_e32 v53, 1.0, v53
	v_rcp_f32_e32 v57, v50
	v_mul_f32_e32 v50, 0x3d372713, v48
	v_rcp_f32_e32 v53, v53
	v_mul_f32_e32 v50, v48, v50
	v_fma_f32 v50, v48, v50, v48
	v_mul_f32_e32 v50, 0x3fcc422a, v50
	v_mul_f32_e32 v50, 0xbfb8aa3b, v50
	v_pk_mul_f32 v[42:43], v[42:43], v[52:53]
	v_exp_f32_e32 v52, v50
	v_mul_f32_e32 v50, 0x3d372713, v44
	v_mul_f32_e32 v50, v44, v50
	v_mul_f32_e32 v55, v39, v55
	v_fma_f32 v50, v44, v50, v44
	v_fma_f32 v55, v39, v55, v39
	v_mul_f32_e32 v50, 0x3fcc422a, v50
	v_mul_f32_e32 v55, 0x3fcc422a, v55
	v_mul_f32_e32 v50, 0xbfb8aa3b, v50
	v_mul_f32_e32 v55, 0xbfb8aa3b, v55
	v_exp_f32_e32 v53, v50
	v_pk_mul_f32 v[50:51], v[34:35], v[56:57]
	v_add_f32_e32 v34, 1.0, v52
	v_mul_f32_e32 v52, 0x3d372713, v40
	v_exp_f32_e32 v55, v55
	v_mul_f32_e32 v52, v40, v52
	v_fma_f32 v52, v40, v52, v40
	v_mul_f32_e32 v52, 0x3fcc422a, v52
	v_mul_f32_e32 v52, 0xbfb8aa3b, v52
	v_add_f32_e32 v55, 1.0, v55
	v_add_f32_e32 v35, 1.0, v53
	v_exp_f32_e32 v53, v52
	v_mul_f32_e32 v52, 0x3d372713, v36
	v_rcp_f32_e32 v55, v55
	v_mul_f32_e32 v52, v36, v52
	v_fma_f32 v52, v36, v52, v36
	v_mul_f32_e32 v52, 0x3fcc422a, v52
	v_mul_f32_e32 v52, 0xbfb8aa3b, v52
	v_pk_mul_f32 v[38:39], v[38:39], v[54:55]
; __device__ __forceinline__ unsigned pk_bf16(float lo, float hi) { const bf16x2_t r = __builtin_convertvector((f32x2){lo, hi}, bf16x2_t); return __builtin_bit_cast(unsigned, r); }
; __device__ __forceinline__ float fsigmoid(float x) { return __builtin_amdgcn_rcpf(1.0f + __builtin_amdgcn_exp2f(-1.44269504f * x)); }
; __device__ __forceinline__ void st16_bf16(bf16* dst, f32x4 a, f32x4 b, f32x4 c, f32x4 d) {
;     u32x4 w0, w1; w0.x = pk_bf16(a[0], a[1]); w0.y = pk_bf16(a[2], a[3]); w0.z = pk_bf16(b[0], b[1]); w0.w = pk_bf16(b[2], b[3]);
;     w1.x = pk_bf16(c[0], c[1]); w1.y = pk_bf16(c[2], c[3]); w1.z = pk_bf16(d[0], d[1]); w1.w = pk_bf16(d[2], d[3]);
;     *(u32x4*)dst = w0; *(u32x4*)(dst + 8) = w1; }
; __device__ __forceinline__ unsigned pk4_u8(float a, float b, float c, float d) {
;     const unsigned ya = __builtin_bit_cast(unsigned, a * 255.0f + 8388608.0f), yb = __builtin_bit_cast(unsigned, b * 255.0f + 8388608.0f), yc = __builtin_bit_cast(unsigned, c * 255.0f + 8388608.0f), yd = __builtin_bit_cast(unsigned, d * 255.0f + 8388608.0f);
;     const unsigned w01 = __builtin_amdgcn_perm(yb, ya, 0x0c0c0400u), w23 = __builtin_amdgcn_perm(yd, yc, 0x0c0c0400u);
;     return __builtin_amdgcn_perm(w23, w01, 0x05040100u); }
; __device__ __forceinline__ f32x4 u8x4_f32(unsigned w) { return (f32x4){(float)(w & 0xffu), (float)((w >> 8) & 0xffu), (float)((w >> 16) & 0xffu), (float)(w >> 24)}; }
; __device__ __forceinline__ float gelu_tanh(float x) { return x * fsigmoid(1.5957691216f * (x + 0.044715f * x * x * x)); }
;     __device__ __forceinline__ void operator()(AccRef acc, const GUnit& u, int wr, int wc, int fr, int fq) const {
;         const int g = u.x0, b = u.x1, pn = u.x2; const int tt = (pn * 256 + wc * 64 + 16 * fq) >> 4;
; #pragma unroll
;         for (int ai = 0; ai < 2; ++ai)
; #pragma unroll
;             for (int m = 0; m < 4; ++m) { const int ch = ai * 128 + wr * 64 + m * 16 + fr; const size_t tok = (size_t)b * SEQ + ch * LC + tt;
;                 f32x4 v0 = acc[ai][0][m][0], v1 = acc[ai][0][m][1], v2 = acc[ai][1][m][0], v3 = acc[ai][1][m][1];
; #pragma unroll
;                 for (int j = 0; j < 4; ++j) { v0[j] = gelu_tanh(v0[j]); v1[j] = gelu_tanh(v1[j]); v2[j] = gelu_tanh(v2[j]); v3[j] = gelu_tanh(v3[j]); }
;                 st16_bf16(YS + tok * SW + g * 16, v0, v1, v2, v3); }
	v_exp_f32_e32 v55, v52
	v_rcp_f32_e32 v52, v35
	v_add_f32_e32 v35, 1.0, v53
	v_rcp_f32_e32 v54, v35
	v_add_f32_e32 v35, 1.0, v55
	v_mul_f32_e32 v53, 0x3d372713, v49
	v_mul_f32_e32 v55, 0x3d372713, v45
	v_mul_f32_e32 v53, v49, v53
	v_mul_f32_e32 v55, v45, v55
	v_fma_f32 v53, v49, v53, v49
	v_fma_f32 v55, v45, v55, v45
	v_mul_f32_e32 v53, 0x3fcc422a, v53
	v_mul_f32_e32 v55, 0x3fcc422a, v55
	v_mul_f32_e32 v53, 0xbfb8aa3b, v53
	v_mul_f32_e32 v55, 0xbfb8aa3b, v55
	v_exp_f32_e32 v53, v53
	v_exp_f32_e32 v55, v55
	v_rcp_f32_e32 v56, v35
	v_mul_f32_e32 v57, 0x3d372713, v37
	v_add_f32_e32 v35, 1.0, v53
	v_add_f32_e32 v53, 1.0, v55
	v_mul_f32_e32 v55, 0x3d372713, v41
	v_mul_f32_e32 v55, v41, v55
	v_fma_f32 v55, v41, v55, v41
	v_mul_f32_e32 v55, 0x3fcc422a, v55
	v_mul_f32_e32 v55, 0xbfb8aa3b, v55
	v_exp_f32_e32 v55, v55
	v_mul_f32_e32 v57, v37, v57
	v_fma_f32 v57, v37, v57, v37
	v_mul_f32_e32 v57, 0x3fcc422a, v57
	v_mul_f32_e32 v57, 0xbfb8aa3b, v57
	v_add_f32_e32 v55, 1.0, v55
	v_exp_f32_e32 v57, v57
	v_rcp_f32_e32 v55, v55
	v_rcp_f32_e32 v34, v34
	v_rcp_f32_e32 v35, v35
	v_rcp_f32_e32 v53, v53
	v_add_f32_e32 v57, 1.0, v57
	v_pk_mul_f32 v[40:41], v[40:41], v[54:55]
	v_rcp_f32_e32 v57, v57
	v_cvt_pk_bf16_f32 v38, v38, v39
	v_cvt_pk_bf16_f32 v39, v40, v41
	v_mul_f32_e32 v41, 0x3d372713, v30
	v_pk_mul_f32 v[48:49], v[48:49], v[34:35]
	v_lshl_add_u64 v[34:35], v[166:167], 0, v[156:157]
	v_mul_f32_e32 v41, v30, v41
	v_lshlrev_b64 v[34:35], 10, v[34:35]
	v_fma_f32 v41, v30, v41, v30
	v_pk_mul_f32 v[44:45], v[44:45], v[52:53]
	v_lshl_add_u64 v[34:35], s[6:7], 0, v[34:35]
	v_mul_f32_e32 v41, 0x3fcc422a, v41
	v_pk_mul_f32 v[52:53], v[36:37], v[56:57]
	v_lshl_add_u64 v[54:55], v[34:35], 0, s[18:19]
	v_cvt_pk_bf16_f32 v34, v46, v47
	v_cvt_pk_bf16_f32 v35, v48, v49
	v_cvt_pk_bf16_f32 v36, v42, v43
	v_cvt_pk_bf16_f32 v37, v44, v45
	v_mul_f32_e32 v41, 0xbfb8aa3b, v41
	v_cvt_pk_bf16_f32 v40, v50, v51
	v_exp_f32_e32 v42, v41
	v_cvt_pk_bf16_f32 v41, v52, v53
	flat_store_dwordx4 v[54:55], v[34:37]
	flat_store_dwordx4 v[54:55], v[38:41] offset:16
	s_nop 0
	v_mul_f32_e32 v35, 0x3d372713, v26
	v_mul_f32_e32 v35, v26, v35
	v_mul_f32_e32 v36, 0x3d372713, v22
	v_fma_f32 v35, v26, v35, v26
	v_mul_f32_e32 v36, v22, v36
	v_mul_f32_e32 v35, 0x3fcc422a, v35
	v_fma_f32 v36, v22, v36, v22
	v_mul_f32_e32 v35, 0xbfb8aa3b, v35
	v_mul_f32_e32 v36, 0x3fcc422a, v36
	v_exp_f32_e32 v35, v35
	v_mul_f32_e32 v36, 0xbfb8aa3b, v36
	v_exp_f32_e32 v37, v36
	v_mul_f32_e32 v38, 0x3d372713, v31
	v_add_f32_e32 v35, 1.0, v35
	v_rcp_f32_e32 v36, v35
	v_add_f32_e32 v35, 1.0, v37
	v_mul_f32_e32 v37, 0x3d372713, v18
	v_mul_f32_e32 v37, v18, v37
	v_fma_f32 v37, v18, v37, v18
	v_mul_f32_e32 v37, 0x3fcc422a, v37
	v_mul_f32_e32 v37, 0xbfb8aa3b, v37
	v_mul_f32_e32 v38, v31, v38
	v_exp_f32_e32 v37, v37
	v_fma_f32 v38, v31, v38, v31
	v_mul_f32_e32 v38, 0x3fcc422a, v38
	v_mul_f32_e32 v38, 0xbfb8aa3b, v38
	v_exp_f32_e32 v39, v38
	v_mul_f32_e32 v41, 0x3d372713, v19
	v_rcp_f32_e32 v38, v35
	v_add_f32_e32 v35, 1.0, v37
	v_mul_f32_e32 v37, 0x3d372713, v27
	v_mul_f32_e32 v41, v19, v41
	v_mul_f32_e32 v37, v27, v37
	v_fma_f32 v41, v19, v41, v19
	v_fma_f32 v37, v27, v37, v27
	v_mul_f32_e32 v41, 0x3fcc422a, v41
	v_add_f32_e32 v34, 1.0, v42
	v_rcp_f32_e32 v40, v35
	v_add_f32_e32 v35, 1.0, v39
	v_mul_f32_e32 v37, 0x3fcc422a, v37
	v_mul_f32_e32 v41, 0xbfb8aa3b, v41
	v_rcp_f32_e32 v34, v34
	v_mul_f32_e32 v37, 0xbfb8aa3b, v37
	v_rcp_f32_e32 v35, v35
	v_exp_f32_e32 v41, v41
	v_exp_f32_e32 v37, v37
	v_mul_f32_e32 v39, 0x3d372713, v23
	v_pk_mul_f32 v[30:31], v[30:31], v[34:35]
	v_add_f32_e32 v34, 1.0, v41
	v_add_f32_e32 v37, 1.0, v37
	v_rcp_f32_e32 v41, v34
	v_mul_f32_e32 v34, 0x3d372713, v32
	v_rcp_f32_e32 v37, v37
	v_mul_f32_e32 v34, v32, v34
	v_fma_f32 v34, v32, v34, v32
	v_mul_f32_e32 v34, 0x3fcc422a, v34
	v_mul_f32_e32 v34, 0xbfb8aa3b, v34
	v_pk_mul_f32 v[26:27], v[26:27], v[36:37]
	v_exp_f32_e32 v36, v34
	v_mul_f32_e32 v34, 0x3d372713, v28
	v_mul_f32_e32 v34, v28, v34
	v_mul_f32_e32 v39, v23, v39
	v_fma_f32 v34, v28, v34, v28
	v_fma_f32 v39, v23, v39, v23
	v_mul_f32_e32 v34, 0x3fcc422a, v34
	v_mul_f32_e32 v39, 0x3fcc422a, v39
	v_mul_f32_e32 v34, 0xbfb8aa3b, v34
	v_mul_f32_e32 v39, 0xbfb8aa3b, v39
	v_exp_f32_e32 v37, v34
	v_pk_mul_f32 v[34:35], v[18:19], v[40:41]
	v_add_f32_e32 v18, 1.0, v36
	v_mul_f32_e32 v36, 0x3d372713, v24
	v_exp_f32_e32 v39, v39
	v_mul_f32_e32 v36, v24, v36
	v_fma_f32 v36, v24, v36, v24
	v_mul_f32_e32 v36, 0x3fcc422a, v36
	v_mul_f32_e32 v36, 0xbfb8aa3b, v36
	v_add_f32_e32 v39, 1.0, v39
	v_add_f32_e32 v19, 1.0, v37
	v_exp_f32_e32 v37, v36
	v_mul_f32_e32 v36, 0x3d372713, v20
	v_rcp_f32_e32 v39, v39
	v_mul_f32_e32 v36, v20, v36
	v_fma_f32 v36, v20, v36, v20
	v_mul_f32_e32 v36, 0x3fcc422a, v36
	v_mul_f32_e32 v36, 0xbfb8aa3b, v36
	v_pk_mul_f32 v[22:23], v[22:23], v[38:39]
	v_exp_f32_e32 v39, v36
	v_rcp_f32_e32 v36, v19
	v_add_f32_e32 v19, 1.0, v37
	v_rcp_f32_e32 v38, v19
	v_add_f32_e32 v19, 1.0, v39
	v_mul_f32_e32 v37, 0x3d372713, v33
	v_mul_f32_e32 v39, 0x3d372713, v29
	v_mul_f32_e32 v37, v33, v37
	v_mul_f32_e32 v39, v29, v39
	v_fma_f32 v37, v33, v37, v33
	v_fma_f32 v39, v29, v39, v29
	v_mul_f32_e32 v37, 0x3fcc422a, v37
	v_mul_f32_e32 v39, 0x3fcc422a, v39
	v_mul_f32_e32 v37, 0xbfb8aa3b, v37
	v_mul_f32_e32 v39, 0xbfb8aa3b, v39
	v_exp_f32_e32 v37, v37
	v_exp_f32_e32 v39, v39
	v_rcp_f32_e32 v40, v19
	v_mul_f32_e32 v41, 0x3d372713, v21
	v_add_f32_e32 v19, 1.0, v37
	v_add_f32_e32 v37, 1.0, v39
	v_mul_f32_e32 v39, 0x3d372713, v25
	v_mul_f32_e32 v39, v25, v39
	v_fma_f32 v39, v25, v39, v25
	v_mul_f32_e32 v39, 0x3fcc422a, v39
	v_mul_f32_e32 v39, 0xbfb8aa3b, v39
	v_exp_f32_e32 v39, v39
	v_mul_f32_e32 v41, v21, v41
; __device__ __forceinline__ float gelu_tanh(float x) { return x * fsigmoid(1.5957691216f * (x + 0.044715f * x * x * x)); }
; #define PG8_BAR __builtin_amdgcn_s_barrier()
; template <class Epi, class Sched, bool ALIGN_EPI = true, bool F8 = false>
; __device__ __forceinline__ void gemm_phase(PG8_LAS unsigned char* lds, const Sched& S, const Epi& E) {
;     ...
;         if (!has_next) break;
;         if (!(HasSeg<Epi>::v && cur.x2 == 0)) {
; #pragma unroll
;         for (int a = 0; a < 2; ++a)
; #pragma unroll
;             for (int b = 0; b < 2; ++b)
; #pragma unroll
;                 for (int m = 0; m < 4; ++m)
; #pragma unroll
;                     for (int n = 0; n < 2; ++n) acc[a][b][m][n] = (f32x4){0.f, 0.f, 0.f, 0.f};
;         }
;         cur = nxt; cA = nA; cB = nB; ++ui;
; #pragma unroll
;         for (int h = 0; h < 2; ++h)
; #pragma unroll
;             for (int i = 0; i < 2; ++i) voffA[h][i] = voffAn[h][i];
;         if constexpr (ALIGN_EPI) { if (wr == 1) PG8_BAR; }
;     }
;     __device__ __forceinline__ void operator()(AccRef acc, const GUnit& u, int wr, int wc, int fr, int fq) const {
;         const int g = u.x0, b = u.x1, pn = u.x2; const int tt = (pn * 256 + wc * 64 + 16 * fq) >> 4;
; #pragma unroll
;         for (int ai = 0; ai < 2; ++ai)
; #pragma unroll
;             for (int m = 0; m < 4; ++m) { const int ch = ai * 128 + wr * 64 + m * 16 + fr; const size_t tok = (size_t)b * SEQ + ch * LC + tt;
;                 f32x4 v0 = acc[ai][0][m][0], v1 = acc[ai][0][m][1], v2 = acc[ai][1][m][0], v3 = acc[ai][1][m][1];
; #pragma unroll
;                 for (int j = 0; j < 4; ++j) { v0[j] = gelu_tanh(v0[j]); v1[j] = gelu_tanh(v1[j]); v2[j] = gelu_tanh(v2[j]); v3[j] = gelu_tanh(v3[j]); }
;                 st16_bf16(YS + tok * SW + g * 16, v0, v1, v2, v3); }
	v_fma_f32 v41, v21, v41, v21
	v_mul_f32_e32 v41, 0x3fcc422a, v41
	v_mul_f32_e32 v41, 0xbfb8aa3b, v41
	v_add_f32_e32 v39, 1.0, v39
	v_exp_f32_e32 v41, v41
	v_rcp_f32_e32 v39, v39
	v_rcp_f32_e32 v18, v18
	v_rcp_f32_e32 v19, v19
	v_rcp_f32_e32 v37, v37
	v_add_f32_e32 v41, 1.0, v41
	v_pk_mul_f32 v[24:25], v[24:25], v[38:39]
	v_rcp_f32_e32 v41, v41
	v_cvt_pk_bf16_f32 v22, v22, v23
	v_cvt_pk_bf16_f32 v23, v24, v25
	v_mul_f32_e32 v25, 0x3d372713, v14
	v_pk_mul_f32 v[32:33], v[32:33], v[18:19]
	v_lshl_add_u64 v[18:19], v[166:167], 0, v[158:159]
	v_mul_f32_e32 v25, v14, v25
	v_lshlrev_b64 v[18:19], 10, v[18:19]
	v_fma_f32 v25, v14, v25, v14
	v_pk_mul_f32 v[28:29], v[28:29], v[36:37]
	v_lshl_add_u64 v[18:19], s[6:7], 0, v[18:19]
	v_mul_f32_e32 v25, 0x3fcc422a, v25
	v_pk_mul_f32 v[36:37], v[20:21], v[40:41]
	v_lshl_add_u64 v[38:39], v[18:19], 0, s[18:19]
	v_cvt_pk_bf16_f32 v18, v30, v31
	v_cvt_pk_bf16_f32 v19, v32, v33
	v_cvt_pk_bf16_f32 v20, v26, v27
	v_cvt_pk_bf16_f32 v21, v28, v29
	v_mul_f32_e32 v25, 0xbfb8aa3b, v25
	v_cvt_pk_bf16_f32 v24, v34, v35
	v_exp_f32_e32 v26, v25
	v_cvt_pk_bf16_f32 v25, v36, v37
	flat_store_dwordx4 v[38:39], v[18:21]
	flat_store_dwordx4 v[38:39], v[22:25] offset:16
	s_nop 0
	v_mul_f32_e32 v19, 0x3d372713, v10
	v_mul_f32_e32 v19, v10, v19
	v_mul_f32_e32 v20, 0x3d372713, v6
	v_fma_f32 v19, v10, v19, v10
	v_mul_f32_e32 v20, v6, v20
	v_mul_f32_e32 v19, 0x3fcc422a, v19
	v_fma_f32 v20, v6, v20, v6
	v_mul_f32_e32 v19, 0xbfb8aa3b, v19
	v_mul_f32_e32 v20, 0x3fcc422a, v20
	v_exp_f32_e32 v19, v19
	v_mul_f32_e32 v20, 0xbfb8aa3b, v20
	v_exp_f32_e32 v21, v20
	v_mul_f32_e32 v22, 0x3d372713, v15
	v_add_f32_e32 v19, 1.0, v19
	v_rcp_f32_e32 v20, v19
	v_add_f32_e32 v19, 1.0, v21
	v_mul_f32_e32 v21, 0x3d372713, v2
	v_mul_f32_e32 v21, v2, v21
	v_fma_f32 v21, v2, v21, v2
	v_mul_f32_e32 v21, 0x3fcc422a, v21
	v_mul_f32_e32 v21, 0xbfb8aa3b, v21
	v_mul_f32_e32 v22, v15, v22
	v_exp_f32_e32 v21, v21
	v_fma_f32 v22, v15, v22, v15
	v_mul_f32_e32 v22, 0x3fcc422a, v22
	v_mul_f32_e32 v22, 0xbfb8aa3b, v22
	v_exp_f32_e32 v23, v22
	v_mul_f32_e32 v25, 0x3d372713, v3
	v_rcp_f32_e32 v22, v19
	v_add_f32_e32 v19, 1.0, v21
	v_mul_f32_e32 v21, 0x3d372713, v11
	v_mul_f32_e32 v25, v3, v25
	v_mul_f32_e32 v21, v11, v21
	v_fma_f32 v25, v3, v25, v3
	v_fma_f32 v21, v11, v21, v11
	v_mul_f32_e32 v25, 0x3fcc422a, v25
	v_add_f32_e32 v18, 1.0, v26
	v_rcp_f32_e32 v24, v19
	v_add_f32_e32 v19, 1.0, v23
	v_mul_f32_e32 v21, 0x3fcc422a, v21
	v_mul_f32_e32 v25, 0xbfb8aa3b, v25
	v_rcp_f32_e32 v18, v18
	v_mul_f32_e32 v21, 0xbfb8aa3b, v21
	v_rcp_f32_e32 v19, v19
	v_exp_f32_e32 v25, v25
	v_exp_f32_e32 v21, v21
	v_mul_f32_e32 v23, 0x3d372713, v7
	v_pk_mul_f32 v[14:15], v[14:15], v[18:19]
	v_add_f32_e32 v18, 1.0, v25
	v_add_f32_e32 v21, 1.0, v21
	v_rcp_f32_e32 v25, v18
	v_mul_f32_e32 v18, 0x3d372713, v16
	v_rcp_f32_e32 v21, v21
	v_mul_f32_e32 v18, v16, v18
	v_fma_f32 v18, v16, v18, v16
	v_mul_f32_e32 v18, 0x3fcc422a, v18
	v_mul_f32_e32 v18, 0xbfb8aa3b, v18
	v_pk_mul_f32 v[10:11], v[10:11], v[20:21]
	v_exp_f32_e32 v20, v18
	v_mul_f32_e32 v18, 0x3d372713, v12
	v_mul_f32_e32 v18, v12, v18
	v_mul_f32_e32 v23, v7, v23
	v_fma_f32 v18, v12, v18, v12
	v_fma_f32 v23, v7, v23, v7
	v_mul_f32_e32 v18, 0x3fcc422a, v18
	v_mul_f32_e32 v23, 0x3fcc422a, v23
	v_mul_f32_e32 v18, 0xbfb8aa3b, v18
	v_mul_f32_e32 v23, 0xbfb8aa3b, v23
	v_exp_f32_e32 v21, v18
	v_pk_mul_f32 v[18:19], v[2:3], v[24:25]
	v_add_f32_e32 v2, 1.0, v20
	v_mul_f32_e32 v20, 0x3d372713, v8
	v_exp_f32_e32 v23, v23
	v_mul_f32_e32 v20, v8, v20
	v_fma_f32 v20, v8, v20, v8
	v_mul_f32_e32 v20, 0x3fcc422a, v20
	v_mul_f32_e32 v20, 0xbfb8aa3b, v20
	v_add_f32_e32 v23, 1.0, v23
	v_add_f32_e32 v3, 1.0, v21
	v_exp_f32_e32 v21, v20
	v_mul_f32_e32 v20, 0x3d372713, v4
	v_rcp_f32_e32 v23, v23
	v_mul_f32_e32 v20, v4, v20
	v_fma_f32 v20, v4, v20, v4
	v_mul_f32_e32 v20, 0x3fcc422a, v20
	v_mul_f32_e32 v20, 0xbfb8aa3b, v20
	v_pk_mul_f32 v[6:7], v[6:7], v[22:23]
	v_exp_f32_e32 v23, v20
	v_rcp_f32_e32 v20, v3
	v_add_f32_e32 v3, 1.0, v21
	v_rcp_f32_e32 v22, v3
	v_add_f32_e32 v3, 1.0, v23
	v_mul_f32_e32 v21, 0x3d372713, v17
	v_mul_f32_e32 v23, 0x3d372713, v13
	v_mul_f32_e32 v21, v17, v21
	v_mul_f32_e32 v23, v13, v23
	v_fma_f32 v21, v17, v21, v17
	v_fma_f32 v23, v13, v23, v13
	v_mul_f32_e32 v21, 0x3fcc422a, v21
	v_mul_f32_e32 v23, 0x3fcc422a, v23
	v_mul_f32_e32 v21, 0xbfb8aa3b, v21
	v_mul_f32_e32 v23, 0xbfb8aa3b, v23
	v_exp_f32_e32 v21, v21
	v_exp_f32_e32 v23, v23
	v_rcp_f32_e32 v24, v3
	v_mul_f32_e32 v25, 0x3d372713, v5
	v_add_f32_e32 v3, 1.0, v21
	v_add_f32_e32 v21, 1.0, v23
	v_mul_f32_e32 v23, 0x3d372713, v9
	v_mul_f32_e32 v23, v9, v23
	v_mul_f32_e32 v25, v5, v25
	v_fma_f32 v23, v9, v23, v9
	v_fma_f32 v25, v5, v25, v5
	v_mul_f32_e32 v23, 0x3fcc422a, v23
	v_mul_f32_e32 v25, 0x3fcc422a, v25
	v_mul_f32_e32 v23, 0xbfb8aa3b, v23
	v_mul_f32_e32 v25, 0xbfb8aa3b, v25
	v_exp_f32_e32 v23, v23
	v_exp_f32_e32 v25, v25
	v_rcp_f32_e32 v2, v2
	v_rcp_f32_e32 v3, v3
	v_rcp_f32_e32 v21, v21
	v_add_f32_e32 v23, 1.0, v23
	v_add_f32_e32 v25, 1.0, v25
	v_rcp_f32_e32 v23, v23
	v_rcp_f32_e32 v25, v25
	v_pk_mul_f32 v[16:17], v[16:17], v[2:3]
	v_lshl_add_u64 v[2:3], v[166:167], 0, v[160:161]
	v_lshlrev_b64 v[2:3], 10, v[2:3]
	v_pk_mul_f32 v[12:13], v[12:13], v[20:21]
	v_lshl_add_u64 v[2:3], s[6:7], 0, v[2:3]
	v_pk_mul_f32 v[8:9], v[8:9], v[22:23]
	v_pk_mul_f32 v[20:21], v[4:5], v[24:25]
	v_lshl_add_u64 v[22:23], v[2:3], 0, s[18:19]
	v_cvt_pk_bf16_f32 v2, v14, v15
	v_cvt_pk_bf16_f32 v3, v16, v17
	v_cvt_pk_bf16_f32 v4, v10, v11
	v_cvt_pk_bf16_f32 v5, v12, v13
	v_cvt_pk_bf16_f32 v6, v6, v7
	v_cvt_pk_bf16_f32 v7, v8, v9
	v_cvt_pk_bf16_f32 v8, v18, v19
	v_cvt_pk_bf16_f32 v9, v20, v21
	flat_store_dwordx4 v[22:23], v[2:5]
	flat_store_dwordx4 v[22:23], v[6:9] offset:16
	s_cbranch_vccnz .LBB0_672
	s_andn2_b64 vcc, exec, s[4:5]
	s_cbranch_vccnz .LBB0_671
	s_branch .LBB0_671

; #define PG8_WAIT_V(n) asm volatile("s_waitcnt vmcnt(" #n ")" ::: "memory")
; template <class Epi, class Sched, bool ALIGN_EPI = true, bool F8 = false>
; __device__ __forceinline__ void gemm_phase(PG8_LAS unsigned char* lds, const Sched& S, const Epi& E) {
;     const int tid = threadIdx.x, wid = __builtin_amdgcn_readfirstlane(tid >> 6), lane = tid & 63, wr = wid >> 2, wc = wid & 3, fr = lane & 15, fq = lane >> 4;
;     int Rs[2], Cs[2];
; #pragma unroll
;     for (int i = 0; i < 2; ++i) stage_rc(tid * 16 + i * 8192, Rs[i], Cs[i]);
;     unsigned voffB[2][2], voffA[2][2], voffAn[2][2];
; #pragma unroll
;     for (int h = 0; h < 2; ++h)
; #pragma unroll
;         for (int i = 0; i < 2; ++i) {
;             if constexpr (HasP16<Epi>::v) { const int r = Rs[i]; voffB[h][i] = S.b_off(64 * (r >> 5) + 16 * ((r & 15) >> 2) + 8 * h + 4 * ((r >> 4) & 1) + (r & 3), Cs[i]); }
;             else { const int Rb = Epi::PERM ? ((Rs[i] & ~31) + perm32(Rs[i] & 31)) : Rs[i]; voffB[h][i] = S.b_off(h * HALF + Rb, Cs[i]); } }
;     const size_t kstep = (size_t)SchedKstep<Sched>::v, kstepB = (size_t)SchedKstepB<Sched>::v;
;     const unsigned ldsw = (unsigned)wid * 1024u;
;     const int aoff = lds_byte(wr * 64 + fr, fq * 8), boff = lds_byte(wc * 32 + fr, fq * 8);
;     ...
;     GUnit cur, nxt; int ui = 0;
;     if (!S.next(0, cur)) return;
;     S.a_off(cur, Rs, Cs, voffA);
; #pragma unroll
;     for (int h = 0; h < 2; ++h)
; #pragma unroll
;         for (int i = 0; i < 2; ++i) voffAn[h][i] = voffA[h][i];
;     f32x4 acc[2][2][4][2];
; #pragma unroll
;     for (int a = 0; a < 2; ++a)
; #pragma unroll
;         for (int b = 0; b < 2; ++b)
; #pragma unroll
;             for (int m = 0; m < 4; ++m)
; #pragma unroll
;                 for (int n = 0; n < 2; ++n) acc[a][b][m][n] = (f32x4){0.f, 0.f, 0.f, 0.f};
;     bf16x8 At[4][2], B0[2][2], B1[2][2]; i32x8 At8[4], B08[2], B18[2];
;     const int f8scale = 0x7F7F7F7F;
;     const char* cA = cur.A; const char* cB = cur.B;
;     PG8_STAGE(PG8_SB(0, 0), cB, voffB[0]); PG8_STAGE(PG8_SB(0, 1), cB, voffB[1]); PG8_STAGE(PG8_SA(0, 0), cA, voffA[0]); PG8_STAGE(PG8_SA(0, 1), cA, voffA[1]);
;     if (wr == 1) PG8_BAR;
;     PG8_WAIT_V(2); PG8_BAR;
;     PG8_STAGE(PG8_SB(1, 0), cB + kstepB, voffB[0]); PG8_STAGE(PG8_SA(1, 0), cA + kstep, voffA[0]); PG8_STAGE(PG8_SB(1, 1), cB + kstepB, voffB[1]);
;     PG8_WAIT_V(6); PG8_BAR;
.LBB0_683:
	s_cmpk_gt_i32 s2, 0x3ff
	v_readfirstlane_b32 s12, v0
	s_cbranch_scc1 .LBB0_699
	v_lshlrev_b32_e32 v2, 4, v0
	v_or_b32_e32 v3, 0x2000, v2
	s_add_u32 s4, s36, 0x1180000
	v_lshrrev_b32_e32 v4, 7, v3
	v_lshrrev_b32_e32 v3, 6, v3
	v_lshrrev_b32_e32 v5, 5, v0
	v_lshrrev_b32_e32 v6, 2, v0
	s_movk_i32 s6, 0xc0
	v_and_b32_e32 v8, 32, v0
	s_addc_u32 s5, s37, 0
	v_and_b32_e32 v5, 4, v5
	v_bfe_u32 v7, v0, 2, 2
	v_and_or_b32 v3, v3, s6, v168
	v_bitop3_b32 v2, v2, v8, 48 bitop3:0x6c
	v_and_or_b32 v6, v6, 64, v168
	s_add_u32 s40, s36, 0x26000000
	v_or3_b32 v3, v3, v5, v7
	v_and_or_b32 v2, v0, 64, v2
	v_or3_b32 v5, v6, v5, v7
	s_addc_u32 s41, s37, 0
	v_lshl_or_b32 v70, v5, 15, v2
	v_bfe_u32 v5, v0, 2, 4
	s_movk_i32 s6, 0x70
	s_ashr_i32 s18, s2, 8
	s_and_b32 s68, s2, 3
	v_and_or_b32 v4, v4, s6, v5
	s_lshl_b32 s6, s18, 10
	s_lshl_b32 s7, s68, 8
	s_or_b32 s6, s6, s7
	s_lshr_b32 s10, s12, 6
	s_bfe_u32 s69, s2, 0x60002
	s_ashr_i32 s7, s6, 31
	s_lshr_b32 s15, s12, 8
	s_lshl_b32 s14, s10, 10
	s_lshl_b32 s8, s69, 9
	s_lshl_b64 s[6:7], s[6:7], 15
	s_add_u32 s6, s40, s6
	s_addc_u32 s7, s41, s7
	s_add_u32 s20, s6, s8
	s_addc_u32 s21, s7, 0
	s_add_i32 s42, s14, 0
	s_add_i32 m0, s42, 0x10000
	v_lshl_or_b32 v66, v3, 15, v2
	global_load_lds_dwordx4 v70, s[20:21]
	s_add_i32 m0, s42, 0x12000
	v_lshrrev_b32_e32 v3, 3, v0
	v_or_b32_e32 v72, 0x40000, v70
	global_load_lds_dwordx4 v66, s[20:21]
	s_add_i32 m0, s42, 0x14000
	v_or_b32_e32 v68, 0x40000, v66
	v_and_or_b32 v3, v3, 48, v5
	global_load_lds_dwordx4 v72, s[20:21]
	s_add_i32 m0, s42, 0x16000
	v_lshl_or_b32 v74, v3, 9, v2
	global_load_lds_dwordx4 v68, s[20:21]
	s_mov_b32 m0, s42
	s_add_i32 s43, s42, 0x2000
	v_lshl_or_b32 v76, v4, 9, v2
	global_load_lds_dwordx4 v74, s[4:5]
	s_mov_b32 m0, s43
	s_add_i32 s44, s42, 0x4000
	v_or_b32_e32 v78, 0x10000, v74
	global_load_lds_dwordx4 v76, s[4:5]
	s_mov_b32 m0, s44
	s_add_i32 s45, s42, 0x6000
	v_or_b32_e32 v80, 0x10000, v76
	global_load_lds_dwordx4 v78, s[4:5]
	s_mov_b32 m0, s45
	v_mov_b32_e32 v83, 0
	global_load_lds_dwordx4 v80, s[4:5]
	v_mov_b32_e32 v71, v83
	v_mov_b32_e32 v67, v83
	s_cmp_eq_u32 s15, 1
	s_mov_b32 s46, 0
	v_lshl_add_u64 v[4:5], s[20:21], 0, v[70:71]
	v_lshl_add_u64 v[2:3], s[20:21], 0, v[66:67]
	v_mov_b32_e32 v73, v83
	v_mov_b32_e32 v69, v83
	v_mov_b32_e32 v75, v83
	s_cselect_b64 s[6:7], -1, 0
	s_cmp_lg_u32 s15, 1
	v_mov_b32_e32 v77, v83
	s_cbranch_scc1 .LBB0_686
.LBB0_686:
	s_add_u32 s8, s36, 0x1e000000
	s_addc_u32 s9, s37, 0
	s_and_b32 s19, s10, 3
	s_mov_b64 s[10:11], 0x80
	s_add_u32 s16, s20, 0x80
	s_addc_u32 s17, s21, 0
	s_add_i32 m0, s42, 0x18000
	v_lshl_add_u64 v[4:5], v[4:5], 0, s[10:11]
	s_waitcnt vmcnt(2)
	s_barrier
	global_load_lds_dwordx4 v[4:5], off
	s_add_i32 m0, s42, 0x1a000
	s_add_u32 s22, s36, 0x1180080
	v_lshl_add_u64 v[2:3], v[2:3], 0, s[10:11]
	s_addc_u32 s23, s37, 0
	s_add_i32 s47, s42, 0x8000
	global_load_lds_dwordx4 v[2:3], off
	v_lshl_add_u64 v[2:3], s[22:23], 0, v[74:75]
	s_mov_b32 m0, s47
	s_add_i32 s48, s42, 0xa000
	global_load_lds_dwordx4 v[2:3], off
	v_lshl_add_u64 v[2:3], s[22:23], 0, v[76:77]
	s_mov_b32 m0, s48
	v_lshl_or_b32 v86, s15, 12, v169
	global_load_lds_dwordx4 v[2:3], off
	s_add_i32 m0, s42, 0x1c000
	v_lshl_add_u64 v[2:3], s[16:17], 0, v[72:73]
	global_load_lds_dwordx4 v[2:3], off
	v_lshl_add_u64 v[2:3], s[16:17], 0, v[68:69]
	s_add_i32 m0, s42, 0x1e000
	s_cmpk_lt_u32 s12, 0x100
	global_load_lds_dwordx4 v[2:3], off
	s_cselect_b64 s[12:13], -1, 0
	s_lshl_b32 s16, s19, 6
	v_lshl_or_b32 v2, s15, 13, v172
	v_lshl_or_b32 v3, s19, 12, v172
	s_waitcnt vmcnt(6)
	s_or_b32 s49, s16, 0x200
	v_and_or_b32 v84, s16, 64, v168
	s_add_i32 s53, 0, 0x10000
	s_add_i32 s59, 0, 0x14000
	s_add_i32 s15, 0, 0x18000
	s_add_i32 s16, 0, 0x1c000
	v_or_b32_e32 v88, 0x400, v86
	v_or_b32_e32 v90, 0x800, v86
	v_or_b32_e32 v92, 0xc00, v86
	v_add_u32_e32 v94, s53, v3
	v_add_u32_e32 v95, s59, v3
	s_add_i32 s53, s53, s14
	s_add_i32 s59, s59, s14
	s_add_i32 s61, s15, s14
	s_add_i32 s63, s16, s14
	v_mov_b32_e32 v79, v83
	v_mov_b32_e32 v81, v83
	v_mov_b32_e32 v85, v83
	v_ashrrev_i32_e32 v87, 31, v86
	v_ashrrev_i32_e32 v89, 31, v88
	v_ashrrev_i32_e32 v91, 31, v90
	v_ashrrev_i32_e32 v93, 31, v92
	v_add_u32_e32 v96, 0, v2
	s_mov_b32 s50, 0xc3e00000
	s_add_i32 s51, s42, 0xc000
	s_add_i32 s52, s42, 0xe000
	s_add_i32 s58, s53, 0x2000
	s_add_i32 s60, s59, 0x2000
	s_add_i32 s62, s61, 0x2000
	s_add_i32 s64, s63, 0x2000
	v_add_u32_e32 v97, s15, v3
	v_add_u32_e32 v98, s16, v3
	v_mov_b32_e32 v99, 0x43e00000
	s_mov_b64 s[14:15], s[20:21]
	s_barrier
	s_branch .LBB0_689

; #define PG8_WAIT_V(n) asm volatile("s_waitcnt vmcnt(" #n ")" ::: "memory")
; #define PG8_WAIT_L(n) asm volatile("s_waitcnt lgkmcnt(" #n ")" ::: "memory")
; #define PG8_BAR __builtin_amdgcn_s_barrier()
; #define PG8_SCHED __builtin_amdgcn_sched_barrier(0)
; template <class Epi, class Sched, bool ALIGN_EPI = true, bool F8 = false>
; __device__ __forceinline__ void gemm_phase(PG8_LAS unsigned char* lds, const Sched& S, const Epi& E) {
;     ...
;     for (;;) {
;         const bool has_next = S.next(ui + 1, nxt);
;         const char* nA = has_next ? nxt.A : cA; const char* nB = has_next ? nxt.B : cB;
;         const int nt = cur.nt;
; #pragma unroll 1
;         for (int t = 0; t < nt; t += 2) {
;             const bool last = (t == nt - 2);
;             if constexpr (Sched::GATHER) { if (last && has_next) S.a_off(nxt, Rs, Cs, voffAn); }
;             const char* a1 = cA + (size_t)(t + 1) * kstep;
;             const char* a2 = last ? nA : cA + (size_t)(t + 2) * kstep; const char* b2 = last ? nB : cB + (size_t)(t + 2) * kstepB;
;             const char* a3 = a2 + kstep; const char* b3 = b2 + kstepB;
;             unsigned vA2[2][2];
; #pragma unroll
;             for (int h = 0; h < 2; ++h)
; #pragma unroll
;                 for (int i = 0; i < 2; ++i) { if constexpr (Sched::GATHER) vA2[h][i] = (last && has_next) ? voffAn[h][i] : voffA[h][i]; else vA2[h][i] = voffA[h][i]; }
;             PG8_LDB(B0, 0, 0); PG8_LDB(B1, 0, 1); PG8_SCHED; PG8_LDA(At, 0, 0); PG8_STAGE(PG8_SA(1, 1), a1, voffA[1]);
;             PG8_WAIT_V(8); PG8_WAIT_L(0); PG8_BAR; PG8_MMA(0, 0, At, B0); PG8_MMA(0, 1, At, B1); PG8_BAR; PG8_SCHED;
;             PG8_LDA(At, 0, 1); PG8_STAGE(PG8_SB(0, 0), b2, voffB[0]); PG8_STAGE(PG8_SB(0, 1), b2, voffB[1]); PG8_STAGE(PG8_SA(0, 0), a2, vA2[0]);
;             PG8_WAIT_V(8); PG8_WAIT_L(0); PG8_BAR; PG8_MMA(1, 0, At, B0); PG8_MMA(1, 1, At, B1); PG8_BAR; PG8_SCHED;
;             PG8_LDB(B0, 1, 0); PG8_LDB(B1, 1, 1); PG8_SCHED; PG8_LDA(At, 1, 0); PG8_STAGE(PG8_SA(0, 1), a2, vA2[1]);
;             PG8_WAIT_V(8); PG8_WAIT_L(0); PG8_BAR; PG8_MMA(0, 0, At, B0); PG8_MMA(0, 1, At, B1); PG8_BAR; PG8_SCHED;
;             PG8_LDA(At, 1, 1); PG8_STAGE(PG8_SB(1, 0), b3, voffB[0]); PG8_STAGE(PG8_SB(1, 1), b3, voffB[1]); PG8_STAGE(PG8_SA(1, 0), a3, vA2[0]);
;             PG8_WAIT_V(8); PG8_WAIT_L(0); PG8_BAR; PG8_MMA(1, 0, At, B0); PG8_MMA(1, 1, At, B1); PG8_BAR; PG8_SCHED;
.LBB0_691:
	v_mov_b32_e32 v2, 0
	s_mov_b32 s19, 0
	s_mov_b64 s[22:23], -1
	s_mov_b64 s[24:25], 0
	v_mov_b32_e32 v3, v2
	v_mov_b32_e32 v4, v2
	v_mov_b32_e32 v5, v2
	v_mov_b32_e32 v6, v2
	v_mov_b32_e32 v7, v2
	v_mov_b32_e32 v8, v2
	v_mov_b32_e32 v9, v2
	v_mov_b32_e32 v14, v2
	v_mov_b32_e32 v15, v2
	v_mov_b32_e32 v16, v2
	v_mov_b32_e32 v17, v2
	v_mov_b32_e32 v22, v2
	v_mov_b32_e32 v23, v2
	v_mov_b32_e32 v24, v2
	v_mov_b32_e32 v25, v2
	v_mov_b32_e32 v30, v2
	v_mov_b32_e32 v31, v2
	v_mov_b32_e32 v32, v2
	v_mov_b32_e32 v33, v2
	v_mov_b32_e32 v38, v2
	v_mov_b32_e32 v39, v2
	v_mov_b32_e32 v40, v2
	v_mov_b32_e32 v41, v2
	v_mov_b32_e32 v46, v2
	v_mov_b32_e32 v47, v2
	v_mov_b32_e32 v48, v2
	v_mov_b32_e32 v49, v2
	v_mov_b32_e32 v54, v2
	v_mov_b32_e32 v55, v2
	v_mov_b32_e32 v56, v2
	v_mov_b32_e32 v57, v2
	v_mov_b32_e32 v10, v2
	v_mov_b32_e32 v11, v2
	v_mov_b32_e32 v12, v2
	v_mov_b32_e32 v13, v2
	v_mov_b32_e32 v18, v2
	v_mov_b32_e32 v19, v2
	v_mov_b32_e32 v20, v2
	v_mov_b32_e32 v21, v2
	v_mov_b32_e32 v26, v2
	v_mov_b32_e32 v27, v2
	v_mov_b32_e32 v28, v2
	v_mov_b32_e32 v29, v2
	v_mov_b32_e32 v34, v2
	v_mov_b32_e32 v35, v2
	v_mov_b32_e32 v36, v2
	v_mov_b32_e32 v37, v2
	v_mov_b32_e32 v42, v2
	v_mov_b32_e32 v43, v2
	v_mov_b32_e32 v44, v2
	v_mov_b32_e32 v45, v2
	v_mov_b32_e32 v50, v2
	v_mov_b32_e32 v51, v2
	v_mov_b32_e32 v52, v2
	v_mov_b32_e32 v53, v2
	v_mov_b32_e32 v58, v2
	v_mov_b32_e32 v59, v2
	v_mov_b32_e32 v60, v2
	v_mov_b32_e32 v61, v2
	v_mov_b32_e32 v62, v2
	v_mov_b32_e32 v63, v2
	v_mov_b32_e32 v64, v2
	v_mov_b32_e32 v65, v2
	s_bitcmp1_b32 s3, 2
	s_cbranch_scc1 .Lh1e_19328
.LBB0_692:
	s_add_u32 s30, s4, s19
	s_addc_u32 s31, s5, 0
	s_add_i32 s28, s19, 0x100
	s_and_b64 s[26:27], s[24:25], exec
	s_cselect_b32 s26, 0, s28
	s_cselect_b32 s27, 0, 0
	s_add_u32 s26, s4, s26
	ds_read_b128 v[100:103], v94
	ds_read_b128 v[104:107], v94 offset:1024
	ds_read_b128 v[108:111], v94 offset:2048
	ds_read_b128 v[112:115], v94 offset:3072
	ds_read_b128 v[116:119], v95
	ds_read_b128 v[120:123], v95 offset:1024
	ds_read_b128 v[124:127], v95 offset:2048
	ds_read_b128 v[128:131], v95 offset:3072
	s_addc_u32 s27, s5, s27
	s_add_u32 s19, s20, s19
	s_addc_u32 s28, s21, 0
	s_add_u32 s19, s19, 0x100
	s_addc_u32 s28, s28, 0
	s_and_b64 s[24:25], s[24:25], exec
	s_cselect_b32 s29, s15, s28
	s_cselect_b32 s28, s14, s19
	s_add_u32 s30, s30, 0x80
	s_addc_u32 s31, s31, 0
	s_add_u32 s24, s28, 0x80
	s_addc_u32 s25, s29, 0
	s_mov_b32 m0, s51
	v_lshl_add_u64 v[164:165], s[30:31], 0, v[78:79]
	ds_read_b128 v[132:135], v96
	ds_read_b128 v[136:139], v96 offset:1024
	ds_read_b128 v[140:143], v96 offset:2048
	ds_read_b128 v[144:147], v96 offset:3072
	ds_read_b128 v[148:151], v96 offset:4096
	ds_read_b128 v[152:155], v96 offset:5120
	ds_read_b128 v[156:159], v96 offset:6144
	ds_read_b128 v[160:163], v96 offset:7168
	global_load_lds_dwordx4 v[164:165], off
	v_lshl_add_u64 v[164:165], s[30:31], 0, v[80:81]
	s_mov_b32 m0, s52
	s_nop 0
	global_load_lds_dwordx4 v[164:165], off
	s_waitcnt vmcnt(8)
	s_waitcnt lgkmcnt(0)
	s_setprio 1
	v_mfma_f32_16x16x32_bf16 v[62:65], v[100:103], v[132:135], v[62:65]
	v_mfma_f32_16x16x32_bf16 v[58:61], v[108:111], v[132:135], v[58:61]
	v_mfma_f32_16x16x32_bf16 v[50:53], v[100:103], v[140:143], v[50:53]
	v_mfma_f32_16x16x32_bf16 v[42:45], v[108:111], v[140:143], v[42:45]
	v_mfma_f32_16x16x32_bf16 v[34:37], v[100:103], v[148:151], v[34:37]
	v_mfma_f32_16x16x32_bf16 v[26:29], v[108:111], v[148:151], v[26:29]
	v_mfma_f32_16x16x32_bf16 v[18:21], v[100:103], v[156:159], v[18:21]
	v_mfma_f32_16x16x32_bf16 v[10:13], v[108:111], v[156:159], v[10:13]
	v_mfma_f32_16x16x32_bf16 v[62:65], v[104:107], v[136:139], v[62:65]
	v_mfma_f32_16x16x32_bf16 v[58:61], v[112:115], v[136:139], v[58:61]
	v_mfma_f32_16x16x32_bf16 v[50:53], v[104:107], v[144:147], v[50:53]
	v_mfma_f32_16x16x32_bf16 v[42:45], v[112:115], v[144:147], v[42:45]
	v_mfma_f32_16x16x32_bf16 v[34:37], v[104:107], v[152:155], v[34:37]
	v_mfma_f32_16x16x32_bf16 v[26:29], v[112:115], v[152:155], v[26:29]
	v_mfma_f32_16x16x32_bf16 v[18:21], v[104:107], v[160:163], v[18:21]
	v_mfma_f32_16x16x32_bf16 v[10:13], v[112:115], v[160:163], v[10:13]
	s_setprio 0
	s_setprio 1
	v_mfma_f32_16x16x32_bf16 v[54:57], v[116:119], v[132:135], v[54:57]
	v_mfma_f32_16x16x32_bf16 v[46:49], v[124:127], v[132:135], v[46:49]
	v_mfma_f32_16x16x32_bf16 v[38:41], v[116:119], v[140:143], v[38:41]
	v_mfma_f32_16x16x32_bf16 v[30:33], v[124:127], v[140:143], v[30:33]
	v_mfma_f32_16x16x32_bf16 v[22:25], v[116:119], v[148:151], v[22:25]
	v_mfma_f32_16x16x32_bf16 v[14:17], v[124:127], v[148:151], v[14:17]
	v_mfma_f32_16x16x32_bf16 v[6:9], v[116:119], v[156:159], v[6:9]
	v_mfma_f32_16x16x32_bf16 v[2:5], v[124:127], v[156:159], v[2:5]
	v_mfma_f32_16x16x32_bf16 v[54:57], v[120:123], v[136:139], v[54:57]
	v_mfma_f32_16x16x32_bf16 v[46:49], v[128:131], v[136:139], v[46:49]
	v_mfma_f32_16x16x32_bf16 v[38:41], v[120:123], v[144:147], v[38:41]
	v_mfma_f32_16x16x32_bf16 v[30:33], v[128:131], v[144:147], v[30:33]
	v_mfma_f32_16x16x32_bf16 v[22:25], v[120:123], v[152:155], v[22:25]
	v_mfma_f32_16x16x32_bf16 v[14:17], v[128:131], v[152:155], v[14:17]
	v_mfma_f32_16x16x32_bf16 v[6:9], v[120:123], v[160:163], v[6:9]
	v_mfma_f32_16x16x32_bf16 v[2:5], v[128:131], v[160:163], v[2:5]
	s_setprio 0
	s_barrier
; #define PG8_STAGE(bufoff, gbase, voff) do { _Pragma("unroll") for (int _i = 0; _i < 2; ++_i) \
;         __builtin_amdgcn_global_load_lds((const unsigned*)((const char*)(gbase) + (voff)[_i]), (PG8_LAS unsigned*)(lds + (bufoff) + ldsw + _i * 8192), 16, 0, 0); } while (0)
; #define PG8_WAIT_V(n) asm volatile("s_waitcnt vmcnt(" #n ")" ::: "memory")
; #define PG8_WAIT_L(n) asm volatile("s_waitcnt lgkmcnt(" #n ")" ::: "memory")
; #define PG8_BAR __builtin_amdgcn_s_barrier()
; #define PG8_SCHED __builtin_amdgcn_sched_barrier(0)
; template <class Epi, class Sched, bool ALIGN_EPI = true, bool F8 = false>
; __device__ __forceinline__ void gemm_phase(PG8_LAS unsigned char* lds, const Sched& S, const Epi& E) {
;     ...
;             PG8_LDB(B0, 0, 0); PG8_LDB(B1, 0, 1); PG8_SCHED; PG8_LDA(At, 0, 0); PG8_STAGE(PG8_SA(1, 1), a1, voffA[1]);
;             PG8_WAIT_V(8); PG8_WAIT_L(0); PG8_BAR; PG8_MMA(0, 0, At, B0); PG8_MMA(0, 1, At, B1); PG8_BAR; PG8_SCHED;
;             PG8_LDA(At, 0, 1); PG8_STAGE(PG8_SB(0, 0), b2, voffB[0]); PG8_STAGE(PG8_SB(0, 1), b2, voffB[1]); PG8_STAGE(PG8_SA(0, 0), a2, vA2[0]);
;             PG8_WAIT_V(8); PG8_WAIT_L(0); PG8_BAR; PG8_MMA(1, 0, At, B0); PG8_MMA(1, 1, At, B1); PG8_BAR; PG8_SCHED;
;             PG8_LDB(B0, 1, 0); PG8_LDB(B1, 1, 1); PG8_SCHED; PG8_LDA(At, 1, 0); PG8_STAGE(PG8_SA(0, 1), a2, vA2[1]);
;             PG8_WAIT_V(8); PG8_WAIT_L(0); PG8_BAR; PG8_MMA(0, 0, At, B0); PG8_MMA(0, 1, At, B1); PG8_BAR; PG8_SCHED;
;             PG8_LDA(At, 1, 1); PG8_STAGE(PG8_SB(1, 0), b3, voffB[0]); PG8_STAGE(PG8_SB(1, 1), b3, voffB[1]); PG8_STAGE(PG8_SA(1, 0), a3, vA2[0]);
;             PG8_WAIT_V(8); PG8_WAIT_L(0); PG8_BAR; PG8_MMA(1, 0, At, B0); PG8_MMA(1, 1, At, B1); PG8_BAR; PG8_SCHED;
	s_mov_b32 m0, s53
	v_lshl_add_u64 v[164:165], s[28:29], 0, v[70:71]
	global_load_lds_dwordx4 v[164:165], off
	v_lshl_add_u64 v[166:167], s[28:29], 0, v[66:67]
	s_mov_b32 m0, s58
	v_lshl_add_u64 v[100:101], s[28:29], 0, v[72:73]
	global_load_lds_dwordx4 v[166:167], off
	s_mov_b32 m0, s59
	v_lshl_add_u64 v[168:169], s[26:27], 0, v[74:75]
	global_load_lds_dwordx4 v[100:101], off
	v_lshl_add_u64 v[100:101], s[28:29], 0, v[68:69]
	s_mov_b32 m0, s60
	v_lshl_add_u64 v[172:173], s[26:27], 0, v[76:77]
	global_load_lds_dwordx4 v[100:101], off
	s_mov_b32 m0, s42
	s_nop 0
	global_load_lds_dwordx4 v[168:169], off
	s_mov_b32 m0, s43
	s_nop 0
	global_load_lds_dwordx4 v[172:173], off
	s_waitcnt vmcnt(8)
	s_waitcnt lgkmcnt(0)
	s_setprio 1
	s_setprio 0
	s_setprio 1
	s_setprio 0
	s_barrier
	ds_read_b128 v[100:103], v97
	ds_read_b128 v[104:107], v97 offset:1024
	ds_read_b128 v[108:111], v97 offset:2048
	ds_read_b128 v[112:115], v97 offset:3072
	ds_read_b128 v[116:119], v98
	ds_read_b128 v[120:123], v98 offset:1024
	ds_read_b128 v[124:127], v98 offset:2048
	ds_read_b128 v[128:131], v98 offset:3072
	s_mov_b32 m0, s44
	v_lshl_add_u64 v[174:175], s[26:27], 0, v[78:79]
	ds_read_b128 v[132:135], v96 offset:32768
	ds_read_b128 v[136:139], v96 offset:33792
	ds_read_b128 v[140:143], v96 offset:34816
	ds_read_b128 v[144:147], v96 offset:35840
	ds_read_b128 v[148:151], v96 offset:36864
	ds_read_b128 v[152:155], v96 offset:37888
	ds_read_b128 v[156:159], v96 offset:38912
	ds_read_b128 v[160:163], v96 offset:39936
	global_load_lds_dwordx4 v[174:175], off
	v_lshl_add_u64 v[174:175], s[26:27], 0, v[80:81]
	s_mov_b32 m0, s45
	s_nop 0
	global_load_lds_dwordx4 v[174:175], off
	s_waitcnt vmcnt(8)
	s_waitcnt lgkmcnt(0)
	s_setprio 1
	v_mfma_f32_16x16x32_bf16 v[62:65], v[100:103], v[132:135], v[62:65]
	v_mfma_f32_16x16x32_bf16 v[58:61], v[108:111], v[132:135], v[58:61]
	v_mfma_f32_16x16x32_bf16 v[50:53], v[100:103], v[140:143], v[50:53]
	v_mfma_f32_16x16x32_bf16 v[42:45], v[108:111], v[140:143], v[42:45]
	v_mfma_f32_16x16x32_bf16 v[34:37], v[100:103], v[148:151], v[34:37]
	v_mfma_f32_16x16x32_bf16 v[26:29], v[108:111], v[148:151], v[26:29]
	v_mfma_f32_16x16x32_bf16 v[18:21], v[100:103], v[156:159], v[18:21]
	v_mfma_f32_16x16x32_bf16 v[10:13], v[108:111], v[156:159], v[10:13]
	v_mfma_f32_16x16x32_bf16 v[62:65], v[104:107], v[136:139], v[62:65]
	v_mfma_f32_16x16x32_bf16 v[58:61], v[112:115], v[136:139], v[58:61]
	v_mfma_f32_16x16x32_bf16 v[50:53], v[104:107], v[144:147], v[50:53]
	v_mfma_f32_16x16x32_bf16 v[42:45], v[112:115], v[144:147], v[42:45]
	v_mfma_f32_16x16x32_bf16 v[34:37], v[104:107], v[152:155], v[34:37]
	v_mfma_f32_16x16x32_bf16 v[26:29], v[112:115], v[152:155], v[26:29]
	v_mfma_f32_16x16x32_bf16 v[18:21], v[104:107], v[160:163], v[18:21]
	v_mfma_f32_16x16x32_bf16 v[10:13], v[112:115], v[160:163], v[10:13]
	s_setprio 0
	s_setprio 1
	v_mfma_f32_16x16x32_bf16 v[54:57], v[116:119], v[132:135], v[54:57]
	v_mfma_f32_16x16x32_bf16 v[46:49], v[124:127], v[132:135], v[46:49]
	v_mfma_f32_16x16x32_bf16 v[38:41], v[116:119], v[140:143], v[38:41]
	v_mfma_f32_16x16x32_bf16 v[30:33], v[124:127], v[140:143], v[30:33]
	v_mfma_f32_16x16x32_bf16 v[22:25], v[116:119], v[148:151], v[22:25]
	v_mfma_f32_16x16x32_bf16 v[14:17], v[124:127], v[148:151], v[14:17]
	v_mfma_f32_16x16x32_bf16 v[6:9], v[116:119], v[156:159], v[6:9]
	v_mfma_f32_16x16x32_bf16 v[2:5], v[124:127], v[156:159], v[2:5]
	v_mfma_f32_16x16x32_bf16 v[54:57], v[120:123], v[136:139], v[54:57]
	v_mfma_f32_16x16x32_bf16 v[46:49], v[128:131], v[136:139], v[46:49]
	v_mfma_f32_16x16x32_bf16 v[38:41], v[120:123], v[144:147], v[38:41]
	v_mfma_f32_16x16x32_bf16 v[30:33], v[128:131], v[144:147], v[30:33]
	v_mfma_f32_16x16x32_bf16 v[22:25], v[120:123], v[152:155], v[22:25]
	v_mfma_f32_16x16x32_bf16 v[14:17], v[128:131], v[152:155], v[14:17]
	v_mfma_f32_16x16x32_bf16 v[6:9], v[120:123], v[160:163], v[6:9]
	v_mfma_f32_16x16x32_bf16 v[2:5], v[128:131], v[160:163], v[2:5]
	s_setprio 0
	s_barrier
	s_mov_b32 m0, s61
	v_lshl_add_u64 v[100:101], v[164:165], 0, s[10:11]
	global_load_lds_dwordx4 v[100:101], off
	v_lshl_add_u64 v[100:101], v[166:167], 0, s[10:11]
	s_mov_b32 m0, s62
	s_nop 0
	global_load_lds_dwordx4 v[100:101], off
	v_lshl_add_u64 v[100:101], s[24:25], 0, v[72:73]
	s_mov_b32 m0, s63
	s_nop 0
	global_load_lds_dwordx4 v[100:101], off
	v_lshl_add_u64 v[100:101], s[24:25], 0, v[68:69]
	s_mov_b32 m0, s64
	s_nop 0
	global_load_lds_dwordx4 v[100:101], off
	v_lshl_add_u64 v[100:101], v[168:169], 0, s[10:11]
	s_mov_b32 m0, s47
	s_nop 0
	global_load_lds_dwordx4 v[100:101], off
	v_lshl_add_u64 v[100:101], v[172:173], 0, s[10:11]
	s_mov_b32 m0, s48
	s_nop 0
	global_load_lds_dwordx4 v[100:101], off
	s_waitcnt vmcnt(8)
	s_waitcnt lgkmcnt(0)
	s_setprio 1
	s_setprio 0
	s_setprio 1
	s_setprio 0
	s_barrier
	s_andn2_b64 vcc, exec, s[22:23]
	s_mov_b64 s[24:25], -1
	s_mov_b64 s[22:23], 0
	s_movk_i32 s19, 0x100
	s_cbranch_vccz .LBB0_692
	s_branch .Lfx_19328
; #define PG8_STAGE(bufoff, gbase, voff) do { _Pragma("unroll") for (int _i = 0; _i < 2; ++_i) \
;         __builtin_amdgcn_global_load_lds((const unsigned*)((const char*)(gbase) + (voff)[_i]), (PG8_LAS unsigned*)(lds + (bufoff) + ldsw + _i * 8192), 16, 0, 0); } while (0)
; #define PG8_WAIT_V(n) asm volatile("s_waitcnt vmcnt(" #n ")" ::: "memory")
; #define PG8_WAIT_L(n) asm volatile("s_waitcnt lgkmcnt(" #n ")" ::: "memory")
; #define PG8_BAR __builtin_amdgcn_s_barrier()
; #define PG8_SCHED __builtin_amdgcn_sched_barrier(0)
; template <class Epi, class Sched, bool ALIGN_EPI = true, bool F8 = false>
; __device__ __forceinline__ void gemm_phase(PG8_LAS unsigned char* lds, const Sched& S, const Epi& E) {
;     ...
;             PG8_LDB(B0, 0, 0); PG8_LDB(B1, 0, 1); PG8_SCHED; PG8_LDA(At, 0, 0); PG8_STAGE(PG8_SA(1, 1), a1, voffA[1]);
;             PG8_WAIT_V(8); PG8_WAIT_L(0); PG8_BAR; PG8_MMA(0, 0, At, B0); PG8_MMA(0, 1, At, B1); PG8_BAR; PG8_SCHED;
;             PG8_LDA(At, 0, 1); PG8_STAGE(PG8_SB(0, 0), b2, voffB[0]); PG8_STAGE(PG8_SB(0, 1), b2, voffB[1]); PG8_STAGE(PG8_SA(0, 0), a2, vA2[0]);
;             PG8_WAIT_V(8); PG8_WAIT_L(0); PG8_BAR; PG8_MMA(1, 0, At, B0); PG8_MMA(1, 1, At, B1); PG8_BAR; PG8_SCHED;
.Lh1e_19328:
.Lh1_692:
	s_add_u32 s30, s4, s19
	s_addc_u32 s31, s5, 0
	s_add_i32 s28, s19, 0x100
	s_and_b64 s[26:27], s[24:25], exec
	s_cselect_b32 s26, 0, s28
	s_cselect_b32 s27, 0, 0
	s_add_u32 s26, s4, s26
	ds_read_b128 v[100:103], v94
	ds_read_b128 v[104:107], v94 offset:1024
	ds_read_b128 v[108:111], v94 offset:2048
	ds_read_b128 v[112:115], v94 offset:3072
	ds_read_b128 v[116:119], v95
	ds_read_b128 v[120:123], v95 offset:1024
	ds_read_b128 v[124:127], v95 offset:2048
	ds_read_b128 v[128:131], v95 offset:3072
	s_addc_u32 s27, s5, s27
	s_add_u32 s19, s20, s19
	s_addc_u32 s28, s21, 0
	s_add_u32 s19, s19, 0x100
	s_addc_u32 s28, s28, 0
	s_and_b64 s[24:25], s[24:25], exec
	s_cselect_b32 s29, s15, s28
	s_cselect_b32 s28, s14, s19
	s_add_u32 s30, s30, 0x80
	s_addc_u32 s31, s31, 0
	s_add_u32 s24, s28, 0x80
	s_addc_u32 s25, s29, 0
	s_mov_b32 m0, s51
	v_lshl_add_u64 v[164:165], s[30:31], 0, v[78:79]
	ds_read_b128 v[132:135], v96
	ds_read_b128 v[136:139], v96 offset:1024
	ds_read_b128 v[140:143], v96 offset:2048
	ds_read_b128 v[144:147], v96 offset:3072
	ds_read_b128 v[148:151], v96 offset:4096
	ds_read_b128 v[152:155], v96 offset:5120
	ds_read_b128 v[156:159], v96 offset:6144
	ds_read_b128 v[160:163], v96 offset:7168
	global_load_lds_dwordx4 v[164:165], off
	v_lshl_add_u64 v[164:165], s[30:31], 0, v[80:81]
	s_mov_b32 m0, s52
	s_nop 0
	global_load_lds_dwordx4 v[164:165], off
	s_waitcnt vmcnt(8)
	s_waitcnt lgkmcnt(0)
	s_barrier
	s_setprio 2
	v_mfma_f32_16x16x32_bf16 v[62:65], v[100:103], v[132:135], v[62:65]
	v_mfma_f32_16x16x32_bf16 v[58:61], v[108:111], v[132:135], v[58:61]
	v_mfma_f32_16x16x32_bf16 v[50:53], v[100:103], v[140:143], v[50:53]
	v_mfma_f32_16x16x32_bf16 v[42:45], v[108:111], v[140:143], v[42:45]
	v_mfma_f32_16x16x32_bf16 v[34:37], v[100:103], v[148:151], v[34:37]
	v_mfma_f32_16x16x32_bf16 v[26:29], v[108:111], v[148:151], v[26:29]
	v_mfma_f32_16x16x32_bf16 v[18:21], v[100:103], v[156:159], v[18:21]
	v_mfma_f32_16x16x32_bf16 v[10:13], v[108:111], v[156:159], v[10:13]
	v_mfma_f32_16x16x32_bf16 v[62:65], v[104:107], v[136:139], v[62:65]
	v_mfma_f32_16x16x32_bf16 v[58:61], v[112:115], v[136:139], v[58:61]
	v_mfma_f32_16x16x32_bf16 v[50:53], v[104:107], v[144:147], v[50:53]
	v_mfma_f32_16x16x32_bf16 v[42:45], v[112:115], v[144:147], v[42:45]
	v_mfma_f32_16x16x32_bf16 v[34:37], v[104:107], v[152:155], v[34:37]
	v_mfma_f32_16x16x32_bf16 v[26:29], v[112:115], v[152:155], v[26:29]
	v_mfma_f32_16x16x32_bf16 v[18:21], v[104:107], v[160:163], v[18:21]
	v_mfma_f32_16x16x32_bf16 v[10:13], v[112:115], v[160:163], v[10:13]
	s_setprio 0
	s_setprio 2
	v_mfma_f32_16x16x32_bf16 v[54:57], v[116:119], v[132:135], v[54:57]
	v_mfma_f32_16x16x32_bf16 v[46:49], v[124:127], v[132:135], v[46:49]
	v_mfma_f32_16x16x32_bf16 v[38:41], v[116:119], v[140:143], v[38:41]
	v_mfma_f32_16x16x32_bf16 v[30:33], v[124:127], v[140:143], v[30:33]
	v_mfma_f32_16x16x32_bf16 v[22:25], v[116:119], v[148:151], v[22:25]
	v_mfma_f32_16x16x32_bf16 v[14:17], v[124:127], v[148:151], v[14:17]
	v_mfma_f32_16x16x32_bf16 v[6:9], v[116:119], v[156:159], v[6:9]
	v_mfma_f32_16x16x32_bf16 v[2:5], v[124:127], v[156:159], v[2:5]
	v_mfma_f32_16x16x32_bf16 v[54:57], v[120:123], v[136:139], v[54:57]
	v_mfma_f32_16x16x32_bf16 v[46:49], v[128:131], v[136:139], v[46:49]
	v_mfma_f32_16x16x32_bf16 v[38:41], v[120:123], v[144:147], v[38:41]
	v_mfma_f32_16x16x32_bf16 v[30:33], v[128:131], v[144:147], v[30:33]
	v_mfma_f32_16x16x32_bf16 v[22:25], v[120:123], v[152:155], v[22:25]
	v_mfma_f32_16x16x32_bf16 v[14:17], v[128:131], v[152:155], v[14:17]
	v_mfma_f32_16x16x32_bf16 v[6:9], v[120:123], v[160:163], v[6:9]
	v_mfma_f32_16x16x32_bf16 v[2:5], v[128:131], v[160:163], v[2:5]
	s_setprio 0
	s_mov_b32 m0, s53
	v_lshl_add_u64 v[164:165], s[28:29], 0, v[70:71]
	global_load_lds_dwordx4 v[164:165], off
	v_lshl_add_u64 v[166:167], s[28:29], 0, v[66:67]
	s_mov_b32 m0, s58
	v_lshl_add_u64 v[100:101], s[28:29], 0, v[72:73]
	global_load_lds_dwordx4 v[166:167], off
	s_mov_b32 m0, s59
	v_lshl_add_u64 v[168:169], s[26:27], 0, v[74:75]
	global_load_lds_dwordx4 v[100:101], off
	v_lshl_add_u64 v[100:101], s[28:29], 0, v[68:69]
	s_mov_b32 m0, s60
	v_lshl_add_u64 v[172:173], s[26:27], 0, v[76:77]
	global_load_lds_dwordx4 v[100:101], off
	s_mov_b32 m0, s42
	s_nop 0
	global_load_lds_dwordx4 v[168:169], off
	s_mov_b32 m0, s43
	s_nop 0
	global_load_lds_dwordx4 v[172:173], off
	s_waitcnt vmcnt(8)
	s_waitcnt lgkmcnt(0)
	s_barrier
; #define PG8_STAGE(bufoff, gbase, voff) do { _Pragma("unroll") for (int _i = 0; _i < 2; ++_i) \
;         __builtin_amdgcn_global_load_lds((const unsigned*)((const char*)(gbase) + (voff)[_i]), (PG8_LAS unsigned*)(lds + (bufoff) + ldsw + _i * 8192), 16, 0, 0); } while (0)
; #define PG8_WAIT_V(n) asm volatile("s_waitcnt vmcnt(" #n ")" ::: "memory")
; #define PG8_WAIT_L(n) asm volatile("s_waitcnt lgkmcnt(" #n ")" ::: "memory")
; #define PG8_BAR __builtin_amdgcn_s_barrier()
; #define PG8_SCHED __builtin_amdgcn_sched_barrier(0)
; template <class Epi, class Sched, bool ALIGN_EPI = true, bool F8 = false>
; __device__ __forceinline__ void gemm_phase(PG8_LAS unsigned char* lds, const Sched& S, const Epi& E) {
;     ...
;             PG8_WAIT_V(8); PG8_WAIT_L(0); PG8_BAR; PG8_MMA(1, 0, At, B0); PG8_MMA(1, 1, At, B1); PG8_BAR; PG8_SCHED;
;             PG8_LDB(B0, 1, 0); PG8_LDB(B1, 1, 1); PG8_SCHED; PG8_LDA(At, 1, 0); PG8_STAGE(PG8_SA(0, 1), a2, vA2[1]);
;             PG8_WAIT_V(8); PG8_WAIT_L(0); PG8_BAR; PG8_MMA(0, 0, At, B0); PG8_MMA(0, 1, At, B1); PG8_BAR; PG8_SCHED;
;             PG8_LDA(At, 1, 1); PG8_STAGE(PG8_SB(1, 0), b3, voffB[0]); PG8_STAGE(PG8_SB(1, 1), b3, voffB[1]); PG8_STAGE(PG8_SA(1, 0), a3, vA2[0]);
;             PG8_WAIT_V(8); PG8_WAIT_L(0); PG8_BAR; PG8_MMA(1, 0, At, B0); PG8_MMA(1, 1, At, B1); PG8_BAR; PG8_SCHED;
	s_setprio 2
	s_setprio 0
	s_setprio 2
	s_setprio 0
	ds_read_b128 v[100:103], v97
	ds_read_b128 v[104:107], v97 offset:1024
	ds_read_b128 v[108:111], v97 offset:2048
	ds_read_b128 v[112:115], v97 offset:3072
	ds_read_b128 v[116:119], v98
	ds_read_b128 v[120:123], v98 offset:1024
	ds_read_b128 v[124:127], v98 offset:2048
	ds_read_b128 v[128:131], v98 offset:3072
	s_mov_b32 m0, s44
	v_lshl_add_u64 v[174:175], s[26:27], 0, v[78:79]
	ds_read_b128 v[132:135], v96 offset:32768
	ds_read_b128 v[136:139], v96 offset:33792
	ds_read_b128 v[140:143], v96 offset:34816
	ds_read_b128 v[144:147], v96 offset:35840
	ds_read_b128 v[148:151], v96 offset:36864
	ds_read_b128 v[152:155], v96 offset:37888
	ds_read_b128 v[156:159], v96 offset:38912
	ds_read_b128 v[160:163], v96 offset:39936
	global_load_lds_dwordx4 v[174:175], off
	v_lshl_add_u64 v[174:175], s[26:27], 0, v[80:81]
	s_mov_b32 m0, s45
	s_nop 0
	global_load_lds_dwordx4 v[174:175], off
	s_waitcnt vmcnt(8)
	s_waitcnt lgkmcnt(0)
	s_barrier
	s_setprio 2
	v_mfma_f32_16x16x32_bf16 v[62:65], v[100:103], v[132:135], v[62:65]
	v_mfma_f32_16x16x32_bf16 v[58:61], v[108:111], v[132:135], v[58:61]
	v_mfma_f32_16x16x32_bf16 v[50:53], v[100:103], v[140:143], v[50:53]
	v_mfma_f32_16x16x32_bf16 v[42:45], v[108:111], v[140:143], v[42:45]
	v_mfma_f32_16x16x32_bf16 v[34:37], v[100:103], v[148:151], v[34:37]
	v_mfma_f32_16x16x32_bf16 v[26:29], v[108:111], v[148:151], v[26:29]
	v_mfma_f32_16x16x32_bf16 v[18:21], v[100:103], v[156:159], v[18:21]
	v_mfma_f32_16x16x32_bf16 v[10:13], v[108:111], v[156:159], v[10:13]
	v_mfma_f32_16x16x32_bf16 v[62:65], v[104:107], v[136:139], v[62:65]
	v_mfma_f32_16x16x32_bf16 v[58:61], v[112:115], v[136:139], v[58:61]
	v_mfma_f32_16x16x32_bf16 v[50:53], v[104:107], v[144:147], v[50:53]
	v_mfma_f32_16x16x32_bf16 v[42:45], v[112:115], v[144:147], v[42:45]
	v_mfma_f32_16x16x32_bf16 v[34:37], v[104:107], v[152:155], v[34:37]
	v_mfma_f32_16x16x32_bf16 v[26:29], v[112:115], v[152:155], v[26:29]
	v_mfma_f32_16x16x32_bf16 v[18:21], v[104:107], v[160:163], v[18:21]
	v_mfma_f32_16x16x32_bf16 v[10:13], v[112:115], v[160:163], v[10:13]
	s_setprio 0
	s_setprio 2
	v_mfma_f32_16x16x32_bf16 v[54:57], v[116:119], v[132:135], v[54:57]
	v_mfma_f32_16x16x32_bf16 v[46:49], v[124:127], v[132:135], v[46:49]
	v_mfma_f32_16x16x32_bf16 v[38:41], v[116:119], v[140:143], v[38:41]
	v_mfma_f32_16x16x32_bf16 v[30:33], v[124:127], v[140:143], v[30:33]
	v_mfma_f32_16x16x32_bf16 v[22:25], v[116:119], v[148:151], v[22:25]
	v_mfma_f32_16x16x32_bf16 v[14:17], v[124:127], v[148:151], v[14:17]
	v_mfma_f32_16x16x32_bf16 v[6:9], v[116:119], v[156:159], v[6:9]
	v_mfma_f32_16x16x32_bf16 v[2:5], v[124:127], v[156:159], v[2:5]
	v_mfma_f32_16x16x32_bf16 v[54:57], v[120:123], v[136:139], v[54:57]
	v_mfma_f32_16x16x32_bf16 v[46:49], v[128:131], v[136:139], v[46:49]
	v_mfma_f32_16x16x32_bf16 v[38:41], v[120:123], v[144:147], v[38:41]
	v_mfma_f32_16x16x32_bf16 v[30:33], v[128:131], v[144:147], v[30:33]
	v_mfma_f32_16x16x32_bf16 v[22:25], v[120:123], v[152:155], v[22:25]
	v_mfma_f32_16x16x32_bf16 v[14:17], v[128:131], v[152:155], v[14:17]
	v_mfma_f32_16x16x32_bf16 v[6:9], v[120:123], v[160:163], v[6:9]
	v_mfma_f32_16x16x32_bf16 v[2:5], v[128:131], v[160:163], v[2:5]
	s_setprio 0
	s_mov_b32 m0, s61
	v_lshl_add_u64 v[100:101], v[164:165], 0, s[10:11]
	global_load_lds_dwordx4 v[100:101], off
	v_lshl_add_u64 v[100:101], v[166:167], 0, s[10:11]
	s_mov_b32 m0, s62
	s_nop 0
	global_load_lds_dwordx4 v[100:101], off
	v_lshl_add_u64 v[100:101], s[24:25], 0, v[72:73]
	s_mov_b32 m0, s63
	s_nop 0
	global_load_lds_dwordx4 v[100:101], off
	v_lshl_add_u64 v[100:101], s[24:25], 0, v[68:69]
	s_mov_b32 m0, s64
	s_nop 0
	global_load_lds_dwordx4 v[100:101], off
	v_lshl_add_u64 v[100:101], v[168:169], 0, s[10:11]
	s_mov_b32 m0, s47
	s_nop 0
	global_load_lds_dwordx4 v[100:101], off
	v_lshl_add_u64 v[100:101], v[172:173], 0, s[10:11]
	s_mov_b32 m0, s48
	s_nop 0
	global_load_lds_dwordx4 v[100:101], off
	s_waitcnt vmcnt(8)
	s_waitcnt lgkmcnt(0)
	s_barrier
	s_setprio 2
	s_setprio 0
	s_setprio 2
	s_setprio 0
	s_andn2_b64 vcc, exec, s[22:23]
	s_mov_b64 s[24:25], -1
	s_mov_b64 s[22:23], 0
	s_movk_i32 s19, 0x100
	s_cbranch_vccz .Lh1_692

; __device__ __forceinline__ unsigned pk4_fp8(float a, float b, float c, float d) { int w = 0; w = __builtin_amdgcn_cvt_pk_fp8_f32(clamp8(a), clamp8(b), w, false); w = __builtin_amdgcn_cvt_pk_fp8_f32(clamp8(c), clamp8(d), w, true); return (unsigned)w; }
; __host__ __device__ __forceinline__ size_t tiled_off(size_t r, int kb, int ktiles) { return (((r >> 8) * ktiles + (kb >> 7)) << 15) + ((r & 255) << 7) + (kb & 127); }
; __device__ __forceinline__ float clamp8(float x) { return __builtin_amdgcn_fmed3f(x, -448.0f, 448.0f); }
;     __device__ __forceinline__ void operator()(AccRef acc, const GUnit& u, int wr, int wc, int fr, int fq) const {
;         const int b = u.x0, cp = u.x1, g = u.x2;
; #pragma unroll
;         for (int m = 0; m < 4; ++m) { const int rr = wr * 64 + m * 16 + fr; const size_t tok = (size_t)b * SEQ + rr * 64 + cp; u32x4 w;
; #pragma unroll
;             for (int q = 0; q < 4; ++q) { const f32x4 v = acc[0][q >> 1][m][q & 1]; w[q] = pk4_fp8(v[0], v[1], v[2], v[3]); }
;             *(u32x4*)(FO + tiled_off(tok, SW + g * 256 + wc * 64 + 16 * fq, (SW + FW) / 128)) = w; }
;     }
.LBB0_695:
	v_med3_f32 v82, v62, s50, v99
	v_med3_f32 v63, v63, s50, v99
	v_mov_b32_e32 v62, 0
	v_cvt_pk_fp8_f32 v62, v82, v63
	v_med3_f32 v64, v64, s50, v99
	v_med3_f32 v65, v65, s50, v99
	s_ashr_i32 s19, s18, 31
	v_cvt_pk_fp8_f32 v62, v64, v65 op_sel:[0,0,1]
	v_med3_f32 v46, v46, s50, v99
	v_med3_f32 v47, v47, s50, v99
	v_mov_b32_e32 v65, 0
	s_lshl_b64 s[18:19], s[18:19], 13
	s_ashr_i32 s20, s69, 31
	v_cvt_pk_fp8_f32 v65, v46, v47
	s_add_u32 s18, s18, s69
	s_addc_u32 s19, s19, s20
	s_lshl_b32 s20, s68, 8
	s_add_i32 s20, s49, s20
	v_med3_f32 v58, v58, s50, v99
	v_med3_f32 v59, v59, s50, v99
	v_mov_b32_e32 v63, 0
	v_med3_f32 v54, v54, s50, v99
	v_med3_f32 v55, v55, s50, v99
	v_mov_b32_e32 v64, 0
	v_med3_f32 v46, v48, s50, v99
	v_med3_f32 v47, v49, s50, v99
	s_ashr_i32 s20, s20, 7
	v_cvt_pk_fp8_f32 v63, v58, v59
	v_cvt_pk_fp8_f32 v64, v54, v55
	v_cvt_pk_fp8_f32 v65, v46, v47 op_sel:[0,0,1]
	v_lshl_add_u64 v[46:47], s[18:19], 0, v[86:87]
	s_ashr_i32 s21, s20, 31
	v_alignbit_b32 v48, v47, v46, 8
	v_mad_u64_u32 v[48:49], s[22:23], v48, 12, s[20:21]
	v_lshrrev_b32_e32 v47, 8, v47
	v_med3_f32 v58, v60, s50, v99
	v_med3_f32 v59, v61, s50, v99
	v_med3_f32 v54, v56, s50, v99
	v_med3_f32 v55, v57, s50, v99
	v_mad_u32_u24 v49, v47, 12, v49
	v_cvt_pk_fp8_f32 v63, v58, v59 op_sel:[0,0,1]
	v_cvt_pk_fp8_f32 v64, v54, v55 op_sel:[0,0,1]
	v_lshlrev_b64 v[48:49], 15, v[48:49]
	v_lshlrev_b32_e32 v46, 7, v46
	v_and_b32_e32 v82, 0x7f80, v46
	v_lshl_add_u64 v[46:47], s[8:9], 0, v[48:49]
	v_lshl_add_u64 v[46:47], v[46:47], 0, v[82:83]
	v_lshl_add_u64 v[46:47], v[46:47], 0, v[84:85]
	flat_store_dwordx4 v[46:47], v[62:65]
	v_med3_f32 v47, v50, s50, v99
	v_med3_f32 v48, v51, s50, v99
	v_mov_b32_e32 v46, v83
	v_cvt_pk_fp8_f32 v46, v47, v48
	v_med3_f32 v48, v52, s50, v99
	v_med3_f32 v49, v53, s50, v99
	v_med3_f32 v30, v30, s50, v99
	v_cvt_pk_fp8_f32 v46, v48, v49 op_sel:[0,0,1]
	v_med3_f32 v31, v31, s50, v99
	v_mov_b32_e32 v49, v83
	v_cvt_pk_fp8_f32 v49, v30, v31
	v_med3_f32 v42, v42, s50, v99
	v_med3_f32 v43, v43, s50, v99
	v_mov_b32_e32 v47, v83
	v_med3_f32 v38, v38, s50, v99
	v_med3_f32 v39, v39, s50, v99
	v_mov_b32_e32 v48, v83
	v_med3_f32 v30, v32, s50, v99
	v_med3_f32 v31, v33, s50, v99
	v_cvt_pk_fp8_f32 v47, v42, v43
	v_cvt_pk_fp8_f32 v48, v38, v39
	v_cvt_pk_fp8_f32 v49, v30, v31 op_sel:[0,0,1]
	v_lshl_add_u64 v[30:31], s[18:19], 0, v[88:89]
	v_alignbit_b32 v32, v31, v30, 8
	v_mad_u64_u32 v[32:33], s[22:23], v32, 12, s[20:21]
	v_lshrrev_b32_e32 v31, 8, v31
	v_med3_f32 v42, v44, s50, v99
	v_med3_f32 v43, v45, s50, v99
	v_med3_f32 v38, v40, s50, v99
	v_med3_f32 v39, v41, s50, v99
	v_mad_u32_u24 v33, v31, 12, v33
	v_cvt_pk_fp8_f32 v47, v42, v43 op_sel:[0,0,1]
	v_cvt_pk_fp8_f32 v48, v38, v39 op_sel:[0,0,1]
	v_lshlrev_b64 v[32:33], 15, v[32:33]
	v_lshlrev_b32_e32 v30, 7, v30
	v_and_b32_e32 v82, 0x7f80, v30
	v_lshl_add_u64 v[30:31], s[8:9], 0, v[32:33]
	v_lshl_add_u64 v[30:31], v[30:31], 0, v[82:83]
	v_lshl_add_u64 v[30:31], v[30:31], 0, v[84:85]
	flat_store_dwordx4 v[30:31], v[46:49]
	v_med3_f32 v31, v34, s50, v99
	v_med3_f32 v32, v35, s50, v99
	v_mov_b32_e32 v30, v83
	v_cvt_pk_fp8_f32 v30, v31, v32
	v_med3_f32 v32, v36, s50, v99
	v_med3_f32 v33, v37, s50, v99
	v_med3_f32 v14, v14, s50, v99
	v_cvt_pk_fp8_f32 v30, v32, v33 op_sel:[0,0,1]
	v_med3_f32 v15, v15, s50, v99
	v_mov_b32_e32 v33, v83
	v_cvt_pk_fp8_f32 v33, v14, v15
	v_med3_f32 v26, v26, s50, v99
	v_med3_f32 v27, v27, s50, v99
	v_mov_b32_e32 v31, v83
	v_med3_f32 v22, v22, s50, v99
	v_med3_f32 v23, v23, s50, v99
	v_mov_b32_e32 v32, v83
	v_med3_f32 v14, v16, s50, v99
	v_med3_f32 v15, v17, s50, v99
	v_cvt_pk_fp8_f32 v31, v26, v27
	v_cvt_pk_fp8_f32 v32, v22, v23
	v_cvt_pk_fp8_f32 v33, v14, v15 op_sel:[0,0,1]
	v_lshl_add_u64 v[14:15], s[18:19], 0, v[90:91]
	v_alignbit_b32 v16, v15, v14, 8
	v_mad_u64_u32 v[16:17], s[22:23], v16, 12, s[20:21]
	v_lshrrev_b32_e32 v15, 8, v15
	v_med3_f32 v26, v28, s50, v99
	v_med3_f32 v27, v29, s50, v99
	v_med3_f32 v22, v24, s50, v99
	v_med3_f32 v23, v25, s50, v99
	v_mad_u32_u24 v17, v15, 12, v17
	v_cvt_pk_fp8_f32 v31, v26, v27 op_sel:[0,0,1]
	v_cvt_pk_fp8_f32 v32, v22, v23 op_sel:[0,0,1]
	v_lshlrev_b64 v[16:17], 15, v[16:17]
	v_lshlrev_b32_e32 v14, 7, v14
	v_and_b32_e32 v82, 0x7f80, v14
	v_lshl_add_u64 v[14:15], s[8:9], 0, v[16:17]
	v_lshl_add_u64 v[14:15], v[14:15], 0, v[82:83]
	v_lshl_add_u64 v[14:15], v[14:15], 0, v[84:85]
	flat_store_dwordx4 v[14:15], v[30:33]
	v_med3_f32 v15, v18, s50, v99
	v_med3_f32 v16, v19, s50, v99
	v_mov_b32_e32 v14, v83
	v_cvt_pk_fp8_f32 v14, v15, v16
	v_med3_f32 v16, v20, s50, v99
	v_med3_f32 v17, v21, s50, v99
	v_med3_f32 v2, v2, s50, v99
	v_cvt_pk_fp8_f32 v14, v16, v17 op_sel:[0,0,1]
	v_med3_f32 v3, v3, s50, v99
	v_mov_b32_e32 v17, v83
	v_cvt_pk_fp8_f32 v17, v2, v3
	v_med3_f32 v10, v10, s50, v99
	v_med3_f32 v11, v11, s50, v99
	v_mov_b32_e32 v15, v83
	v_med3_f32 v6, v6, s50, v99
	v_med3_f32 v7, v7, s50, v99
	v_mov_b32_e32 v16, v83
	v_med3_f32 v2, v4, s50, v99
	v_med3_f32 v3, v5, s50, v99
	v_cvt_pk_fp8_f32 v15, v10, v11
	v_cvt_pk_fp8_f32 v16, v6, v7
	v_cvt_pk_fp8_f32 v17, v2, v3 op_sel:[0,0,1]
	v_lshl_add_u64 v[2:3], s[18:19], 0, v[92:93]
	v_alignbit_b32 v4, v3, v2, 8
	v_mad_u64_u32 v[4:5], s[18:19], v4, 12, s[20:21]
	v_lshrrev_b32_e32 v3, 8, v3
	v_med3_f32 v10, v12, s50, v99
	v_med3_f32 v11, v13, s50, v99
	v_med3_f32 v6, v8, s50, v99
	v_med3_f32 v7, v9, s50, v99
	v_mad_u32_u24 v5, v3, 12, v5
	v_cvt_pk_fp8_f32 v15, v10, v11 op_sel:[0,0,1]
	v_cvt_pk_fp8_f32 v16, v6, v7 op_sel:[0,0,1]
	v_lshlrev_b64 v[4:5], 15, v[4:5]
	v_lshlrev_b32_e32 v2, 7, v2
	v_and_b32_e32 v82, 0x7f80, v2
	v_lshl_add_u64 v[2:3], s[8:9], 0, v[4:5]
	v_lshl_add_u64 v[2:3], v[2:3], 0, v[82:83]
	v_lshl_add_u64 v[2:3], v[2:3], 0, v[84:85]
	s_andn2_b64 vcc, exec, s[16:17]
	s_mov_b64 s[16:17], -1
	flat_store_dwordx4 v[2:3], v[14:17]
	s_cbranch_vccnz .LBB0_688
	s_andn2_b64 vcc, exec, s[6:7]
	s_cbranch_vccnz .LBB0_687
	s_branch .LBB0_687

; #define PG8_WAIT_V(n) asm volatile("s_waitcnt vmcnt(" #n ")" ::: "memory")
; template <class Epi, class Sched, bool ALIGN_EPI = true, bool F8 = false>
; __device__ __forceinline__ void gemm_phase(PG8_LAS unsigned char* lds, const Sched& S, const Epi& E) {
;     const int tid = threadIdx.x, wid = __builtin_amdgcn_readfirstlane(tid >> 6), lane = tid & 63, wr = wid >> 2, wc = wid & 3, fr = lane & 15, fq = lane >> 4;
;     int Rs[2], Cs[2];
; #pragma unroll
;     for (int i = 0; i < 2; ++i) stage_rc(tid * 16 + i * 8192, Rs[i], Cs[i]);
;     unsigned voffB[2][2], voffA[2][2], voffAn[2][2];
; #pragma unroll
;     for (int h = 0; h < 2; ++h)
; #pragma unroll
;         for (int i = 0; i < 2; ++i) {
;             if constexpr (HasP16<Epi>::v) { const int r = Rs[i]; voffB[h][i] = S.b_off(64 * (r >> 5) + 16 * ((r & 15) >> 2) + 8 * h + 4 * ((r >> 4) & 1) + (r & 3), Cs[i]); }
;             else { const int Rb = Epi::PERM ? ((Rs[i] & ~31) + perm32(Rs[i] & 31)) : Rs[i]; voffB[h][i] = S.b_off(h * HALF + Rb, Cs[i]); } }
;     const size_t kstep = (size_t)SchedKstep<Sched>::v, kstepB = (size_t)SchedKstepB<Sched>::v;
;     const unsigned ldsw = (unsigned)wid * 1024u;
;     const int aoff = lds_byte(wr * 64 + fr, fq * 8), boff = lds_byte(wc * 32 + fr, fq * 8);
;     ...
;     GUnit cur, nxt; int ui = 0;
;     if (!S.next(0, cur)) return;
;     S.a_off(cur, Rs, Cs, voffA);
; #pragma unroll
;     for (int h = 0; h < 2; ++h)
; #pragma unroll
;         for (int i = 0; i < 2; ++i) voffAn[h][i] = voffA[h][i];
;     f32x4 acc[2][2][4][2];
; #pragma unroll
;     for (int a = 0; a < 2; ++a)
; #pragma unroll
;         for (int b = 0; b < 2; ++b)
; #pragma unroll
;             for (int m = 0; m < 4; ++m)
; #pragma unroll
;                 for (int n = 0; n < 2; ++n) acc[a][b][m][n] = (f32x4){0.f, 0.f, 0.f, 0.f};
;     bf16x8 At[4][2], B0[2][2], B1[2][2]; i32x8 At8[4], B08[2], B18[2];
;     const int f8scale = 0x7F7F7F7F;
;     const char* cA = cur.A; const char* cB = cur.B;
;     PG8_STAGE(PG8_SB(0, 0), cB, voffB[0]); PG8_STAGE(PG8_SB(0, 1), cB, voffB[1]); PG8_STAGE(PG8_SA(0, 0), cA, voffA[0]); PG8_STAGE(PG8_SA(0, 1), cA, voffA[1]);
;     if (wr == 1) PG8_BAR;
;     PG8_WAIT_V(2); PG8_BAR;
;     PG8_STAGE(PG8_SB(1, 0), cB + kstepB, voffB[0]); PG8_STAGE(PG8_SA(1, 0), cA + kstep, voffA[0]); PG8_STAGE(PG8_SB(1, 1), cB + kstepB, voffB[1]);
;     PG8_WAIT_V(6); PG8_BAR;
.LBB0_751:
	s_ashr_i32 s0, s6, 3
	s_add_u32 s6, s36, 0x37400000
	s_addc_u32 s7, s37, 0
	s_add_u32 s41, s36, 0x3c00000
	s_addc_u32 s42, s37, 0
	s_add_i32 s0, s8, s0
	s_ashr_i32 s8, s0, 31
	s_lshr_b32 s8, s8, 28
	s_add_i32 s8, s0, s8
	s_ashr_i32 s9, s8, 4
	s_and_b32 s8, s8, -16
	s_sub_i32 s8, s0, s8
	s_bfe_i32 s0, s8, 0x80000
	v_lshlrev_b32_e32 v2, 4, v0
	s_bfe_u32 s0, s0, 0x3000c
	v_and_b32_e32 v3, 32, v0
	v_or_b32_e32 v14, 0x2000, v2
	s_add_i32 s10, s8, s0
	v_bfe_u32 v13, v0, 2, 4
	v_bitop3_b32 v3, v2, v3, 48 bitop3:0x6c
	v_lshrrev_b32_e32 v2, 7, v14
	s_movk_i32 s1, 0x70
	s_bfe_i32 s0, s10, 0x80000
	s_and_b32 s10, s10, 0xf8
	v_lshrrev_b32_e32 v4, 2, v0
	v_and_or_b32 v7, v2, s1, v13
	v_and_b32_e32 v2, 48, v0
	v_lshrrev_b32_e32 v8, 5, v0
	s_sub_i32 s8, s8, s10
	v_and_b32_e32 v12, 64, v0
	v_and_b32_e32 v8, 4, v8
	v_bfe_u32 v9, v0, 2, 2
	v_and_or_b32 v4, v4, 64, v2
	s_lshl_b32 s9, s9, 3
	s_sext_i32_i8 s8, s8
	v_or_b32_e32 v5, v3, v12
	v_or3_b32 v4, v4, v8, v9
	s_add_i32 s8, s9, s8
	s_lshr_b32 s14, s16, 6
	v_lshl_or_b32 v172, v4, 10, v5
	v_lshrrev_b32_e32 v4, 6, v14
	s_movk_i32 s1, 0xc0
	s_sext_i32_i16 s0, s0
	s_ashr_i32 s9, s8, 31
	v_and_or_b32 v4, v4, s1, v2
	s_lshr_b32 s1, s16, 8
	s_lshl_b32 s43, s14, 10
	s_lshr_b32 s0, s0, 3
	s_lshl_b64 s[10:11], s[8:9], 18
	s_add_u32 s26, s6, s10
	s_addc_u32 s27, s7, s11
	s_bfe_i64 s[10:11], s[0:1], 0x100000
	s_lshl_b64 s[10:11], s[10:11], 18
	s_add_u32 s28, s41, s10
	s_addc_u32 s29, s42, s11
	s_add_i32 s44, s43, 0
	v_or3_b32 v4, v4, v8, v9
	s_add_i32 m0, s44, 0x10000
	v_lshl_or_b32 v174, v4, 10, v5
	global_load_lds_dwordx4 v172, s[28:29]
	s_add_i32 m0, s44, 0x12000
	v_lshrrev_b32_e32 v6, 3, v0
	v_or_b32_e32 v176, 0x2000, v172
	global_load_lds_dwordx4 v174, s[28:29]
	s_add_i32 m0, s44, 0x14000
	v_and_or_b32 v6, v6, 48, v13
	v_or_b32_e32 v178, 0x2000, v174
	global_load_lds_dwordx4 v176, s[28:29]
	s_add_i32 m0, s44, 0x16000
	v_lshl_or_b32 v180, v6, 10, v5
	global_load_lds_dwordx4 v178, s[28:29]
	s_mov_b32 m0, s44
	s_add_i32 s45, s44, 0x2000
	v_lshl_or_b32 v182, v7, 10, v5
	global_load_lds_dwordx4 v180, s[26:27]
	s_mov_b32 m0, s45
	s_add_i32 s46, s44, 0x4000
	v_or_b32_e32 v184, 0x20000, v180
	global_load_lds_dwordx4 v182, s[26:27]
	s_mov_b32 m0, s46
	s_add_i32 s47, s44, 0x6000
	v_or_b32_e32 v186, 0x20000, v182
	global_load_lds_dwordx4 v184, s[26:27]
	s_mov_b32 m0, s47
	v_mov_b32_e32 v189, 0
	global_load_lds_dwordx4 v186, s[26:27]
	v_mov_b32_e32 v173, v189
	v_mov_b32_e32 v175, v189
	v_mov_b32_e32 v181, v189
	v_mov_b32_e32 v183, v189
	s_cmp_eq_u32 s1, 1
	s_mov_b32 s48, 0x20000
	s_mov_b32 s9, 0
	v_lshl_add_u64 v[10:11], s[28:29], 0, v[172:173]
	v_lshl_add_u64 v[6:7], s[28:29], 0, v[174:175]
	v_mov_b32_e32 v177, v189
	v_mov_b32_e32 v179, v189
	v_lshl_add_u64 v[8:9], s[26:27], 0, v[180:181]
	v_lshl_add_u64 v[4:5], s[26:27], 0, v[182:183]
	s_cselect_b64 s[10:11], -1, 0
	s_cmp_lg_u32 s1, 1
	s_movk_i32 s49, 0x4000
	s_cbranch_scc1 .LBB0_753
.LBB0_753:
	s_add_u32 s12, s36, 0x1e000000
	s_addc_u32 s13, s37, 0
	s_and_b32 s22, s14, 3
	s_lshl_b32 s17, s1, 13
	s_lshl_b32 s23, s22, 12
	s_mov_b64 s[14:15], 0x80
	s_add_u32 s20, s28, 0x80
	s_addc_u32 s21, s29, 0
	s_add_i32 m0, s44, 0x18000
	v_lshl_add_u64 v[10:11], v[10:11], 0, s[14:15]
	s_waitcnt vmcnt(2)
	s_barrier
	global_load_lds_dwordx4 v[10:11], off
	v_lshl_add_u64 v[6:7], v[6:7], 0, s[14:15]
	s_add_i32 m0, s44, 0x1a000
	s_add_i32 s50, s44, 0x8000
	global_load_lds_dwordx4 v[6:7], off
	v_lshl_add_u64 v[6:7], v[8:9], 0, s[14:15]
	s_mov_b32 m0, s50
	s_add_i32 s51, s44, 0xa000
	global_load_lds_dwordx4 v[6:7], off
	v_lshl_add_u64 v[4:5], v[4:5], 0, s[14:15]
	s_mov_b32 m0, s51
	s_sext_i32_i8 s68, s0
	global_load_lds_dwordx4 v[4:5], off
	s_add_i32 m0, s44, 0x1c000
	v_lshl_add_u64 v[4:5], s[20:21], 0, v[176:177]
	global_load_lds_dwordx4 v[4:5], off
	v_lshl_add_u64 v[4:5], s[20:21], 0, v[178:179]
	s_add_i32 m0, s44, 0x1e000
	v_lshlrev_b32_e32 v6, 6, v0
	global_load_lds_dwordx4 v[4:5], off
	v_and_b32_e32 v4, 15, v0
	v_lshlrev_b32_e32 v5, 2, v0
	s_movk_i32 s0, 0x3c0
	v_lshl_or_b32 v206, s1, 6, v4
	v_lshl_or_b32 v4, v4, 6, v2
	v_and_b32_e32 v5, 32, v5
	v_and_or_b32 v6, v6, s0, v2
	v_bitop3_b32 v4, v4, s17, v5 bitop3:0xde
	v_bitop3_b32 v207, s23, v6, v5 bitop3:0xf6
	v_lshlrev_b32_e32 v5, 3, v14
	v_and_b32_e32 v5, 0x1c000, v5
	v_lshlrev_b32_e32 v6, 10, v13
	v_or3_b32 v5, v3, v5, v6
	v_add_u32_e32 v5, v5, v12
	s_cmpk_lt_u32 s16, 0x100
	v_or_b32_e32 v194, 0x20000, v5
	v_lshlrev_b32_e32 v5, 7, v0
	s_cselect_b64 s[16:17], -1, 0
	s_lshl_b32 s53, s22, 6
	s_ashr_i32 s58, s33, 31
	s_lshl_b32 s0, s22, 8
	v_and_b32_e32 v5, 0xc000, v5
	s_waitcnt vmcnt(6)
	s_add_u32 s0, s18, s0
	v_or3_b32 v3, v3, v5, v6
	s_addc_u32 s1, s19, 0
	v_lshlrev_b32_e32 v188, 2, v2
	v_add_u32_e32 v3, v3, v12
	s_add_i32 s60, 0, 0x10000
	s_add_i32 s61, 0, 0x14000
	v_mov_b32_e32 v185, v189
	v_mov_b32_e32 v187, v189
	s_mov_b32 s52, 0x8000
	v_and_or_b32 v190, s53, 64, v2
	v_mov_b32_e32 v191, v189
	v_lshl_add_u64 v[192:193], s[0:1], 0, v[188:189]
	v_mov_b32_e32 v195, v189
	s_mov_b32 s59, 0xc000
	v_or_b32_e32 v196, 0x20000, v3
	v_mov_b32_e32 v197, v189
	v_mov_b64_e32 v[198:199], 0x100
	v_mov_b64_e32 v[200:201], 0xff
	v_add_u32_e32 v208, s60, v207
	v_add_u32_e32 v209, s61, v207
	v_add_u32_e32 v210, 0, v4
	v_lshlrev_b32_e32 v188, 1, v2
	s_mov_b32 s62, 0xc3e00000
	s_movk_i32 s63, 0x7f80
	s_mov_b32 s64, 0x24000
	s_mov_b32 s65, 0x28000
	s_mov_b32 s66, 0x2c000
	v_mov_b32_e32 v211, 0x43e00000
	v_mov_b32_e32 v212, 0x800
	v_mov_b32_e32 v213, 0x1000
	v_mov_b32_e32 v214, 0x1800
	s_mov_b32 s67, 0
	s_mov_b64 s[22:23], s[26:27]
	s_mov_b64 s[24:25], s[28:29]
	s_barrier
	s_branch .LBB0_756

; #define PG8_STAGE(bufoff, gbase, voff) do { _Pragma("unroll") for (int _i = 0; _i < 2; ++_i) \
;         __builtin_amdgcn_global_load_lds((const unsigned*)((const char*)(gbase) + (voff)[_i]), (PG8_LAS unsigned*)(lds + (bufoff) + ldsw + _i * 8192), 16, 0, 0); } while (0)
; #define PG8_WAIT_V(n) asm volatile("s_waitcnt vmcnt(" #n ")" ::: "memory")
; #define PG8_WAIT_L(n) asm volatile("s_waitcnt lgkmcnt(" #n ")" ::: "memory")
; #define PG8_BAR __builtin_amdgcn_s_barrier()
; #define PG8_SCHED __builtin_amdgcn_sched_barrier(0)
; template <class Epi, class Sched, bool ALIGN_EPI = true, bool F8 = false>
; __device__ __forceinline__ void gemm_phase(PG8_LAS unsigned char* lds, const Sched& S, const Epi& E) {
;     ...
;     for (;;) {
;         const bool has_next = S.next(ui + 1, nxt);
;         const char* nA = has_next ? nxt.A : cA; const char* nB = has_next ? nxt.B : cB;
;         const int nt = cur.nt;
; #pragma unroll 1
;         for (int t = 0; t < nt; t += 2) {
;             const bool last = (t == nt - 2);
;             if constexpr (Sched::GATHER) { if (last && has_next) S.a_off(nxt, Rs, Cs, voffAn); }
;             const char* a1 = cA + (size_t)(t + 1) * kstep;
;             const char* a2 = last ? nA : cA + (size_t)(t + 2) * kstep; const char* b2 = last ? nB : cB + (size_t)(t + 2) * kstepB;
;             const char* a3 = a2 + kstep; const char* b3 = b2 + kstepB;
;             unsigned vA2[2][2];
; #pragma unroll
;             for (int h = 0; h < 2; ++h)
; #pragma unroll
;                 for (int i = 0; i < 2; ++i) { if constexpr (Sched::GATHER) vA2[h][i] = (last && has_next) ? voffAn[h][i] : voffA[h][i]; else vA2[h][i] = voffA[h][i]; }
;             PG8_LDB(B0, 0, 0); PG8_LDB(B1, 0, 1); PG8_SCHED; PG8_LDA(At, 0, 0); PG8_STAGE(PG8_SA(1, 1), a1, voffA[1]);
;             PG8_WAIT_V(8); PG8_WAIT_L(0); PG8_BAR; PG8_MMA(0, 0, At, B0); PG8_MMA(0, 1, At, B1); PG8_BAR; PG8_SCHED;
;             PG8_LDA(At, 0, 1); PG8_STAGE(PG8_SB(0, 0), b2, voffB[0]); PG8_STAGE(PG8_SB(0, 1), b2, voffB[1]); PG8_STAGE(PG8_SA(0, 0), a2, vA2[0]);
;             PG8_WAIT_V(8); PG8_WAIT_L(0); PG8_BAR; PG8_MMA(1, 0, At, B0); PG8_MMA(1, 1, At, B1); PG8_BAR; PG8_SCHED;
.LBB0_762:
	s_add_u32 s19, s28, 0x100
	s_addc_u32 s21, s29, 0
	s_add_u32 s26, s26, 0x80
	v_mov_b32_e32 v2, 0
	s_addc_u32 s27, s27, 0
	s_mov_b32 s69, -2
	v_mov_b32_e32 v3, v2
	v_mov_b32_e32 v4, v2
	v_mov_b32_e32 v5, v2
	v_mov_b32_e32 v6, v2
	v_mov_b32_e32 v7, v2
	v_mov_b32_e32 v8, v2
	v_mov_b32_e32 v9, v2
	v_mov_b32_e32 v18, v2
	v_mov_b32_e32 v19, v2
	v_mov_b32_e32 v20, v2
	v_mov_b32_e32 v21, v2
	v_mov_b32_e32 v22, v2
	v_mov_b32_e32 v23, v2
	v_mov_b32_e32 v24, v2
	v_mov_b32_e32 v25, v2
	v_mov_b32_e32 v34, v2
	v_mov_b32_e32 v35, v2
	v_mov_b32_e32 v36, v2
	v_mov_b32_e32 v37, v2
	v_mov_b32_e32 v38, v2
	v_mov_b32_e32 v39, v2
	v_mov_b32_e32 v40, v2
	v_mov_b32_e32 v41, v2
	v_mov_b32_e32 v50, v2
	v_mov_b32_e32 v51, v2
	v_mov_b32_e32 v52, v2
	v_mov_b32_e32 v53, v2
	v_mov_b32_e32 v54, v2
	v_mov_b32_e32 v55, v2
	v_mov_b32_e32 v56, v2
	v_mov_b32_e32 v57, v2
	v_mov_b32_e32 v10, v2
	v_mov_b32_e32 v11, v2
	v_mov_b32_e32 v12, v2
	v_mov_b32_e32 v13, v2
	v_mov_b32_e32 v14, v2
	v_mov_b32_e32 v15, v2
	v_mov_b32_e32 v16, v2
	v_mov_b32_e32 v17, v2
	v_mov_b32_e32 v26, v2
	v_mov_b32_e32 v27, v2
	v_mov_b32_e32 v28, v2
	v_mov_b32_e32 v29, v2
	v_mov_b32_e32 v30, v2
	v_mov_b32_e32 v31, v2
	v_mov_b32_e32 v32, v2
	v_mov_b32_e32 v33, v2
	v_mov_b32_e32 v42, v2
	v_mov_b32_e32 v43, v2
	v_mov_b32_e32 v44, v2
	v_mov_b32_e32 v45, v2
	v_mov_b32_e32 v46, v2
	v_mov_b32_e32 v47, v2
	v_mov_b32_e32 v48, v2
	v_mov_b32_e32 v49, v2
	v_mov_b32_e32 v58, v2
	v_mov_b32_e32 v59, v2
	v_mov_b32_e32 v60, v2
	v_mov_b32_e32 v61, v2
	v_mov_b32_e32 v66, v2
	v_mov_b32_e32 v67, v2
	v_mov_b32_e32 v68, v2
	v_mov_b32_e32 v69, v2
	v_mov_b32_e32 v82, v2
	v_mov_b32_e32 v83, v2
	v_mov_b32_e32 v84, v2
	v_mov_b32_e32 v85, v2
	v_mov_b32_e32 v86, v2
	v_mov_b32_e32 v87, v2
	v_mov_b32_e32 v88, v2
	v_mov_b32_e32 v89, v2
	v_mov_b32_e32 v98, v2
	v_mov_b32_e32 v99, v2
	v_mov_b32_e32 v100, v2
	v_mov_b32_e32 v101, v2
	v_mov_b32_e32 v102, v2
	v_mov_b32_e32 v103, v2
	v_mov_b32_e32 v104, v2
	v_mov_b32_e32 v105, v2
	v_mov_b32_e32 v114, v2
	v_mov_b32_e32 v115, v2
	v_mov_b32_e32 v116, v2
	v_mov_b32_e32 v117, v2
	v_mov_b32_e32 v118, v2
	v_mov_b32_e32 v119, v2
	v_mov_b32_e32 v120, v2
	v_mov_b32_e32 v121, v2
	v_mov_b32_e32 v130, v2
	v_mov_b32_e32 v131, v2
	v_mov_b32_e32 v132, v2
	v_mov_b32_e32 v133, v2
	v_mov_b32_e32 v134, v2
	v_mov_b32_e32 v135, v2
	v_mov_b32_e32 v136, v2
	v_mov_b32_e32 v137, v2
	v_mov_b32_e32 v90, v2
	v_mov_b32_e32 v91, v2
	v_mov_b32_e32 v92, v2
	v_mov_b32_e32 v93, v2
	v_mov_b32_e32 v94, v2
	v_mov_b32_e32 v95, v2
	v_mov_b32_e32 v96, v2
	v_mov_b32_e32 v97, v2
	v_mov_b32_e32 v106, v2
	v_mov_b32_e32 v107, v2
	v_mov_b32_e32 v108, v2
	v_mov_b32_e32 v109, v2
	v_mov_b32_e32 v110, v2
	v_mov_b32_e32 v111, v2
	v_mov_b32_e32 v112, v2
	v_mov_b32_e32 v113, v2
	v_mov_b32_e32 v122, v2
	v_mov_b32_e32 v123, v2
	v_mov_b32_e32 v124, v2
	v_mov_b32_e32 v125, v2
	v_mov_b32_e32 v126, v2
	v_mov_b32_e32 v127, v2
	v_mov_b32_e32 v128, v2
	v_mov_b32_e32 v129, v2
	v_mov_b32_e32 v142, v2
	v_mov_b32_e32 v143, v2
	v_mov_b32_e32 v144, v2
	v_mov_b32_e32 v145, v2
	v_mov_b32_e32 v146, v2
	v_mov_b32_e32 v147, v2
	v_mov_b32_e32 v148, v2
	v_mov_b32_e32 v149, v2
	s_bitcmp1_b32 s3, 2
	s_cbranch_scc1 .Lh1e_20766
.LBB0_763:
	ds_read_b128 v[62:65], v208
	ds_read_b128 v[70:73], v208 offset:1024
	ds_read_b128 v[74:77], v208 offset:2048
	ds_read_b128 v[78:81], v208 offset:3072
	ds_read_b128 v[138:141], v209
	ds_read_b128 v[150:153], v209 offset:1024
	ds_read_b128 v[154:157], v209 offset:2048
	ds_read_b128 v[158:161], v209 offset:3072
	s_add_u32 s28, s26, 0x80
	s_addc_u32 s29, s27, 0
	s_cmp_eq_u32 s69, 4
	s_cselect_b32 s31, s23, s29
	s_cselect_b32 s30, s22, s28
	s_cselect_b32 s29, s25, s21
	s_cselect_b32 s28, s24, s19
	v_lshl_add_u64 v[236:237], s[26:27], 0, v[196:197]
	s_add_i32 m0, s44, 0xc000
	ds_read_b128 v[162:165], v210
	ds_read_b128 v[166:169], v210 offset:1024
	ds_read_b128 v[202:205], v210 offset:2048
	ds_read_b128 v[216:219], v210 offset:3072
	ds_read_b128 v[220:223], v210 offset:4096
	ds_read_b128 v[224:227], v210 offset:5120
	ds_read_b128 v[228:231], v210 offset:6144
	ds_read_b128 v[232:235], v210 offset:7168
	global_load_lds_dwordx4 v[236:237], off
	v_lshl_add_u64 v[236:237], s[26:27], 0, v[194:195]
	s_add_i32 m0, s44, 0xe000
	s_nop 0
	global_load_lds_dwordx4 v[236:237], off
	s_waitcnt vmcnt(8)
	s_waitcnt lgkmcnt(0)
	s_setprio 1
	v_mfma_f32_16x16x32_bf16 v[146:149], v[62:65], v[162:165], v[146:149]
	v_mfma_f32_16x16x32_bf16 v[142:145], v[74:77], v[162:165], v[142:145]
	v_mfma_f32_16x16x32_bf16 v[126:129], v[62:65], v[202:205], v[126:129]
	v_mfma_f32_16x16x32_bf16 v[122:125], v[74:77], v[202:205], v[122:125]
	v_mfma_f32_16x16x32_bf16 v[110:113], v[62:65], v[220:223], v[110:113]
	v_mfma_f32_16x16x32_bf16 v[106:109], v[74:77], v[220:223], v[106:109]
	v_mfma_f32_16x16x32_bf16 v[94:97], v[62:65], v[228:231], v[94:97]
	v_mfma_f32_16x16x32_bf16 v[90:93], v[74:77], v[228:231], v[90:93]
	v_mfma_f32_16x16x32_bf16 v[146:149], v[70:73], v[166:169], v[146:149]
	v_mfma_f32_16x16x32_bf16 v[142:145], v[78:81], v[166:169], v[142:145]
	v_mfma_f32_16x16x32_bf16 v[126:129], v[70:73], v[216:219], v[126:129]
	v_mfma_f32_16x16x32_bf16 v[122:125], v[78:81], v[216:219], v[122:125]
	v_mfma_f32_16x16x32_bf16 v[110:113], v[70:73], v[224:227], v[110:113]
	v_mfma_f32_16x16x32_bf16 v[106:109], v[78:81], v[224:227], v[106:109]
	v_mfma_f32_16x16x32_bf16 v[94:97], v[70:73], v[232:235], v[94:97]
	v_mfma_f32_16x16x32_bf16 v[90:93], v[78:81], v[232:235], v[90:93]
	s_setprio 0
	s_setprio 1
	v_mfma_f32_16x16x32_bf16 v[134:137], v[138:141], v[162:165], v[134:137]
	v_mfma_f32_16x16x32_bf16 v[130:133], v[154:157], v[162:165], v[130:133]
	v_mfma_f32_16x16x32_bf16 v[118:121], v[138:141], v[202:205], v[118:121]
	v_mfma_f32_16x16x32_bf16 v[114:117], v[154:157], v[202:205], v[114:117]
	v_mfma_f32_16x16x32_bf16 v[102:105], v[138:141], v[220:223], v[102:105]
	v_mfma_f32_16x16x32_bf16 v[98:101], v[154:157], v[220:223], v[98:101]
	v_mfma_f32_16x16x32_bf16 v[86:89], v[138:141], v[228:231], v[86:89]
	v_mfma_f32_16x16x32_bf16 v[82:85], v[154:157], v[228:231], v[82:85]
	v_mfma_f32_16x16x32_bf16 v[134:137], v[150:153], v[166:169], v[134:137]
	v_mfma_f32_16x16x32_bf16 v[130:133], v[158:161], v[166:169], v[130:133]
	v_mfma_f32_16x16x32_bf16 v[118:121], v[150:153], v[216:219], v[118:121]
	v_mfma_f32_16x16x32_bf16 v[114:117], v[158:161], v[216:219], v[114:117]
	v_mfma_f32_16x16x32_bf16 v[102:105], v[150:153], v[224:227], v[102:105]
	v_mfma_f32_16x16x32_bf16 v[98:101], v[158:161], v[224:227], v[98:101]
	v_mfma_f32_16x16x32_bf16 v[86:89], v[150:153], v[232:235], v[86:89]
	v_mfma_f32_16x16x32_bf16 v[82:85], v[158:161], v[232:235], v[82:85]
	s_setprio 0
	s_barrier
; #define PG8_STAGE(bufoff, gbase, voff) do { _Pragma("unroll") for (int _i = 0; _i < 2; ++_i) \
;         __builtin_amdgcn_global_load_lds((const unsigned*)((const char*)(gbase) + (voff)[_i]), (PG8_LAS unsigned*)(lds + (bufoff) + ldsw + _i * 8192), 16, 0, 0); } while (0)
; #define PG8_WAIT_V(n) asm volatile("s_waitcnt vmcnt(" #n ")" ::: "memory")
; #define PG8_WAIT_L(n) asm volatile("s_waitcnt lgkmcnt(" #n ")" ::: "memory")
; #define PG8_BAR __builtin_amdgcn_s_barrier()
; #define PG8_SCHED __builtin_amdgcn_sched_barrier(0)
; template <class Epi, class Sched, bool ALIGN_EPI = true, bool F8 = false>
; __device__ __forceinline__ void gemm_phase(PG8_LAS unsigned char* lds, const Sched& S, const Epi& E) {
;     ...
;             PG8_LDB(B0, 0, 0); PG8_LDB(B1, 0, 1); PG8_SCHED; PG8_LDA(At, 0, 0); PG8_STAGE(PG8_SA(1, 1), a1, voffA[1]);
;             PG8_WAIT_V(8); PG8_WAIT_L(0); PG8_BAR; PG8_MMA(0, 0, At, B0); PG8_MMA(0, 1, At, B1); PG8_BAR; PG8_SCHED;
;             PG8_LDA(At, 0, 1); PG8_STAGE(PG8_SB(0, 0), b2, voffB[0]); PG8_STAGE(PG8_SB(0, 1), b2, voffB[1]); PG8_STAGE(PG8_SA(0, 0), a2, vA2[0]);
;             PG8_WAIT_V(8); PG8_WAIT_L(0); PG8_BAR; PG8_MMA(1, 0, At, B0); PG8_MMA(1, 1, At, B1); PG8_BAR; PG8_SCHED;
;             PG8_LDB(B0, 1, 0); PG8_LDB(B1, 1, 1); PG8_SCHED; PG8_LDA(At, 1, 0); PG8_STAGE(PG8_SA(0, 1), a2, vA2[1]);
;             PG8_WAIT_V(8); PG8_WAIT_L(0); PG8_BAR; PG8_MMA(0, 0, At, B0); PG8_MMA(0, 1, At, B1); PG8_BAR; PG8_SCHED;
;             PG8_LDA(At, 1, 1); PG8_STAGE(PG8_SB(1, 0), b3, voffB[0]); PG8_STAGE(PG8_SB(1, 1), b3, voffB[1]); PG8_STAGE(PG8_SA(1, 0), a3, vA2[0]);
;             PG8_WAIT_V(8); PG8_WAIT_L(0); PG8_BAR; PG8_MMA(1, 0, At, B0); PG8_MMA(1, 1, At, B1); PG8_BAR; PG8_SCHED;
	s_add_i32 s70, s60, s43
	v_lshl_add_u64 v[236:237], s[28:29], 0, v[172:173]
	s_mov_b32 m0, s70
	ds_read_b128 v[162:165], v210 offset:16384
	ds_read_b128 v[166:169], v210 offset:17408
	ds_read_b128 v[202:205], v210 offset:18432
	ds_read_b128 v[216:219], v210 offset:19456
	ds_read_b128 v[220:223], v210 offset:20480
	ds_read_b128 v[224:227], v210 offset:21504
	ds_read_b128 v[228:231], v210 offset:22528
	ds_read_b128 v[232:235], v210 offset:23552
	global_load_lds_dwordx4 v[236:237], off
	v_lshl_add_u64 v[238:239], s[28:29], 0, v[174:175]
	s_add_i32 m0, s70, 0x2000
	s_add_i32 s70, s61, s43
	global_load_lds_dwordx4 v[238:239], off
	v_lshl_add_u64 v[240:241], s[28:29], 0, v[176:177]
	s_mov_b32 m0, s70
	v_lshl_add_u64 v[242:243], s[30:31], 0, v[182:183]
	global_load_lds_dwordx4 v[240:241], off
	v_lshl_add_u64 v[240:241], s[28:29], 0, v[178:179]
	s_add_i32 m0, s70, 0x2000
	s_nop 0
	global_load_lds_dwordx4 v[240:241], off
	v_lshl_add_u64 v[240:241], s[30:31], 0, v[180:181]
	s_mov_b32 m0, s44
	s_nop 0
	global_load_lds_dwordx4 v[240:241], off
	s_mov_b32 m0, s45
	s_nop 0
	global_load_lds_dwordx4 v[242:243], off
	s_waitcnt vmcnt(8)
	s_waitcnt lgkmcnt(0)
	s_setprio 1
	v_mfma_f32_16x16x32_bf16 v[66:69], v[62:65], v[162:165], v[66:69]
	v_mfma_f32_16x16x32_bf16 v[58:61], v[74:77], v[162:165], v[58:61]
	v_mfma_f32_16x16x32_bf16 v[46:49], v[62:65], v[202:205], v[46:49]
	v_mfma_f32_16x16x32_bf16 v[42:45], v[74:77], v[202:205], v[42:45]
	v_mfma_f32_16x16x32_bf16 v[30:33], v[62:65], v[220:223], v[30:33]
	v_mfma_f32_16x16x32_bf16 v[26:29], v[74:77], v[220:223], v[26:29]
	v_mfma_f32_16x16x32_bf16 v[14:17], v[62:65], v[228:231], v[14:17]
	v_mfma_f32_16x16x32_bf16 v[10:13], v[74:77], v[228:231], v[10:13]
	v_mfma_f32_16x16x32_bf16 v[66:69], v[70:73], v[166:169], v[66:69]
	v_mfma_f32_16x16x32_bf16 v[58:61], v[78:81], v[166:169], v[58:61]
	v_mfma_f32_16x16x32_bf16 v[46:49], v[70:73], v[216:219], v[46:49]
	v_mfma_f32_16x16x32_bf16 v[42:45], v[78:81], v[216:219], v[42:45]
	v_mfma_f32_16x16x32_bf16 v[30:33], v[70:73], v[224:227], v[30:33]
	v_mfma_f32_16x16x32_bf16 v[26:29], v[78:81], v[224:227], v[26:29]
	v_mfma_f32_16x16x32_bf16 v[14:17], v[70:73], v[232:235], v[14:17]
	v_mfma_f32_16x16x32_bf16 v[10:13], v[78:81], v[232:235], v[10:13]
	s_setprio 0
	s_setprio 1
	v_mfma_f32_16x16x32_bf16 v[54:57], v[138:141], v[162:165], v[54:57]
	v_mfma_f32_16x16x32_bf16 v[50:53], v[154:157], v[162:165], v[50:53]
	v_mfma_f32_16x16x32_bf16 v[38:41], v[138:141], v[202:205], v[38:41]
	v_mfma_f32_16x16x32_bf16 v[34:37], v[154:157], v[202:205], v[34:37]
	v_mfma_f32_16x16x32_bf16 v[22:25], v[138:141], v[220:223], v[22:25]
	v_mfma_f32_16x16x32_bf16 v[18:21], v[154:157], v[220:223], v[18:21]
	v_mfma_f32_16x16x32_bf16 v[6:9], v[138:141], v[228:231], v[6:9]
	v_mfma_f32_16x16x32_bf16 v[2:5], v[154:157], v[228:231], v[2:5]
	v_mfma_f32_16x16x32_bf16 v[54:57], v[150:153], v[166:169], v[54:57]
	v_mfma_f32_16x16x32_bf16 v[50:53], v[158:161], v[166:169], v[50:53]
	v_mfma_f32_16x16x32_bf16 v[38:41], v[150:153], v[216:219], v[38:41]
	v_mfma_f32_16x16x32_bf16 v[34:37], v[158:161], v[216:219], v[34:37]
	v_mfma_f32_16x16x32_bf16 v[22:25], v[150:153], v[224:227], v[22:25]
	v_mfma_f32_16x16x32_bf16 v[18:21], v[158:161], v[224:227], v[18:21]
	v_mfma_f32_16x16x32_bf16 v[6:9], v[150:153], v[232:235], v[6:9]
	v_mfma_f32_16x16x32_bf16 v[2:5], v[158:161], v[232:235], v[2:5]
	s_setprio 0
	s_barrier
	s_add_i32 s70, 0, 0x18000
	s_add_i32 s71, 0, 0x1c000
	v_add_u32_e32 v78, s70, v207
	v_add_u32_e32 v158, s71, v207
	ds_read_b128 v[62:65], v78
	ds_read_b128 v[70:73], v78 offset:1024
	ds_read_b128 v[74:77], v78 offset:2048
	ds_read_b128 v[78:81], v78 offset:3072
	ds_read_b128 v[138:141], v158
	ds_read_b128 v[150:153], v158 offset:1024
	ds_read_b128 v[154:157], v158 offset:2048
	ds_read_b128 v[158:161], v158 offset:3072
	s_mov_b32 m0, s46
	v_lshl_add_u64 v[244:245], s[30:31], 0, v[184:185]
	ds_read_b128 v[162:165], v210 offset:32768
	ds_read_b128 v[166:169], v210 offset:33792
	ds_read_b128 v[202:205], v210 offset:34816
	ds_read_b128 v[216:219], v210 offset:35840
	ds_read_b128 v[220:223], v210 offset:36864
	ds_read_b128 v[224:227], v210 offset:37888
	ds_read_b128 v[228:231], v210 offset:38912
	ds_read_b128 v[232:235], v210 offset:39936
	global_load_lds_dwordx4 v[244:245], off
	v_lshl_add_u64 v[244:245], s[30:31], 0, v[186:187]
	s_mov_b32 m0, s47
	s_nop 0
	global_load_lds_dwordx4 v[244:245], off
	s_waitcnt vmcnt(8)
	s_waitcnt lgkmcnt(0)
	s_setprio 1
	v_mfma_f32_16x16x32_bf16 v[146:149], v[62:65], v[162:165], v[146:149]
	v_mfma_f32_16x16x32_bf16 v[142:145], v[74:77], v[162:165], v[142:145]
	v_mfma_f32_16x16x32_bf16 v[126:129], v[62:65], v[202:205], v[126:129]
	v_mfma_f32_16x16x32_bf16 v[122:125], v[74:77], v[202:205], v[122:125]
	v_mfma_f32_16x16x32_bf16 v[110:113], v[62:65], v[220:223], v[110:113]
	v_mfma_f32_16x16x32_bf16 v[106:109], v[74:77], v[220:223], v[106:109]
	v_mfma_f32_16x16x32_bf16 v[94:97], v[62:65], v[228:231], v[94:97]
	v_mfma_f32_16x16x32_bf16 v[90:93], v[74:77], v[228:231], v[90:93]
	v_mfma_f32_16x16x32_bf16 v[146:149], v[70:73], v[166:169], v[146:149]
	v_mfma_f32_16x16x32_bf16 v[142:145], v[78:81], v[166:169], v[142:145]
	v_mfma_f32_16x16x32_bf16 v[126:129], v[70:73], v[216:219], v[126:129]
	v_mfma_f32_16x16x32_bf16 v[122:125], v[78:81], v[216:219], v[122:125]
	v_mfma_f32_16x16x32_bf16 v[110:113], v[70:73], v[224:227], v[110:113]
	v_mfma_f32_16x16x32_bf16 v[106:109], v[78:81], v[224:227], v[106:109]
	v_mfma_f32_16x16x32_bf16 v[94:97], v[70:73], v[232:235], v[94:97]
	v_mfma_f32_16x16x32_bf16 v[90:93], v[78:81], v[232:235], v[90:93]
	s_setprio 0
	s_setprio 1
	v_mfma_f32_16x16x32_bf16 v[134:137], v[138:141], v[162:165], v[134:137]
	v_mfma_f32_16x16x32_bf16 v[130:133], v[154:157], v[162:165], v[130:133]
	v_mfma_f32_16x16x32_bf16 v[118:121], v[138:141], v[202:205], v[118:121]
	v_mfma_f32_16x16x32_bf16 v[114:117], v[154:157], v[202:205], v[114:117]
	v_mfma_f32_16x16x32_bf16 v[102:105], v[138:141], v[220:223], v[102:105]
	v_mfma_f32_16x16x32_bf16 v[98:101], v[154:157], v[220:223], v[98:101]
	v_mfma_f32_16x16x32_bf16 v[86:89], v[138:141], v[228:231], v[86:89]
	v_mfma_f32_16x16x32_bf16 v[82:85], v[154:157], v[228:231], v[82:85]
	v_mfma_f32_16x16x32_bf16 v[134:137], v[150:153], v[166:169], v[134:137]
	v_mfma_f32_16x16x32_bf16 v[130:133], v[158:161], v[166:169], v[130:133]
	v_mfma_f32_16x16x32_bf16 v[118:121], v[150:153], v[216:219], v[118:121]
	v_mfma_f32_16x16x32_bf16 v[114:117], v[158:161], v[216:219], v[114:117]
	v_mfma_f32_16x16x32_bf16 v[102:105], v[150:153], v[224:227], v[102:105]
	v_mfma_f32_16x16x32_bf16 v[98:101], v[158:161], v[224:227], v[98:101]
	v_mfma_f32_16x16x32_bf16 v[86:89], v[150:153], v[232:235], v[86:89]
	v_mfma_f32_16x16x32_bf16 v[82:85], v[158:161], v[232:235], v[82:85]
	s_setprio 0
	s_barrier
; #define PG8_STAGE(bufoff, gbase, voff) do { _Pragma("unroll") for (int _i = 0; _i < 2; ++_i) \
;         __builtin_amdgcn_global_load_lds((const unsigned*)((const char*)(gbase) + (voff)[_i]), (PG8_LAS unsigned*)(lds + (bufoff) + ldsw + _i * 8192), 16, 0, 0); } while (0)
; #define PG8_WAIT_V(n) asm volatile("s_waitcnt vmcnt(" #n ")" ::: "memory")
; #define PG8_WAIT_L(n) asm volatile("s_waitcnt lgkmcnt(" #n ")" ::: "memory")
; #define PG8_BAR __builtin_amdgcn_s_barrier()
; #define PG8_SCHED __builtin_amdgcn_sched_barrier(0)
; template <class Epi, class Sched, bool ALIGN_EPI = true, bool F8 = false>
; __device__ __forceinline__ void gemm_phase(PG8_LAS unsigned char* lds, const Sched& S, const Epi& E) {
;     ...
;             PG8_LDB(B0, 0, 0); PG8_LDB(B1, 0, 1); PG8_SCHED; PG8_LDA(At, 0, 0); PG8_STAGE(PG8_SA(1, 1), a1, voffA[1]);
;             PG8_WAIT_V(8); PG8_WAIT_L(0); PG8_BAR; PG8_MMA(0, 0, At, B0); PG8_MMA(0, 1, At, B1); PG8_BAR; PG8_SCHED;
;             PG8_LDA(At, 0, 1); PG8_STAGE(PG8_SB(0, 0), b2, voffB[0]); PG8_STAGE(PG8_SB(0, 1), b2, voffB[1]); PG8_STAGE(PG8_SA(0, 0), a2, vA2[0]);
;             PG8_WAIT_V(8); PG8_WAIT_L(0); PG8_BAR; PG8_MMA(1, 0, At, B0); PG8_MMA(1, 1, At, B1); PG8_BAR; PG8_SCHED;
;             PG8_LDB(B0, 1, 0); PG8_LDB(B1, 1, 1); PG8_SCHED; PG8_LDA(At, 1, 0); PG8_STAGE(PG8_SA(0, 1), a2, vA2[1]);
;             PG8_WAIT_V(8); PG8_WAIT_L(0); PG8_BAR; PG8_MMA(0, 0, At, B0); PG8_MMA(0, 1, At, B1); PG8_BAR; PG8_SCHED;
;             PG8_LDA(At, 1, 1); PG8_STAGE(PG8_SB(1, 0), b3, voffB[0]); PG8_STAGE(PG8_SB(1, 1), b3, voffB[1]); PG8_STAGE(PG8_SA(1, 0), a3, vA2[0]);
;             PG8_WAIT_V(8); PG8_WAIT_L(0); PG8_BAR; PG8_MMA(1, 0, At, B0); PG8_MMA(1, 1, At, B1); PG8_BAR; PG8_SCHED;
	s_add_u32 s28, s28, 0x80
	s_addc_u32 s29, s29, 0
	s_add_i32 s30, s70, s43
	v_lshl_add_u64 v[236:237], v[236:237], 0, s[14:15]
	s_mov_b32 m0, s30
	ds_read_b128 v[162:165], v210 offset:49152
	ds_read_b128 v[166:169], v210 offset:50176
	ds_read_b128 v[202:205], v210 offset:51200
	ds_read_b128 v[216:219], v210 offset:52224
	ds_read_b128 v[220:223], v210 offset:53248
	ds_read_b128 v[224:227], v210 offset:54272
	ds_read_b128 v[228:231], v210 offset:55296
	ds_read_b128 v[232:235], v210 offset:56320
	global_load_lds_dwordx4 v[236:237], off
	v_lshl_add_u64 v[236:237], v[238:239], 0, s[14:15]
	s_add_i32 m0, s30, 0x2000
	s_add_i32 s30, s71, s43
	global_load_lds_dwordx4 v[236:237], off
	v_lshl_add_u64 v[236:237], s[28:29], 0, v[176:177]
	s_mov_b32 m0, s30
	s_nop 0
	global_load_lds_dwordx4 v[236:237], off
	v_lshl_add_u64 v[236:237], s[28:29], 0, v[178:179]
	s_add_i32 m0, s30, 0x2000
	s_nop 0
	global_load_lds_dwordx4 v[236:237], off
	v_lshl_add_u64 v[236:237], v[240:241], 0, s[14:15]
	s_mov_b32 m0, s50
	s_nop 0
	global_load_lds_dwordx4 v[236:237], off
	v_lshl_add_u64 v[236:237], v[242:243], 0, s[14:15]
	s_mov_b32 m0, s51
	s_nop 0
	global_load_lds_dwordx4 v[236:237], off
	s_waitcnt vmcnt(8)
	s_waitcnt lgkmcnt(0)
	s_setprio 1
	v_mfma_f32_16x16x32_bf16 v[66:69], v[62:65], v[162:165], v[66:69]
	v_mfma_f32_16x16x32_bf16 v[58:61], v[74:77], v[162:165], v[58:61]
	v_mfma_f32_16x16x32_bf16 v[46:49], v[62:65], v[202:205], v[46:49]
	v_mfma_f32_16x16x32_bf16 v[42:45], v[74:77], v[202:205], v[42:45]
	v_mfma_f32_16x16x32_bf16 v[30:33], v[62:65], v[220:223], v[30:33]
	v_mfma_f32_16x16x32_bf16 v[26:29], v[74:77], v[220:223], v[26:29]
	v_mfma_f32_16x16x32_bf16 v[14:17], v[62:65], v[228:231], v[14:17]
	v_mfma_f32_16x16x32_bf16 v[10:13], v[74:77], v[228:231], v[10:13]
	v_mfma_f32_16x16x32_bf16 v[66:69], v[70:73], v[166:169], v[66:69]
	v_mfma_f32_16x16x32_bf16 v[58:61], v[78:81], v[166:169], v[58:61]
	v_mfma_f32_16x16x32_bf16 v[46:49], v[70:73], v[216:219], v[46:49]
	v_mfma_f32_16x16x32_bf16 v[42:45], v[78:81], v[216:219], v[42:45]
	v_mfma_f32_16x16x32_bf16 v[30:33], v[70:73], v[224:227], v[30:33]
	v_mfma_f32_16x16x32_bf16 v[26:29], v[78:81], v[224:227], v[26:29]
	v_mfma_f32_16x16x32_bf16 v[14:17], v[70:73], v[232:235], v[14:17]
	v_mfma_f32_16x16x32_bf16 v[10:13], v[78:81], v[232:235], v[10:13]
	s_setprio 0
	s_setprio 1
	v_mfma_f32_16x16x32_bf16 v[54:57], v[138:141], v[162:165], v[54:57]
	v_mfma_f32_16x16x32_bf16 v[50:53], v[154:157], v[162:165], v[50:53]
	v_mfma_f32_16x16x32_bf16 v[38:41], v[138:141], v[202:205], v[38:41]
	v_mfma_f32_16x16x32_bf16 v[34:37], v[154:157], v[202:205], v[34:37]
	v_mfma_f32_16x16x32_bf16 v[22:25], v[138:141], v[220:223], v[22:25]
	v_mfma_f32_16x16x32_bf16 v[18:21], v[154:157], v[220:223], v[18:21]
	v_mfma_f32_16x16x32_bf16 v[6:9], v[138:141], v[228:231], v[6:9]
	v_mfma_f32_16x16x32_bf16 v[2:5], v[154:157], v[228:231], v[2:5]
	v_mfma_f32_16x16x32_bf16 v[54:57], v[150:153], v[166:169], v[54:57]
	v_mfma_f32_16x16x32_bf16 v[50:53], v[158:161], v[166:169], v[50:53]
	v_mfma_f32_16x16x32_bf16 v[38:41], v[150:153], v[216:219], v[38:41]
	v_mfma_f32_16x16x32_bf16 v[34:37], v[158:161], v[216:219], v[34:37]
	v_mfma_f32_16x16x32_bf16 v[22:25], v[150:153], v[224:227], v[22:25]
	v_mfma_f32_16x16x32_bf16 v[18:21], v[158:161], v[224:227], v[18:21]
	v_mfma_f32_16x16x32_bf16 v[6:9], v[150:153], v[232:235], v[6:9]
	v_mfma_f32_16x16x32_bf16 v[2:5], v[158:161], v[232:235], v[2:5]
	s_setprio 0
	s_barrier
	s_add_i32 s69, s69, 2
	s_add_u32 s19, s19, 0x100
	s_addc_u32 s21, s21, 0
	s_add_u32 s26, s26, 0x100
	s_addc_u32 s27, s27, 0
	s_cmp_gt_u32 s69, 5
	s_cbranch_scc0 .LBB0_763
	s_branch .Lfx_20766
.Lh1e_20766:
.Lh1_763:
	ds_read_b128 v[62:65], v208
	ds_read_b128 v[70:73], v208 offset:1024
	ds_read_b128 v[74:77], v208 offset:2048
	ds_read_b128 v[78:81], v208 offset:3072
	ds_read_b128 v[138:141], v209
	ds_read_b128 v[150:153], v209 offset:1024
	ds_read_b128 v[154:157], v209 offset:2048
	ds_read_b128 v[158:161], v209 offset:3072
	s_add_u32 s28, s26, 0x80
	s_addc_u32 s29, s27, 0
	s_cmp_eq_u32 s69, 4
	s_cselect_b32 s31, s23, s29
	s_cselect_b32 s30, s22, s28
	s_cselect_b32 s29, s25, s21
	s_cselect_b32 s28, s24, s19
	v_lshl_add_u64 v[236:237], s[26:27], 0, v[196:197]
	s_add_i32 m0, s44, 0xc000
	ds_read_b128 v[162:165], v210
	ds_read_b128 v[166:169], v210 offset:1024
	ds_read_b128 v[202:205], v210 offset:2048
	ds_read_b128 v[216:219], v210 offset:3072
	ds_read_b128 v[220:223], v210 offset:4096
	ds_read_b128 v[224:227], v210 offset:5120
	ds_read_b128 v[228:231], v210 offset:6144
	ds_read_b128 v[232:235], v210 offset:7168
	global_load_lds_dwordx4 v[236:237], off
	v_lshl_add_u64 v[236:237], s[26:27], 0, v[194:195]
	s_add_i32 m0, s44, 0xe000
	s_nop 0
	global_load_lds_dwordx4 v[236:237], off
	s_waitcnt vmcnt(8)
	s_waitcnt lgkmcnt(0)
	s_barrier
; #define PG8_STAGE(bufoff, gbase, voff) do { _Pragma("unroll") for (int _i = 0; _i < 2; ++_i) \
;         __builtin_amdgcn_global_load_lds((const unsigned*)((const char*)(gbase) + (voff)[_i]), (PG8_LAS unsigned*)(lds + (bufoff) + ldsw + _i * 8192), 16, 0, 0); } while (0)
; #define PG8_WAIT_V(n) asm volatile("s_waitcnt vmcnt(" #n ")" ::: "memory")
; #define PG8_WAIT_L(n) asm volatile("s_waitcnt lgkmcnt(" #n ")" ::: "memory")
; #define PG8_BAR __builtin_amdgcn_s_barrier()
; #define PG8_SCHED __builtin_amdgcn_sched_barrier(0)
; template <class Epi, class Sched, bool ALIGN_EPI = true, bool F8 = false>
; __device__ __forceinline__ void gemm_phase(PG8_LAS unsigned char* lds, const Sched& S, const Epi& E) {
;     ...
;             PG8_LDB(B0, 0, 0); PG8_LDB(B1, 0, 1); PG8_SCHED; PG8_LDA(At, 0, 0); PG8_STAGE(PG8_SA(1, 1), a1, voffA[1]);
;             PG8_WAIT_V(8); PG8_WAIT_L(0); PG8_BAR; PG8_MMA(0, 0, At, B0); PG8_MMA(0, 1, At, B1); PG8_BAR; PG8_SCHED;
;             PG8_LDA(At, 0, 1); PG8_STAGE(PG8_SB(0, 0), b2, voffB[0]); PG8_STAGE(PG8_SB(0, 1), b2, voffB[1]); PG8_STAGE(PG8_SA(0, 0), a2, vA2[0]);
;             PG8_WAIT_V(8); PG8_WAIT_L(0); PG8_BAR; PG8_MMA(1, 0, At, B0); PG8_MMA(1, 1, At, B1); PG8_BAR; PG8_SCHED;
;             PG8_LDB(B0, 1, 0); PG8_LDB(B1, 1, 1); PG8_SCHED; PG8_LDA(At, 1, 0); PG8_STAGE(PG8_SA(0, 1), a2, vA2[1]);
;             PG8_WAIT_V(8); PG8_WAIT_L(0); PG8_BAR; PG8_MMA(0, 0, At, B0); PG8_MMA(0, 1, At, B1); PG8_BAR; PG8_SCHED;
	s_setprio 2
	v_mfma_f32_16x16x32_bf16 v[146:149], v[62:65], v[162:165], v[146:149]
	v_mfma_f32_16x16x32_bf16 v[142:145], v[74:77], v[162:165], v[142:145]
	v_mfma_f32_16x16x32_bf16 v[126:129], v[62:65], v[202:205], v[126:129]
	v_mfma_f32_16x16x32_bf16 v[122:125], v[74:77], v[202:205], v[122:125]
	v_mfma_f32_16x16x32_bf16 v[110:113], v[62:65], v[220:223], v[110:113]
	v_mfma_f32_16x16x32_bf16 v[106:109], v[74:77], v[220:223], v[106:109]
	v_mfma_f32_16x16x32_bf16 v[94:97], v[62:65], v[228:231], v[94:97]
	v_mfma_f32_16x16x32_bf16 v[90:93], v[74:77], v[228:231], v[90:93]
	v_mfma_f32_16x16x32_bf16 v[146:149], v[70:73], v[166:169], v[146:149]
	v_mfma_f32_16x16x32_bf16 v[142:145], v[78:81], v[166:169], v[142:145]
	v_mfma_f32_16x16x32_bf16 v[126:129], v[70:73], v[216:219], v[126:129]
	v_mfma_f32_16x16x32_bf16 v[122:125], v[78:81], v[216:219], v[122:125]
	v_mfma_f32_16x16x32_bf16 v[110:113], v[70:73], v[224:227], v[110:113]
	v_mfma_f32_16x16x32_bf16 v[106:109], v[78:81], v[224:227], v[106:109]
	v_mfma_f32_16x16x32_bf16 v[94:97], v[70:73], v[232:235], v[94:97]
	v_mfma_f32_16x16x32_bf16 v[90:93], v[78:81], v[232:235], v[90:93]
	s_setprio 0
	s_setprio 2
	v_mfma_f32_16x16x32_bf16 v[134:137], v[138:141], v[162:165], v[134:137]
	v_mfma_f32_16x16x32_bf16 v[130:133], v[154:157], v[162:165], v[130:133]
	v_mfma_f32_16x16x32_bf16 v[118:121], v[138:141], v[202:205], v[118:121]
	v_mfma_f32_16x16x32_bf16 v[114:117], v[154:157], v[202:205], v[114:117]
	v_mfma_f32_16x16x32_bf16 v[102:105], v[138:141], v[220:223], v[102:105]
	v_mfma_f32_16x16x32_bf16 v[98:101], v[154:157], v[220:223], v[98:101]
	v_mfma_f32_16x16x32_bf16 v[86:89], v[138:141], v[228:231], v[86:89]
	v_mfma_f32_16x16x32_bf16 v[82:85], v[154:157], v[228:231], v[82:85]
	v_mfma_f32_16x16x32_bf16 v[134:137], v[150:153], v[166:169], v[134:137]
	v_mfma_f32_16x16x32_bf16 v[130:133], v[158:161], v[166:169], v[130:133]
	v_mfma_f32_16x16x32_bf16 v[118:121], v[150:153], v[216:219], v[118:121]
	v_mfma_f32_16x16x32_bf16 v[114:117], v[158:161], v[216:219], v[114:117]
	v_mfma_f32_16x16x32_bf16 v[102:105], v[150:153], v[224:227], v[102:105]
	v_mfma_f32_16x16x32_bf16 v[98:101], v[158:161], v[224:227], v[98:101]
	v_mfma_f32_16x16x32_bf16 v[86:89], v[150:153], v[232:235], v[86:89]
	v_mfma_f32_16x16x32_bf16 v[82:85], v[158:161], v[232:235], v[82:85]
	s_setprio 0
	s_add_i32 s70, s60, s43
	v_lshl_add_u64 v[236:237], s[28:29], 0, v[172:173]
	s_mov_b32 m0, s70
	ds_read_b128 v[162:165], v210 offset:16384
	ds_read_b128 v[166:169], v210 offset:17408
	ds_read_b128 v[202:205], v210 offset:18432
	ds_read_b128 v[216:219], v210 offset:19456
	ds_read_b128 v[220:223], v210 offset:20480
	ds_read_b128 v[224:227], v210 offset:21504
	ds_read_b128 v[228:231], v210 offset:22528
	ds_read_b128 v[232:235], v210 offset:23552
	global_load_lds_dwordx4 v[236:237], off
	v_lshl_add_u64 v[238:239], s[28:29], 0, v[174:175]
	s_add_i32 m0, s70, 0x2000
	s_add_i32 s70, s61, s43
	global_load_lds_dwordx4 v[238:239], off
	v_lshl_add_u64 v[240:241], s[28:29], 0, v[176:177]
	s_mov_b32 m0, s70
	v_lshl_add_u64 v[242:243], s[30:31], 0, v[182:183]
	global_load_lds_dwordx4 v[240:241], off
	v_lshl_add_u64 v[240:241], s[28:29], 0, v[178:179]
	s_add_i32 m0, s70, 0x2000
	s_nop 0
	global_load_lds_dwordx4 v[240:241], off
	v_lshl_add_u64 v[240:241], s[30:31], 0, v[180:181]
	s_mov_b32 m0, s44
	s_nop 0
	global_load_lds_dwordx4 v[240:241], off
	s_mov_b32 m0, s45
	s_nop 0
	global_load_lds_dwordx4 v[242:243], off
	s_waitcnt vmcnt(8)
	s_waitcnt lgkmcnt(0)
	s_barrier
	s_setprio 2
	v_mfma_f32_16x16x32_bf16 v[66:69], v[62:65], v[162:165], v[66:69]
	v_mfma_f32_16x16x32_bf16 v[58:61], v[74:77], v[162:165], v[58:61]
	v_mfma_f32_16x16x32_bf16 v[46:49], v[62:65], v[202:205], v[46:49]
	v_mfma_f32_16x16x32_bf16 v[42:45], v[74:77], v[202:205], v[42:45]
	v_mfma_f32_16x16x32_bf16 v[30:33], v[62:65], v[220:223], v[30:33]
	v_mfma_f32_16x16x32_bf16 v[26:29], v[74:77], v[220:223], v[26:29]
	v_mfma_f32_16x16x32_bf16 v[14:17], v[62:65], v[228:231], v[14:17]
	v_mfma_f32_16x16x32_bf16 v[10:13], v[74:77], v[228:231], v[10:13]
	v_mfma_f32_16x16x32_bf16 v[66:69], v[70:73], v[166:169], v[66:69]
	v_mfma_f32_16x16x32_bf16 v[58:61], v[78:81], v[166:169], v[58:61]
	v_mfma_f32_16x16x32_bf16 v[46:49], v[70:73], v[216:219], v[46:49]
	v_mfma_f32_16x16x32_bf16 v[42:45], v[78:81], v[216:219], v[42:45]
	v_mfma_f32_16x16x32_bf16 v[30:33], v[70:73], v[224:227], v[30:33]
	v_mfma_f32_16x16x32_bf16 v[26:29], v[78:81], v[224:227], v[26:29]
	v_mfma_f32_16x16x32_bf16 v[14:17], v[70:73], v[232:235], v[14:17]
	v_mfma_f32_16x16x32_bf16 v[10:13], v[78:81], v[232:235], v[10:13]
	s_setprio 0
	s_setprio 2
	v_mfma_f32_16x16x32_bf16 v[54:57], v[138:141], v[162:165], v[54:57]
	v_mfma_f32_16x16x32_bf16 v[50:53], v[154:157], v[162:165], v[50:53]
	v_mfma_f32_16x16x32_bf16 v[38:41], v[138:141], v[202:205], v[38:41]
	v_mfma_f32_16x16x32_bf16 v[34:37], v[154:157], v[202:205], v[34:37]
	v_mfma_f32_16x16x32_bf16 v[22:25], v[138:141], v[220:223], v[22:25]
	v_mfma_f32_16x16x32_bf16 v[18:21], v[154:157], v[220:223], v[18:21]
	v_mfma_f32_16x16x32_bf16 v[6:9], v[138:141], v[228:231], v[6:9]
	v_mfma_f32_16x16x32_bf16 v[2:5], v[154:157], v[228:231], v[2:5]
	v_mfma_f32_16x16x32_bf16 v[54:57], v[150:153], v[166:169], v[54:57]
	v_mfma_f32_16x16x32_bf16 v[50:53], v[158:161], v[166:169], v[50:53]
	v_mfma_f32_16x16x32_bf16 v[38:41], v[150:153], v[216:219], v[38:41]
	v_mfma_f32_16x16x32_bf16 v[34:37], v[158:161], v[216:219], v[34:37]
	v_mfma_f32_16x16x32_bf16 v[22:25], v[150:153], v[224:227], v[22:25]
	v_mfma_f32_16x16x32_bf16 v[18:21], v[158:161], v[224:227], v[18:21]
	v_mfma_f32_16x16x32_bf16 v[6:9], v[150:153], v[232:235], v[6:9]
	v_mfma_f32_16x16x32_bf16 v[2:5], v[158:161], v[232:235], v[2:5]
	s_setprio 0
	s_add_i32 s70, 0, 0x18000
	s_add_i32 s71, 0, 0x1c000
	v_add_u32_e32 v78, s70, v207
	v_add_u32_e32 v158, s71, v207
	ds_read_b128 v[62:65], v78
	ds_read_b128 v[70:73], v78 offset:1024
	ds_read_b128 v[74:77], v78 offset:2048
	ds_read_b128 v[78:81], v78 offset:3072
	ds_read_b128 v[138:141], v158
	ds_read_b128 v[150:153], v158 offset:1024
	ds_read_b128 v[154:157], v158 offset:2048
	ds_read_b128 v[158:161], v158 offset:3072
	s_mov_b32 m0, s46
	v_lshl_add_u64 v[244:245], s[30:31], 0, v[184:185]
	ds_read_b128 v[162:165], v210 offset:32768
	ds_read_b128 v[166:169], v210 offset:33792
	ds_read_b128 v[202:205], v210 offset:34816
	ds_read_b128 v[216:219], v210 offset:35840
	ds_read_b128 v[220:223], v210 offset:36864
	ds_read_b128 v[224:227], v210 offset:37888
	ds_read_b128 v[228:231], v210 offset:38912
	ds_read_b128 v[232:235], v210 offset:39936
	global_load_lds_dwordx4 v[244:245], off
	v_lshl_add_u64 v[244:245], s[30:31], 0, v[186:187]
	s_mov_b32 m0, s47
	s_nop 0
	global_load_lds_dwordx4 v[244:245], off
	s_waitcnt vmcnt(8)
	s_waitcnt lgkmcnt(0)
	s_barrier
; #define PG8_STAGE(bufoff, gbase, voff) do { _Pragma("unroll") for (int _i = 0; _i < 2; ++_i) \
;         __builtin_amdgcn_global_load_lds((const unsigned*)((const char*)(gbase) + (voff)[_i]), (PG8_LAS unsigned*)(lds + (bufoff) + ldsw + _i * 8192), 16, 0, 0); } while (0)
; #define PG8_WAIT_V(n) asm volatile("s_waitcnt vmcnt(" #n ")" ::: "memory")
; #define PG8_WAIT_L(n) asm volatile("s_waitcnt lgkmcnt(" #n ")" ::: "memory")
; #define PG8_BAR __builtin_amdgcn_s_barrier()
; #define PG8_SCHED __builtin_amdgcn_sched_barrier(0)
; template <class Epi, class Sched, bool ALIGN_EPI = true, bool F8 = false>
; __device__ __forceinline__ void gemm_phase(PG8_LAS unsigned char* lds, const Sched& S, const Epi& E) {
;     ...
;             PG8_WAIT_V(8); PG8_WAIT_L(0); PG8_BAR; PG8_MMA(1, 0, At, B0); PG8_MMA(1, 1, At, B1); PG8_BAR; PG8_SCHED;
;             PG8_LDB(B0, 1, 0); PG8_LDB(B1, 1, 1); PG8_SCHED; PG8_LDA(At, 1, 0); PG8_STAGE(PG8_SA(0, 1), a2, vA2[1]);
;             PG8_WAIT_V(8); PG8_WAIT_L(0); PG8_BAR; PG8_MMA(0, 0, At, B0); PG8_MMA(0, 1, At, B1); PG8_BAR; PG8_SCHED;
;             PG8_LDA(At, 1, 1); PG8_STAGE(PG8_SB(1, 0), b3, voffB[0]); PG8_STAGE(PG8_SB(1, 1), b3, voffB[1]); PG8_STAGE(PG8_SA(1, 0), a3, vA2[0]);
;             PG8_WAIT_V(8); PG8_WAIT_L(0); PG8_BAR; PG8_MMA(1, 0, At, B0); PG8_MMA(1, 1, At, B1); PG8_BAR; PG8_SCHED;
	s_setprio 2
	v_mfma_f32_16x16x32_bf16 v[146:149], v[62:65], v[162:165], v[146:149]
	v_mfma_f32_16x16x32_bf16 v[142:145], v[74:77], v[162:165], v[142:145]
	v_mfma_f32_16x16x32_bf16 v[126:129], v[62:65], v[202:205], v[126:129]
	v_mfma_f32_16x16x32_bf16 v[122:125], v[74:77], v[202:205], v[122:125]
	v_mfma_f32_16x16x32_bf16 v[110:113], v[62:65], v[220:223], v[110:113]
	v_mfma_f32_16x16x32_bf16 v[106:109], v[74:77], v[220:223], v[106:109]
	v_mfma_f32_16x16x32_bf16 v[94:97], v[62:65], v[228:231], v[94:97]
	v_mfma_f32_16x16x32_bf16 v[90:93], v[74:77], v[228:231], v[90:93]
	v_mfma_f32_16x16x32_bf16 v[146:149], v[70:73], v[166:169], v[146:149]
	v_mfma_f32_16x16x32_bf16 v[142:145], v[78:81], v[166:169], v[142:145]
	v_mfma_f32_16x16x32_bf16 v[126:129], v[70:73], v[216:219], v[126:129]
	v_mfma_f32_16x16x32_bf16 v[122:125], v[78:81], v[216:219], v[122:125]
	v_mfma_f32_16x16x32_bf16 v[110:113], v[70:73], v[224:227], v[110:113]
	v_mfma_f32_16x16x32_bf16 v[106:109], v[78:81], v[224:227], v[106:109]
	v_mfma_f32_16x16x32_bf16 v[94:97], v[70:73], v[232:235], v[94:97]
	v_mfma_f32_16x16x32_bf16 v[90:93], v[78:81], v[232:235], v[90:93]
	s_setprio 0
	s_setprio 2
	v_mfma_f32_16x16x32_bf16 v[134:137], v[138:141], v[162:165], v[134:137]
	v_mfma_f32_16x16x32_bf16 v[130:133], v[154:157], v[162:165], v[130:133]
	v_mfma_f32_16x16x32_bf16 v[118:121], v[138:141], v[202:205], v[118:121]
	v_mfma_f32_16x16x32_bf16 v[114:117], v[154:157], v[202:205], v[114:117]
	v_mfma_f32_16x16x32_bf16 v[102:105], v[138:141], v[220:223], v[102:105]
	v_mfma_f32_16x16x32_bf16 v[98:101], v[154:157], v[220:223], v[98:101]
	v_mfma_f32_16x16x32_bf16 v[86:89], v[138:141], v[228:231], v[86:89]
	v_mfma_f32_16x16x32_bf16 v[82:85], v[154:157], v[228:231], v[82:85]
	v_mfma_f32_16x16x32_bf16 v[134:137], v[150:153], v[166:169], v[134:137]
	v_mfma_f32_16x16x32_bf16 v[130:133], v[158:161], v[166:169], v[130:133]
	v_mfma_f32_16x16x32_bf16 v[118:121], v[150:153], v[216:219], v[118:121]
	v_mfma_f32_16x16x32_bf16 v[114:117], v[158:161], v[216:219], v[114:117]
	v_mfma_f32_16x16x32_bf16 v[102:105], v[150:153], v[224:227], v[102:105]
	v_mfma_f32_16x16x32_bf16 v[98:101], v[158:161], v[224:227], v[98:101]
	v_mfma_f32_16x16x32_bf16 v[86:89], v[150:153], v[232:235], v[86:89]
	v_mfma_f32_16x16x32_bf16 v[82:85], v[158:161], v[232:235], v[82:85]
	s_setprio 0
	s_add_u32 s28, s28, 0x80
	s_addc_u32 s29, s29, 0
	s_add_i32 s30, s70, s43
	v_lshl_add_u64 v[236:237], v[236:237], 0, s[14:15]
	s_mov_b32 m0, s30
	ds_read_b128 v[162:165], v210 offset:49152
	ds_read_b128 v[166:169], v210 offset:50176
	ds_read_b128 v[202:205], v210 offset:51200
	ds_read_b128 v[216:219], v210 offset:52224
	ds_read_b128 v[220:223], v210 offset:53248
	ds_read_b128 v[224:227], v210 offset:54272
	ds_read_b128 v[228:231], v210 offset:55296
	ds_read_b128 v[232:235], v210 offset:56320
	global_load_lds_dwordx4 v[236:237], off
	v_lshl_add_u64 v[236:237], v[238:239], 0, s[14:15]
	s_add_i32 m0, s30, 0x2000
	s_add_i32 s30, s71, s43
	global_load_lds_dwordx4 v[236:237], off
	v_lshl_add_u64 v[236:237], s[28:29], 0, v[176:177]
	s_mov_b32 m0, s30
	s_nop 0
	global_load_lds_dwordx4 v[236:237], off
	v_lshl_add_u64 v[236:237], s[28:29], 0, v[178:179]
	s_add_i32 m0, s30, 0x2000
	s_nop 0
	global_load_lds_dwordx4 v[236:237], off
	v_lshl_add_u64 v[236:237], v[240:241], 0, s[14:15]
	s_mov_b32 m0, s50
	s_nop 0
	global_load_lds_dwordx4 v[236:237], off
	v_lshl_add_u64 v[236:237], v[242:243], 0, s[14:15]
	s_mov_b32 m0, s51
	s_nop 0
	global_load_lds_dwordx4 v[236:237], off
	s_waitcnt vmcnt(8)
	s_waitcnt lgkmcnt(0)
	s_barrier
	s_setprio 2
	v_mfma_f32_16x16x32_bf16 v[66:69], v[62:65], v[162:165], v[66:69]
	v_mfma_f32_16x16x32_bf16 v[58:61], v[74:77], v[162:165], v[58:61]
	v_mfma_f32_16x16x32_bf16 v[46:49], v[62:65], v[202:205], v[46:49]
	v_mfma_f32_16x16x32_bf16 v[42:45], v[74:77], v[202:205], v[42:45]
	v_mfma_f32_16x16x32_bf16 v[30:33], v[62:65], v[220:223], v[30:33]
	v_mfma_f32_16x16x32_bf16 v[26:29], v[74:77], v[220:223], v[26:29]
	v_mfma_f32_16x16x32_bf16 v[14:17], v[62:65], v[228:231], v[14:17]
	v_mfma_f32_16x16x32_bf16 v[10:13], v[74:77], v[228:231], v[10:13]
	v_mfma_f32_16x16x32_bf16 v[66:69], v[70:73], v[166:169], v[66:69]
	v_mfma_f32_16x16x32_bf16 v[58:61], v[78:81], v[166:169], v[58:61]
	v_mfma_f32_16x16x32_bf16 v[46:49], v[70:73], v[216:219], v[46:49]
	v_mfma_f32_16x16x32_bf16 v[42:45], v[78:81], v[216:219], v[42:45]
	v_mfma_f32_16x16x32_bf16 v[30:33], v[70:73], v[224:227], v[30:33]
	v_mfma_f32_16x16x32_bf16 v[26:29], v[78:81], v[224:227], v[26:29]
	v_mfma_f32_16x16x32_bf16 v[14:17], v[70:73], v[232:235], v[14:17]
	v_mfma_f32_16x16x32_bf16 v[10:13], v[78:81], v[232:235], v[10:13]
	s_setprio 0
	s_setprio 2
	v_mfma_f32_16x16x32_bf16 v[54:57], v[138:141], v[162:165], v[54:57]
	v_mfma_f32_16x16x32_bf16 v[50:53], v[154:157], v[162:165], v[50:53]
	v_mfma_f32_16x16x32_bf16 v[38:41], v[138:141], v[202:205], v[38:41]
	v_mfma_f32_16x16x32_bf16 v[34:37], v[154:157], v[202:205], v[34:37]
	v_mfma_f32_16x16x32_bf16 v[22:25], v[138:141], v[220:223], v[22:25]
	v_mfma_f32_16x16x32_bf16 v[18:21], v[154:157], v[220:223], v[18:21]
	v_mfma_f32_16x16x32_bf16 v[6:9], v[138:141], v[228:231], v[6:9]
	v_mfma_f32_16x16x32_bf16 v[2:5], v[154:157], v[228:231], v[2:5]
	v_mfma_f32_16x16x32_bf16 v[54:57], v[150:153], v[166:169], v[54:57]
	v_mfma_f32_16x16x32_bf16 v[50:53], v[158:161], v[166:169], v[50:53]
	v_mfma_f32_16x16x32_bf16 v[38:41], v[150:153], v[216:219], v[38:41]
	v_mfma_f32_16x16x32_bf16 v[34:37], v[158:161], v[216:219], v[34:37]
	v_mfma_f32_16x16x32_bf16 v[22:25], v[150:153], v[224:227], v[22:25]
	v_mfma_f32_16x16x32_bf16 v[18:21], v[158:161], v[224:227], v[18:21]
	v_mfma_f32_16x16x32_bf16 v[6:9], v[150:153], v[232:235], v[6:9]
	v_mfma_f32_16x16x32_bf16 v[2:5], v[158:161], v[232:235], v[2:5]
	s_setprio 0
	s_add_i32 s69, s69, 2
	s_add_u32 s19, s19, 0x100
	s_addc_u32 s21, s21, 0
	s_add_u32 s26, s26, 0x100
	s_addc_u32 s27, s27, 0
	s_cmp_gt_u32 s69, 5
	s_cbranch_scc0 .Lh1_763

;     __device__ __forceinline__ void operator()(AccRef acc, const GUnit& u, int wr, int wc, int fr, int fq) const {
;         const int pm = u.x0, pn = u.x1;
;         const size_t off0 = (size_t)(pm * 256 + wr * 64 + fr) * ld + pn * 256 + wc * 64 + 16 * fq;
;         f32x4 bv[2][2];
;         if (MODE == 2) {
; #pragma unroll
;             for (int q = 0; q < 4; ++q) bv[q >> 1][q & 1] = *(const f32x4*)(bias + pn * 256 + wc * 64 + 16 * fq + 4 * q); }
; #pragma unroll
;         for (int ai = 0; ai < 2; ++ai) {
;             u32x4 gq[4], yq[4][2], oq[4][2];
; #pragma unroll
;             for (int m = 0; m < 4; ++m) { const size_t off = off0 + (size_t)(ai * 128 + m * 16) * ld;
;                 if (MODE == 2) { yq[m][0] = *(const u32x4*)((const bf16*)G0 + off); yq[m][1] = *(const u32x4*)((const bf16*)G0 + off + 8); }
;                 else gq[m] = __builtin_nontemporal_load((const u32x4*)((const unsigned char*)G0 + off));
;                 if (MODE == 1) { oq[m][0] = *(const u32x4*)(O + off); oq[m][1] = *(const u32x4*)(O + off + 8); } }
; #pragma unroll
;             for (int m = 0; m < 4; ++m) { const size_t off = off0 + (size_t)(ai * 128 + m * 16) * ld;
;                 f32x4 v[2][2];
; #pragma unroll
;                 for (int bj = 0; bj < 2; ++bj)
; #pragma unroll
;                     for (int n = 0; n < 2; ++n) { const int q = bj * 2 + n; const f32x4 a = acc[ai][bj][m][n];
;                         if (MODE == 2) { const unsigned lo = yq[m][bj][2 * n], hi = yq[m][bj][2 * n + 1]; const f32x4 y = (f32x4){bf_lo(lo), bf_hi(lo), bf_lo(hi), bf_hi(hi)};
; #pragma unroll
;                             for (int j = 0; j < 4; ++j) v[bj][n][j] = y[j] * fsigmoid(a[j] + bv[bj][n][j]) * S8_SCALE; }
;                         else { const f32x4 g = u8x4_f32(gq[m][q]);
;                             if (MODE == 0) v[bj][n] = a * g * ASC;
;                             else { const unsigned lo = oq[m][bj][2 * n], hi = oq[m][bj][2 * n + 1]; v[bj][n] = (f32x4){bf_lo(lo), bf_hi(lo), bf_lo(hi), bf_hi(hi)} + a * g * ASC; } } }
;                 if (MODE == 0) {
; #pragma unroll
;                     for (int bj = 0; bj < 2; ++bj) { u32x4 w; w.x = pk_bf16(v[bj][0][0], v[bj][0][1]); w.y = pk_bf16(v[bj][0][2], v[bj][0][3]); w.z = pk_bf16(v[bj][1][0], v[bj][1][1]); w.w = pk_bf16(v[bj][1][2], v[bj][1][3]); *(u32x4*)(O + off + 8 * bj) = w; } }
;                 else { u32x4 w;
.LBB0_766:
	v_lshl_add_u32 v202, s8, 8, v206
	v_ashrrev_i32_e32 v203, 31, v202
	s_lshl_b32 s26, s68, 8
	v_lshlrev_b64 v[64:65], 10, v[202:203]
	s_ashr_i32 s27, s26, 31
	v_lshl_add_u64 v[64:65], s[6:7], 0, v[64:65]
	s_lshl_b32 s8, s53, 1
	v_lshl_add_u64 v[64:65], s[26:27], 1, v[64:65]
	v_lshl_add_u64 v[62:63], s[26:27], 2, v[192:193]
	v_lshl_add_u64 v[64:65], v[64:65], 0, s[8:9]
	flat_load_dwordx4 v[78:81], v[62:63]
	flat_load_dwordx4 v[74:77], v[62:63] offset:16
	v_lshl_add_u64 v[204:205], v[64:65], 0, v[188:189]
	flat_load_dwordx4 v[216:219], v[204:205]
	flat_load_dwordx4 v[70:73], v[62:63] offset:32
	s_nop 0
	flat_load_dwordx4 v[62:65], v[62:63] offset:48
	v_add_co_u32_e32 v138, vcc, s49, v204
	flat_load_dwordx4 v[220:223], v[204:205] offset:16
	s_nop 0
	v_addc_co_u32_e32 v139, vcc, 0, v205, vcc
	v_add_co_u32_e32 v140, vcc, s52, v204
	s_or_b32 s8, s26, s53
	s_nop 0
	v_addc_co_u32_e32 v141, vcc, 0, v205, vcc
	v_add_co_u32_e32 v224, vcc, s59, v204
	s_ashr_i32 s26, s8, 7
	s_nop 0
	v_addc_co_u32_e32 v225, vcc, 0, v205, vcc
	flat_load_dwordx4 v[166:169], v[138:139]
	flat_load_dwordx4 v[162:165], v[138:139] offset:16
	flat_load_dwordx4 v[158:161], v[140:141]
	flat_load_dwordx4 v[154:157], v[140:141] offset:16
	flat_load_dwordx4 v[150:153], v[224:225]
	s_nop 0
	flat_load_dwordx4 v[138:141], v[224:225] offset:16
	s_ashr_i32 s27, s26, 31
	s_waitcnt vmcnt(0) lgkmcnt(0)
	v_add_f32_e32 v146, v146, v78
	v_mul_f32_e32 v146, 0xbfb8aa3b, v146
	v_exp_f32_e32 v146, v146
	v_add_f32_e32 v134, v134, v70
	v_mul_f32_e32 v134, 0xbfb8aa3b, v134
	v_exp_f32_e32 v134, v134
	v_add_f32_e32 v146, 1.0, v146
	v_rcp_f32_e32 v146, v146
	v_add_f32_e32 v135, v135, v71
	v_add_f32_e32 v134, 1.0, v134
	v_rcp_f32_e32 v134, v134
	v_mul_f32_e32 v135, 0xbfb8aa3b, v135
	v_exp_f32_e32 v135, v135
	v_lshlrev_b32_e32 v215, 16, v216
	v_add_f32_e32 v147, v147, v79
	v_mul_f32_e32 v146, v146, v215
	v_lshlrev_b32_e32 v215, 16, v220
	v_add_f32_e32 v149, v149, v81
	v_mul_f32_e32 v147, 0xbfb8aa3b, v147
	v_mul_f32_e32 v134, v134, v215
	v_add_f32_e32 v143, v143, v75
	v_mul_f32_e32 v149, 0xbfb8aa3b, v149
	v_exp_f32_e32 v147, v147
	v_mul_f32_e32 v215, 0x41800000, v134
	v_add_f32_e32 v134, 1.0, v135
	v_add_f32_e32 v135, v136, v72
	v_mul_f32_e32 v143, 0xbfb8aa3b, v143
	v_exp_f32_e32 v149, v149
	v_mul_f32_e32 v135, 0xbfb8aa3b, v135
	v_add_f32_e32 v136, v137, v73
	v_add_f32_e32 v142, v142, v74
	v_exp_f32_e32 v143, v143
	v_exp_f32_e32 v135, v135
	v_mul_f32_e32 v136, 0xbfb8aa3b, v136
	v_mul_f32_e32 v142, 0xbfb8aa3b, v142
	v_exp_f32_e32 v136, v136
	v_add_f32_e32 v130, v130, v62
	v_add_f32_e32 v131, v131, v63
	v_add_f32_e32 v132, v132, v64
	v_exp_f32_e32 v142, v142
	v_add_f32_e32 v147, 1.0, v147
	v_mul_f32_e32 v130, 0xbfb8aa3b, v130
	v_mul_f32_e32 v131, 0xbfb8aa3b, v131
	v_mul_f32_e32 v132, 0xbfb8aa3b, v132
	v_add_f32_e32 v148, v148, v80
	v_add_f32_e32 v149, 1.0, v149
	v_rcp_f32_e32 v147, v147
	v_exp_f32_e32 v130, v130
	v_exp_f32_e32 v131, v131
	v_exp_f32_e32 v132, v132
	v_add_f32_e32 v144, v144, v76
	v_add_f32_e32 v145, v145, v77
	v_mul_f32_e32 v148, 0xbfb8aa3b, v148
	v_add_f32_e32 v143, 1.0, v143
	v_rcp_f32_e32 v149, v149
	v_rcp_f32_e32 v134, v134
	v_add_f32_e32 v135, 1.0, v135
	v_mul_f32_e32 v144, 0xbfb8aa3b, v144
	v_mul_f32_e32 v145, 0xbfb8aa3b, v145
	v_exp_f32_e32 v148, v148
	v_rcp_f32_e32 v143, v143
	v_rcp_f32_e32 v135, v135
	v_add_f32_e32 v136, 1.0, v136
	v_exp_f32_e32 v144, v144
	v_exp_f32_e32 v145, v145
	v_and_b32_e32 v216, 0xffff0000, v216
	v_add_f32_e32 v142, 1.0, v142
	v_rcp_f32_e32 v136, v136
	v_lshlrev_b32_e32 v224, 16, v217
	v_and_b32_e32 v217, 0xffff0000, v217
	v_rcp_f32_e32 v142, v142
	v_mul_f32_e32 v147, v147, v216
	v_and_b32_e32 v216, 0xffff0000, v220
	v_add_f32_e32 v130, 1.0, v130
	v_add_f32_e32 v131, 1.0, v131
	v_add_f32_e32 v133, v133, v65
	v_add_f32_e32 v132, 1.0, v132
	v_lshlrev_b32_e32 v225, 16, v218
	v_and_b32_e32 v218, 0xffff0000, v218
	v_mul_f32_e32 v149, v149, v217
	v_lshlrev_b32_e32 v217, 16, v221
	v_mul_f32_e32 v134, v134, v216
	v_rcp_f32_e32 v130, v130
	v_rcp_f32_e32 v131, v131
	v_mul_f32_e32 v133, 0xbfb8aa3b, v133
	v_rcp_f32_e32 v132, v132
	v_add_f32_e32 v148, 1.0, v148
	v_mul_f32_e32 v143, v143, v218
	v_and_b32_e32 v218, 0xffff0000, v221
	v_mul_f32_e32 v137, 0x41800000, v134
	v_mul_f32_e32 v134, v135, v217
	v_exp_f32_e32 v133, v133
	v_add_f32_e32 v144, 1.0, v144
	v_add_f32_e32 v145, 1.0, v145
	v_rcp_f32_e32 v148, v148
	v_mul_f32_e32 v216, 0x41800000, v134
	v_mul_f32_e32 v134, v136, v218
	v_add_f32_e32 v126, v126, v78
	v_rcp_f32_e32 v144, v144
	v_mul_f32_e32 v142, v142, v225
	v_mul_f32_e32 v146, 0x41800000, v146
	v_mul_f32_e32 v147, 0x41800000, v147
	v_rcp_f32_e32 v145, v145
	v_mul_f32_e32 v217, 0x41800000, v134
	v_lshlrev_b32_e32 v134, 16, v222
	v_and_b32_e32 v135, 0xffff0000, v222
	v_lshlrev_b32_e32 v136, 16, v223
	v_mul_f32_e32 v126, 0xbfb8aa3b, v126
	v_add_f32_e32 v122, v122, v74
	v_mul_f32_e32 v142, 0x41800000, v142
	v_mul_f32_e32 v143, 0x41800000, v143
	v_mul_f32_e32 v130, v130, v134
	v_mul_f32_e32 v131, v131, v135
	v_mul_f32_e32 v132, v132, v136
	v_med3_f32 v135, v146, s62, v211
	v_med3_f32 v136, v147, s62, v211
	v_mov_b32_e32 v134, v189
	v_exp_f32_e32 v126, v126
	v_mul_f32_e32 v122, 0xbfb8aa3b, v122
	v_add_f32_e32 v118, v118, v70
	v_add_f32_e32 v133, 1.0, v133
	v_cvt_pk_fp8_f32 v134, v135, v136
	v_med3_f32 v142, v142, s62, v211
	v_med3_f32 v143, v143, s62, v211
	v_mov_b32_e32 v135, v189
	v_exp_f32_e32 v122, v122
	v_mul_f32_e32 v118, 0xbfb8aa3b, v118
	v_add_f32_e32 v114, v114, v62
	v_lshlrev_b32_e32 v226, 16, v219
	v_and_b32_e32 v219, 0xffff0000, v219
	v_mul_f32_e32 v148, v148, v224
	v_rcp_f32_e32 v133, v133
	v_cvt_pk_fp8_f32 v135, v142, v143
	v_exp_f32_e32 v118, v118
;     __device__ __forceinline__ void operator()(AccRef acc, const GUnit& u, int wr, int wc, int fr, int fq) const {
;     ...
;         for (int ai = 0; ai < 2; ++ai) {
;             u32x4 gq[4], yq[4][2], oq[4][2];
; #pragma unroll
;             for (int m = 0; m < 4; ++m) { const size_t off = off0 + (size_t)(ai * 128 + m * 16) * ld;
;                 if (MODE == 2) { yq[m][0] = *(const u32x4*)((const bf16*)G0 + off); yq[m][1] = *(const u32x4*)((const bf16*)G0 + off + 8); }
;                 else gq[m] = __builtin_nontemporal_load((const u32x4*)((const unsigned char*)G0 + off));
;                 if (MODE == 1) { oq[m][0] = *(const u32x4*)(O + off); oq[m][1] = *(const u32x4*)(O + off + 8); } }
; #pragma unroll
;             for (int m = 0; m < 4; ++m) { const size_t off = off0 + (size_t)(ai * 128 + m * 16) * ld;
;                 f32x4 v[2][2];
; #pragma unroll
;                 for (int bj = 0; bj < 2; ++bj)
; #pragma unroll
;                     for (int n = 0; n < 2; ++n) { const int q = bj * 2 + n; const f32x4 a = acc[ai][bj][m][n];
;                         if (MODE == 2) { const unsigned lo = yq[m][bj][2 * n], hi = yq[m][bj][2 * n + 1]; const f32x4 y = (f32x4){bf_lo(lo), bf_hi(lo), bf_lo(hi), bf_hi(hi)};
; #pragma unroll
;                             for (int j = 0; j < 4; ++j) v[bj][n][j] = y[j] * fsigmoid(a[j] + bv[bj][n][j]) * S8_SCALE; }
;                         else { const f32x4 g = u8x4_f32(gq[m][q]);
;                             if (MODE == 0) v[bj][n] = a * g * ASC;
;                             else { const unsigned lo = oq[m][bj][2 * n], hi = oq[m][bj][2 * n + 1]; v[bj][n] = (f32x4){bf_lo(lo), bf_hi(lo), bf_lo(hi), bf_hi(hi)} + a * g * ASC; } } }
;                 if (MODE == 0) {
; #pragma unroll
;                     for (int bj = 0; bj < 2; ++bj) { u32x4 w; w.x = pk_bf16(v[bj][0][0], v[bj][0][1]); w.y = pk_bf16(v[bj][0][2], v[bj][0][3]); w.z = pk_bf16(v[bj][1][0], v[bj][1][1]); w.w = pk_bf16(v[bj][1][2], v[bj][1][3]); *(u32x4*)(O + off + 8 * bj) = w; } }
;                 else { u32x4 w;
; #pragma unroll
;                     for (int q = 0; q < 4; ++q) w[q] = pk4_fp8(v[q >> 1][q & 1][0], v[q >> 1][q & 1][1], v[q >> 1][q & 1][2], v[q >> 1][q & 1][3]);
;                     const size_t offo = MODE == 2 ? tiled_off((size_t)(pm * 256 + wr * 64 + fr + ai * 128 + m * 16), pn * 256 + wc * 64 + 16 * fq, ldo) : off;
	v_mul_f32_e32 v114, 0xbfb8aa3b, v114
	v_mul_f32_e32 v148, 0x41800000, v148
	v_mul_f32_e32 v149, 0x41800000, v149
	v_mul_f32_e32 v144, v144, v226
	v_mul_f32_e32 v145, v145, v219
	v_exp_f32_e32 v114, v114
	v_mul_f32_e32 v144, 0x41800000, v144
	v_mul_f32_e32 v145, 0x41800000, v145
	v_med3_f32 v136, v148, s62, v211
	v_med3_f32 v146, v149, s62, v211
	v_add_f32_e32 v126, 1.0, v126
	v_and_b32_e32 v218, 0xffff0000, v223
	v_cvt_pk_fp8_f32 v134, v136, v146 op_sel:[0,0,1]
	v_med3_f32 v136, v144, s62, v211
	v_med3_f32 v142, v145, s62, v211
	v_rcp_f32_e32 v126, v126
	v_add_f32_e32 v122, 1.0, v122
	v_mul_f32_e32 v130, 0x41800000, v130
	v_mul_f32_e32 v131, 0x41800000, v131
	v_mul_f32_e32 v133, v133, v218
	v_cvt_pk_fp8_f32 v135, v136, v142 op_sel:[0,0,1]
	v_med3_f32 v142, v215, s62, v211
	v_med3_f32 v137, v137, s62, v211
	v_mov_b32_e32 v136, v189
	v_rcp_f32_e32 v122, v122
	v_add_f32_e32 v118, 1.0, v118
	v_mul_f32_e32 v133, 0x41800000, v133
	v_cvt_pk_fp8_f32 v136, v142, v137
	v_med3_f32 v130, v130, s62, v211
	v_med3_f32 v131, v131, s62, v211
	v_mov_b32_e32 v137, v189
	v_rcp_f32_e32 v118, v118
	v_add_f32_e32 v114, 1.0, v114
	v_add_f32_e32 v115, v115, v63
	v_cvt_pk_fp8_f32 v137, v130, v131
	v_med3_f32 v131, v133, s62, v211
	v_lshlrev_b32_e32 v133, 16, v166
	v_rcp_f32_e32 v114, v114
	v_mul_f32_e32 v115, 0xbfb8aa3b, v115
	v_add_f32_e32 v127, v127, v79
	v_mul_f32_e32 v126, v126, v133
	v_lshlrev_b32_e32 v133, 16, v168
	v_exp_f32_e32 v115, v115
	v_mul_f32_e32 v132, 0x41800000, v132
	v_mul_f32_e32 v127, 0xbfb8aa3b, v127
	v_add_f32_e32 v128, v128, v80
	v_add_f32_e32 v123, v123, v75
	v_mul_f32_e32 v122, v122, v133
	v_lshlrev_b32_e32 v133, 16, v162
	v_med3_f32 v130, v132, s62, v211
	v_exp_f32_e32 v127, v127
	v_mul_f32_e32 v128, 0xbfb8aa3b, v128
	v_add_f32_e32 v129, v129, v81
	v_mul_f32_e32 v123, 0xbfb8aa3b, v123
	v_add_f32_e32 v124, v124, v76
	v_add_f32_e32 v119, v119, v71
	v_mul_f32_e32 v118, v118, v133
	v_lshlrev_b32_e32 v133, 16, v164
	v_cvt_pk_fp8_f32 v137, v130, v131 op_sel:[0,0,1]
	v_alignbit_b32 v130, v203, v202, 8
	v_exp_f32_e32 v128, v128
	v_mul_f32_e32 v129, 0xbfb8aa3b, v129
	v_exp_f32_e32 v123, v123
	v_mul_f32_e32 v124, 0xbfb8aa3b, v124
	v_add_f32_e32 v125, v125, v77
	v_mul_f32_e32 v119, 0xbfb8aa3b, v119
	v_add_f32_e32 v120, v120, v72
	v_mul_f32_e32 v114, v114, v133
	v_mad_u64_u32 v[130:131], s[28:29], v130, 12, s[26:27]
	v_exp_f32_e32 v129, v129
	v_exp_f32_e32 v124, v124
	v_mul_f32_e32 v125, 0xbfb8aa3b, v125
	v_exp_f32_e32 v119, v119
	v_mul_f32_e32 v120, 0xbfb8aa3b, v120
	v_add_f32_e32 v121, v121, v73
	v_mul_f32_e32 v133, 0x41800000, v114
	v_add_f32_e32 v114, 1.0, v115
	v_add_f32_e32 v115, v116, v64
	v_med3_f32 v142, v216, s62, v211
	v_med3_f32 v143, v217, s62, v211
	v_mad_u32_u24 v131, v203, 12, v131
	v_exp_f32_e32 v125, v125
	v_exp_f32_e32 v120, v120
	v_mul_f32_e32 v121, 0xbfb8aa3b, v121
	v_mul_f32_e32 v115, 0xbfb8aa3b, v115
	v_add_f32_e32 v116, v117, v65
	v_cvt_pk_fp8_f32 v136, v142, v143 op_sel:[0,0,1]
	v_lshlrev_b64 v[130:131], 15, v[130:131]
	v_lshlrev_b32_e32 v132, 7, v202
	v_add_f32_e32 v127, 1.0, v127
	v_exp_f32_e32 v121, v121
	v_exp_f32_e32 v115, v115
	v_mul_f32_e32 v116, 0xbfb8aa3b, v116
	v_and_b32_e32 v142, 0x6780, v132
	v_mov_b32_e32 v143, v189
	v_lshl_add_u64 v[130:131], s[12:13], 0, v[130:131]
	v_rcp_f32_e32 v127, v127
	v_add_f32_e32 v128, 1.0, v128
	v_add_f32_e32 v123, 1.0, v123
	v_exp_f32_e32 v116, v116
	v_lshl_add_u64 v[142:143], v[130:131], 0, v[142:143]
	v_rcp_f32_e32 v128, v128
	v_add_f32_e32 v129, 1.0, v129
	v_rcp_f32_e32 v123, v123
	v_add_f32_e32 v124, 1.0, v124
	v_add_f32_e32 v119, 1.0, v119
	v_lshl_add_u64 v[142:143], v[142:143], 0, v[190:191]
	v_rcp_f32_e32 v129, v129
	v_rcp_f32_e32 v124, v124
	v_add_f32_e32 v125, 1.0, v125
	v_rcp_f32_e32 v119, v119
	v_add_f32_e32 v120, 1.0, v120
	flat_store_dwordx4 v[142:143], v[134:137]
	v_rcp_f32_e32 v125, v125
	v_rcp_f32_e32 v120, v120
	v_and_b32_e32 v134, 0xffff0000, v166
	v_add_f32_e32 v121, 1.0, v121
	v_rcp_f32_e32 v114, v114
	v_add_f32_e32 v115, 1.0, v115
	v_lshlrev_b32_e32 v135, 16, v167
	v_mul_f32_e32 v127, v127, v134
	v_and_b32_e32 v134, 0xffff0000, v168
	v_rcp_f32_e32 v121, v121
	v_rcp_f32_e32 v115, v115
	v_add_f32_e32 v116, 1.0, v116
	v_and_b32_e32 v136, 0xffff0000, v167
	v_mul_f32_e32 v128, v128, v135
	v_lshlrev_b32_e32 v135, 16, v169
	v_mul_f32_e32 v123, v123, v134
	v_and_b32_e32 v134, 0xffff0000, v162
	v_rcp_f32_e32 v116, v116
	v_mul_f32_e32 v129, v129, v136
	v_and_b32_e32 v136, 0xffff0000, v169
	v_mul_f32_e32 v124, v124, v135
	v_lshlrev_b32_e32 v135, 16, v163
	v_mul_f32_e32 v119, v119, v134
	v_and_b32_e32 v134, 0xffff0000, v164
	v_mul_f32_e32 v125, v125, v136
	v_and_b32_e32 v136, 0xffff0000, v163
	v_mul_f32_e32 v120, v120, v135
	v_lshlrev_b32_e32 v135, 16, v165
	v_mul_f32_e32 v114, v114, v134
	v_mul_f32_e32 v121, v121, v136
	v_and_b32_e32 v136, 0xffff0000, v165
	v_mul_f32_e32 v117, 0x41800000, v114
	v_mul_f32_e32 v114, v115, v135
	v_mul_f32_e32 v126, 0x41800000, v126
	v_mul_f32_e32 v127, 0x41800000, v127
	v_mul_f32_e32 v134, 0x41800000, v114
	v_mul_f32_e32 v114, v116, v136
	v_mul_f32_e32 v122, 0x41800000, v122
	v_mul_f32_e32 v123, 0x41800000, v123
	v_mul_f32_e32 v135, 0x41800000, v114
	v_med3_f32 v115, v126, s62, v211
	v_med3_f32 v116, v127, s62, v211
	v_mov_b32_e32 v114, v189
	v_cvt_pk_fp8_f32 v114, v115, v116
	v_med3_f32 v122, v122, s62, v211
	v_med3_f32 v123, v123, s62, v211
	v_mov_b32_e32 v115, v189
	v_cvt_pk_fp8_f32 v115, v122, v123
	v_mul_f32_e32 v128, 0x41800000, v128
	v_mul_f32_e32 v129, 0x41800000, v129
	v_mul_f32_e32 v124, 0x41800000, v124
	v_mul_f32_e32 v125, 0x41800000, v125
	v_med3_f32 v116, v128, s62, v211
	v_med3_f32 v126, v129, s62, v211
	v_mul_f32_e32 v118, 0x41800000, v118
;     __device__ __forceinline__ void operator()(AccRef acc, const GUnit& u, int wr, int wc, int fr, int fq) const {
;     ...
;         for (int ai = 0; ai < 2; ++ai) {
;             u32x4 gq[4], yq[4][2], oq[4][2];
; #pragma unroll
;             for (int m = 0; m < 4; ++m) { const size_t off = off0 + (size_t)(ai * 128 + m * 16) * ld;
;                 if (MODE == 2) { yq[m][0] = *(const u32x4*)((const bf16*)G0 + off); yq[m][1] = *(const u32x4*)((const bf16*)G0 + off + 8); }
;                 else gq[m] = __builtin_nontemporal_load((const u32x4*)((const unsigned char*)G0 + off));
;                 if (MODE == 1) { oq[m][0] = *(const u32x4*)(O + off); oq[m][1] = *(const u32x4*)(O + off + 8); } }
; #pragma unroll
;             for (int m = 0; m < 4; ++m) { const size_t off = off0 + (size_t)(ai * 128 + m * 16) * ld;
;                 f32x4 v[2][2];
; #pragma unroll
;                 for (int bj = 0; bj < 2; ++bj)
; #pragma unroll
;                     for (int n = 0; n < 2; ++n) { const int q = bj * 2 + n; const f32x4 a = acc[ai][bj][m][n];
;                         if (MODE == 2) { const unsigned lo = yq[m][bj][2 * n], hi = yq[m][bj][2 * n + 1]; const f32x4 y = (f32x4){bf_lo(lo), bf_hi(lo), bf_lo(hi), bf_hi(hi)};
; #pragma unroll
;                             for (int j = 0; j < 4; ++j) v[bj][n][j] = y[j] * fsigmoid(a[j] + bv[bj][n][j]) * S8_SCALE; }
;                         else { const f32x4 g = u8x4_f32(gq[m][q]);
;                             if (MODE == 0) v[bj][n] = a * g * ASC;
;                             else { const unsigned lo = oq[m][bj][2 * n], hi = oq[m][bj][2 * n + 1]; v[bj][n] = (f32x4){bf_lo(lo), bf_hi(lo), bf_lo(hi), bf_hi(hi)} + a * g * ASC; } } }
;                 if (MODE == 0) {
; #pragma unroll
;                     for (int bj = 0; bj < 2; ++bj) { u32x4 w; w.x = pk_bf16(v[bj][0][0], v[bj][0][1]); w.y = pk_bf16(v[bj][0][2], v[bj][0][3]); w.z = pk_bf16(v[bj][1][0], v[bj][1][1]); w.w = pk_bf16(v[bj][1][2], v[bj][1][3]); *(u32x4*)(O + off + 8 * bj) = w; } }
;                 else { u32x4 w;
; #pragma unroll
;                     for (int q = 0; q < 4; ++q) w[q] = pk4_fp8(v[q >> 1][q & 1][0], v[q >> 1][q & 1][1], v[q >> 1][q & 1][2], v[q >> 1][q & 1][3]);
;                     const size_t offo = MODE == 2 ? tiled_off((size_t)(pm * 256 + wr * 64 + fr + ai * 128 + m * 16), pn * 256 + wc * 64 + 16 * fq, ldo) : off;
	v_mul_f32_e32 v119, 0x41800000, v119
	v_cvt_pk_fp8_f32 v114, v116, v126 op_sel:[0,0,1]
	v_med3_f32 v116, v124, s62, v211
	v_med3_f32 v122, v125, s62, v211
	v_mul_f32_e32 v120, 0x41800000, v120
	v_mul_f32_e32 v121, 0x41800000, v121
	v_cvt_pk_fp8_f32 v115, v116, v122 op_sel:[0,0,1]
	v_med3_f32 v118, v118, s62, v211
	v_med3_f32 v119, v119, s62, v211
	v_mov_b32_e32 v116, v189
	v_add_f32_e32 v110, v110, v78
	v_cvt_pk_fp8_f32 v116, v118, v119
	v_med3_f32 v118, v120, s62, v211
	v_med3_f32 v119, v121, s62, v211
	v_med3_f32 v120, v133, s62, v211
	v_med3_f32 v121, v117, s62, v211
	v_mov_b32_e32 v117, v189
	v_mul_f32_e32 v110, 0xbfb8aa3b, v110
	v_add_f32_e32 v106, v106, v74
	v_cvt_pk_fp8_f32 v117, v120, v121
	v_exp_f32_e32 v110, v110
	v_mul_f32_e32 v106, 0xbfb8aa3b, v106
	v_add_f32_e32 v102, v102, v70
	v_exp_f32_e32 v106, v106
	v_mul_f32_e32 v102, 0xbfb8aa3b, v102
	v_add_f32_e32 v98, v98, v62
	v_exp_f32_e32 v102, v102
	v_mul_f32_e32 v98, 0xbfb8aa3b, v98
	v_cvt_pk_fp8_f32 v116, v118, v119 op_sel:[0,0,1]
	v_med3_f32 v118, v134, s62, v211
	v_med3_f32 v119, v135, s62, v211
	v_exp_f32_e32 v98, v98
	v_cvt_pk_fp8_f32 v117, v118, v119 op_sel:[0,0,1]
	v_add_f32_e32 v110, 1.0, v110
	v_bitop3_b32 v118, v132, s63, v212 bitop3:0xc8
	v_mov_b32_e32 v119, v189
	v_rcp_f32_e32 v110, v110
	v_add_f32_e32 v106, 1.0, v106
	v_lshl_add_u64 v[118:119], v[130:131], 0, v[118:119]
	v_rcp_f32_e32 v106, v106
	v_add_f32_e32 v102, 1.0, v102
	v_lshl_add_u64 v[118:119], v[118:119], 0, v[190:191]
	v_rcp_f32_e32 v102, v102
	v_add_f32_e32 v98, 1.0, v98
	v_add_f32_e32 v99, v99, v63
	flat_store_dwordx4 v[118:119], v[114:117]
	v_rcp_f32_e32 v98, v98
	v_mul_f32_e32 v99, 0xbfb8aa3b, v99
	v_lshlrev_b32_e32 v114, 16, v158
	v_add_f32_e32 v111, v111, v79
	v_mul_f32_e32 v110, v110, v114
	v_lshlrev_b32_e32 v114, 16, v160
	v_exp_f32_e32 v99, v99
	v_mul_f32_e32 v111, 0xbfb8aa3b, v111
	v_add_f32_e32 v112, v112, v80
	v_add_f32_e32 v107, v107, v75
	v_mul_f32_e32 v106, v106, v114
	v_lshlrev_b32_e32 v114, 16, v154
	v_exp_f32_e32 v111, v111
	v_mul_f32_e32 v112, 0xbfb8aa3b, v112
	v_add_f32_e32 v113, v113, v81
	v_mul_f32_e32 v107, 0xbfb8aa3b, v107
	v_add_f32_e32 v108, v108, v76
	v_add_f32_e32 v103, v103, v71
	v_mul_f32_e32 v102, v102, v114
	v_lshlrev_b32_e32 v114, 16, v156
	v_exp_f32_e32 v112, v112
	v_mul_f32_e32 v113, 0xbfb8aa3b, v113
	v_exp_f32_e32 v107, v107
	v_mul_f32_e32 v108, 0xbfb8aa3b, v108
	v_add_f32_e32 v109, v109, v77
	v_mul_f32_e32 v103, 0xbfb8aa3b, v103
	v_add_f32_e32 v104, v104, v72
	v_mul_f32_e32 v98, v98, v114
	v_exp_f32_e32 v113, v113
	v_exp_f32_e32 v108, v108
	v_mul_f32_e32 v109, 0xbfb8aa3b, v109
	v_exp_f32_e32 v103, v103
	v_mul_f32_e32 v104, 0xbfb8aa3b, v104
	v_add_f32_e32 v105, v105, v73
	v_mul_f32_e32 v114, 0x41800000, v98
	v_add_f32_e32 v98, 1.0, v99
	v_add_f32_e32 v99, v100, v64
	v_exp_f32_e32 v109, v109
	v_exp_f32_e32 v104, v104
	v_mul_f32_e32 v105, 0xbfb8aa3b, v105
	v_mul_f32_e32 v99, 0xbfb8aa3b, v99
	v_add_f32_e32 v100, v101, v65
	v_add_f32_e32 v111, 1.0, v111
	v_exp_f32_e32 v105, v105
	v_exp_f32_e32 v99, v99
	v_mul_f32_e32 v100, 0xbfb8aa3b, v100
	v_rcp_f32_e32 v111, v111
	v_add_f32_e32 v112, 1.0, v112
	v_add_f32_e32 v107, 1.0, v107
	v_exp_f32_e32 v100, v100
	v_rcp_f32_e32 v112, v112
	v_add_f32_e32 v113, 1.0, v113
	v_rcp_f32_e32 v107, v107
	v_add_f32_e32 v108, 1.0, v108
	v_add_f32_e32 v103, 1.0, v103
	v_rcp_f32_e32 v113, v113
	v_rcp_f32_e32 v108, v108
	v_add_f32_e32 v109, 1.0, v109
	v_rcp_f32_e32 v103, v103
	v_add_f32_e32 v104, 1.0, v104
	v_and_b32_e32 v115, 0xffff0000, v158
	v_rcp_f32_e32 v109, v109
	v_rcp_f32_e32 v104, v104
	v_add_f32_e32 v105, 1.0, v105
	v_rcp_f32_e32 v98, v98
	v_add_f32_e32 v99, 1.0, v99
	v_lshlrev_b32_e32 v116, 16, v159
	v_mul_f32_e32 v111, v111, v115
	v_and_b32_e32 v115, 0xffff0000, v160
	v_rcp_f32_e32 v105, v105
	v_rcp_f32_e32 v99, v99
	v_add_f32_e32 v100, 1.0, v100
	v_and_b32_e32 v117, 0xffff0000, v159
	v_mul_f32_e32 v112, v112, v116
	v_lshlrev_b32_e32 v116, 16, v161
	v_mul_f32_e32 v107, v107, v115
	v_and_b32_e32 v115, 0xffff0000, v154
	v_rcp_f32_e32 v100, v100
	v_mul_f32_e32 v113, v113, v117
	v_and_b32_e32 v117, 0xffff0000, v161
	v_mul_f32_e32 v108, v108, v116
	v_lshlrev_b32_e32 v116, 16, v155
	v_mul_f32_e32 v103, v103, v115
	v_and_b32_e32 v115, 0xffff0000, v156
	v_mul_f32_e32 v109, v109, v117
	v_and_b32_e32 v117, 0xffff0000, v155
	v_mul_f32_e32 v104, v104, v116
	v_lshlrev_b32_e32 v116, 16, v157
	v_mul_f32_e32 v98, v98, v115
	v_mul_f32_e32 v105, v105, v117
	v_and_b32_e32 v117, 0xffff0000, v157
	v_mul_f32_e32 v101, 0x41800000, v98
	v_mul_f32_e32 v98, v99, v116
	v_mul_f32_e32 v110, 0x41800000, v110
	v_mul_f32_e32 v111, 0x41800000, v111
	v_mul_f32_e32 v115, 0x41800000, v98
	v_mul_f32_e32 v98, v100, v117
	v_mul_f32_e32 v106, 0x41800000, v106
	v_mul_f32_e32 v107, 0x41800000, v107
	v_mul_f32_e32 v116, 0x41800000, v98
	v_med3_f32 v99, v110, s62, v211
	v_med3_f32 v100, v111, s62, v211
	v_mov_b32_e32 v98, v189
	v_cvt_pk_fp8_f32 v98, v99, v100
	v_med3_f32 v106, v106, s62, v211
	v_med3_f32 v107, v107, s62, v211
	v_mov_b32_e32 v99, v189
	v_cvt_pk_fp8_f32 v99, v106, v107
	v_mul_f32_e32 v112, 0x41800000, v112
	v_mul_f32_e32 v113, 0x41800000, v113
	v_mul_f32_e32 v108, 0x41800000, v108
	v_mul_f32_e32 v109, 0x41800000, v109
	v_med3_f32 v100, v112, s62, v211
	v_med3_f32 v110, v113, s62, v211
	v_mul_f32_e32 v102, 0x41800000, v102
	v_mul_f32_e32 v103, 0x41800000, v103
	v_cvt_pk_fp8_f32 v98, v100, v110 op_sel:[0,0,1]
	v_med3_f32 v100, v108, s62, v211
	v_med3_f32 v106, v109, s62, v211
	v_mul_f32_e32 v104, 0x41800000, v104
	v_mul_f32_e32 v105, 0x41800000, v105
	v_cvt_pk_fp8_f32 v99, v100, v106 op_sel:[0,0,1]
	v_med3_f32 v102, v102, s62, v211
	v_med3_f32 v103, v103, s62, v211
;     __device__ __forceinline__ void operator()(AccRef acc, const GUnit& u, int wr, int wc, int fr, int fq) const {
;     ...
;         for (int ai = 0; ai < 2; ++ai) {
;             u32x4 gq[4], yq[4][2], oq[4][2];
; #pragma unroll
;             for (int m = 0; m < 4; ++m) { const size_t off = off0 + (size_t)(ai * 128 + m * 16) * ld;
;                 if (MODE == 2) { yq[m][0] = *(const u32x4*)((const bf16*)G0 + off); yq[m][1] = *(const u32x4*)((const bf16*)G0 + off + 8); }
;                 else gq[m] = __builtin_nontemporal_load((const u32x4*)((const unsigned char*)G0 + off));
;                 if (MODE == 1) { oq[m][0] = *(const u32x4*)(O + off); oq[m][1] = *(const u32x4*)(O + off + 8); } }
; #pragma unroll
;             for (int m = 0; m < 4; ++m) { const size_t off = off0 + (size_t)(ai * 128 + m * 16) * ld;
;                 f32x4 v[2][2];
; #pragma unroll
;                 for (int bj = 0; bj < 2; ++bj)
; #pragma unroll
;                     for (int n = 0; n < 2; ++n) { const int q = bj * 2 + n; const f32x4 a = acc[ai][bj][m][n];
;                         if (MODE == 2) { const unsigned lo = yq[m][bj][2 * n], hi = yq[m][bj][2 * n + 1]; const f32x4 y = (f32x4){bf_lo(lo), bf_hi(lo), bf_lo(hi), bf_hi(hi)};
; #pragma unroll
;                             for (int j = 0; j < 4; ++j) v[bj][n][j] = y[j] * fsigmoid(a[j] + bv[bj][n][j]) * S8_SCALE; }
;                         else { const f32x4 g = u8x4_f32(gq[m][q]);
;                             if (MODE == 0) v[bj][n] = a * g * ASC;
;                             else { const unsigned lo = oq[m][bj][2 * n], hi = oq[m][bj][2 * n + 1]; v[bj][n] = (f32x4){bf_lo(lo), bf_hi(lo), bf_lo(hi), bf_hi(hi)} + a * g * ASC; } } }
;                 if (MODE == 0) {
; #pragma unroll
;                     for (int bj = 0; bj < 2; ++bj) { u32x4 w; w.x = pk_bf16(v[bj][0][0], v[bj][0][1]); w.y = pk_bf16(v[bj][0][2], v[bj][0][3]); w.z = pk_bf16(v[bj][1][0], v[bj][1][1]); w.w = pk_bf16(v[bj][1][2], v[bj][1][3]); *(u32x4*)(O + off + 8 * bj) = w; } }
;                 else { u32x4 w;
; #pragma unroll
;                     for (int q = 0; q < 4; ++q) w[q] = pk4_fp8(v[q >> 1][q & 1][0], v[q >> 1][q & 1][1], v[q >> 1][q & 1][2], v[q >> 1][q & 1][3]);
;                     const size_t offo = MODE == 2 ? tiled_off((size_t)(pm * 256 + wr * 64 + fr + ai * 128 + m * 16), pn * 256 + wc * 64 + 16 * fq, ldo) : off;
	v_mov_b32_e32 v100, v189
	v_add_f32_e32 v94, v94, v78
	v_cvt_pk_fp8_f32 v100, v102, v103
	v_med3_f32 v102, v104, s62, v211
	v_med3_f32 v103, v105, s62, v211
	v_med3_f32 v104, v114, s62, v211
	v_med3_f32 v105, v101, s62, v211
	v_mov_b32_e32 v101, v189
	v_mul_f32_e32 v94, 0xbfb8aa3b, v94
	v_add_f32_e32 v90, v90, v74
	v_cvt_pk_fp8_f32 v101, v104, v105
	v_exp_f32_e32 v94, v94
	v_mul_f32_e32 v90, 0xbfb8aa3b, v90
	v_add_f32_e32 v86, v86, v70
	v_exp_f32_e32 v90, v90
	v_mul_f32_e32 v86, 0xbfb8aa3b, v86
	v_add_f32_e32 v82, v82, v62
	v_exp_f32_e32 v86, v86
	v_mul_f32_e32 v82, 0xbfb8aa3b, v82
	v_cvt_pk_fp8_f32 v100, v102, v103 op_sel:[0,0,1]
	v_med3_f32 v102, v115, s62, v211
	v_med3_f32 v103, v116, s62, v211
	v_exp_f32_e32 v82, v82
	v_cvt_pk_fp8_f32 v101, v102, v103 op_sel:[0,0,1]
	v_add_f32_e32 v94, 1.0, v94
	v_bitop3_b32 v102, v132, s63, v213 bitop3:0xc8
	v_mov_b32_e32 v103, v189
	v_rcp_f32_e32 v94, v94
	v_add_f32_e32 v90, 1.0, v90
	v_lshl_add_u64 v[102:103], v[130:131], 0, v[102:103]
	v_rcp_f32_e32 v90, v90
	v_add_f32_e32 v86, 1.0, v86
	v_lshl_add_u64 v[102:103], v[102:103], 0, v[190:191]
	v_rcp_f32_e32 v86, v86
	v_add_f32_e32 v82, 1.0, v82
	v_add_f32_e32 v83, v83, v63
	flat_store_dwordx4 v[102:103], v[98:101]
	v_rcp_f32_e32 v82, v82
	v_mul_f32_e32 v83, 0xbfb8aa3b, v83
	v_lshlrev_b32_e32 v98, 16, v150
	v_add_f32_e32 v95, v95, v79
	v_mul_f32_e32 v94, v94, v98
	v_lshlrev_b32_e32 v98, 16, v152
	v_exp_f32_e32 v83, v83
	v_mul_f32_e32 v95, 0xbfb8aa3b, v95
	v_add_f32_e32 v96, v96, v80
	v_add_f32_e32 v91, v91, v75
	v_mul_f32_e32 v90, v90, v98
	v_lshlrev_b32_e32 v98, 16, v138
	v_exp_f32_e32 v95, v95
	v_mul_f32_e32 v96, 0xbfb8aa3b, v96
	v_add_f32_e32 v97, v97, v81
	v_mul_f32_e32 v91, 0xbfb8aa3b, v91
	v_add_f32_e32 v92, v92, v76
	v_add_f32_e32 v87, v87, v71
	v_mul_f32_e32 v86, v86, v98
	v_lshlrev_b32_e32 v98, 16, v140
	v_exp_f32_e32 v96, v96
	v_mul_f32_e32 v97, 0xbfb8aa3b, v97
	v_exp_f32_e32 v91, v91
	v_mul_f32_e32 v92, 0xbfb8aa3b, v92
	v_add_f32_e32 v93, v93, v77
	v_mul_f32_e32 v87, 0xbfb8aa3b, v87
	v_add_f32_e32 v88, v88, v72
	v_mul_f32_e32 v82, v82, v98
	v_exp_f32_e32 v97, v97
	v_exp_f32_e32 v92, v92
	v_mul_f32_e32 v93, 0xbfb8aa3b, v93
	v_exp_f32_e32 v87, v87
	v_mul_f32_e32 v88, 0xbfb8aa3b, v88
	v_add_f32_e32 v89, v89, v73
	v_mul_f32_e32 v98, 0x41800000, v82
	v_add_f32_e32 v82, 1.0, v83
	v_add_f32_e32 v83, v84, v64
	v_exp_f32_e32 v93, v93
	v_exp_f32_e32 v88, v88
	v_mul_f32_e32 v89, 0xbfb8aa3b, v89
	v_mul_f32_e32 v83, 0xbfb8aa3b, v83
	v_add_f32_e32 v84, v85, v65
	v_add_f32_e32 v95, 1.0, v95
	v_exp_f32_e32 v89, v89
	v_exp_f32_e32 v83, v83
	v_mul_f32_e32 v84, 0xbfb8aa3b, v84
	v_rcp_f32_e32 v95, v95
	v_add_f32_e32 v96, 1.0, v96
	v_add_f32_e32 v91, 1.0, v91
	v_exp_f32_e32 v84, v84
	v_rcp_f32_e32 v96, v96
	v_add_f32_e32 v97, 1.0, v97
	v_rcp_f32_e32 v91, v91
	v_add_f32_e32 v92, 1.0, v92
	v_add_f32_e32 v87, 1.0, v87
	v_rcp_f32_e32 v97, v97
	v_rcp_f32_e32 v92, v92
	v_add_f32_e32 v93, 1.0, v93
	v_rcp_f32_e32 v87, v87
	v_add_f32_e32 v88, 1.0, v88
	v_and_b32_e32 v99, 0xffff0000, v150
	v_rcp_f32_e32 v93, v93
	v_rcp_f32_e32 v88, v88
	v_add_f32_e32 v89, 1.0, v89
	v_rcp_f32_e32 v82, v82
	v_add_f32_e32 v83, 1.0, v83
	v_lshlrev_b32_e32 v100, 16, v151
	v_mul_f32_e32 v95, v95, v99
	v_and_b32_e32 v99, 0xffff0000, v152
	v_rcp_f32_e32 v89, v89
	v_rcp_f32_e32 v83, v83
	v_add_f32_e32 v84, 1.0, v84
	v_and_b32_e32 v101, 0xffff0000, v151
	v_mul_f32_e32 v96, v96, v100
	v_lshlrev_b32_e32 v100, 16, v153
	v_mul_f32_e32 v91, v91, v99
	v_and_b32_e32 v99, 0xffff0000, v138
	v_rcp_f32_e32 v84, v84
	v_mul_f32_e32 v97, v97, v101
	v_and_b32_e32 v101, 0xffff0000, v153
	v_mul_f32_e32 v92, v92, v100
	v_lshlrev_b32_e32 v100, 16, v139
	v_mul_f32_e32 v87, v87, v99
	v_and_b32_e32 v99, 0xffff0000, v140
	v_mul_f32_e32 v93, v93, v101
	v_and_b32_e32 v101, 0xffff0000, v139
	v_mul_f32_e32 v88, v88, v100
	v_lshlrev_b32_e32 v100, 16, v141
	v_mul_f32_e32 v82, v82, v99
	v_mul_f32_e32 v89, v89, v101
	v_and_b32_e32 v101, 0xffff0000, v141
	v_mul_f32_e32 v85, 0x41800000, v82
	v_mul_f32_e32 v82, v83, v100
	v_mul_f32_e32 v94, 0x41800000, v94
	v_mul_f32_e32 v95, 0x41800000, v95
	v_mul_f32_e32 v99, 0x41800000, v82
	v_mul_f32_e32 v82, v84, v101
	v_mul_f32_e32 v90, 0x41800000, v90
	v_mul_f32_e32 v91, 0x41800000, v91
	v_mul_f32_e32 v100, 0x41800000, v82
	v_med3_f32 v83, v94, s62, v211
	v_med3_f32 v84, v95, s62, v211
	v_mov_b32_e32 v82, v189
	v_cvt_pk_fp8_f32 v82, v83, v84
	v_med3_f32 v90, v90, s62, v211
	v_med3_f32 v91, v91, s62, v211
	v_mov_b32_e32 v83, v189
	v_cvt_pk_fp8_f32 v83, v90, v91
	v_mul_f32_e32 v96, 0x41800000, v96
	v_mul_f32_e32 v97, 0x41800000, v97
	v_mul_f32_e32 v92, 0x41800000, v92
	v_mul_f32_e32 v93, 0x41800000, v93
	v_med3_f32 v84, v96, s62, v211
	v_med3_f32 v94, v97, s62, v211
	v_mul_f32_e32 v86, 0x41800000, v86
	v_mul_f32_e32 v87, 0x41800000, v87
	v_cvt_pk_fp8_f32 v82, v84, v94 op_sel:[0,0,1]
	v_med3_f32 v84, v92, s62, v211
	v_med3_f32 v90, v93, s62, v211
	v_mul_f32_e32 v88, 0x41800000, v88
	v_mul_f32_e32 v89, 0x41800000, v89
	v_cvt_pk_fp8_f32 v83, v84, v90 op_sel:[0,0,1]
	v_med3_f32 v86, v86, s62, v211
	v_med3_f32 v87, v87, s62, v211
	v_mov_b32_e32 v84, v189
	v_cvt_pk_fp8_f32 v84, v86, v87
	v_med3_f32 v86, v88, s62, v211
	v_med3_f32 v87, v89, s62, v211
	v_med3_f32 v88, v98, s62, v211
	v_med3_f32 v89, v85, s62, v211
	v_mov_b32_e32 v85, v189
	v_cvt_pk_fp8_f32 v85, v88, v89
	v_cvt_pk_fp8_f32 v84, v86, v87 op_sel:[0,0,1]
	v_med3_f32 v86, v99, s62, v211
	v_med3_f32 v87, v100, s62, v211
	v_cvt_pk_fp8_f32 v85, v86, v87 op_sel:[0,0,1]
	v_bitop3_b32 v86, v132, s63, v214 bitop3:0xc8
	v_mov_b32_e32 v87, v189
	v_lshl_add_u64 v[86:87], v[130:131], 0, v[86:87]
	v_lshl_add_u64 v[86:87], v[86:87], 0, v[190:191]
;     __device__ __forceinline__ void operator()(AccRef acc, const GUnit& u, int wr, int wc, int fr, int fq) const {
;     ...
;         for (int ai = 0; ai < 2; ++ai) {
;             u32x4 gq[4], yq[4][2], oq[4][2];
; #pragma unroll
;             for (int m = 0; m < 4; ++m) { const size_t off = off0 + (size_t)(ai * 128 + m * 16) * ld;
;                 if (MODE == 2) { yq[m][0] = *(const u32x4*)((const bf16*)G0 + off); yq[m][1] = *(const u32x4*)((const bf16*)G0 + off + 8); }
;                 else gq[m] = __builtin_nontemporal_load((const u32x4*)((const unsigned char*)G0 + off));
;                 if (MODE == 1) { oq[m][0] = *(const u32x4*)(O + off); oq[m][1] = *(const u32x4*)(O + off + 8); } }
; #pragma unroll
;             for (int m = 0; m < 4; ++m) { const size_t off = off0 + (size_t)(ai * 128 + m * 16) * ld;
;                 f32x4 v[2][2];
; #pragma unroll
;                 for (int bj = 0; bj < 2; ++bj)
; #pragma unroll
;                     for (int n = 0; n < 2; ++n) { const int q = bj * 2 + n; const f32x4 a = acc[ai][bj][m][n];
;                         if (MODE == 2) { const unsigned lo = yq[m][bj][2 * n], hi = yq[m][bj][2 * n + 1]; const f32x4 y = (f32x4){bf_lo(lo), bf_hi(lo), bf_lo(hi), bf_hi(hi)};
; #pragma unroll
;                             for (int j = 0; j < 4; ++j) v[bj][n][j] = y[j] * fsigmoid(a[j] + bv[bj][n][j]) * S8_SCALE; }
;                         else { const f32x4 g = u8x4_f32(gq[m][q]);
;                             if (MODE == 0) v[bj][n] = a * g * ASC;
;                             else { const unsigned lo = oq[m][bj][2 * n], hi = oq[m][bj][2 * n + 1]; v[bj][n] = (f32x4){bf_lo(lo), bf_hi(lo), bf_lo(hi), bf_hi(hi)} + a * g * ASC; } } }
;                 if (MODE == 0) {
; #pragma unroll
;                     for (int bj = 0; bj < 2; ++bj) { u32x4 w; w.x = pk_bf16(v[bj][0][0], v[bj][0][1]); w.y = pk_bf16(v[bj][0][2], v[bj][0][3]); w.z = pk_bf16(v[bj][1][0], v[bj][1][1]); w.w = pk_bf16(v[bj][1][2], v[bj][1][3]); *(u32x4*)(O + off + 8 * bj) = w; } }
;                 else { u32x4 w;
; #pragma unroll
;                     for (int q = 0; q < 4; ++q) w[q] = pk4_fp8(v[q >> 1][q & 1][0], v[q >> 1][q & 1][1], v[q >> 1][q & 1][2], v[q >> 1][q & 1][3]);
;                     const size_t offo = MODE == 2 ? tiled_off((size_t)(pm * 256 + wr * 64 + fr + ai * 128 + m * 16), pn * 256 + wc * 64 + 16 * fq, ldo) : off;
	flat_store_dwordx4 v[86:87], v[82:85]
	v_add_f32_e32 v67, v67, v79
	v_mul_f32_e32 v67, 0xbfb8aa3b, v67
	v_add_co_u32_e32 v82, vcc, s48, v204
	v_add_f32_e32 v58, v58, v74
	s_nop 0
	v_addc_co_u32_e32 v83, vcc, 0, v205, vcc
	flat_load_dwordx4 v[106:109], v[82:83]
	flat_load_dwordx4 v[110:113], v[82:83] offset:16
	v_add_co_u32_e32 v82, vcc, s64, v204
	v_exp_f32_e32 v67, v67
	s_nop 0
	v_addc_co_u32_e32 v83, vcc, 0, v205, vcc
	flat_load_dwordx4 v[102:105], v[82:83]
	flat_load_dwordx4 v[98:101], v[82:83] offset:16
	v_mul_f32_e32 v58, 0xbfb8aa3b, v58
	v_add_f32_e32 v54, v54, v70
	v_add_co_u32_e32 v82, vcc, s65, v204
	v_exp_f32_e32 v58, v58
	v_mul_f32_e32 v54, 0xbfb8aa3b, v54
	v_add_f32_e32 v50, v50, v62
	v_addc_co_u32_e32 v83, vcc, 0, v205, vcc
	v_exp_f32_e32 v54, v54
	v_mul_f32_e32 v50, 0xbfb8aa3b, v50
	flat_load_dwordx4 v[94:97], v[82:83]
	flat_load_dwordx4 v[90:93], v[82:83] offset:16
	v_exp_f32_e32 v50, v50
	v_add_f32_e32 v67, 1.0, v67
	v_rcp_f32_e32 v67, v67
	v_add_f32_e32 v58, 1.0, v58
	v_rcp_f32_e32 v58, v58
	v_add_f32_e32 v54, 1.0, v54
	v_rcp_f32_e32 v54, v54
	v_add_f32_e32 v50, 1.0, v50
	v_add_f32_e32 v51, v51, v63
	v_rcp_f32_e32 v50, v50
	v_mul_f32_e32 v51, 0xbfb8aa3b, v51
	v_add_f32_e32 v69, v69, v81
	v_exp_f32_e32 v51, v51
	v_mul_f32_e32 v69, 0xbfb8aa3b, v69
	v_add_f32_e32 v59, v59, v75
	v_exp_f32_e32 v69, v69
	v_mul_f32_e32 v59, 0xbfb8aa3b, v59
	v_add_f32_e32 v60, v60, v76
	v_add_f32_e32 v55, v55, v71
	v_exp_f32_e32 v59, v59
	v_mul_f32_e32 v60, 0xbfb8aa3b, v60
	v_add_f32_e32 v61, v61, v77
	v_mul_f32_e32 v55, 0xbfb8aa3b, v55
	v_add_f32_e32 v56, v56, v72
	v_add_f32_e32 v66, v66, v78
	v_exp_f32_e32 v60, v60
	v_mul_f32_e32 v61, 0xbfb8aa3b, v61
	v_exp_f32_e32 v55, v55
	v_mul_f32_e32 v56, 0xbfb8aa3b, v56
	v_add_f32_e32 v57, v57, v73
	v_mul_f32_e32 v66, 0xbfb8aa3b, v66
	v_exp_f32_e32 v61, v61
	v_exp_f32_e32 v56, v56
	v_mul_f32_e32 v57, 0xbfb8aa3b, v57
	v_exp_f32_e32 v66, v66
	v_add_f32_e32 v69, 1.0, v69
	v_exp_f32_e32 v57, v57
	v_rcp_f32_e32 v69, v69
	v_add_f32_e32 v59, 1.0, v59
	v_add_f32_e32 v68, v68, v80
	v_rcp_f32_e32 v59, v59
	v_add_f32_e32 v60, 1.0, v60
	v_add_f32_e32 v55, 1.0, v55
	v_mul_f32_e32 v68, 0xbfb8aa3b, v68
	v_rcp_f32_e32 v60, v60
	v_add_f32_e32 v61, 1.0, v61
	v_rcp_f32_e32 v55, v55
	v_add_f32_e32 v56, 1.0, v56
	v_add_f32_e32 v66, 1.0, v66
	v_exp_f32_e32 v68, v68
	v_rcp_f32_e32 v61, v61
	v_rcp_f32_e32 v56, v56
	v_add_f32_e32 v57, 1.0, v57
	v_rcp_f32_e32 v66, v66
	v_rcp_f32_e32 v57, v57
	v_add_f32_e32 v68, 1.0, v68
	v_rcp_f32_e32 v68, v68
	v_add_f32_e32 v46, v46, v78
	v_add_u32_e32 v114, 0x80, v202
	v_mul_f32_e32 v46, 0xbfb8aa3b, v46
	s_waitcnt vmcnt(0) lgkmcnt(0)
	v_lshlrev_b32_e32 v115, 16, v106
	v_and_b32_e32 v106, 0xffff0000, v106
	v_mul_f32_e32 v67, v67, v106
	v_lshlrev_b32_e32 v106, 16, v108
	v_mul_f32_e32 v58, v58, v106
	v_lshlrev_b32_e32 v106, 16, v110
	v_mul_f32_e32 v54, v54, v106
	v_lshlrev_b32_e32 v106, 16, v112
	v_mul_f32_e32 v50, v50, v106
	v_mul_f32_e32 v106, 0x41800000, v50
	v_add_f32_e32 v50, 1.0, v51
	v_add_f32_e32 v51, v52, v64
	v_mul_f32_e32 v51, 0xbfb8aa3b, v51
	v_add_f32_e32 v52, v53, v65
	v_exp_f32_e32 v51, v51
	v_mul_f32_e32 v52, 0xbfb8aa3b, v52
	v_exp_f32_e32 v52, v52
	v_lshlrev_b32_e32 v116, 16, v107
	v_and_b32_e32 v107, 0xffff0000, v107
	v_rcp_f32_e32 v50, v50
	v_add_f32_e32 v51, 1.0, v51
	v_mul_f32_e32 v69, v69, v107
	v_and_b32_e32 v107, 0xffff0000, v108
	v_rcp_f32_e32 v51, v51
	v_add_f32_e32 v52, 1.0, v52
	v_lshlrev_b32_e32 v108, 16, v109
	v_mul_f32_e32 v59, v59, v107
	v_and_b32_e32 v107, 0xffff0000, v110
	v_rcp_f32_e32 v52, v52
	v_and_b32_e32 v109, 0xffff0000, v109
	v_mul_f32_e32 v60, v60, v108
	v_lshlrev_b32_e32 v108, 16, v111
	v_mul_f32_e32 v55, v55, v107
	v_and_b32_e32 v107, 0xffff0000, v112
	v_mul_f32_e32 v61, v61, v109
	v_and_b32_e32 v109, 0xffff0000, v111
	v_mul_f32_e32 v56, v56, v108
	v_lshlrev_b32_e32 v108, 16, v113
	v_mul_f32_e32 v50, v50, v107
	v_mul_f32_e32 v66, v66, v115
	v_mul_f32_e32 v57, v57, v109
	v_and_b32_e32 v109, 0xffff0000, v113
	v_mul_f32_e32 v53, 0x41800000, v50
	v_mul_f32_e32 v50, v51, v108
	v_mul_f32_e32 v66, 0x41800000, v66
	v_mul_f32_e32 v67, 0x41800000, v67
	v_mul_f32_e32 v107, 0x41800000, v50
	v_mul_f32_e32 v50, v52, v109
	v_mul_f32_e32 v58, 0x41800000, v58
	v_mul_f32_e32 v59, 0x41800000, v59
	v_mul_f32_e32 v108, 0x41800000, v50
	v_med3_f32 v51, v66, s62, v211
	v_med3_f32 v52, v67, s62, v211
	v_mov_b32_e32 v50, v189
	v_cvt_pk_fp8_f32 v50, v51, v52
	v_med3_f32 v58, v58, s62, v211
	v_med3_f32 v59, v59, s62, v211
	v_mov_b32_e32 v51, v189
	v_mul_f32_e32 v68, v68, v116
	v_cvt_pk_fp8_f32 v51, v58, v59
	v_mul_f32_e32 v68, 0x41800000, v68
	v_mul_f32_e32 v69, 0x41800000, v69
	v_mul_f32_e32 v60, 0x41800000, v60
	v_mul_f32_e32 v61, 0x41800000, v61
	v_med3_f32 v52, v68, s62, v211
	v_med3_f32 v66, v69, s62, v211
	v_mul_f32_e32 v54, 0x41800000, v54
	v_mul_f32_e32 v55, 0x41800000, v55
	v_cvt_pk_fp8_f32 v50, v52, v66 op_sel:[0,0,1]
	v_med3_f32 v52, v60, s62, v211
	v_med3_f32 v58, v61, s62, v211
	v_mul_f32_e32 v56, 0x41800000, v56
	v_mul_f32_e32 v57, 0x41800000, v57
	v_cvt_pk_fp8_f32 v51, v52, v58 op_sel:[0,0,1]
	v_med3_f32 v54, v54, s62, v211
	v_med3_f32 v55, v55, s62, v211
	v_mov_b32_e32 v52, v189
	v_cvt_pk_fp8_f32 v52, v54, v55
	v_med3_f32 v54, v56, s62, v211
	v_med3_f32 v55, v57, s62, v211
	v_med3_f32 v56, v106, s62, v211
	v_med3_f32 v57, v53, s62, v211
	v_mov_b32_e32 v53, v189
	v_cvt_pk_fp8_f32 v53, v56, v57
	v_add_f32_e32 v42, v42, v74
	v_cvt_pk_fp8_f32 v52, v54, v55 op_sel:[0,0,1]
	v_med3_f32 v54, v107, s62, v211
	v_med3_f32 v55, v108, s62, v211
	v_ashrrev_i32_e32 v56, 31, v114
	v_exp_f32_e32 v46, v46
	v_mul_f32_e32 v42, 0xbfb8aa3b, v42
	v_add_f32_e32 v38, v38, v70
;     __device__ __forceinline__ void operator()(AccRef acc, const GUnit& u, int wr, int wc, int fr, int fq) const {
;     ...
;         for (int ai = 0; ai < 2; ++ai) {
;             u32x4 gq[4], yq[4][2], oq[4][2];
; #pragma unroll
;             for (int m = 0; m < 4; ++m) { const size_t off = off0 + (size_t)(ai * 128 + m * 16) * ld;
;                 if (MODE == 2) { yq[m][0] = *(const u32x4*)((const bf16*)G0 + off); yq[m][1] = *(const u32x4*)((const bf16*)G0 + off + 8); }
;                 else gq[m] = __builtin_nontemporal_load((const u32x4*)((const unsigned char*)G0 + off));
;                 if (MODE == 1) { oq[m][0] = *(const u32x4*)(O + off); oq[m][1] = *(const u32x4*)(O + off + 8); } }
; #pragma unroll
;             for (int m = 0; m < 4; ++m) { const size_t off = off0 + (size_t)(ai * 128 + m * 16) * ld;
;                 f32x4 v[2][2];
; #pragma unroll
;                 for (int bj = 0; bj < 2; ++bj)
; #pragma unroll
;                     for (int n = 0; n < 2; ++n) { const int q = bj * 2 + n; const f32x4 a = acc[ai][bj][m][n];
;                         if (MODE == 2) { const unsigned lo = yq[m][bj][2 * n], hi = yq[m][bj][2 * n + 1]; const f32x4 y = (f32x4){bf_lo(lo), bf_hi(lo), bf_lo(hi), bf_hi(hi)};
; #pragma unroll
;                             for (int j = 0; j < 4; ++j) v[bj][n][j] = y[j] * fsigmoid(a[j] + bv[bj][n][j]) * S8_SCALE; }
;                         else { const f32x4 g = u8x4_f32(gq[m][q]);
;                             if (MODE == 0) v[bj][n] = a * g * ASC;
;                             else { const unsigned lo = oq[m][bj][2 * n], hi = oq[m][bj][2 * n + 1]; v[bj][n] = (f32x4){bf_lo(lo), bf_hi(lo), bf_lo(hi), bf_hi(hi)} + a * g * ASC; } } }
;                 if (MODE == 0) {
; #pragma unroll
;                     for (int bj = 0; bj < 2; ++bj) { u32x4 w; w.x = pk_bf16(v[bj][0][0], v[bj][0][1]); w.y = pk_bf16(v[bj][0][2], v[bj][0][3]); w.z = pk_bf16(v[bj][1][0], v[bj][1][1]); w.w = pk_bf16(v[bj][1][2], v[bj][1][3]); *(u32x4*)(O + off + 8 * bj) = w; } }
;                 else { u32x4 w;
; #pragma unroll
;                     for (int q = 0; q < 4; ++q) w[q] = pk4_fp8(v[q >> 1][q & 1][0], v[q >> 1][q & 1][1], v[q >> 1][q & 1][2], v[q >> 1][q & 1][3]);
;                     const size_t offo = MODE == 2 ? tiled_off((size_t)(pm * 256 + wr * 64 + fr + ai * 128 + m * 16), pn * 256 + wc * 64 + 16 * fq, ldo) : off;
	v_add_co_u32_e32 v82, vcc, s66, v204
	v_cvt_pk_fp8_f32 v53, v54, v55 op_sel:[0,0,1]
	v_alignbit_b32 v54, v56, v114, 8
	v_exp_f32_e32 v42, v42
	v_mul_f32_e32 v38, 0xbfb8aa3b, v38
	v_add_f32_e32 v34, v34, v62
	v_addc_co_u32_e32 v83, vcc, 0, v205, vcc
	v_mad_u64_u32 v[54:55], s[28:29], v54, 12, s[26:27]
	v_exp_f32_e32 v38, v38
	v_mul_f32_e32 v34, 0xbfb8aa3b, v34
	flat_load_dwordx4 v[86:89], v[82:83]
	s_nop 0
	flat_load_dwordx4 v[82:85], v[82:83] offset:16
	v_mad_u32_u24 v55, v56, 12, v55
	v_exp_f32_e32 v34, v34
	v_lshlrev_b64 v[54:55], 15, v[54:55]
	v_lshlrev_b32_e32 v56, 7, v114
	v_add_f32_e32 v46, 1.0, v46
	v_and_b32_e32 v56, 0x7f80, v56
	v_mov_b32_e32 v57, v189
	v_lshl_add_u64 v[54:55], s[12:13], 0, v[54:55]
	v_rcp_f32_e32 v46, v46
	v_add_f32_e32 v42, 1.0, v42
	v_lshl_add_u64 v[54:55], v[54:55], 0, v[56:57]
	v_rcp_f32_e32 v42, v42
	v_add_f32_e32 v38, 1.0, v38
	v_lshl_add_u64 v[54:55], v[54:55], 0, v[190:191]
	v_rcp_f32_e32 v38, v38
	v_add_f32_e32 v34, 1.0, v34
	v_add_f32_e32 v35, v35, v63
	flat_store_dwordx4 v[54:55], v[50:53]
	v_rcp_f32_e32 v34, v34
	v_mul_f32_e32 v35, 0xbfb8aa3b, v35
	v_lshlrev_b32_e32 v50, 16, v102
	v_add_f32_e32 v47, v47, v79
	v_mul_f32_e32 v46, v46, v50
	v_lshlrev_b32_e32 v50, 16, v104
	v_exp_f32_e32 v35, v35
	v_mul_f32_e32 v47, 0xbfb8aa3b, v47
	v_add_f32_e32 v48, v48, v80
	v_add_f32_e32 v43, v43, v75
	v_mul_f32_e32 v42, v42, v50
	v_lshlrev_b32_e32 v50, 16, v98
	v_exp_f32_e32 v47, v47
	v_mul_f32_e32 v48, 0xbfb8aa3b, v48
	v_add_f32_e32 v49, v49, v81
	v_mul_f32_e32 v43, 0xbfb8aa3b, v43
	v_add_f32_e32 v44, v44, v76
	v_add_f32_e32 v39, v39, v71
	v_mul_f32_e32 v38, v38, v50
	v_lshlrev_b32_e32 v50, 16, v100
	v_exp_f32_e32 v48, v48
	v_mul_f32_e32 v49, 0xbfb8aa3b, v49
	v_exp_f32_e32 v43, v43
	v_mul_f32_e32 v44, 0xbfb8aa3b, v44
	v_add_f32_e32 v45, v45, v77
	v_mul_f32_e32 v39, 0xbfb8aa3b, v39
	v_add_f32_e32 v40, v40, v72
	v_mul_f32_e32 v34, v34, v50
	v_exp_f32_e32 v49, v49
	v_exp_f32_e32 v44, v44
	v_mul_f32_e32 v45, 0xbfb8aa3b, v45
	v_exp_f32_e32 v39, v39
	v_mul_f32_e32 v40, 0xbfb8aa3b, v40
	v_add_f32_e32 v41, v41, v73
	v_mul_f32_e32 v50, 0x41800000, v34
	v_add_f32_e32 v34, 1.0, v35
	v_add_f32_e32 v35, v36, v64
	v_exp_f32_e32 v45, v45
	v_exp_f32_e32 v40, v40
	v_mul_f32_e32 v41, 0xbfb8aa3b, v41
	v_mul_f32_e32 v35, 0xbfb8aa3b, v35
	v_add_f32_e32 v36, v37, v65
	v_add_f32_e32 v47, 1.0, v47
	v_exp_f32_e32 v41, v41
	v_exp_f32_e32 v35, v35
	v_mul_f32_e32 v36, 0xbfb8aa3b, v36
	v_rcp_f32_e32 v47, v47
	v_add_f32_e32 v48, 1.0, v48
	v_add_f32_e32 v43, 1.0, v43
	v_exp_f32_e32 v36, v36
	v_rcp_f32_e32 v48, v48
	v_add_f32_e32 v49, 1.0, v49
	v_rcp_f32_e32 v43, v43
	v_add_f32_e32 v44, 1.0, v44
	v_add_f32_e32 v39, 1.0, v39
	v_rcp_f32_e32 v49, v49
	v_rcp_f32_e32 v44, v44
	v_add_f32_e32 v45, 1.0, v45
	v_rcp_f32_e32 v39, v39
	v_add_f32_e32 v40, 1.0, v40
	v_and_b32_e32 v51, 0xffff0000, v102
	v_rcp_f32_e32 v45, v45
	v_rcp_f32_e32 v40, v40
	v_add_f32_e32 v41, 1.0, v41
	v_rcp_f32_e32 v34, v34
	v_add_f32_e32 v35, 1.0, v35
	v_lshlrev_b32_e32 v52, 16, v103
	v_mul_f32_e32 v47, v47, v51
	v_and_b32_e32 v51, 0xffff0000, v104
	v_rcp_f32_e32 v41, v41
	v_rcp_f32_e32 v35, v35
	v_add_f32_e32 v36, 1.0, v36
	v_and_b32_e32 v53, 0xffff0000, v103
	v_mul_f32_e32 v48, v48, v52
	v_lshlrev_b32_e32 v52, 16, v105
	v_mul_f32_e32 v43, v43, v51
	v_and_b32_e32 v51, 0xffff0000, v98
	v_rcp_f32_e32 v36, v36
	v_mul_f32_e32 v49, v49, v53
	v_and_b32_e32 v53, 0xffff0000, v105
	v_mul_f32_e32 v44, v44, v52
	v_lshlrev_b32_e32 v52, 16, v99
	v_mul_f32_e32 v39, v39, v51
	v_and_b32_e32 v51, 0xffff0000, v100
	v_mul_f32_e32 v45, v45, v53
	v_and_b32_e32 v53, 0xffff0000, v99
	v_mul_f32_e32 v40, v40, v52
	v_lshlrev_b32_e32 v52, 16, v101
	v_mul_f32_e32 v34, v34, v51
	v_mul_f32_e32 v41, v41, v53
	v_and_b32_e32 v53, 0xffff0000, v101
	v_mul_f32_e32 v37, 0x41800000, v34
	v_mul_f32_e32 v34, v35, v52
	v_mul_f32_e32 v46, 0x41800000, v46
	v_mul_f32_e32 v47, 0x41800000, v47
	v_mul_f32_e32 v51, 0x41800000, v34
	v_mul_f32_e32 v34, v36, v53
	v_mul_f32_e32 v42, 0x41800000, v42
	v_mul_f32_e32 v43, 0x41800000, v43
	v_mul_f32_e32 v52, 0x41800000, v34
	v_med3_f32 v35, v46, s62, v211
	v_med3_f32 v36, v47, s62, v211
	v_mov_b32_e32 v34, v189
	v_cvt_pk_fp8_f32 v34, v35, v36
	v_med3_f32 v42, v42, s62, v211
	v_med3_f32 v43, v43, s62, v211
	v_mov_b32_e32 v35, v189
	v_cvt_pk_fp8_f32 v35, v42, v43
	v_mul_f32_e32 v48, 0x41800000, v48
	v_mul_f32_e32 v49, 0x41800000, v49
	v_mul_f32_e32 v44, 0x41800000, v44
	v_mul_f32_e32 v45, 0x41800000, v45
	v_med3_f32 v36, v48, s62, v211
	v_med3_f32 v46, v49, s62, v211
	v_mul_f32_e32 v38, 0x41800000, v38
	v_mul_f32_e32 v39, 0x41800000, v39
	v_cvt_pk_fp8_f32 v34, v36, v46 op_sel:[0,0,1]
	v_med3_f32 v36, v44, s62, v211
	v_med3_f32 v42, v45, s62, v211
	v_mul_f32_e32 v40, 0x41800000, v40
	v_mul_f32_e32 v41, 0x41800000, v41
	v_cvt_pk_fp8_f32 v35, v36, v42 op_sel:[0,0,1]
	v_med3_f32 v38, v38, s62, v211
	v_med3_f32 v39, v39, s62, v211
	v_mov_b32_e32 v36, v189
	v_cvt_pk_fp8_f32 v36, v38, v39
	v_med3_f32 v38, v40, s62, v211
	v_med3_f32 v39, v41, s62, v211
	v_med3_f32 v40, v50, s62, v211
	v_med3_f32 v41, v37, s62, v211
	v_mov_b32_e32 v37, v189
	v_cvt_pk_fp8_f32 v37, v40, v41
	v_add_f32_e32 v30, v30, v78
	v_add_u32_e32 v40, 0x90, v202
	v_mul_f32_e32 v30, 0xbfb8aa3b, v30
	v_add_f32_e32 v26, v26, v74
	v_cvt_pk_fp8_f32 v36, v38, v39 op_sel:[0,0,1]
	v_med3_f32 v38, v51, s62, v211
	v_med3_f32 v39, v52, s62, v211
	v_ashrrev_i32_e32 v41, 31, v40
	v_exp_f32_e32 v30, v30
	v_mul_f32_e32 v26, 0xbfb8aa3b, v26
	v_add_f32_e32 v22, v22, v70
	v_cvt_pk_fp8_f32 v37, v38, v39 op_sel:[0,0,1]
	v_alignbit_b32 v38, v41, v40, 8
	v_exp_f32_e32 v26, v26
	v_mul_f32_e32 v22, 0xbfb8aa3b, v22
	v_add_f32_e32 v18, v18, v62
;     __device__ __forceinline__ void operator()(AccRef acc, const GUnit& u, int wr, int wc, int fr, int fq) const {
;     ...
;         for (int ai = 0; ai < 2; ++ai) {
;             u32x4 gq[4], yq[4][2], oq[4][2];
; #pragma unroll
;             for (int m = 0; m < 4; ++m) { const size_t off = off0 + (size_t)(ai * 128 + m * 16) * ld;
;                 if (MODE == 2) { yq[m][0] = *(const u32x4*)((const bf16*)G0 + off); yq[m][1] = *(const u32x4*)((const bf16*)G0 + off + 8); }
;                 else gq[m] = __builtin_nontemporal_load((const u32x4*)((const unsigned char*)G0 + off));
;                 if (MODE == 1) { oq[m][0] = *(const u32x4*)(O + off); oq[m][1] = *(const u32x4*)(O + off + 8); } }
; #pragma unroll
;             for (int m = 0; m < 4; ++m) { const size_t off = off0 + (size_t)(ai * 128 + m * 16) * ld;
;                 f32x4 v[2][2];
; #pragma unroll
;                 for (int bj = 0; bj < 2; ++bj)
; #pragma unroll
;                     for (int n = 0; n < 2; ++n) { const int q = bj * 2 + n; const f32x4 a = acc[ai][bj][m][n];
;                         if (MODE == 2) { const unsigned lo = yq[m][bj][2 * n], hi = yq[m][bj][2 * n + 1]; const f32x4 y = (f32x4){bf_lo(lo), bf_hi(lo), bf_lo(hi), bf_hi(hi)};
; #pragma unroll
;                             for (int j = 0; j < 4; ++j) v[bj][n][j] = y[j] * fsigmoid(a[j] + bv[bj][n][j]) * S8_SCALE; }
;                         else { const f32x4 g = u8x4_f32(gq[m][q]);
;                             if (MODE == 0) v[bj][n] = a * g * ASC;
;                             else { const unsigned lo = oq[m][bj][2 * n], hi = oq[m][bj][2 * n + 1]; v[bj][n] = (f32x4){bf_lo(lo), bf_hi(lo), bf_lo(hi), bf_hi(hi)} + a * g * ASC; } } }
;                 if (MODE == 0) {
; #pragma unroll
;                     for (int bj = 0; bj < 2; ++bj) { u32x4 w; w.x = pk_bf16(v[bj][0][0], v[bj][0][1]); w.y = pk_bf16(v[bj][0][2], v[bj][0][3]); w.z = pk_bf16(v[bj][1][0], v[bj][1][1]); w.w = pk_bf16(v[bj][1][2], v[bj][1][3]); *(u32x4*)(O + off + 8 * bj) = w; } }
;                 else { u32x4 w;
; #pragma unroll
;                     for (int q = 0; q < 4; ++q) w[q] = pk4_fp8(v[q >> 1][q & 1][0], v[q >> 1][q & 1][1], v[q >> 1][q & 1][2], v[q >> 1][q & 1][3]);
;                     const size_t offo = MODE == 2 ? tiled_off((size_t)(pm * 256 + wr * 64 + fr + ai * 128 + m * 16), pn * 256 + wc * 64 + 16 * fq, ldo) : off;
	v_mad_u64_u32 v[38:39], s[28:29], v38, 12, s[26:27]
	v_exp_f32_e32 v22, v22
	v_mul_f32_e32 v18, 0xbfb8aa3b, v18
	v_mad_u32_u24 v39, v41, 12, v39
	v_exp_f32_e32 v18, v18
	v_lshlrev_b64 v[38:39], 15, v[38:39]
	v_lshlrev_b32_e32 v40, 7, v40
	v_add_f32_e32 v30, 1.0, v30
	v_and_b32_e32 v40, 0x7f80, v40
	v_mov_b32_e32 v41, v189
	v_lshl_add_u64 v[38:39], s[12:13], 0, v[38:39]
	v_rcp_f32_e32 v30, v30
	v_add_f32_e32 v26, 1.0, v26
	v_lshl_add_u64 v[38:39], v[38:39], 0, v[40:41]
	v_rcp_f32_e32 v26, v26
	v_add_f32_e32 v22, 1.0, v22
	v_lshl_add_u64 v[38:39], v[38:39], 0, v[190:191]
	v_rcp_f32_e32 v22, v22
	v_add_f32_e32 v18, 1.0, v18
	v_add_f32_e32 v19, v19, v63
	flat_store_dwordx4 v[38:39], v[34:37]
	v_rcp_f32_e32 v18, v18
	v_mul_f32_e32 v19, 0xbfb8aa3b, v19
	v_lshlrev_b32_e32 v34, 16, v94
	v_add_f32_e32 v31, v31, v79
	v_mul_f32_e32 v30, v30, v34
	v_lshlrev_b32_e32 v34, 16, v96
	v_exp_f32_e32 v19, v19
	v_mul_f32_e32 v31, 0xbfb8aa3b, v31
	v_add_f32_e32 v32, v32, v80
	v_add_f32_e32 v27, v27, v75
	v_mul_f32_e32 v26, v26, v34
	v_lshlrev_b32_e32 v34, 16, v90
	v_exp_f32_e32 v31, v31
	v_mul_f32_e32 v32, 0xbfb8aa3b, v32
	v_add_f32_e32 v33, v33, v81
	v_mul_f32_e32 v27, 0xbfb8aa3b, v27
	v_add_f32_e32 v28, v28, v76
	v_add_f32_e32 v23, v23, v71
	v_mul_f32_e32 v22, v22, v34
	v_lshlrev_b32_e32 v34, 16, v92
	v_exp_f32_e32 v32, v32
	v_mul_f32_e32 v33, 0xbfb8aa3b, v33
	v_exp_f32_e32 v27, v27
	v_mul_f32_e32 v28, 0xbfb8aa3b, v28
	v_add_f32_e32 v29, v29, v77
	v_mul_f32_e32 v23, 0xbfb8aa3b, v23
	v_add_f32_e32 v24, v24, v72
	v_mul_f32_e32 v18, v18, v34
	v_exp_f32_e32 v33, v33
	v_exp_f32_e32 v28, v28
	v_mul_f32_e32 v29, 0xbfb8aa3b, v29
	v_exp_f32_e32 v23, v23
	v_mul_f32_e32 v24, 0xbfb8aa3b, v24
	v_add_f32_e32 v25, v25, v73
	v_mul_f32_e32 v34, 0x41800000, v18
	v_add_f32_e32 v18, 1.0, v19
	v_add_f32_e32 v19, v20, v64
	v_exp_f32_e32 v29, v29
	v_exp_f32_e32 v24, v24
	v_mul_f32_e32 v25, 0xbfb8aa3b, v25
	v_mul_f32_e32 v19, 0xbfb8aa3b, v19
	v_add_f32_e32 v20, v21, v65
	v_add_f32_e32 v31, 1.0, v31
	v_exp_f32_e32 v25, v25
	v_exp_f32_e32 v19, v19
	v_mul_f32_e32 v20, 0xbfb8aa3b, v20
	v_rcp_f32_e32 v31, v31
	v_add_f32_e32 v32, 1.0, v32
	v_add_f32_e32 v27, 1.0, v27
	v_exp_f32_e32 v20, v20
	v_rcp_f32_e32 v32, v32
	v_add_f32_e32 v33, 1.0, v33
	v_rcp_f32_e32 v27, v27
	v_add_f32_e32 v28, 1.0, v28
	v_add_f32_e32 v23, 1.0, v23
	v_rcp_f32_e32 v33, v33
	v_rcp_f32_e32 v28, v28
	v_add_f32_e32 v29, 1.0, v29
	v_rcp_f32_e32 v23, v23
	v_add_f32_e32 v24, 1.0, v24
	v_and_b32_e32 v35, 0xffff0000, v94
	v_rcp_f32_e32 v29, v29
	v_rcp_f32_e32 v24, v24
	v_add_f32_e32 v25, 1.0, v25
	v_rcp_f32_e32 v18, v18
	v_add_f32_e32 v19, 1.0, v19
	v_lshlrev_b32_e32 v36, 16, v95
	v_mul_f32_e32 v31, v31, v35
	v_and_b32_e32 v35, 0xffff0000, v96
	v_rcp_f32_e32 v25, v25
	v_rcp_f32_e32 v19, v19
	v_add_f32_e32 v20, 1.0, v20
	v_and_b32_e32 v37, 0xffff0000, v95
	v_mul_f32_e32 v32, v32, v36
	v_lshlrev_b32_e32 v36, 16, v97
	v_mul_f32_e32 v27, v27, v35
	v_and_b32_e32 v35, 0xffff0000, v90
	v_rcp_f32_e32 v20, v20
	v_mul_f32_e32 v33, v33, v37
	v_and_b32_e32 v37, 0xffff0000, v97
	v_mul_f32_e32 v28, v28, v36
	v_lshlrev_b32_e32 v36, 16, v91
	v_mul_f32_e32 v23, v23, v35
	v_and_b32_e32 v35, 0xffff0000, v92
	v_mul_f32_e32 v29, v29, v37
	v_and_b32_e32 v37, 0xffff0000, v91
	v_mul_f32_e32 v24, v24, v36
	v_lshlrev_b32_e32 v36, 16, v93
	v_mul_f32_e32 v18, v18, v35
	v_mul_f32_e32 v25, v25, v37
	v_and_b32_e32 v37, 0xffff0000, v93
	v_mul_f32_e32 v21, 0x41800000, v18
	v_mul_f32_e32 v18, v19, v36
	v_mul_f32_e32 v30, 0x41800000, v30
	v_mul_f32_e32 v31, 0x41800000, v31
	v_mul_f32_e32 v35, 0x41800000, v18
	v_mul_f32_e32 v18, v20, v37
	v_mul_f32_e32 v26, 0x41800000, v26
	v_mul_f32_e32 v27, 0x41800000, v27
	v_mul_f32_e32 v36, 0x41800000, v18
	v_med3_f32 v19, v30, s62, v211
	v_med3_f32 v20, v31, s62, v211
	v_mov_b32_e32 v18, v189
	v_cvt_pk_fp8_f32 v18, v19, v20
	v_med3_f32 v26, v26, s62, v211
	v_med3_f32 v27, v27, s62, v211
	v_mov_b32_e32 v19, v189
	v_cvt_pk_fp8_f32 v19, v26, v27
	v_mul_f32_e32 v32, 0x41800000, v32
	v_mul_f32_e32 v33, 0x41800000, v33
	v_mul_f32_e32 v28, 0x41800000, v28
	v_mul_f32_e32 v29, 0x41800000, v29
	v_med3_f32 v20, v32, s62, v211
	v_med3_f32 v30, v33, s62, v211
	v_mul_f32_e32 v22, 0x41800000, v22
	v_mul_f32_e32 v23, 0x41800000, v23
	v_cvt_pk_fp8_f32 v18, v20, v30 op_sel:[0,0,1]
	v_med3_f32 v20, v28, s62, v211
	v_med3_f32 v26, v29, s62, v211
	v_mul_f32_e32 v24, 0x41800000, v24
	v_mul_f32_e32 v25, 0x41800000, v25
	v_cvt_pk_fp8_f32 v19, v20, v26 op_sel:[0,0,1]
	v_med3_f32 v22, v22, s62, v211
	v_med3_f32 v23, v23, s62, v211
	v_mov_b32_e32 v20, v189
	v_cvt_pk_fp8_f32 v20, v22, v23
	v_med3_f32 v22, v24, s62, v211
	v_med3_f32 v23, v25, s62, v211
	v_med3_f32 v24, v34, s62, v211
	v_med3_f32 v25, v21, s62, v211
	v_mov_b32_e32 v21, v189
	v_cvt_pk_fp8_f32 v21, v24, v25
	v_add_f32_e32 v14, v14, v78
	v_add_u32_e32 v24, 0xa0, v202
	v_mul_f32_e32 v14, 0xbfb8aa3b, v14
	v_add_f32_e32 v10, v10, v74
	v_cvt_pk_fp8_f32 v20, v22, v23 op_sel:[0,0,1]
	v_med3_f32 v22, v35, s62, v211
	v_med3_f32 v23, v36, s62, v211
	v_ashrrev_i32_e32 v25, 31, v24
	v_exp_f32_e32 v14, v14
	v_mul_f32_e32 v10, 0xbfb8aa3b, v10
	v_add_f32_e32 v6, v6, v70
	v_cvt_pk_fp8_f32 v21, v22, v23 op_sel:[0,0,1]
	v_alignbit_b32 v22, v25, v24, 8
	v_exp_f32_e32 v10, v10
	v_mul_f32_e32 v6, 0xbfb8aa3b, v6
	v_add_f32_e32 v2, v2, v62
	v_mad_u64_u32 v[22:23], s[28:29], v22, 12, s[26:27]
	v_exp_f32_e32 v6, v6
	v_mul_f32_e32 v2, 0xbfb8aa3b, v2
	v_mad_u32_u24 v23, v25, 12, v23
	v_exp_f32_e32 v2, v2
	v_lshlrev_b64 v[22:23], 15, v[22:23]
	v_lshlrev_b32_e32 v24, 7, v24
	v_add_f32_e32 v14, 1.0, v14
	v_and_b32_e32 v24, 0x7f80, v24
	v_mov_b32_e32 v25, v189
	v_lshl_add_u64 v[22:23], s[12:13], 0, v[22:23]
	v_rcp_f32_e32 v14, v14
	v_add_f32_e32 v10, 1.0, v10
	v_lshl_add_u64 v[22:23], v[22:23], 0, v[24:25]
	v_rcp_f32_e32 v10, v10
	v_add_f32_e32 v6, 1.0, v6
	v_lshl_add_u64 v[22:23], v[22:23], 0, v[190:191]
	v_rcp_f32_e32 v6, v6
	v_add_f32_e32 v2, 1.0, v2
	v_add_f32_e32 v3, v3, v63
	flat_store_dwordx4 v[22:23], v[18:21]
	v_rcp_f32_e32 v2, v2
	v_mul_f32_e32 v3, 0xbfb8aa3b, v3
	s_waitcnt vmcnt(0) lgkmcnt(0)
;     __device__ __forceinline__ void operator()(AccRef acc, const GUnit& u, int wr, int wc, int fr, int fq) const {
;     ...
;         for (int ai = 0; ai < 2; ++ai) {
;             u32x4 gq[4], yq[4][2], oq[4][2];
; #pragma unroll
;             for (int m = 0; m < 4; ++m) { const size_t off = off0 + (size_t)(ai * 128 + m * 16) * ld;
;                 if (MODE == 2) { yq[m][0] = *(const u32x4*)((const bf16*)G0 + off); yq[m][1] = *(const u32x4*)((const bf16*)G0 + off + 8); }
;                 else gq[m] = __builtin_nontemporal_load((const u32x4*)((const unsigned char*)G0 + off));
;                 if (MODE == 1) { oq[m][0] = *(const u32x4*)(O + off); oq[m][1] = *(const u32x4*)(O + off + 8); } }
; #pragma unroll
;             for (int m = 0; m < 4; ++m) { const size_t off = off0 + (size_t)(ai * 128 + m * 16) * ld;
;                 f32x4 v[2][2];
; #pragma unroll
;                 for (int bj = 0; bj < 2; ++bj)
; #pragma unroll
;                     for (int n = 0; n < 2; ++n) { const int q = bj * 2 + n; const f32x4 a = acc[ai][bj][m][n];
;                         if (MODE == 2) { const unsigned lo = yq[m][bj][2 * n], hi = yq[m][bj][2 * n + 1]; const f32x4 y = (f32x4){bf_lo(lo), bf_hi(lo), bf_lo(hi), bf_hi(hi)};
; #pragma unroll
;                             for (int j = 0; j < 4; ++j) v[bj][n][j] = y[j] * fsigmoid(a[j] + bv[bj][n][j]) * S8_SCALE; }
;                         else { const f32x4 g = u8x4_f32(gq[m][q]);
;                             if (MODE == 0) v[bj][n] = a * g * ASC;
;                             else { const unsigned lo = oq[m][bj][2 * n], hi = oq[m][bj][2 * n + 1]; v[bj][n] = (f32x4){bf_lo(lo), bf_hi(lo), bf_lo(hi), bf_hi(hi)} + a * g * ASC; } } }
;                 if (MODE == 0) {
; #pragma unroll
;                     for (int bj = 0; bj < 2; ++bj) { u32x4 w; w.x = pk_bf16(v[bj][0][0], v[bj][0][1]); w.y = pk_bf16(v[bj][0][2], v[bj][0][3]); w.z = pk_bf16(v[bj][1][0], v[bj][1][1]); w.w = pk_bf16(v[bj][1][2], v[bj][1][3]); *(u32x4*)(O + off + 8 * bj) = w; } }
;                 else { u32x4 w;
; #pragma unroll
;                     for (int q = 0; q < 4; ++q) w[q] = pk4_fp8(v[q >> 1][q & 1][0], v[q >> 1][q & 1][1], v[q >> 1][q & 1][2], v[q >> 1][q & 1][3]);
;                     const size_t offo = MODE == 2 ? tiled_off((size_t)(pm * 256 + wr * 64 + fr + ai * 128 + m * 16), pn * 256 + wc * 64 + 16 * fq, ldo) : off;
	v_lshlrev_b32_e32 v18, 16, v86
	v_add_f32_e32 v15, v15, v79
	v_mul_f32_e32 v14, v14, v18
	v_lshlrev_b32_e32 v18, 16, v88
	v_exp_f32_e32 v3, v3
	v_mul_f32_e32 v15, 0xbfb8aa3b, v15
	v_add_f32_e32 v16, v16, v80
	v_add_f32_e32 v11, v11, v75
	v_mul_f32_e32 v10, v10, v18
	v_lshlrev_b32_e32 v18, 16, v82
	v_exp_f32_e32 v15, v15
	v_mul_f32_e32 v16, 0xbfb8aa3b, v16
	v_add_f32_e32 v17, v17, v81
	v_mul_f32_e32 v11, 0xbfb8aa3b, v11
	v_add_f32_e32 v12, v12, v76
	v_add_f32_e32 v7, v7, v71
	v_mul_f32_e32 v6, v6, v18
	v_lshlrev_b32_e32 v18, 16, v84
	v_exp_f32_e32 v16, v16
	v_mul_f32_e32 v17, 0xbfb8aa3b, v17
	v_exp_f32_e32 v11, v11
	v_mul_f32_e32 v12, 0xbfb8aa3b, v12
	v_add_f32_e32 v13, v13, v77
	v_mul_f32_e32 v7, 0xbfb8aa3b, v7
	v_add_f32_e32 v8, v8, v72
	v_mul_f32_e32 v2, v2, v18
	v_exp_f32_e32 v17, v17
	v_exp_f32_e32 v12, v12
	v_mul_f32_e32 v13, 0xbfb8aa3b, v13
	v_exp_f32_e32 v7, v7
	v_mul_f32_e32 v8, 0xbfb8aa3b, v8
	v_add_f32_e32 v9, v9, v73
	v_mul_f32_e32 v18, 0x41800000, v2
	v_add_f32_e32 v2, 1.0, v3
	v_add_f32_e32 v3, v4, v64
	v_exp_f32_e32 v13, v13
	v_exp_f32_e32 v8, v8
	v_mul_f32_e32 v9, 0xbfb8aa3b, v9
	v_mul_f32_e32 v3, 0xbfb8aa3b, v3
	v_add_f32_e32 v4, v5, v65
	v_add_f32_e32 v15, 1.0, v15
	v_exp_f32_e32 v9, v9
	v_exp_f32_e32 v3, v3
	v_mul_f32_e32 v4, 0xbfb8aa3b, v4
	v_rcp_f32_e32 v15, v15
	v_add_f32_e32 v16, 1.0, v16
	v_add_f32_e32 v11, 1.0, v11
	v_exp_f32_e32 v4, v4
	v_rcp_f32_e32 v16, v16
	v_add_f32_e32 v17, 1.0, v17
	v_rcp_f32_e32 v11, v11
	v_add_f32_e32 v12, 1.0, v12
	v_add_f32_e32 v7, 1.0, v7
	v_rcp_f32_e32 v17, v17
	v_rcp_f32_e32 v12, v12
	v_add_f32_e32 v13, 1.0, v13
	v_rcp_f32_e32 v7, v7
	v_add_f32_e32 v8, 1.0, v8
	v_and_b32_e32 v19, 0xffff0000, v86
	v_rcp_f32_e32 v13, v13
	v_rcp_f32_e32 v8, v8
	v_add_f32_e32 v9, 1.0, v9
	v_rcp_f32_e32 v2, v2
	v_add_f32_e32 v3, 1.0, v3
	v_lshlrev_b32_e32 v20, 16, v87
	v_mul_f32_e32 v15, v15, v19
	v_and_b32_e32 v19, 0xffff0000, v88
	v_rcp_f32_e32 v9, v9
	v_rcp_f32_e32 v3, v3
	v_add_f32_e32 v4, 1.0, v4
	v_and_b32_e32 v21, 0xffff0000, v87
	v_mul_f32_e32 v16, v16, v20
	v_lshlrev_b32_e32 v20, 16, v89
	v_mul_f32_e32 v11, v11, v19
	v_and_b32_e32 v19, 0xffff0000, v82
	v_rcp_f32_e32 v4, v4
	v_mul_f32_e32 v17, v17, v21
	v_and_b32_e32 v21, 0xffff0000, v89
	v_mul_f32_e32 v12, v12, v20
	v_lshlrev_b32_e32 v20, 16, v83
	v_mul_f32_e32 v7, v7, v19
	v_and_b32_e32 v19, 0xffff0000, v84
	v_mul_f32_e32 v13, v13, v21
	v_and_b32_e32 v21, 0xffff0000, v83
	v_mul_f32_e32 v8, v8, v20
	v_lshlrev_b32_e32 v20, 16, v85
	v_mul_f32_e32 v2, v2, v19
	v_mul_f32_e32 v9, v9, v21
	v_and_b32_e32 v21, 0xffff0000, v85
	v_mul_f32_e32 v5, 0x41800000, v2
	v_mul_f32_e32 v2, v3, v20
	v_mul_f32_e32 v14, 0x41800000, v14
	v_mul_f32_e32 v15, 0x41800000, v15
	v_mul_f32_e32 v19, 0x41800000, v2
	v_mul_f32_e32 v2, v4, v21
	v_mul_f32_e32 v10, 0x41800000, v10
	v_mul_f32_e32 v11, 0x41800000, v11
	v_mul_f32_e32 v20, 0x41800000, v2
	v_med3_f32 v3, v14, s62, v211
	v_med3_f32 v4, v15, s62, v211
	v_mov_b32_e32 v2, v189
	v_cvt_pk_fp8_f32 v2, v3, v4
	v_med3_f32 v10, v10, s62, v211
	v_med3_f32 v11, v11, s62, v211
	v_mov_b32_e32 v3, v189
	v_cvt_pk_fp8_f32 v3, v10, v11
	v_mul_f32_e32 v16, 0x41800000, v16
	v_mul_f32_e32 v17, 0x41800000, v17
	v_mul_f32_e32 v12, 0x41800000, v12
	v_mul_f32_e32 v13, 0x41800000, v13
	v_med3_f32 v4, v16, s62, v211
	v_med3_f32 v14, v17, s62, v211
	v_mul_f32_e32 v6, 0x41800000, v6
	v_mul_f32_e32 v7, 0x41800000, v7
	v_cvt_pk_fp8_f32 v2, v4, v14 op_sel:[0,0,1]
	v_med3_f32 v4, v12, s62, v211
	v_med3_f32 v10, v13, s62, v211
	v_mul_f32_e32 v8, 0x41800000, v8
	v_mul_f32_e32 v9, 0x41800000, v9
	v_cvt_pk_fp8_f32 v3, v4, v10 op_sel:[0,0,1]
	v_med3_f32 v6, v6, s62, v211
	v_med3_f32 v7, v7, s62, v211
	v_mov_b32_e32 v4, v189
	v_cvt_pk_fp8_f32 v4, v6, v7
	v_med3_f32 v6, v8, s62, v211
	v_med3_f32 v7, v9, s62, v211
	v_med3_f32 v8, v18, s62, v211
	v_med3_f32 v9, v5, s62, v211
	v_mov_b32_e32 v5, v189
	v_cvt_pk_fp8_f32 v5, v8, v9
	v_add_u32_e32 v8, 0xb0, v202
	v_cvt_pk_fp8_f32 v4, v6, v7 op_sel:[0,0,1]
	v_med3_f32 v6, v19, s62, v211
	v_med3_f32 v7, v20, s62, v211
	v_ashrrev_i32_e32 v9, 31, v8
	v_cvt_pk_fp8_f32 v5, v6, v7 op_sel:[0,0,1]
	v_alignbit_b32 v6, v9, v8, 8
	v_mad_u64_u32 v[6:7], s[26:27], v6, 12, s[26:27]
	v_mad_u32_u24 v7, v9, 12, v7
	v_lshlrev_b64 v[6:7], 15, v[6:7]
	v_lshlrev_b32_e32 v8, 7, v8
	v_and_b32_e32 v8, 0x7f80, v8
	v_mov_b32_e32 v9, v189
	v_lshl_add_u64 v[6:7], s[12:13], 0, v[6:7]
	v_lshl_add_u64 v[6:7], v[6:7], 0, v[8:9]
	v_lshl_add_u64 v[6:7], v[6:7], 0, v[190:191]
	flat_store_dwordx4 v[6:7], v[2:5]
	s_andn2_b64 vcc, exec, s[0:1]
	s_mov_b64 s[0:1], -1
	s_cbranch_vccnz .LBB0_755
	s_andn2_b64 vcc, exec, s[10:11]
	s_cbranch_vccnz .LBB0_754
	s_branch .LBB0_754
